# baseline (speedup 1.0000x reference)
_Z16closed_form_mainPKfS0_PKiPf:
	s_load_dwordx8 s[16:23], s[0:1], 0x0
	s_lshr_b32 s6, s2, 3
	v_readfirstlane_b32 s0, v0
	s_mul_hi_u32 s7, s6, 0x24924925
	s_lshr_b32 s4, s0, 6
	s_and_b32 s0, s2, 7
	s_mul_i32 s1, s7, 7
	s_bfe_u32 s5, s2, 0x10003
	s_sub_i32 s1, s6, s1
	s_mul_i32 s36, s0, 7
	s_xor_b32 s3, s4, s5
	s_add_i32 s36, s36, s1
	s_waitcnt lgkmcnt(0)
	s_mov_b64 s[28:29], s[22:23]
	v_and_b32_e32 v19, 63, v0
	s_cmp_lt_u32 s36, 52
	s_mov_b64 s[0:1], -1
	s_cbranch_scc0 .LBB0_32
	s_mul_hi_u32 s0, s6, 0x20820821
	s_lshr_b32 s38, s0, 3
	s_mul_hi_u32 s0, s7, 0x1c71c71d
	s_mul_i32 s0, s0, 9
	s_sub_i32 s0, s7, s0
	v_add_u32_e32 v2, -3, v19
	v_mad_u64_u32 v[0:1], s[0:1], s0, 57, v[2:3]
	s_mov_b64 s[24:25], s[18:19]
	v_mov_b32_e32 v1, 0x200
	v_med3_i32 v1, v0, 0, v1
	s_mul_i32 s34, s36, 10
	s_and_b32 s17, s17, 0xffff
	s_and_b32 s25, s25, 0xffff
	v_cmp_gt_u32_e64 s[0:1], 57, v2
	s_mov_b32 s19, 0x20000
	s_mov_b32 s18, 0xe0e038
	s_mov_b32 s26, 0x606018
	s_mul_i32 s35, s38, 0x70701c
	s_mul_i32 s33, s38, 0x30300c
	v_lshlrev_b32_e32 v28, 2, v1
	v_mul_u32_u24_e32 v27, 12, v1
	v_lshlrev_b32_e32 v23, 4, v19
	s_cmp_lg_u32 s4, s5
	v_sub_u32_e64 v29, s34, 2 clamp
	s_cbranch_scc0 .LBB0_15
	s_mov_b32 s27, s19
	s_and_b32 s21, s21, 0xffff
	s_mov_b32 s22, 0x202008
	s_mov_b32 s23, s19
	s_mul_i32 s38, s38, 0x101004
	s_movk_i32 s37, 0x80
	v_add_u32_e32 v18, -1, v0
	s_movk_i32 s4, 0x201
	s_movk_i32 s5, 0x1ff
	v_cmp_gt_u32_e64 s[40:41], s4, v0
	v_cmp_gt_u32_e64 s[42:43], s5, v18
	v_mov_b32_e32 v18, 0x42c80000
	v_mov_b32_e32 v22, 0x3de38e39
	v_mov_b32_e32 v26, 0x3a3d6628
	v_mov_b32_e32 v1, 0
	s_add_i32 s4, s34, -3
	s_max_i32 s4, s4, 0
	s_mul_i32 s4, s4, 0x804
	s_add_i32 s4, s4, s38
	buffer_load_dword v29, v28, s[20:23], s4 offen nt
	s_add_i32 s4, s34, -2
	s_max_i32 s4, s4, 0
	s_mul_i32 s4, s4, 0x804
	s_add_i32 s4, s4, s38
	buffer_load_dword v2, v28, s[20:23], s4 offen nt
	s_add_i32 s5, s34, -2
	s_max_i32 s5, s5, 0
	s_mul_i32 s6, s5, 0x804
	s_add_i32 s6, s6, s35
	s_add_i32 s7, s6, 0x505014
	s_add_i32 s8, s6, 0x606018
	s_mul_i32 s9, s5, 0x180c
	s_add_i32 s9, s9, s33
	s_add_i32 s4, s34, -1
	s_max_i32 s4, s4, 0
	s_mul_i32 s4, s4, 0x804
	s_add_i32 s4, s4, s38
	buffer_load_dword v3, v28, s[20:23], s4 offen nt
	buffer_load_dwordx3 v[8:10], v27, s[24:27], s9 offen nt
	buffer_load_dword v4, v28, s[16:19], s7 offen nt
	buffer_load_dword v5, v28, s[16:19], s8 offen nt
	s_add_i32 s5, s34, -1
	s_max_i32 s5, s5, 0
	s_mul_i32 s6, s5, 0x804
	s_add_i32 s6, s6, s35
	s_add_i32 s7, s6, 0x505014
	s_add_i32 s8, s6, 0x606018
	s_mul_i32 s9, s5, 0x180c
	s_add_i32 s9, s9, s33
	s_add_i32 s4, s34, 0
	s_min_i32 s4, s4, 0x200
	s_mul_i32 s4, s4, 0x804
	s_add_i32 s4, s4, s38
	buffer_load_dword v16, v28, s[20:23], s4 offen nt
	buffer_load_dwordx3 v[12:14], v27, s[24:27], s9 offen nt
	buffer_load_dword v6, v28, s[16:19], s7 offen nt
	buffer_load_dword v7, v28, s[16:19], s8 offen nt
	s_waitcnt vmcnt(8)
	s_add_i32 s4, s34, -3
	s_cmpk_lt_u32 s4, 0x201
	s_cselect_b64 s[12:13], s[40:41], 0
	v_cmp_eq_u32_e64 s[14:15], s37, v29
	s_and_b64 s[14:15], s[14:15], s[12:13]
	v_cndmask_b32_e64 v17, 0, 1, s[14:15]
	s_add_i32 s4, s34, -2
	s_cmpk_lt_u32 s4, 0x201
	s_cselect_b64 s[12:13], s[40:41], 0
	v_cmp_eq_u32_e64 s[14:15], s37, v2
	s_and_b64 s[14:15], s[14:15], s[12:13]
	v_cndmask_b32_e64 v20, 0, 1, s[14:15]
	s_nop 0
	v_or_b32_dpp v21, v17, v17 wave_shr:1 row_mask:0xf bank_mask:0xf bound_ctrl:1
	v_or_b32_dpp v24, v20, v20 wave_shr:1 row_mask:0xf bank_mask:0xf bound_ctrl:1
	s_nop 1
	v_or_b32_dpp v21, v17, v21 wave_shl:1 row_mask:0xf bank_mask:0xf bound_ctrl:1
	v_or_b32_dpp v24, v20, v24 wave_shl:1 row_mask:0xf bank_mask:0xf bound_ctrl:1
	s_nop 1
	v_or_b32_dpp v25, v21, v21 wave_shr:1 row_mask:0xf bank_mask:0xf bound_ctrl:1
	v_or_b32_dpp v30, v24, v24 wave_shr:1 row_mask:0xf bank_mask:0xf bound_ctrl:1
	s_nop 1
	v_or_b32_dpp v25, v21, v25 wave_shl:1 row_mask:0xf bank_mask:0xf bound_ctrl:1
	v_or_b32_dpp v30, v24, v30 wave_shl:1 row_mask:0xf bank_mask:0xf bound_ctrl:1
	v_mov_b32_e32 v17, 0
	v_mov_b32_e32 v24, 0
	s_add_i32 s5, s34, 0
	s_min_i32 s5, s5, 0x200
	s_mul_i32 s6, s5, 0x804
	s_add_i32 s6, s6, s35
	s_add_i32 s7, s6, 0x505014
	s_add_i32 s8, s6, 0x606018
	s_mul_i32 s9, s5, 0x180c
	s_add_i32 s9, s9, s33
	s_add_i32 s4, s34, 1
	s_min_i32 s4, s4, 0x200
	s_mul_i32 s4, s4, 0x804
	s_add_i32 s4, s4, s38
	buffer_load_dword v31, v28, s[20:23], s4 offen nt
	buffer_load_dwordx3 v[32:34], v27, s[24:27], s9 offen nt
	buffer_load_dword v20, v28, s[16:19], s7 offen nt
	buffer_load_dword v21, v28, s[16:19], s8 offen nt
	s_waitcnt vmcnt(8)
	s_add_i32 s4, s34, -1
	s_cmpk_lt_u32 s4, 0x201
	s_cselect_b64 s[12:13], s[40:41], 0
	v_cmp_eq_u32_e64 s[14:15], s37, v3
	s_and_b64 s[14:15], s[14:15], s[12:13]
	v_cndmask_b32_e64 v36, 0, 1, s[14:15]
	v_mul_f32_e64 v38, v8, v8
	v_mul_f32_e64 v39, v8, v9
	v_mul_f32_e64 v40, v8, v10
	v_mul_f32_e64 v41, v9, v9
	v_mul_f32_e64 v42, v9, v10
	v_mul_f32_e64 v43, v10, v10
	v_or_b32_dpp v37, v36, v36 wave_shr:1 row_mask:0xf bank_mask:0xf bound_ctrl:1
	s_nop 1
	v_or_b32_dpp v37, v36, v37 wave_shl:1 row_mask:0xf bank_mask:0xf bound_ctrl:1
	s_nop 1
	v_or_b32_dpp v44, v37, v37 wave_shr:1 row_mask:0xf bank_mask:0xf bound_ctrl:1
	s_nop 1
	v_or_b32_dpp v44, v37, v44 wave_shl:1 row_mask:0xf bank_mask:0xf bound_ctrl:1
	v_or3_b32 v45, v44, v30, v25
	v_or3_b32 v45, v45, v17, v24
	s_add_i32 s4, s34, -4
	s_cmpk_lt_u32 s4, 0x1ff
	s_cselect_b64 s[12:13], s[42:43], 0
	v_cmp_ne_u32_e64 s[30:31], 0, v45
	s_and_b64 s[30:31], s[30:31], s[12:13]
	v_cndmask_b32_e64 v45, 0, 1.0, s[30:31]
	v_add_f32_dpp v36, v8, v8 wave_shr:1 row_mask:0xf bank_mask:0xf bound_ctrl:1
	v_add_f32_dpp v37, v9, v9 wave_shr:1 row_mask:0xf bank_mask:0xf bound_ctrl:1
	v_add_f32_dpp v46, v10, v10 wave_shr:1 row_mask:0xf bank_mask:0xf bound_ctrl:1
	v_add_f32_dpp v47, v38, v38 wave_shr:1 row_mask:0xf bank_mask:0xf bound_ctrl:1
	v_add_f32_dpp v48, v39, v39 wave_shr:1 row_mask:0xf bank_mask:0xf bound_ctrl:1
	v_add_f32_dpp v49, v40, v40 wave_shr:1 row_mask:0xf bank_mask:0xf bound_ctrl:1
	v_add_f32_dpp v50, v41, v41 wave_shr:1 row_mask:0xf bank_mask:0xf bound_ctrl:1
	v_add_f32_dpp v51, v42, v42 wave_shr:1 row_mask:0xf bank_mask:0xf bound_ctrl:1
	v_add_f32_dpp v52, v43, v43 wave_shr:1 row_mask:0xf bank_mask:0xf bound_ctrl:1
	v_add_f32_dpp v53, v45, v45 wave_shr:1 row_mask:0xf bank_mask:0xf bound_ctrl:1
	v_add_f32_dpp v36, v8, v36 wave_shl:1 row_mask:0xf bank_mask:0xf bound_ctrl:1
	v_add_f32_dpp v37, v9, v37 wave_shl:1 row_mask:0xf bank_mask:0xf bound_ctrl:1
	v_add_f32_dpp v46, v10, v46 wave_shl:1 row_mask:0xf bank_mask:0xf bound_ctrl:1
	v_add_f32_dpp v47, v38, v47 wave_shl:1 row_mask:0xf bank_mask:0xf bound_ctrl:1
	v_add_f32_dpp v48, v39, v48 wave_shl:1 row_mask:0xf bank_mask:0xf bound_ctrl:1
	v_add_f32_dpp v49, v40, v49 wave_shl:1 row_mask:0xf bank_mask:0xf bound_ctrl:1
	v_add_f32_dpp v50, v41, v50 wave_shl:1 row_mask:0xf bank_mask:0xf bound_ctrl:1
	v_add_f32_dpp v51, v42, v51 wave_shl:1 row_mask:0xf bank_mask:0xf bound_ctrl:1
	v_add_f32_dpp v52, v43, v52 wave_shl:1 row_mask:0xf bank_mask:0xf bound_ctrl:1
	v_add_f32_dpp v53, v45, v53 wave_shl:1 row_mask:0xf bank_mask:0xf bound_ctrl:1
	s_barrier
	v_pk_mul_f32 v[38:39], v[4:5], v[8:9] op_sel_hi:[1,0]
	v_pk_mul_f32 v[40:41], v[4:5], v[8:9] op_sel:[0,1]
	v_pk_mul_f32 v[42:43], v[4:5], v[10:11] op_sel_hi:[1,0]
	v_add_f32_dpp v54, v4, v4 wave_shr:1 row_mask:0xf bank_mask:0xf bound_ctrl:1
	v_add_f32_dpp v55, v5, v5 wave_shr:1 row_mask:0xf bank_mask:0xf bound_ctrl:1
	v_add_f32_dpp v56, v38, v38 wave_shr:1 row_mask:0xf bank_mask:0xf bound_ctrl:1
	v_add_f32_dpp v57, v39, v39 wave_shr:1 row_mask:0xf bank_mask:0xf bound_ctrl:1
	v_add_f32_dpp v58, v40, v40 wave_shr:1 row_mask:0xf bank_mask:0xf bound_ctrl:1
	v_add_f32_dpp v59, v41, v41 wave_shr:1 row_mask:0xf bank_mask:0xf bound_ctrl:1
	v_add_f32_dpp v60, v42, v42 wave_shr:1 row_mask:0xf bank_mask:0xf bound_ctrl:1
	v_add_f32_dpp v61, v43, v43 wave_shr:1 row_mask:0xf bank_mask:0xf bound_ctrl:1
	v_add_f32_dpp v54, v4, v54 wave_shl:1 row_mask:0xf bank_mask:0xf bound_ctrl:1
	v_add_f32_dpp v55, v5, v55 wave_shl:1 row_mask:0xf bank_mask:0xf bound_ctrl:1
	v_add_f32_dpp v56, v38, v56 wave_shl:1 row_mask:0xf bank_mask:0xf bound_ctrl:1
	v_add_f32_dpp v57, v39, v57 wave_shl:1 row_mask:0xf bank_mask:0xf bound_ctrl:1
	v_add_f32_dpp v58, v40, v58 wave_shl:1 row_mask:0xf bank_mask:0xf bound_ctrl:1
	v_add_f32_dpp v59, v41, v59 wave_shl:1 row_mask:0xf bank_mask:0xf bound_ctrl:1
	v_add_f32_dpp v60, v42, v60 wave_shl:1 row_mask:0xf bank_mask:0xf bound_ctrl:1
	v_add_f32_dpp v61, v43, v61 wave_shl:1 row_mask:0xf bank_mask:0xf bound_ctrl:1
	s_add_i32 s5, s34, 1
	s_min_i32 s5, s5, 0x200
	s_mul_i32 s6, s5, 0x804
	s_add_i32 s6, s6, s35
	s_add_i32 s7, s6, 0x505014
	s_add_i32 s8, s6, 0x606018
	s_mul_i32 s9, s5, 0x180c
	s_add_i32 s9, s9, s33
	s_add_i32 s4, s34, 2
	s_min_i32 s4, s4, 0x200
	s_mul_i32 s4, s4, 0x804
	s_add_i32 s4, s4, s38
	buffer_load_dword v24, v28, s[20:23], s4 offen nt
	buffer_load_dwordx3 v[40:42], v27, s[24:27], s9 offen nt
	buffer_load_dword v38, v28, s[16:19], s7 offen nt
	buffer_load_dword v39, v28, s[16:19], s8 offen nt
	s_waitcnt vmcnt(8)
	s_add_i32 s4, s34, 0
	s_cmpk_lt_u32 s4, 0x201
	s_cselect_b64 s[12:13], s[40:41], 0
	v_cmp_eq_u32_e64 s[14:15], s37, v16
	s_and_b64 s[14:15], s[14:15], s[12:13]
	v_cndmask_b32_e64 v45, 0, 1, s[14:15]
	v_mul_f32_e64 v62, v12, v12
	v_mul_f32_e64 v63, v12, v13
	v_mul_f32_e64 v64, v12, v14
	v_mul_f32_e64 v65, v13, v13
	v_mul_f32_e64 v66, v13, v14
	v_mul_f32_e64 v67, v14, v14
	v_or_b32_dpp v68, v45, v45 wave_shr:1 row_mask:0xf bank_mask:0xf bound_ctrl:1
	s_nop 1
	v_or_b32_dpp v68, v45, v68 wave_shl:1 row_mask:0xf bank_mask:0xf bound_ctrl:1
	s_nop 1
	v_or_b32_dpp v69, v68, v68 wave_shr:1 row_mask:0xf bank_mask:0xf bound_ctrl:1
	s_nop 1
	v_or_b32_dpp v69, v68, v69 wave_shl:1 row_mask:0xf bank_mask:0xf bound_ctrl:1
	v_or3_b32 v45, v69, v44, v30
	v_or3_b32 v45, v45, v25, v17
	s_add_i32 s4, s34, -3
	s_cmpk_lt_u32 s4, 0x1ff
	s_cselect_b64 s[12:13], s[42:43], 0
	v_cmp_ne_u32_e64 s[30:31], 0, v45
	s_and_b64 s[30:31], s[30:31], s[12:13]
	v_cndmask_b32_e64 v45, 0, 1.0, s[30:31]
	v_add_f32_dpp v70, v12, v12 wave_shr:1 row_mask:0xf bank_mask:0xf bound_ctrl:1
	v_add_f32_dpp v71, v13, v13 wave_shr:1 row_mask:0xf bank_mask:0xf bound_ctrl:1
	v_add_f32_dpp v72, v14, v14 wave_shr:1 row_mask:0xf bank_mask:0xf bound_ctrl:1
	v_add_f32_dpp v73, v62, v62 wave_shr:1 row_mask:0xf bank_mask:0xf bound_ctrl:1
	v_add_f32_dpp v74, v63, v63 wave_shr:1 row_mask:0xf bank_mask:0xf bound_ctrl:1
	v_add_f32_dpp v75, v64, v64 wave_shr:1 row_mask:0xf bank_mask:0xf bound_ctrl:1
	v_add_f32_dpp v76, v65, v65 wave_shr:1 row_mask:0xf bank_mask:0xf bound_ctrl:1
	v_add_f32_dpp v77, v66, v66 wave_shr:1 row_mask:0xf bank_mask:0xf bound_ctrl:1
	v_add_f32_dpp v78, v67, v67 wave_shr:1 row_mask:0xf bank_mask:0xf bound_ctrl:1
	v_add_f32_dpp v79, v45, v45 wave_shr:1 row_mask:0xf bank_mask:0xf bound_ctrl:1
	v_add_f32_dpp v70, v12, v70 wave_shl:1 row_mask:0xf bank_mask:0xf bound_ctrl:1
	v_add_f32_dpp v71, v13, v71 wave_shl:1 row_mask:0xf bank_mask:0xf bound_ctrl:1
	v_add_f32_dpp v72, v14, v72 wave_shl:1 row_mask:0xf bank_mask:0xf bound_ctrl:1
	v_add_f32_dpp v73, v62, v73 wave_shl:1 row_mask:0xf bank_mask:0xf bound_ctrl:1
	v_add_f32_dpp v74, v63, v74 wave_shl:1 row_mask:0xf bank_mask:0xf bound_ctrl:1
	v_add_f32_dpp v75, v64, v75 wave_shl:1 row_mask:0xf bank_mask:0xf bound_ctrl:1
	v_add_f32_dpp v76, v65, v76 wave_shl:1 row_mask:0xf bank_mask:0xf bound_ctrl:1
	v_add_f32_dpp v77, v66, v77 wave_shl:1 row_mask:0xf bank_mask:0xf bound_ctrl:1
	v_add_f32_dpp v78, v67, v78 wave_shl:1 row_mask:0xf bank_mask:0xf bound_ctrl:1
	v_add_f32_dpp v79, v45, v79 wave_shl:1 row_mask:0xf bank_mask:0xf bound_ctrl:1
	s_barrier
	v_pk_mul_f32 v[62:63], v[6:7], v[12:13] op_sel_hi:[1,0]
	v_pk_mul_f32 v[64:65], v[6:7], v[12:13] op_sel:[0,1]
	v_pk_mul_f32 v[66:67], v[6:7], v[14:15] op_sel_hi:[1,0]
	v_add_f32_dpp v80, v6, v6 wave_shr:1 row_mask:0xf bank_mask:0xf bound_ctrl:1
	v_add_f32_dpp v81, v7, v7 wave_shr:1 row_mask:0xf bank_mask:0xf bound_ctrl:1
	v_add_f32_dpp v82, v62, v62 wave_shr:1 row_mask:0xf bank_mask:0xf bound_ctrl:1
	v_add_f32_dpp v83, v63, v63 wave_shr:1 row_mask:0xf bank_mask:0xf bound_ctrl:1
	v_add_f32_dpp v84, v64, v64 wave_shr:1 row_mask:0xf bank_mask:0xf bound_ctrl:1
	v_add_f32_dpp v85, v65, v65 wave_shr:1 row_mask:0xf bank_mask:0xf bound_ctrl:1
	v_add_f32_dpp v86, v66, v66 wave_shr:1 row_mask:0xf bank_mask:0xf bound_ctrl:1
	v_add_f32_dpp v87, v67, v67 wave_shr:1 row_mask:0xf bank_mask:0xf bound_ctrl:1
	v_add_f32_dpp v80, v6, v80 wave_shl:1 row_mask:0xf bank_mask:0xf bound_ctrl:1
	v_add_f32_dpp v81, v7, v81 wave_shl:1 row_mask:0xf bank_mask:0xf bound_ctrl:1
	v_add_f32_dpp v82, v62, v82 wave_shl:1 row_mask:0xf bank_mask:0xf bound_ctrl:1
	v_add_f32_dpp v83, v63, v83 wave_shl:1 row_mask:0xf bank_mask:0xf bound_ctrl:1
	v_add_f32_dpp v84, v64, v84 wave_shl:1 row_mask:0xf bank_mask:0xf bound_ctrl:1
	v_add_f32_dpp v85, v65, v85 wave_shl:1 row_mask:0xf bank_mask:0xf bound_ctrl:1
	v_add_f32_dpp v86, v66, v86 wave_shl:1 row_mask:0xf bank_mask:0xf bound_ctrl:1
	v_add_f32_dpp v87, v67, v87 wave_shl:1 row_mask:0xf bank_mask:0xf bound_ctrl:1
	s_add_i32 s5, s34, 2
	s_min_i32 s5, s5, 0x200
	s_mul_i32 s6, s5, 0x804
	s_add_i32 s6, s6, s35
	s_add_i32 s7, s6, 0x505014
	s_add_i32 s8, s6, 0x606018
	s_mul_i32 s9, s5, 0x180c
	s_add_i32 s9, s9, s33
	s_add_i32 s4, s34, 3
	s_min_i32 s4, s4, 0x200
	s_mul_i32 s4, s4, 0x804
	s_add_i32 s4, s4, s38
	buffer_load_dword v17, v28, s[20:23], s4 offen nt
	buffer_load_dwordx3 v[64:66], v27, s[24:27], s9 offen nt
	buffer_load_dword v62, v28, s[16:19], s7 offen nt
	buffer_load_dword v63, v28, s[16:19], s8 offen nt
	s_waitcnt vmcnt(8)
	s_add_i32 s4, s34, 1
	s_cmpk_lt_u32 s4, 0x201
	s_cselect_b64 s[12:13], s[40:41], 0
	v_cmp_eq_u32_e64 s[14:15], s37, v31
	s_and_b64 s[14:15], s[14:15], s[12:13]
	v_cndmask_b32_e64 v29, 0, 1, s[14:15]
	v_mul_f32_e64 v88, v32, v32
	v_mul_f32_e64 v89, v32, v33
	v_mul_f32_e64 v90, v32, v34
	v_mul_f32_e64 v91, v33, v33
	v_mul_f32_e64 v92, v33, v34
	v_mul_f32_e64 v93, v34, v34
	v_or_b32_dpp v45, v29, v29 wave_shr:1 row_mask:0xf bank_mask:0xf bound_ctrl:1
	s_nop 1
	v_or_b32_dpp v45, v29, v45 wave_shl:1 row_mask:0xf bank_mask:0xf bound_ctrl:1
	s_nop 1
	v_or_b32_dpp v68, v45, v45 wave_shr:1 row_mask:0xf bank_mask:0xf bound_ctrl:1
	s_nop 1
	v_or_b32_dpp v68, v45, v68 wave_shl:1 row_mask:0xf bank_mask:0xf bound_ctrl:1
	v_or3_b32 v29, v68, v69, v44
	v_or3_b32 v29, v29, v30, v25
	s_add_i32 s4, s34, -2
	s_cmpk_lt_u32 s4, 0x1ff
	s_cselect_b64 s[12:13], s[42:43], 0
	v_cmp_ne_u32_e64 s[30:31], 0, v29
	s_and_b64 s[30:31], s[30:31], s[12:13]
	v_cndmask_b32_e64 v29, 0, 1.0, s[30:31]
	v_add_f32_dpp v94, v32, v32 wave_shr:1 row_mask:0xf bank_mask:0xf bound_ctrl:1
	v_add_f32_dpp v95, v33, v33 wave_shr:1 row_mask:0xf bank_mask:0xf bound_ctrl:1
	v_add_f32_dpp v96, v34, v34 wave_shr:1 row_mask:0xf bank_mask:0xf bound_ctrl:1
	v_add_f32_dpp v97, v88, v88 wave_shr:1 row_mask:0xf bank_mask:0xf bound_ctrl:1
	v_add_f32_dpp v98, v89, v89 wave_shr:1 row_mask:0xf bank_mask:0xf bound_ctrl:1
	v_add_f32_dpp v99, v90, v90 wave_shr:1 row_mask:0xf bank_mask:0xf bound_ctrl:1
	v_add_f32_dpp v100, v91, v91 wave_shr:1 row_mask:0xf bank_mask:0xf bound_ctrl:1
	v_add_f32_dpp v101, v92, v92 wave_shr:1 row_mask:0xf bank_mask:0xf bound_ctrl:1
	v_add_f32_dpp v102, v93, v93 wave_shr:1 row_mask:0xf bank_mask:0xf bound_ctrl:1
	v_add_f32_dpp v103, v29, v29 wave_shr:1 row_mask:0xf bank_mask:0xf bound_ctrl:1
	v_add_f32_dpp v94, v32, v94 wave_shl:1 row_mask:0xf bank_mask:0xf bound_ctrl:1
	v_add_f32_dpp v95, v33, v95 wave_shl:1 row_mask:0xf bank_mask:0xf bound_ctrl:1
	v_add_f32_dpp v96, v34, v96 wave_shl:1 row_mask:0xf bank_mask:0xf bound_ctrl:1
	v_add_f32_dpp v97, v88, v97 wave_shl:1 row_mask:0xf bank_mask:0xf bound_ctrl:1
	v_add_f32_dpp v98, v89, v98 wave_shl:1 row_mask:0xf bank_mask:0xf bound_ctrl:1
	v_add_f32_dpp v99, v90, v99 wave_shl:1 row_mask:0xf bank_mask:0xf bound_ctrl:1
	v_add_f32_dpp v100, v91, v100 wave_shl:1 row_mask:0xf bank_mask:0xf bound_ctrl:1
	v_add_f32_dpp v101, v92, v101 wave_shl:1 row_mask:0xf bank_mask:0xf bound_ctrl:1
	v_add_f32_dpp v102, v93, v102 wave_shl:1 row_mask:0xf bank_mask:0xf bound_ctrl:1
	v_add_f32_dpp v103, v29, v103 wave_shl:1 row_mask:0xf bank_mask:0xf bound_ctrl:1
	v_pk_add_f32 v[88:89], v[70:71], v[94:95]
	v_pk_add_f32 v[90:91], v[36:37], v[88:89]
	v_pk_add_f32 v[36:37], v[72:73], v[96:97]
	v_pk_add_f32 v[70:71], v[46:47], v[36:37]
	v_pk_add_f32 v[46:47], v[74:75], v[98:99]
	v_pk_add_f32 v[72:73], v[48:49], v[46:47]
	v_pk_add_f32 v[48:49], v[76:77], v[100:101]
	v_pk_add_f32 v[74:75], v[50:51], v[48:49]
	v_pk_add_f32 v[50:51], v[78:79], v[102:103]
	v_pk_add_f32 v[76:77], v[52:53], v[50:51]
	v_mul_f32_e64 v104, v90, v22
	v_mul_f32_e64 v105, v91, v22
	v_mul_f32_e64 v106, v70, v22
	v_fma_f32 v29, v71, v22, v26
	v_mul_f32_e64 v45, v72, v22
	v_mul_f32_e64 v52, v73, v22
	v_fma_f32 v53, v74, v22, v26
	v_mul_f32_e64 v78, v75, v22
	v_fma_f32 v79, v76, v22, v26
	v_fma_f32 v29, -v104, v104, v29
	v_fma_f32 v45, -v104, v105, v45
	v_fma_f32 v52, -v104, v106, v52
	v_fma_f32 v53, -v105, v105, v53
	v_fma_f32 v78, -v105, v106, v78
	v_fma_f32 v79, -v106, v106, v79
	v_mul_f32_e64 v92, v78, v78
	v_mul_f32_e64 v93, v45, v79
	v_mul_f32_e64 v116, v52, v53
	v_mul_f32_e64 v117, v52, v52
	v_mul_f32_e64 v118, v29, v78
	v_mul_f32_e64 v119, v45, v45
	v_fma_f32 v92, v53, v79, -v92
	v_fma_f32 v93, v52, v78, -v93
	v_fma_f32 v116, v45, v78, -v116
	v_fma_f32 v117, v29, v79, -v117
	v_fma_f32 v118, v45, v52, -v118
	v_fma_f32 v119, v29, v53, -v119
	v_mul_f32_e64 v120, v29, v92
	v_fma_f32 v120, v45, v93, v120
	v_fma_f32 v120, v52, v116, v120
	v_rcp_f32_e32 v120, v120
	v_cmp_ne_u32_e64 vcc, s37, v2
	v_mul_f32_e64 v120, v120, v22
	v_cndmask_b32_e64 v120, 0, v120, s[30:31]
	v_cndmask_b32_e64 v29, 0, v18, vcc
	v_cndmask_b32_e64 v113, 0, v22, s[30:31]
	v_mul_f32_e64 v107, v92, v120
	v_mul_f32_e64 v108, v93, v120
	v_mul_f32_e64 v109, v116, v120
	v_mul_f32_e64 v110, v117, v120
	v_mul_f32_e64 v111, v118, v120
	v_mul_f32_e64 v112, v119, v120
	v_add_f32_e64 v114, v77, v29
	v_mov_b32_e32 v115, v2
	ds_write_b128 v23, v[104:107]
	ds_write_b128 v23, v[108:111] offset:1024
	ds_write_b128 v23, v[112:115] offset:2048
	s_waitcnt lgkmcnt(0)
	s_barrier
	v_pk_mul_f32 v[52:53], v[20:21], v[32:33] op_sel_hi:[1,0]
	v_pk_mul_f32 v[70:71], v[20:21], v[32:33] op_sel:[0,1]
	v_pk_mul_f32 v[72:73], v[20:21], v[34:35] op_sel_hi:[1,0]
	v_add_f32_dpp v74, v20, v20 wave_shr:1 row_mask:0xf bank_mask:0xf bound_ctrl:1
	v_add_f32_dpp v75, v21, v21 wave_shr:1 row_mask:0xf bank_mask:0xf bound_ctrl:1
	v_add_f32_dpp v76, v52, v52 wave_shr:1 row_mask:0xf bank_mask:0xf bound_ctrl:1
	v_add_f32_dpp v77, v53, v53 wave_shr:1 row_mask:0xf bank_mask:0xf bound_ctrl:1
	v_add_f32_dpp v78, v70, v70 wave_shr:1 row_mask:0xf bank_mask:0xf bound_ctrl:1
	v_add_f32_dpp v79, v71, v71 wave_shr:1 row_mask:0xf bank_mask:0xf bound_ctrl:1
	v_add_f32_dpp v90, v72, v72 wave_shr:1 row_mask:0xf bank_mask:0xf bound_ctrl:1
	v_add_f32_dpp v91, v73, v73 wave_shr:1 row_mask:0xf bank_mask:0xf bound_ctrl:1
	v_add_f32_dpp v74, v20, v74 wave_shl:1 row_mask:0xf bank_mask:0xf bound_ctrl:1
	v_add_f32_dpp v75, v21, v75 wave_shl:1 row_mask:0xf bank_mask:0xf bound_ctrl:1
	v_add_f32_dpp v76, v52, v76 wave_shl:1 row_mask:0xf bank_mask:0xf bound_ctrl:1
	v_add_f32_dpp v77, v53, v77 wave_shl:1 row_mask:0xf bank_mask:0xf bound_ctrl:1
	v_add_f32_dpp v78, v70, v78 wave_shl:1 row_mask:0xf bank_mask:0xf bound_ctrl:1
	v_add_f32_dpp v79, v71, v79 wave_shl:1 row_mask:0xf bank_mask:0xf bound_ctrl:1
	v_add_f32_dpp v90, v72, v90 wave_shl:1 row_mask:0xf bank_mask:0xf bound_ctrl:1
	v_add_f32_dpp v91, v73, v91 wave_shl:1 row_mask:0xf bank_mask:0xf bound_ctrl:1
	v_pk_add_f32 v[52:53], v[80:81], v[74:75]
	v_pk_add_f32 v[70:71], v[54:55], v[52:53]
	v_pk_add_f32 v[54:55], v[82:83], v[76:77]
	v_pk_add_f32 v[72:73], v[56:57], v[54:55]
	v_pk_add_f32 v[56:57], v[84:85], v[78:79]
	v_pk_add_f32 v[80:81], v[58:59], v[56:57]
	v_pk_add_f32 v[58:59], v[86:87], v[90:91]
	v_pk_add_f32 v[82:83], v[60:61], v[58:59]
	v_pk_fma_f32 v[72:73], v[104:105], v[70:71], v[72:73] op_sel_hi:[0,1,1] neg_lo:[1,0,0] neg_hi:[1,0,0]
	v_pk_fma_f32 v[80:81], v[104:105], v[70:71], v[80:81] op_sel:[1,0,0] neg_lo:[1,0,0] neg_hi:[1,0,0]
	v_pk_fma_f32 v[82:83], v[106:107], v[70:71], v[82:83] op_sel_hi:[0,1,1] neg_lo:[1,0,0] neg_hi:[1,0,0]
	v_pk_mul_f32 v[60:61], v[106:107], v[72:73] op_sel:[1,0]
	v_pk_mul_f32 v[84:85], v[108:109], v[72:73] op_sel_hi:[0,1]
	v_pk_mul_f32 v[86:87], v[108:109], v[72:73] op_sel:[1,0]
	v_pk_fma_f32 v[60:61], v[108:109], v[80:81], v[60:61] op_sel_hi:[0,1,1]
	v_pk_fma_f32 v[84:85], v[110:111], v[80:81], v[84:85] op_sel_hi:[0,1,1]
	v_pk_fma_f32 v[86:87], v[110:111], v[80:81], v[86:87] op_sel:[1,0,0]
	v_pk_fma_f32 v[60:61], v[108:109], v[82:83], v[60:61] op_sel:[1,0,0]
	v_pk_fma_f32 v[84:85], v[110:111], v[82:83], v[84:85] op_sel:[1,0,0]
	v_pk_fma_f32 v[86:87], v[112:113], v[82:83], v[86:87] op_sel_hi:[0,1,1]
	v_pk_mul_f32 v[92:93], v[104:105], v[60:61] op_sel_hi:[0,1]
	v_pk_fma_f32 v[92:93], v[104:105], v[84:85], v[92:93] op_sel:[1,0,0]
	v_pk_fma_f32 v[92:93], v[106:107], v[86:87], v[92:93] op_sel_hi:[0,1,1]
	v_pk_fma_f32 v[92:93], v[112:113], v[70:71], v[92:93] op_sel:[1,0,0] neg_lo:[0,0,1] neg_hi:[0,0,1]
	v_add_f32_dpp v70, v60, v60 wave_shr:1 row_mask:0xf bank_mask:0xf bound_ctrl:1
	v_add_f32_dpp v71, v61, v61 wave_shr:1 row_mask:0xf bank_mask:0xf bound_ctrl:1
	v_add_f32_dpp v72, v84, v84 wave_shr:1 row_mask:0xf bank_mask:0xf bound_ctrl:1
	v_add_f32_dpp v73, v85, v85 wave_shr:1 row_mask:0xf bank_mask:0xf bound_ctrl:1
	v_add_f32_dpp v80, v86, v86 wave_shr:1 row_mask:0xf bank_mask:0xf bound_ctrl:1
	v_add_f32_dpp v81, v87, v87 wave_shr:1 row_mask:0xf bank_mask:0xf bound_ctrl:1
	v_add_f32_dpp v82, v92, v92 wave_shr:1 row_mask:0xf bank_mask:0xf bound_ctrl:1
	v_add_f32_dpp v83, v93, v93 wave_shr:1 row_mask:0xf bank_mask:0xf bound_ctrl:1
	v_add_f32_dpp v70, v60, v70 wave_shl:1 row_mask:0xf bank_mask:0xf bound_ctrl:1
	v_add_f32_dpp v71, v61, v71 wave_shl:1 row_mask:0xf bank_mask:0xf bound_ctrl:1
	v_add_f32_dpp v72, v84, v72 wave_shl:1 row_mask:0xf bank_mask:0xf bound_ctrl:1
	v_add_f32_dpp v73, v85, v73 wave_shl:1 row_mask:0xf bank_mask:0xf bound_ctrl:1
	v_add_f32_dpp v80, v86, v80 wave_shl:1 row_mask:0xf bank_mask:0xf bound_ctrl:1
	v_add_f32_dpp v81, v87, v81 wave_shl:1 row_mask:0xf bank_mask:0xf bound_ctrl:1
	v_add_f32_dpp v82, v92, v82 wave_shl:1 row_mask:0xf bank_mask:0xf bound_ctrl:1
	v_add_f32_dpp v83, v93, v83 wave_shl:1 row_mask:0xf bank_mask:0xf bound_ctrl:1
	s_add_i32 s5, s34, 3
	s_min_i32 s5, s5, 0x200
	s_mul_i32 s6, s5, 0x804
	s_add_i32 s6, s6, s35
	s_add_i32 s7, s6, 0x505014
	s_add_i32 s8, s6, 0x606018
	s_mul_i32 s9, s5, 0x180c
	s_add_i32 s9, s9, s33
	s_add_i32 s4, s34, 4
	s_min_i32 s4, s4, 0x200
	s_mul_i32 s4, s4, 0x804
	s_add_i32 s4, s4, s38
	buffer_load_dword v2, v28, s[20:23], s4 offen nt
	buffer_load_dwordx3 v[8:10], v27, s[24:27], s9 offen nt
	buffer_load_dword v4, v28, s[16:19], s7 offen nt
	buffer_load_dword v5, v28, s[16:19], s8 offen nt
	s_waitcnt vmcnt(8)
	s_add_i32 s4, s34, 2
	s_cmpk_lt_u32 s4, 0x201
	s_cselect_b64 s[12:13], s[40:41], 0
	v_cmp_eq_u32_e64 s[14:15], s37, v24
	s_and_b64 s[14:15], s[14:15], s[12:13]
	v_cndmask_b32_e64 v25, 0, 1, s[14:15]
	v_mul_f32_e64 v60, v40, v40
	v_mul_f32_e64 v61, v40, v41
	v_mul_f32_e64 v84, v40, v42
	v_mul_f32_e64 v85, v41, v41
	v_mul_f32_e64 v86, v41, v42
	v_mul_f32_e64 v87, v42, v42
	v_or_b32_dpp v29, v25, v25 wave_shr:1 row_mask:0xf bank_mask:0xf bound_ctrl:1
	s_nop 1
	v_or_b32_dpp v29, v25, v29 wave_shl:1 row_mask:0xf bank_mask:0xf bound_ctrl:1
	s_nop 1
	v_or_b32_dpp v45, v29, v29 wave_shr:1 row_mask:0xf bank_mask:0xf bound_ctrl:1
	s_nop 1
	v_or_b32_dpp v45, v29, v45 wave_shl:1 row_mask:0xf bank_mask:0xf bound_ctrl:1
	v_or3_b32 v25, v45, v68, v69
	v_or3_b32 v25, v25, v44, v30
	s_add_i32 s4, s34, -1
	s_cmpk_lt_u32 s4, 0x1ff
	s_cselect_b64 s[12:13], s[42:43], 0
	v_cmp_ne_u32_e64 s[30:31], 0, v25
	s_and_b64 s[30:31], s[30:31], s[12:13]
	v_cndmask_b32_e64 v25, 0, 1.0, s[30:31]
	v_add_f32_dpp v92, v40, v40 wave_shr:1 row_mask:0xf bank_mask:0xf bound_ctrl:1
	v_add_f32_dpp v93, v41, v41 wave_shr:1 row_mask:0xf bank_mask:0xf bound_ctrl:1
	v_add_f32_dpp v104, v42, v42 wave_shr:1 row_mask:0xf bank_mask:0xf bound_ctrl:1
	v_add_f32_dpp v105, v60, v60 wave_shr:1 row_mask:0xf bank_mask:0xf bound_ctrl:1
	v_add_f32_dpp v106, v61, v61 wave_shr:1 row_mask:0xf bank_mask:0xf bound_ctrl:1
	v_add_f32_dpp v107, v84, v84 wave_shr:1 row_mask:0xf bank_mask:0xf bound_ctrl:1
	v_add_f32_dpp v108, v85, v85 wave_shr:1 row_mask:0xf bank_mask:0xf bound_ctrl:1
	v_add_f32_dpp v109, v86, v86 wave_shr:1 row_mask:0xf bank_mask:0xf bound_ctrl:1
	v_add_f32_dpp v110, v87, v87 wave_shr:1 row_mask:0xf bank_mask:0xf bound_ctrl:1
	v_add_f32_dpp v111, v25, v25 wave_shr:1 row_mask:0xf bank_mask:0xf bound_ctrl:1
	v_add_f32_dpp v92, v40, v92 wave_shl:1 row_mask:0xf bank_mask:0xf bound_ctrl:1
	v_add_f32_dpp v93, v41, v93 wave_shl:1 row_mask:0xf bank_mask:0xf bound_ctrl:1
	v_add_f32_dpp v104, v42, v104 wave_shl:1 row_mask:0xf bank_mask:0xf bound_ctrl:1
	v_add_f32_dpp v105, v60, v105 wave_shl:1 row_mask:0xf bank_mask:0xf bound_ctrl:1
	v_add_f32_dpp v106, v61, v106 wave_shl:1 row_mask:0xf bank_mask:0xf bound_ctrl:1
	v_add_f32_dpp v107, v84, v107 wave_shl:1 row_mask:0xf bank_mask:0xf bound_ctrl:1
	v_add_f32_dpp v108, v85, v108 wave_shl:1 row_mask:0xf bank_mask:0xf bound_ctrl:1
	v_add_f32_dpp v109, v86, v109 wave_shl:1 row_mask:0xf bank_mask:0xf bound_ctrl:1
	v_add_f32_dpp v110, v87, v110 wave_shl:1 row_mask:0xf bank_mask:0xf bound_ctrl:1
	v_add_f32_dpp v111, v25, v111 wave_shl:1 row_mask:0xf bank_mask:0xf bound_ctrl:1
	v_pk_add_f32 v[60:61], v[88:89], v[92:93]
	v_pk_add_f32 v[84:85], v[36:37], v[104:105]
	v_pk_add_f32 v[36:37], v[46:47], v[106:107]
	v_pk_add_f32 v[46:47], v[48:49], v[108:109]
	v_pk_add_f32 v[48:49], v[50:51], v[110:111]
	v_mul_f32_e64 v112, v60, v22
	v_mul_f32_e64 v113, v61, v22
	v_mul_f32_e64 v114, v84, v22
	v_fma_f32 v25, v85, v22, v26
	v_mul_f32_e64 v29, v36, v22
	v_mul_f32_e64 v50, v37, v22
	v_fma_f32 v51, v46, v22, v26
	v_mul_f32_e64 v86, v47, v22
	v_fma_f32 v87, v48, v22, v26
	v_fma_f32 v25, -v112, v112, v25
	v_fma_f32 v29, -v112, v113, v29
	v_fma_f32 v50, -v112, v114, v50
	v_fma_f32 v51, -v113, v113, v51
	v_fma_f32 v86, -v113, v114, v86
	v_fma_f32 v87, -v114, v114, v87
	v_mul_f32_e64 v88, v86, v86
	v_mul_f32_e64 v89, v29, v87
	v_mul_f32_e64 v124, v50, v51
	v_mul_f32_e64 v125, v50, v50
	v_mul_f32_e64 v126, v25, v86
	v_mul_f32_e64 v127, v29, v29
	v_fma_f32 v88, v51, v87, -v88
	v_fma_f32 v89, v50, v86, -v89
	v_fma_f32 v124, v29, v86, -v124
	v_fma_f32 v125, v25, v87, -v125
	v_fma_f32 v126, v29, v50, -v126
	v_fma_f32 v127, v25, v51, -v127
	v_mul_f32_e64 v128, v25, v88
	v_fma_f32 v128, v29, v89, v128
	v_fma_f32 v128, v50, v124, v128
	v_rcp_f32_e32 v128, v128
	v_cmp_ne_u32_e64 vcc, s37, v3
	v_mul_f32_e64 v128, v128, v22
	v_cndmask_b32_e64 v128, 0, v128, s[30:31]
	v_cndmask_b32_e64 v25, 0, v18, vcc
	v_cndmask_b32_e64 v121, 0, v22, s[30:31]
	v_mul_f32_e64 v115, v88, v128
	v_mul_f32_e64 v116, v89, v128
	v_mul_f32_e64 v117, v124, v128
	v_mul_f32_e64 v118, v125, v128
	v_mul_f32_e64 v119, v126, v128
	v_mul_f32_e64 v120, v127, v128
	v_add_f32_e64 v122, v49, v25
	v_mov_b32_e32 v123, v3
	ds_write_b128 v23, v[112:115] offset:3072
	ds_write_b128 v23, v[116:119] offset:4096
	ds_write_b128 v23, v[120:123] offset:5120
	s_waitcnt lgkmcnt(0)
	s_barrier
	v_pk_mul_f32 v[36:37], v[38:39], v[40:41] op_sel_hi:[1,0]
	v_pk_mul_f32 v[46:47], v[38:39], v[40:41] op_sel:[0,1]
	v_pk_mul_f32 v[48:49], v[38:39], v[42:43] op_sel_hi:[1,0]
	v_add_f32_dpp v50, v38, v38 wave_shr:1 row_mask:0xf bank_mask:0xf bound_ctrl:1
	v_add_f32_dpp v51, v39, v39 wave_shr:1 row_mask:0xf bank_mask:0xf bound_ctrl:1
	v_add_f32_dpp v60, v36, v36 wave_shr:1 row_mask:0xf bank_mask:0xf bound_ctrl:1
	v_add_f32_dpp v61, v37, v37 wave_shr:1 row_mask:0xf bank_mask:0xf bound_ctrl:1
	v_add_f32_dpp v84, v46, v46 wave_shr:1 row_mask:0xf bank_mask:0xf bound_ctrl:1
	v_add_f32_dpp v85, v47, v47 wave_shr:1 row_mask:0xf bank_mask:0xf bound_ctrl:1
	v_add_f32_dpp v86, v48, v48 wave_shr:1 row_mask:0xf bank_mask:0xf bound_ctrl:1
	v_add_f32_dpp v87, v49, v49 wave_shr:1 row_mask:0xf bank_mask:0xf bound_ctrl:1
	v_add_f32_dpp v50, v38, v50 wave_shl:1 row_mask:0xf bank_mask:0xf bound_ctrl:1
	v_add_f32_dpp v51, v39, v51 wave_shl:1 row_mask:0xf bank_mask:0xf bound_ctrl:1
	v_add_f32_dpp v60, v36, v60 wave_shl:1 row_mask:0xf bank_mask:0xf bound_ctrl:1
	v_add_f32_dpp v61, v37, v61 wave_shl:1 row_mask:0xf bank_mask:0xf bound_ctrl:1
	v_add_f32_dpp v84, v46, v84 wave_shl:1 row_mask:0xf bank_mask:0xf bound_ctrl:1
	v_add_f32_dpp v85, v47, v85 wave_shl:1 row_mask:0xf bank_mask:0xf bound_ctrl:1
	v_add_f32_dpp v86, v48, v86 wave_shl:1 row_mask:0xf bank_mask:0xf bound_ctrl:1
	v_add_f32_dpp v87, v49, v87 wave_shl:1 row_mask:0xf bank_mask:0xf bound_ctrl:1
	v_pk_add_f32 v[36:37], v[52:53], v[50:51]
	v_pk_add_f32 v[46:47], v[54:55], v[60:61]
	v_pk_add_f32 v[48:49], v[56:57], v[84:85]
	v_pk_add_f32 v[52:53], v[58:59], v[86:87]
	v_pk_fma_f32 v[46:47], v[112:113], v[36:37], v[46:47] op_sel_hi:[0,1,1] neg_lo:[1,0,0] neg_hi:[1,0,0]
	v_pk_fma_f32 v[48:49], v[112:113], v[36:37], v[48:49] op_sel:[1,0,0] neg_lo:[1,0,0] neg_hi:[1,0,0]
	v_pk_fma_f32 v[52:53], v[114:115], v[36:37], v[52:53] op_sel_hi:[0,1,1] neg_lo:[1,0,0] neg_hi:[1,0,0]
	v_pk_mul_f32 v[54:55], v[114:115], v[46:47] op_sel:[1,0]
	v_pk_mul_f32 v[56:57], v[116:117], v[46:47] op_sel_hi:[0,1]
	v_pk_mul_f32 v[58:59], v[116:117], v[46:47] op_sel:[1,0]
	v_pk_fma_f32 v[54:55], v[116:117], v[48:49], v[54:55] op_sel_hi:[0,1,1]
	v_pk_fma_f32 v[56:57], v[118:119], v[48:49], v[56:57] op_sel_hi:[0,1,1]
	v_pk_fma_f32 v[58:59], v[118:119], v[48:49], v[58:59] op_sel:[1,0,0]
	v_pk_fma_f32 v[54:55], v[116:117], v[52:53], v[54:55] op_sel:[1,0,0]
	v_pk_fma_f32 v[56:57], v[118:119], v[52:53], v[56:57] op_sel:[1,0,0]
	v_pk_fma_f32 v[58:59], v[120:121], v[52:53], v[58:59] op_sel_hi:[0,1,1]
	v_pk_mul_f32 v[88:89], v[112:113], v[54:55] op_sel_hi:[0,1]
	v_pk_fma_f32 v[88:89], v[112:113], v[56:57], v[88:89] op_sel:[1,0,0]
	v_pk_fma_f32 v[88:89], v[114:115], v[58:59], v[88:89] op_sel_hi:[0,1,1]
	v_pk_fma_f32 v[88:89], v[120:121], v[36:37], v[88:89] op_sel:[1,0,0] neg_lo:[0,0,1] neg_hi:[0,0,1]
	v_add_f32_dpp v36, v54, v54 wave_shr:1 row_mask:0xf bank_mask:0xf bound_ctrl:1
	v_add_f32_dpp v37, v55, v55 wave_shr:1 row_mask:0xf bank_mask:0xf bound_ctrl:1
	v_add_f32_dpp v46, v56, v56 wave_shr:1 row_mask:0xf bank_mask:0xf bound_ctrl:1
	v_add_f32_dpp v47, v57, v57 wave_shr:1 row_mask:0xf bank_mask:0xf bound_ctrl:1
	v_add_f32_dpp v48, v58, v58 wave_shr:1 row_mask:0xf bank_mask:0xf bound_ctrl:1
	v_add_f32_dpp v49, v59, v59 wave_shr:1 row_mask:0xf bank_mask:0xf bound_ctrl:1
	v_add_f32_dpp v52, v88, v88 wave_shr:1 row_mask:0xf bank_mask:0xf bound_ctrl:1
	v_add_f32_dpp v53, v89, v89 wave_shr:1 row_mask:0xf bank_mask:0xf bound_ctrl:1
	v_add_f32_dpp v36, v54, v36 wave_shl:1 row_mask:0xf bank_mask:0xf bound_ctrl:1
	v_add_f32_dpp v37, v55, v37 wave_shl:1 row_mask:0xf bank_mask:0xf bound_ctrl:1
	v_add_f32_dpp v46, v56, v46 wave_shl:1 row_mask:0xf bank_mask:0xf bound_ctrl:1
	v_add_f32_dpp v47, v57, v47 wave_shl:1 row_mask:0xf bank_mask:0xf bound_ctrl:1
	v_add_f32_dpp v48, v58, v48 wave_shl:1 row_mask:0xf bank_mask:0xf bound_ctrl:1
	v_add_f32_dpp v49, v59, v49 wave_shl:1 row_mask:0xf bank_mask:0xf bound_ctrl:1
	v_add_f32_dpp v52, v88, v52 wave_shl:1 row_mask:0xf bank_mask:0xf bound_ctrl:1
	v_add_f32_dpp v53, v89, v53 wave_shl:1 row_mask:0xf bank_mask:0xf bound_ctrl:1
	s_add_i32 s5, s34, 4
	s_min_i32 s5, s5, 0x200
	s_mul_i32 s6, s5, 0x804
	s_add_i32 s6, s6, s35
	s_add_i32 s7, s6, 0x505014
	s_add_i32 s8, s6, 0x606018
	s_mul_i32 s9, s5, 0x180c
	s_add_i32 s9, s9, s33
	s_add_i32 s4, s34, 5
	s_min_i32 s4, s4, 0x200
	s_mul_i32 s4, s4, 0x804
	s_add_i32 s4, s4, s38
	buffer_load_dword v3, v28, s[20:23], s4 offen nt
	buffer_load_dwordx3 v[12:14], v27, s[24:27], s9 offen nt
	buffer_load_dword v6, v28, s[16:19], s7 offen nt
	buffer_load_dword v7, v28, s[16:19], s8 offen nt
	s_waitcnt vmcnt(8)
	s_add_i32 s4, s34, 3
	s_cmpk_lt_u32 s4, 0x201
	s_cselect_b64 s[12:13], s[40:41], 0
	v_cmp_eq_u32_e64 s[14:15], s37, v17
	s_and_b64 s[14:15], s[14:15], s[12:13]
	v_cndmask_b32_e64 v25, 0, 1, s[14:15]
	v_mul_f32_e64 v54, v64, v64
	v_mul_f32_e64 v55, v64, v65
	v_mul_f32_e64 v56, v64, v66
	v_mul_f32_e64 v57, v65, v65
	v_mul_f32_e64 v58, v65, v66
	v_mul_f32_e64 v59, v66, v66
	v_or_b32_dpp v29, v25, v25 wave_shr:1 row_mask:0xf bank_mask:0xf bound_ctrl:1
	s_nop 1
	v_or_b32_dpp v29, v25, v29 wave_shl:1 row_mask:0xf bank_mask:0xf bound_ctrl:1
	s_nop 1
	v_or_b32_dpp v30, v29, v29 wave_shr:1 row_mask:0xf bank_mask:0xf bound_ctrl:1
	s_nop 1
	v_or_b32_dpp v30, v29, v30 wave_shl:1 row_mask:0xf bank_mask:0xf bound_ctrl:1
	v_or3_b32 v25, v30, v45, v68
	v_or3_b32 v25, v25, v69, v44
	s_add_i32 s4, s34, 0
	s_cmpk_lt_u32 s4, 0x1ff
	s_cselect_b64 s[12:13], s[42:43], 0
	v_cmp_ne_u32_e64 s[30:31], 0, v25
	s_and_b64 s[30:31], s[30:31], s[12:13]
	v_cndmask_b32_e64 v25, 0, 1.0, s[30:31]
	v_add_f32_dpp v88, v64, v64 wave_shr:1 row_mask:0xf bank_mask:0xf bound_ctrl:1
	v_add_f32_dpp v89, v65, v65 wave_shr:1 row_mask:0xf bank_mask:0xf bound_ctrl:1
	v_add_f32_dpp v112, v66, v66 wave_shr:1 row_mask:0xf bank_mask:0xf bound_ctrl:1
	v_add_f32_dpp v113, v54, v54 wave_shr:1 row_mask:0xf bank_mask:0xf bound_ctrl:1
	v_add_f32_dpp v114, v55, v55 wave_shr:1 row_mask:0xf bank_mask:0xf bound_ctrl:1
	v_add_f32_dpp v115, v56, v56 wave_shr:1 row_mask:0xf bank_mask:0xf bound_ctrl:1
	v_add_f32_dpp v116, v57, v57 wave_shr:1 row_mask:0xf bank_mask:0xf bound_ctrl:1
	v_add_f32_dpp v117, v58, v58 wave_shr:1 row_mask:0xf bank_mask:0xf bound_ctrl:1
	v_add_f32_dpp v118, v59, v59 wave_shr:1 row_mask:0xf bank_mask:0xf bound_ctrl:1
	v_add_f32_dpp v119, v25, v25 wave_shr:1 row_mask:0xf bank_mask:0xf bound_ctrl:1
	v_add_f32_dpp v88, v64, v88 wave_shl:1 row_mask:0xf bank_mask:0xf bound_ctrl:1
	v_add_f32_dpp v89, v65, v89 wave_shl:1 row_mask:0xf bank_mask:0xf bound_ctrl:1
	v_add_f32_dpp v112, v66, v112 wave_shl:1 row_mask:0xf bank_mask:0xf bound_ctrl:1
	v_add_f32_dpp v113, v54, v113 wave_shl:1 row_mask:0xf bank_mask:0xf bound_ctrl:1
	v_add_f32_dpp v114, v55, v114 wave_shl:1 row_mask:0xf bank_mask:0xf bound_ctrl:1
	v_add_f32_dpp v115, v56, v115 wave_shl:1 row_mask:0xf bank_mask:0xf bound_ctrl:1
	v_add_f32_dpp v116, v57, v116 wave_shl:1 row_mask:0xf bank_mask:0xf bound_ctrl:1
	v_add_f32_dpp v117, v58, v117 wave_shl:1 row_mask:0xf bank_mask:0xf bound_ctrl:1
	v_add_f32_dpp v118, v59, v118 wave_shl:1 row_mask:0xf bank_mask:0xf bound_ctrl:1
	v_add_f32_dpp v119, v25, v119 wave_shl:1 row_mask:0xf bank_mask:0xf bound_ctrl:1
	v_pk_add_f32 v[54:55], v[92:93], v[88:89]
	v_pk_add_f32 v[56:57], v[94:95], v[54:55]
	v_pk_add_f32 v[58:59], v[104:105], v[112:113]
	v_pk_add_f32 v[92:93], v[96:97], v[58:59]
	v_pk_add_f32 v[94:95], v[106:107], v[114:115]
	v_pk_add_f32 v[96:97], v[98:99], v[94:95]
	v_pk_add_f32 v[98:99], v[108:109], v[116:117]
	v_pk_add_f32 v[104:105], v[100:101], v[98:99]
	v_pk_add_f32 v[100:101], v[110:111], v[118:119]
	v_pk_add_f32 v[106:107], v[102:103], v[100:101]
	v_mul_f32_e64 v108, v56, v22
	v_mul_f32_e64 v109, v57, v22
	v_mul_f32_e64 v110, v92, v22
	v_fma_f32 v25, v93, v22, v26
	v_mul_f32_e64 v29, v96, v22
	v_mul_f32_e64 v102, v97, v22
	v_fma_f32 v103, v104, v22, v26
	v_mul_f32_e64 v128, v105, v22
	v_fma_f32 v129, v106, v22, v26
	v_fma_f32 v25, -v108, v108, v25
	v_fma_f32 v29, -v108, v109, v29
	v_fma_f32 v102, -v108, v110, v102
	v_fma_f32 v103, -v109, v109, v103
	v_fma_f32 v128, -v109, v110, v128
	v_fma_f32 v129, -v110, v110, v129
	v_mul_f32_e64 v130, v128, v128
	v_mul_f32_e64 v131, v29, v129
	v_mul_f32_e64 v132, v102, v103
	v_mul_f32_e64 v133, v102, v102
	v_mul_f32_e64 v134, v25, v128
	v_mul_f32_e64 v135, v29, v29
	v_fma_f32 v130, v103, v129, -v130
	v_fma_f32 v131, v102, v128, -v131
	v_fma_f32 v132, v29, v128, -v132
	v_fma_f32 v133, v25, v129, -v133
	v_fma_f32 v134, v29, v102, -v134
	v_fma_f32 v135, v25, v103, -v135
	v_mul_f32_e64 v136, v25, v130
	v_fma_f32 v136, v29, v131, v136
	v_fma_f32 v136, v102, v132, v136
	v_rcp_f32_e32 v136, v136
	v_cmp_ne_u32_e64 vcc, s37, v16
	v_mul_f32_e64 v136, v136, v22
	v_cndmask_b32_e64 v136, 0, v136, s[30:31]
	v_cndmask_b32_e64 v25, 0, v18, vcc
	v_cndmask_b32_e64 v125, 0, v22, s[30:31]
	v_mul_f32_e64 v111, v130, v136
	v_mul_f32_e64 v120, v131, v136
	v_mul_f32_e64 v121, v132, v136
	v_mul_f32_e64 v122, v133, v136
	v_mul_f32_e64 v123, v134, v136
	v_mul_f32_e64 v124, v135, v136
	v_add_f32_e64 v126, v107, v25
	v_mov_b32_e32 v127, v16
	ds_write_b128 v23, v[108:111]
	ds_write_b128 v23, v[120:123] offset:1024
	ds_write_b128 v23, v[124:127] offset:2048
	s_waitcnt lgkmcnt(0)
	s_barrier
	v_pk_mul_f32 v[56:57], v[62:63], v[64:65] op_sel_hi:[1,0]
	v_pk_mul_f32 v[92:93], v[62:63], v[64:65] op_sel:[0,1]
	v_pk_mul_f32 v[96:97], v[62:63], v[66:67] op_sel_hi:[1,0]
	v_add_f32_dpp v102, v62, v62 wave_shr:1 row_mask:0xf bank_mask:0xf bound_ctrl:1
	v_add_f32_dpp v103, v63, v63 wave_shr:1 row_mask:0xf bank_mask:0xf bound_ctrl:1
	v_add_f32_dpp v104, v56, v56 wave_shr:1 row_mask:0xf bank_mask:0xf bound_ctrl:1
	v_add_f32_dpp v105, v57, v57 wave_shr:1 row_mask:0xf bank_mask:0xf bound_ctrl:1
	v_add_f32_dpp v106, v92, v92 wave_shr:1 row_mask:0xf bank_mask:0xf bound_ctrl:1
	v_add_f32_dpp v107, v93, v93 wave_shr:1 row_mask:0xf bank_mask:0xf bound_ctrl:1
	v_add_f32_dpp v128, v96, v96 wave_shr:1 row_mask:0xf bank_mask:0xf bound_ctrl:1
	v_add_f32_dpp v129, v97, v97 wave_shr:1 row_mask:0xf bank_mask:0xf bound_ctrl:1
	v_add_f32_dpp v102, v62, v102 wave_shl:1 row_mask:0xf bank_mask:0xf bound_ctrl:1
	v_add_f32_dpp v103, v63, v103 wave_shl:1 row_mask:0xf bank_mask:0xf bound_ctrl:1
	v_add_f32_dpp v104, v56, v104 wave_shl:1 row_mask:0xf bank_mask:0xf bound_ctrl:1
	v_add_f32_dpp v105, v57, v105 wave_shl:1 row_mask:0xf bank_mask:0xf bound_ctrl:1
	v_add_f32_dpp v106, v92, v106 wave_shl:1 row_mask:0xf bank_mask:0xf bound_ctrl:1
	v_add_f32_dpp v107, v93, v107 wave_shl:1 row_mask:0xf bank_mask:0xf bound_ctrl:1
	v_add_f32_dpp v128, v96, v128 wave_shl:1 row_mask:0xf bank_mask:0xf bound_ctrl:1
	v_add_f32_dpp v129, v97, v129 wave_shl:1 row_mask:0xf bank_mask:0xf bound_ctrl:1
	v_pk_add_f32 v[56:57], v[50:51], v[102:103]
	v_pk_add_f32 v[92:93], v[74:75], v[56:57]
	v_pk_add_f32 v[50:51], v[60:61], v[104:105]
	v_pk_add_f32 v[74:75], v[76:77], v[50:51]
	v_pk_add_f32 v[60:61], v[84:85], v[106:107]
	v_pk_add_f32 v[76:77], v[78:79], v[60:61]
	v_pk_add_f32 v[78:79], v[86:87], v[128:129]
	v_pk_add_f32 v[84:85], v[90:91], v[78:79]
	v_pk_fma_f32 v[74:75], v[108:109], v[92:93], v[74:75] op_sel_hi:[0,1,1] neg_lo:[1,0,0] neg_hi:[1,0,0]
	v_pk_fma_f32 v[76:77], v[108:109], v[92:93], v[76:77] op_sel:[1,0,0] neg_lo:[1,0,0] neg_hi:[1,0,0]
	v_pk_fma_f32 v[84:85], v[110:111], v[92:93], v[84:85] op_sel_hi:[0,1,1] neg_lo:[1,0,0] neg_hi:[1,0,0]
	v_pk_mul_f32 v[86:87], v[110:111], v[74:75] op_sel:[1,0]
	v_pk_mul_f32 v[90:91], v[120:121], v[74:75] op_sel_hi:[0,1]
	v_pk_mul_f32 v[96:97], v[120:121], v[74:75] op_sel:[1,0]
	v_pk_fma_f32 v[86:87], v[120:121], v[76:77], v[86:87] op_sel_hi:[0,1,1]
	v_pk_fma_f32 v[90:91], v[122:123], v[76:77], v[90:91] op_sel_hi:[0,1,1]
	v_pk_fma_f32 v[96:97], v[122:123], v[76:77], v[96:97] op_sel:[1,0,0]
	v_pk_fma_f32 v[86:87], v[120:121], v[84:85], v[86:87] op_sel:[1,0,0]
	v_pk_fma_f32 v[90:91], v[122:123], v[84:85], v[90:91] op_sel:[1,0,0]
	v_pk_fma_f32 v[96:97], v[124:125], v[84:85], v[96:97] op_sel_hi:[0,1,1]
	v_pk_mul_f32 v[130:131], v[108:109], v[86:87] op_sel_hi:[0,1]
	v_pk_fma_f32 v[130:131], v[108:109], v[90:91], v[130:131] op_sel:[1,0,0]
	v_pk_fma_f32 v[130:131], v[110:111], v[96:97], v[130:131] op_sel_hi:[0,1,1]
	v_pk_fma_f32 v[130:131], v[124:125], v[92:93], v[130:131] op_sel:[1,0,0] neg_lo:[0,0,1] neg_hi:[0,0,1]
	v_cmp_eq_u32_e64 s[10:11], 6, v127
	v_cmp_eq_u32_e64 s[14:15], 7, v127
	v_add_f32_dpp v74, v86, v86 wave_shr:1 row_mask:0xf bank_mask:0xf bound_ctrl:1
	v_add_f32_dpp v75, v87, v87 wave_shr:1 row_mask:0xf bank_mask:0xf bound_ctrl:1
	v_add_f32_dpp v76, v90, v90 wave_shr:1 row_mask:0xf bank_mask:0xf bound_ctrl:1
	v_add_f32_dpp v77, v91, v91 wave_shr:1 row_mask:0xf bank_mask:0xf bound_ctrl:1
	v_add_f32_dpp v84, v96, v96 wave_shr:1 row_mask:0xf bank_mask:0xf bound_ctrl:1
	v_add_f32_dpp v85, v97, v97 wave_shr:1 row_mask:0xf bank_mask:0xf bound_ctrl:1
	v_add_f32_dpp v92, v130, v130 wave_shr:1 row_mask:0xf bank_mask:0xf bound_ctrl:1
	v_add_f32_dpp v93, v131, v131 wave_shr:1 row_mask:0xf bank_mask:0xf bound_ctrl:1
	v_add_f32_dpp v74, v86, v74 wave_shl:1 row_mask:0xf bank_mask:0xf bound_ctrl:1
	v_add_f32_dpp v75, v87, v75 wave_shl:1 row_mask:0xf bank_mask:0xf bound_ctrl:1
	v_add_f32_dpp v76, v90, v76 wave_shl:1 row_mask:0xf bank_mask:0xf bound_ctrl:1
	v_add_f32_dpp v77, v91, v77 wave_shl:1 row_mask:0xf bank_mask:0xf bound_ctrl:1
	v_add_f32_dpp v84, v96, v84 wave_shl:1 row_mask:0xf bank_mask:0xf bound_ctrl:1
	v_add_f32_dpp v85, v97, v85 wave_shl:1 row_mask:0xf bank_mask:0xf bound_ctrl:1
	v_add_f32_dpp v92, v130, v92 wave_shl:1 row_mask:0xf bank_mask:0xf bound_ctrl:1
	v_add_f32_dpp v93, v131, v93 wave_shl:1 row_mask:0xf bank_mask:0xf bound_ctrl:1
	v_pk_add_f32 v[86:87], v[36:37], v[74:75]
	v_pk_add_f32 v[90:91], v[70:71], v[86:87]
	v_pk_add_f32 v[36:37], v[46:47], v[76:77]
	v_pk_add_f32 v[70:71], v[72:73], v[36:37]
	v_pk_add_f32 v[46:47], v[48:49], v[84:85]
	v_pk_add_f32 v[72:73], v[80:81], v[46:47]
	v_pk_add_f32 v[48:49], v[52:53], v[92:93]
	v_pk_add_f32 v[80:81], v[82:83], v[48:49]
	v_pk_fma_f32 v[80:81], v[32:33], v[90:91], v[80:81] op_sel_hi:[0,1,1]
	v_pk_fma_f32 v[80:81], v[32:33], v[70:71], v[80:81] op_sel:[1,0,0]
	v_pk_fma_f32 v[80:81], v[34:35], v[72:73], v[80:81] op_sel_hi:[0,1,1]
	v_cndmask_b32_e64 v52, 0, v18, s[10:11]
	v_cndmask_b32_e64 v53, 0, v18, s[14:15]
	v_pk_fma_f32 v[80:81], v[20:21], v[126:127], v[80:81] op_sel_hi:[1,0,1] neg_lo:[0,0,1] neg_hi:[0,0,1]
	s_add_i32 s4, s34, 0
	s_cmpk_lt_i32 s4, 0x201
	s_cselect_b64 s[12:13], s[0:1], 0
	v_pk_add_f32 v[80:81], v[80:81], v[52:53] neg_lo:[0,1] neg_hi:[0,1]
	v_pk_mul_f32 v[82:83], v[80:81], v[80:81]
	v_add_f32_e32 v82, v82, v83
	v_cndmask_b32_e64 v83, 0, v82, s[12:13]
	v_add_f32_e32 v1, v1, v83
	s_add_i32 s5, s34, 5
	s_min_i32 s5, s5, 0x200
	s_mul_i32 s6, s5, 0x804
	s_add_i32 s6, s6, s35
	s_add_i32 s7, s6, 0x505014
	s_add_i32 s8, s6, 0x606018
	s_mul_i32 s9, s5, 0x180c
	s_add_i32 s9, s9, s33
	s_add_i32 s4, s34, 6
	s_min_i32 s4, s4, 0x200
	s_mul_i32 s4, s4, 0x804
	s_add_i32 s4, s4, s38
	buffer_load_dword v16, v28, s[20:23], s4 offen nt
	buffer_load_dwordx3 v[32:34], v27, s[24:27], s9 offen nt
	buffer_load_dword v20, v28, s[16:19], s7 offen nt
	buffer_load_dword v21, v28, s[16:19], s8 offen nt
	s_waitcnt vmcnt(8)
	s_add_i32 s4, s34, 4
	s_cmpk_lt_u32 s4, 0x201
	s_cselect_b64 s[12:13], s[40:41], 0
	v_cmp_eq_u32_e64 s[14:15], s37, v2
	s_and_b64 s[14:15], s[14:15], s[12:13]
	v_cndmask_b32_e64 v25, 0, 1, s[14:15]
	v_mul_f32_e64 v52, v8, v8
	v_mul_f32_e64 v53, v8, v9
	v_mul_f32_e64 v70, v8, v10
	v_mul_f32_e64 v71, v9, v9
	v_mul_f32_e64 v72, v9, v10
	v_mul_f32_e64 v73, v10, v10
	v_or_b32_dpp v29, v25, v25 wave_shr:1 row_mask:0xf bank_mask:0xf bound_ctrl:1
	s_nop 1
	v_or_b32_dpp v29, v25, v29 wave_shl:1 row_mask:0xf bank_mask:0xf bound_ctrl:1
	s_nop 1
	v_or_b32_dpp v44, v29, v29 wave_shr:1 row_mask:0xf bank_mask:0xf bound_ctrl:1
	s_nop 1
	v_or_b32_dpp v44, v29, v44 wave_shl:1 row_mask:0xf bank_mask:0xf bound_ctrl:1
	v_or3_b32 v25, v44, v30, v45
	v_or3_b32 v25, v25, v68, v69
	s_add_i32 s4, s34, 1
	s_cmpk_lt_u32 s4, 0x1ff
	s_cselect_b64 s[12:13], s[42:43], 0
	v_cmp_ne_u32_e64 s[30:31], 0, v25
	s_and_b64 s[30:31], s[30:31], s[12:13]
	v_cndmask_b32_e64 v25, 0, 1.0, s[30:31]
	v_add_f32_dpp v80, v8, v8 wave_shr:1 row_mask:0xf bank_mask:0xf bound_ctrl:1
	v_add_f32_dpp v81, v9, v9 wave_shr:1 row_mask:0xf bank_mask:0xf bound_ctrl:1
	v_add_f32_dpp v82, v10, v10 wave_shr:1 row_mask:0xf bank_mask:0xf bound_ctrl:1
	v_add_f32_dpp v83, v52, v52 wave_shr:1 row_mask:0xf bank_mask:0xf bound_ctrl:1
	v_add_f32_dpp v90, v53, v53 wave_shr:1 row_mask:0xf bank_mask:0xf bound_ctrl:1
	v_add_f32_dpp v91, v70, v70 wave_shr:1 row_mask:0xf bank_mask:0xf bound_ctrl:1
	v_add_f32_dpp v96, v71, v71 wave_shr:1 row_mask:0xf bank_mask:0xf bound_ctrl:1
	v_add_f32_dpp v97, v72, v72 wave_shr:1 row_mask:0xf bank_mask:0xf bound_ctrl:1
	v_add_f32_dpp v108, v73, v73 wave_shr:1 row_mask:0xf bank_mask:0xf bound_ctrl:1
	v_add_f32_dpp v109, v25, v25 wave_shr:1 row_mask:0xf bank_mask:0xf bound_ctrl:1
	v_add_f32_dpp v80, v8, v80 wave_shl:1 row_mask:0xf bank_mask:0xf bound_ctrl:1
	v_add_f32_dpp v81, v9, v81 wave_shl:1 row_mask:0xf bank_mask:0xf bound_ctrl:1
	v_add_f32_dpp v82, v10, v82 wave_shl:1 row_mask:0xf bank_mask:0xf bound_ctrl:1
	v_add_f32_dpp v83, v52, v83 wave_shl:1 row_mask:0xf bank_mask:0xf bound_ctrl:1
	v_add_f32_dpp v90, v53, v90 wave_shl:1 row_mask:0xf bank_mask:0xf bound_ctrl:1
	v_add_f32_dpp v91, v70, v91 wave_shl:1 row_mask:0xf bank_mask:0xf bound_ctrl:1
	v_add_f32_dpp v96, v71, v96 wave_shl:1 row_mask:0xf bank_mask:0xf bound_ctrl:1
	v_add_f32_dpp v97, v72, v97 wave_shl:1 row_mask:0xf bank_mask:0xf bound_ctrl:1
	v_add_f32_dpp v108, v73, v108 wave_shl:1 row_mask:0xf bank_mask:0xf bound_ctrl:1
	v_add_f32_dpp v109, v25, v109 wave_shl:1 row_mask:0xf bank_mask:0xf bound_ctrl:1
	v_pk_add_f32 v[52:53], v[54:55], v[80:81]
	v_pk_add_f32 v[54:55], v[58:59], v[82:83]
	v_pk_add_f32 v[58:59], v[94:95], v[90:91]
	v_pk_add_f32 v[70:71], v[98:99], v[96:97]
	v_pk_add_f32 v[72:73], v[100:101], v[108:109]
	v_mul_f32_e64 v120, v52, v22
	v_mul_f32_e64 v121, v53, v22
	v_mul_f32_e64 v122, v54, v22
	v_fma_f32 v25, v55, v22, v26
	v_mul_f32_e64 v29, v58, v22
	v_mul_f32_e64 v94, v59, v22
	v_fma_f32 v95, v70, v22, v26
	v_mul_f32_e64 v98, v71, v22
	v_fma_f32 v99, v72, v22, v26
	v_fma_f32 v25, -v120, v120, v25
	v_fma_f32 v29, -v120, v121, v29
	v_fma_f32 v94, -v120, v122, v94
	v_fma_f32 v95, -v121, v121, v95
	v_fma_f32 v98, -v121, v122, v98
	v_fma_f32 v99, -v122, v122, v99
	v_mul_f32_e64 v100, v98, v98
	v_mul_f32_e64 v101, v29, v99
	v_mul_f32_e64 v110, v94, v95
	v_mul_f32_e64 v111, v94, v94
	v_mul_f32_e64 v130, v25, v98
	v_mul_f32_e64 v131, v29, v29
	v_fma_f32 v100, v95, v99, -v100
	v_fma_f32 v101, v94, v98, -v101
	v_fma_f32 v110, v29, v98, -v110
	v_fma_f32 v111, v25, v99, -v111
	v_fma_f32 v130, v29, v94, -v130
	v_fma_f32 v131, v25, v95, -v131
	v_mul_f32_e64 v136, v25, v100
	v_fma_f32 v136, v29, v101, v136
	v_fma_f32 v136, v94, v110, v136
	v_rcp_f32_e32 v136, v136
	v_cmp_ne_u32_e64 vcc, s37, v31
	v_mul_f32_e64 v136, v136, v22
	v_cndmask_b32_e64 v136, 0, v136, s[30:31]
	v_cndmask_b32_e64 v25, 0, v18, vcc
	v_cndmask_b32_e64 v133, 0, v22, s[30:31]
	v_mul_f32_e64 v123, v100, v136
	v_mul_f32_e64 v124, v101, v136
	v_mul_f32_e64 v125, v110, v136
	v_mul_f32_e64 v126, v111, v136
	v_mul_f32_e64 v127, v130, v136
	v_mul_f32_e64 v132, v131, v136
	v_add_f32_e64 v134, v73, v25
	v_mov_b32_e32 v135, v31
	ds_write_b128 v23, v[120:123] offset:3072
	ds_write_b128 v23, v[124:127] offset:4096
	ds_write_b128 v23, v[132:135] offset:5120
	s_waitcnt lgkmcnt(0)
	s_barrier
	v_pk_mul_f32 v[52:53], v[4:5], v[8:9] op_sel_hi:[1,0]
	v_pk_mul_f32 v[54:55], v[4:5], v[8:9] op_sel:[0,1]
	v_pk_mul_f32 v[58:59], v[4:5], v[10:11] op_sel_hi:[1,0]
	v_add_f32_dpp v70, v4, v4 wave_shr:1 row_mask:0xf bank_mask:0xf bound_ctrl:1
	v_add_f32_dpp v71, v5, v5 wave_shr:1 row_mask:0xf bank_mask:0xf bound_ctrl:1
	v_add_f32_dpp v72, v52, v52 wave_shr:1 row_mask:0xf bank_mask:0xf bound_ctrl:1
	v_add_f32_dpp v73, v53, v53 wave_shr:1 row_mask:0xf bank_mask:0xf bound_ctrl:1
	v_add_f32_dpp v94, v54, v54 wave_shr:1 row_mask:0xf bank_mask:0xf bound_ctrl:1
	v_add_f32_dpp v95, v55, v55 wave_shr:1 row_mask:0xf bank_mask:0xf bound_ctrl:1
	v_add_f32_dpp v98, v58, v58 wave_shr:1 row_mask:0xf bank_mask:0xf bound_ctrl:1
	v_add_f32_dpp v99, v59, v59 wave_shr:1 row_mask:0xf bank_mask:0xf bound_ctrl:1
	v_add_f32_dpp v70, v4, v70 wave_shl:1 row_mask:0xf bank_mask:0xf bound_ctrl:1
	v_add_f32_dpp v71, v5, v71 wave_shl:1 row_mask:0xf bank_mask:0xf bound_ctrl:1
	v_add_f32_dpp v72, v52, v72 wave_shl:1 row_mask:0xf bank_mask:0xf bound_ctrl:1
	v_add_f32_dpp v73, v53, v73 wave_shl:1 row_mask:0xf bank_mask:0xf bound_ctrl:1
	v_add_f32_dpp v94, v54, v94 wave_shl:1 row_mask:0xf bank_mask:0xf bound_ctrl:1
	v_add_f32_dpp v95, v55, v95 wave_shl:1 row_mask:0xf bank_mask:0xf bound_ctrl:1
	v_add_f32_dpp v98, v58, v98 wave_shl:1 row_mask:0xf bank_mask:0xf bound_ctrl:1
	v_add_f32_dpp v99, v59, v99 wave_shl:1 row_mask:0xf bank_mask:0xf bound_ctrl:1
	v_pk_add_f32 v[52:53], v[56:57], v[70:71]
	v_pk_add_f32 v[54:55], v[50:51], v[72:73]
	v_pk_add_f32 v[50:51], v[60:61], v[94:95]
	v_pk_add_f32 v[56:57], v[78:79], v[98:99]
	v_pk_fma_f32 v[54:55], v[120:121], v[52:53], v[54:55] op_sel_hi:[0,1,1] neg_lo:[1,0,0] neg_hi:[1,0,0]
	v_pk_fma_f32 v[50:51], v[120:121], v[52:53], v[50:51] op_sel:[1,0,0] neg_lo:[1,0,0] neg_hi:[1,0,0]
	v_pk_fma_f32 v[56:57], v[122:123], v[52:53], v[56:57] op_sel_hi:[0,1,1] neg_lo:[1,0,0] neg_hi:[1,0,0]
	v_pk_mul_f32 v[58:59], v[122:123], v[54:55] op_sel:[1,0]
	v_pk_mul_f32 v[60:61], v[124:125], v[54:55] op_sel_hi:[0,1]
	v_pk_mul_f32 v[78:79], v[124:125], v[54:55] op_sel:[1,0]
	v_pk_fma_f32 v[58:59], v[124:125], v[50:51], v[58:59] op_sel_hi:[0,1,1]
	v_pk_fma_f32 v[60:61], v[126:127], v[50:51], v[60:61] op_sel_hi:[0,1,1]
	v_pk_fma_f32 v[78:79], v[126:127], v[50:51], v[78:79] op_sel:[1,0,0]
	v_pk_fma_f32 v[58:59], v[124:125], v[56:57], v[58:59] op_sel:[1,0,0]
	v_pk_fma_f32 v[60:61], v[126:127], v[56:57], v[60:61] op_sel:[1,0,0]
	v_pk_fma_f32 v[78:79], v[132:133], v[56:57], v[78:79] op_sel_hi:[0,1,1]
	v_pk_mul_f32 v[100:101], v[120:121], v[58:59] op_sel_hi:[0,1]
	v_pk_fma_f32 v[100:101], v[120:121], v[60:61], v[100:101] op_sel:[1,0,0]
	v_pk_fma_f32 v[100:101], v[122:123], v[78:79], v[100:101] op_sel_hi:[0,1,1]
	v_pk_fma_f32 v[100:101], v[132:133], v[52:53], v[100:101] op_sel:[1,0,0] neg_lo:[0,0,1] neg_hi:[0,0,1]
	v_cmp_eq_u32_e64 s[10:11], 6, v135
	v_cmp_eq_u32_e64 s[14:15], 7, v135
	v_add_f32_dpp v50, v58, v58 wave_shr:1 row_mask:0xf bank_mask:0xf bound_ctrl:1
	v_add_f32_dpp v51, v59, v59 wave_shr:1 row_mask:0xf bank_mask:0xf bound_ctrl:1
	v_add_f32_dpp v52, v60, v60 wave_shr:1 row_mask:0xf bank_mask:0xf bound_ctrl:1
	v_add_f32_dpp v53, v61, v61 wave_shr:1 row_mask:0xf bank_mask:0xf bound_ctrl:1
	v_add_f32_dpp v54, v78, v78 wave_shr:1 row_mask:0xf bank_mask:0xf bound_ctrl:1
	v_add_f32_dpp v55, v79, v79 wave_shr:1 row_mask:0xf bank_mask:0xf bound_ctrl:1
	v_add_f32_dpp v56, v100, v100 wave_shr:1 row_mask:0xf bank_mask:0xf bound_ctrl:1
	v_add_f32_dpp v57, v101, v101 wave_shr:1 row_mask:0xf bank_mask:0xf bound_ctrl:1
	v_add_f32_dpp v50, v58, v50 wave_shl:1 row_mask:0xf bank_mask:0xf bound_ctrl:1
	v_add_f32_dpp v51, v59, v51 wave_shl:1 row_mask:0xf bank_mask:0xf bound_ctrl:1
	v_add_f32_dpp v52, v60, v52 wave_shl:1 row_mask:0xf bank_mask:0xf bound_ctrl:1
	v_add_f32_dpp v53, v61, v53 wave_shl:1 row_mask:0xf bank_mask:0xf bound_ctrl:1
	v_add_f32_dpp v54, v78, v54 wave_shl:1 row_mask:0xf bank_mask:0xf bound_ctrl:1
	v_add_f32_dpp v55, v79, v55 wave_shl:1 row_mask:0xf bank_mask:0xf bound_ctrl:1
	v_add_f32_dpp v56, v100, v56 wave_shl:1 row_mask:0xf bank_mask:0xf bound_ctrl:1
	v_add_f32_dpp v57, v101, v57 wave_shl:1 row_mask:0xf bank_mask:0xf bound_ctrl:1
	v_pk_add_f32 v[58:59], v[86:87], v[50:51]
	v_pk_add_f32 v[60:61], v[36:37], v[52:53]
	v_pk_add_f32 v[36:37], v[46:47], v[54:55]
	v_pk_add_f32 v[46:47], v[48:49], v[56:57]
	v_pk_fma_f32 v[46:47], v[40:41], v[58:59], v[46:47] op_sel_hi:[0,1,1]
	v_pk_fma_f32 v[46:47], v[40:41], v[60:61], v[46:47] op_sel:[1,0,0]
	v_pk_fma_f32 v[46:47], v[42:43], v[36:37], v[46:47] op_sel_hi:[0,1,1]
	v_cndmask_b32_e64 v48, 0, v18, s[10:11]
	v_cndmask_b32_e64 v49, 0, v18, s[14:15]
	v_pk_fma_f32 v[46:47], v[38:39], v[134:135], v[46:47] op_sel_hi:[1,0,1] neg_lo:[0,0,1] neg_hi:[0,0,1]
	s_add_i32 s4, s34, 1
	s_cmpk_lt_i32 s4, 0x201
	s_cselect_b64 s[12:13], s[0:1], 0
	v_pk_add_f32 v[46:47], v[46:47], v[48:49] neg_lo:[0,1] neg_hi:[0,1]
	v_pk_mul_f32 v[78:79], v[46:47], v[46:47]
	v_add_f32_e32 v78, v78, v79
	v_cndmask_b32_e64 v79, 0, v78, s[12:13]
	v_add_f32_e32 v1, v1, v79
	s_add_i32 s5, s34, 6
	s_min_i32 s5, s5, 0x200
	s_mul_i32 s6, s5, 0x804
	s_add_i32 s6, s6, s35
	s_add_i32 s7, s6, 0x505014
	s_add_i32 s8, s6, 0x606018
	s_mul_i32 s9, s5, 0x180c
	s_add_i32 s9, s9, s33
	s_add_i32 s4, s34, 7
	s_min_i32 s4, s4, 0x200
	s_mul_i32 s4, s4, 0x804
	s_add_i32 s4, s4, s38
	buffer_load_dword v25, v28, s[20:23], s4 offen nt
	buffer_load_dwordx3 v[40:42], v27, s[24:27], s9 offen nt
	buffer_load_dword v36, v28, s[16:19], s7 offen nt
	buffer_load_dword v37, v28, s[16:19], s8 offen nt
	s_waitcnt vmcnt(8)
	s_add_i32 s4, s34, 5
	s_cmpk_lt_u32 s4, 0x201
	s_cselect_b64 s[12:13], s[40:41], 0
	v_cmp_eq_u32_e64 s[14:15], s37, v3
	s_and_b64 s[14:15], s[14:15], s[12:13]
	v_cndmask_b32_e64 v29, 0, 1, s[14:15]
	v_mul_f32_e64 v38, v12, v12
	v_mul_f32_e64 v39, v12, v13
	v_mul_f32_e64 v46, v12, v14
	v_mul_f32_e64 v47, v13, v13
	v_mul_f32_e64 v48, v13, v14
	v_mul_f32_e64 v49, v14, v14
	v_or_b32_dpp v31, v29, v29 wave_shr:1 row_mask:0xf bank_mask:0xf bound_ctrl:1
	s_nop 1
	v_or_b32_dpp v31, v29, v31 wave_shl:1 row_mask:0xf bank_mask:0xf bound_ctrl:1
	s_nop 1
	v_or_b32_dpp v69, v31, v31 wave_shr:1 row_mask:0xf bank_mask:0xf bound_ctrl:1
	s_nop 1
	v_or_b32_dpp v69, v31, v69 wave_shl:1 row_mask:0xf bank_mask:0xf bound_ctrl:1
	v_or3_b32 v29, v69, v44, v30
	v_or3_b32 v29, v29, v45, v68
	s_add_i32 s4, s34, 2
	s_cmpk_lt_u32 s4, 0x1ff
	s_cselect_b64 s[12:13], s[42:43], 0
	v_cmp_ne_u32_e64 s[30:31], 0, v29
	s_and_b64 s[30:31], s[30:31], s[12:13]
	v_cndmask_b32_e64 v29, 0, 1.0, s[30:31]
	v_add_f32_dpp v58, v12, v12 wave_shr:1 row_mask:0xf bank_mask:0xf bound_ctrl:1
	v_add_f32_dpp v59, v13, v13 wave_shr:1 row_mask:0xf bank_mask:0xf bound_ctrl:1
	v_add_f32_dpp v60, v14, v14 wave_shr:1 row_mask:0xf bank_mask:0xf bound_ctrl:1
	v_add_f32_dpp v61, v38, v38 wave_shr:1 row_mask:0xf bank_mask:0xf bound_ctrl:1
	v_add_f32_dpp v78, v39, v39 wave_shr:1 row_mask:0xf bank_mask:0xf bound_ctrl:1
	v_add_f32_dpp v79, v46, v46 wave_shr:1 row_mask:0xf bank_mask:0xf bound_ctrl:1
	v_add_f32_dpp v86, v47, v47 wave_shr:1 row_mask:0xf bank_mask:0xf bound_ctrl:1
	v_add_f32_dpp v87, v48, v48 wave_shr:1 row_mask:0xf bank_mask:0xf bound_ctrl:1
	v_add_f32_dpp v100, v49, v49 wave_shr:1 row_mask:0xf bank_mask:0xf bound_ctrl:1
	v_add_f32_dpp v101, v29, v29 wave_shr:1 row_mask:0xf bank_mask:0xf bound_ctrl:1
	v_add_f32_dpp v58, v12, v58 wave_shl:1 row_mask:0xf bank_mask:0xf bound_ctrl:1
	v_add_f32_dpp v59, v13, v59 wave_shl:1 row_mask:0xf bank_mask:0xf bound_ctrl:1
	v_add_f32_dpp v60, v14, v60 wave_shl:1 row_mask:0xf bank_mask:0xf bound_ctrl:1
	v_add_f32_dpp v61, v38, v61 wave_shl:1 row_mask:0xf bank_mask:0xf bound_ctrl:1
	v_add_f32_dpp v78, v39, v78 wave_shl:1 row_mask:0xf bank_mask:0xf bound_ctrl:1
	v_add_f32_dpp v79, v46, v79 wave_shl:1 row_mask:0xf bank_mask:0xf bound_ctrl:1
	v_add_f32_dpp v86, v47, v86 wave_shl:1 row_mask:0xf bank_mask:0xf bound_ctrl:1
	v_add_f32_dpp v87, v48, v87 wave_shl:1 row_mask:0xf bank_mask:0xf bound_ctrl:1
	v_add_f32_dpp v100, v49, v100 wave_shl:1 row_mask:0xf bank_mask:0xf bound_ctrl:1
	v_add_f32_dpp v101, v29, v101 wave_shl:1 row_mask:0xf bank_mask:0xf bound_ctrl:1
	v_pk_add_f32 v[38:39], v[80:81], v[58:59]
	v_pk_add_f32 v[46:47], v[88:89], v[38:39]
	v_pk_add_f32 v[48:49], v[82:83], v[60:61]
	v_pk_add_f32 v[80:81], v[112:113], v[48:49]
	v_pk_add_f32 v[82:83], v[90:91], v[78:79]
	v_pk_add_f32 v[88:89], v[114:115], v[82:83]
	v_pk_add_f32 v[90:91], v[96:97], v[86:87]
	v_pk_add_f32 v[110:111], v[116:117], v[90:91]
	v_pk_add_f32 v[96:97], v[108:109], v[100:101]
	v_pk_add_f32 v[112:113], v[118:119], v[96:97]
	v_mul_f32_e64 v116, v46, v22
	v_mul_f32_e64 v117, v47, v22
	v_mul_f32_e64 v118, v80, v22
	v_fma_f32 v29, v81, v22, v26
	v_mul_f32_e64 v31, v88, v22
	v_mul_f32_e64 v108, v89, v22
	v_fma_f32 v109, v110, v22, v26
	v_mul_f32_e64 v114, v111, v22
	v_fma_f32 v115, v112, v22, v26
	v_fma_f32 v29, -v116, v116, v29
	v_fma_f32 v31, -v116, v117, v31
	v_fma_f32 v108, -v116, v118, v108
	v_fma_f32 v109, -v117, v117, v109
	v_fma_f32 v114, -v117, v118, v114
	v_fma_f32 v115, -v118, v118, v115
	v_mul_f32_e64 v130, v114, v114
	v_mul_f32_e64 v131, v31, v115
	v_mul_f32_e64 v132, v108, v109
	v_mul_f32_e64 v133, v108, v108
	v_mul_f32_e64 v134, v29, v114
	v_mul_f32_e64 v135, v31, v31
	v_fma_f32 v130, v109, v115, -v130
	v_fma_f32 v131, v108, v114, -v131
	v_fma_f32 v132, v31, v114, -v132
	v_fma_f32 v133, v29, v115, -v133
	v_fma_f32 v134, v31, v108, -v134
	v_fma_f32 v135, v29, v109, -v135
	v_mul_f32_e64 v136, v29, v130
	v_fma_f32 v136, v31, v131, v136
	v_fma_f32 v136, v108, v132, v136
	v_rcp_f32_e32 v136, v136
	v_cmp_ne_u32_e64 vcc, s37, v24
	v_mul_f32_e64 v136, v136, v22
	v_cndmask_b32_e64 v136, 0, v136, s[30:31]
	v_cndmask_b32_e64 v29, 0, v18, vcc
	v_cndmask_b32_e64 v125, 0, v22, s[30:31]
	v_mul_f32_e64 v119, v130, v136
	v_mul_f32_e64 v120, v131, v136
	v_mul_f32_e64 v121, v132, v136
	v_mul_f32_e64 v122, v133, v136
	v_mul_f32_e64 v123, v134, v136
	v_mul_f32_e64 v124, v135, v136
	v_add_f32_e64 v126, v113, v29
	v_mov_b32_e32 v127, v24
	ds_write_b128 v23, v[116:119]
	ds_write_b128 v23, v[120:123] offset:1024
	ds_write_b128 v23, v[124:127] offset:2048
	s_waitcnt lgkmcnt(0)
	s_barrier
	v_pk_mul_f32 v[46:47], v[6:7], v[12:13] op_sel_hi:[1,0]
	v_pk_mul_f32 v[80:81], v[6:7], v[12:13] op_sel:[0,1]
	v_pk_mul_f32 v[88:89], v[6:7], v[14:15] op_sel_hi:[1,0]
	v_add_f32_dpp v108, v6, v6 wave_shr:1 row_mask:0xf bank_mask:0xf bound_ctrl:1
	v_add_f32_dpp v109, v7, v7 wave_shr:1 row_mask:0xf bank_mask:0xf bound_ctrl:1
	v_add_f32_dpp v110, v46, v46 wave_shr:1 row_mask:0xf bank_mask:0xf bound_ctrl:1
	v_add_f32_dpp v111, v47, v47 wave_shr:1 row_mask:0xf bank_mask:0xf bound_ctrl:1
	v_add_f32_dpp v112, v80, v80 wave_shr:1 row_mask:0xf bank_mask:0xf bound_ctrl:1
	v_add_f32_dpp v113, v81, v81 wave_shr:1 row_mask:0xf bank_mask:0xf bound_ctrl:1
	v_add_f32_dpp v114, v88, v88 wave_shr:1 row_mask:0xf bank_mask:0xf bound_ctrl:1
	v_add_f32_dpp v115, v89, v89 wave_shr:1 row_mask:0xf bank_mask:0xf bound_ctrl:1
	v_add_f32_dpp v108, v6, v108 wave_shl:1 row_mask:0xf bank_mask:0xf bound_ctrl:1
	v_add_f32_dpp v109, v7, v109 wave_shl:1 row_mask:0xf bank_mask:0xf bound_ctrl:1
	v_add_f32_dpp v110, v46, v110 wave_shl:1 row_mask:0xf bank_mask:0xf bound_ctrl:1
	v_add_f32_dpp v111, v47, v111 wave_shl:1 row_mask:0xf bank_mask:0xf bound_ctrl:1
	v_add_f32_dpp v112, v80, v112 wave_shl:1 row_mask:0xf bank_mask:0xf bound_ctrl:1
	v_add_f32_dpp v113, v81, v113 wave_shl:1 row_mask:0xf bank_mask:0xf bound_ctrl:1
	v_add_f32_dpp v114, v88, v114 wave_shl:1 row_mask:0xf bank_mask:0xf bound_ctrl:1
	v_add_f32_dpp v115, v89, v115 wave_shl:1 row_mask:0xf bank_mask:0xf bound_ctrl:1
	v_pk_add_f32 v[46:47], v[70:71], v[108:109]
	v_pk_add_f32 v[80:81], v[102:103], v[46:47]
	v_pk_add_f32 v[70:71], v[72:73], v[110:111]
	v_pk_add_f32 v[88:89], v[104:105], v[70:71]
	v_pk_add_f32 v[72:73], v[94:95], v[112:113]
	v_pk_add_f32 v[102:103], v[106:107], v[72:73]
	v_pk_add_f32 v[94:95], v[98:99], v[114:115]
	v_pk_add_f32 v[104:105], v[128:129], v[94:95]
	v_pk_fma_f32 v[88:89], v[116:117], v[80:81], v[88:89] op_sel_hi:[0,1,1] neg_lo:[1,0,0] neg_hi:[1,0,0]
	v_pk_fma_f32 v[102:103], v[116:117], v[80:81], v[102:103] op_sel:[1,0,0] neg_lo:[1,0,0] neg_hi:[1,0,0]
	v_pk_fma_f32 v[104:105], v[118:119], v[80:81], v[104:105] op_sel_hi:[0,1,1] neg_lo:[1,0,0] neg_hi:[1,0,0]
	v_pk_mul_f32 v[98:99], v[118:119], v[88:89] op_sel:[1,0]
	v_pk_mul_f32 v[106:107], v[120:121], v[88:89] op_sel_hi:[0,1]
	v_pk_mul_f32 v[128:129], v[120:121], v[88:89] op_sel:[1,0]
	v_pk_fma_f32 v[98:99], v[120:121], v[102:103], v[98:99] op_sel_hi:[0,1,1]
	v_pk_fma_f32 v[106:107], v[122:123], v[102:103], v[106:107] op_sel_hi:[0,1,1]
	v_pk_fma_f32 v[128:129], v[122:123], v[102:103], v[128:129] op_sel:[1,0,0]
	v_pk_fma_f32 v[98:99], v[120:121], v[104:105], v[98:99] op_sel:[1,0,0]
	v_pk_fma_f32 v[106:107], v[122:123], v[104:105], v[106:107] op_sel:[1,0,0]
	v_pk_fma_f32 v[128:129], v[124:125], v[104:105], v[128:129] op_sel_hi:[0,1,1]
	v_pk_mul_f32 v[130:131], v[116:117], v[98:99] op_sel_hi:[0,1]
	v_pk_fma_f32 v[130:131], v[116:117], v[106:107], v[130:131] op_sel:[1,0,0]
	v_pk_fma_f32 v[130:131], v[118:119], v[128:129], v[130:131] op_sel_hi:[0,1,1]
	v_pk_fma_f32 v[130:131], v[124:125], v[80:81], v[130:131] op_sel:[1,0,0] neg_lo:[0,0,1] neg_hi:[0,0,1]
	v_cmp_eq_u32_e64 s[10:11], 6, v127
	v_cmp_eq_u32_e64 s[14:15], 7, v127
	v_add_f32_dpp v80, v98, v98 wave_shr:1 row_mask:0xf bank_mask:0xf bound_ctrl:1
	v_add_f32_dpp v81, v99, v99 wave_shr:1 row_mask:0xf bank_mask:0xf bound_ctrl:1
	v_add_f32_dpp v88, v106, v106 wave_shr:1 row_mask:0xf bank_mask:0xf bound_ctrl:1
	v_add_f32_dpp v89, v107, v107 wave_shr:1 row_mask:0xf bank_mask:0xf bound_ctrl:1
	v_add_f32_dpp v102, v128, v128 wave_shr:1 row_mask:0xf bank_mask:0xf bound_ctrl:1
	v_add_f32_dpp v103, v129, v129 wave_shr:1 row_mask:0xf bank_mask:0xf bound_ctrl:1
	v_add_f32_dpp v104, v130, v130 wave_shr:1 row_mask:0xf bank_mask:0xf bound_ctrl:1
	v_add_f32_dpp v105, v131, v131 wave_shr:1 row_mask:0xf bank_mask:0xf bound_ctrl:1
	v_add_f32_dpp v80, v98, v80 wave_shl:1 row_mask:0xf bank_mask:0xf bound_ctrl:1
	v_add_f32_dpp v81, v99, v81 wave_shl:1 row_mask:0xf bank_mask:0xf bound_ctrl:1
	v_add_f32_dpp v88, v106, v88 wave_shl:1 row_mask:0xf bank_mask:0xf bound_ctrl:1
	v_add_f32_dpp v89, v107, v89 wave_shl:1 row_mask:0xf bank_mask:0xf bound_ctrl:1
	v_add_f32_dpp v102, v128, v102 wave_shl:1 row_mask:0xf bank_mask:0xf bound_ctrl:1
	v_add_f32_dpp v103, v129, v103 wave_shl:1 row_mask:0xf bank_mask:0xf bound_ctrl:1
	v_add_f32_dpp v104, v130, v104 wave_shl:1 row_mask:0xf bank_mask:0xf bound_ctrl:1
	v_add_f32_dpp v105, v131, v105 wave_shl:1 row_mask:0xf bank_mask:0xf bound_ctrl:1
	v_pk_add_f32 v[98:99], v[50:51], v[80:81]
	v_pk_add_f32 v[106:107], v[74:75], v[98:99]
	v_pk_add_f32 v[50:51], v[52:53], v[88:89]
	v_pk_add_f32 v[74:75], v[76:77], v[50:51]
	v_pk_add_f32 v[52:53], v[54:55], v[102:103]
	v_pk_add_f32 v[76:77], v[84:85], v[52:53]
	v_pk_add_f32 v[54:55], v[56:57], v[104:105]
	v_pk_add_f32 v[84:85], v[92:93], v[54:55]
	v_pk_fma_f32 v[84:85], v[64:65], v[106:107], v[84:85] op_sel_hi:[0,1,1]
	v_pk_fma_f32 v[84:85], v[64:65], v[74:75], v[84:85] op_sel:[1,0,0]
	v_pk_fma_f32 v[84:85], v[66:67], v[76:77], v[84:85] op_sel_hi:[0,1,1]
	v_cndmask_b32_e64 v56, 0, v18, s[10:11]
	v_cndmask_b32_e64 v57, 0, v18, s[14:15]
	v_pk_fma_f32 v[84:85], v[62:63], v[126:127], v[84:85] op_sel_hi:[1,0,1] neg_lo:[0,0,1] neg_hi:[0,0,1]
	s_add_i32 s4, s34, 2
	s_cmpk_lt_i32 s4, 0x201
	s_cselect_b64 s[12:13], s[0:1], 0
	v_pk_add_f32 v[84:85], v[84:85], v[56:57] neg_lo:[0,1] neg_hi:[0,1]
	v_pk_mul_f32 v[92:93], v[84:85], v[84:85]
	v_add_f32_e32 v92, v92, v93
	v_cndmask_b32_e64 v93, 0, v92, s[12:13]
	v_add_f32_e32 v1, v1, v93
	s_add_i32 s5, s34, 7
	s_min_i32 s5, s5, 0x200
	s_mul_i32 s6, s5, 0x804
	s_add_i32 s6, s6, s35
	s_add_i32 s7, s6, 0x505014
	s_add_i32 s8, s6, 0x606018
	s_mul_i32 s9, s5, 0x180c
	s_add_i32 s9, s9, s33
	s_add_i32 s4, s34, 8
	s_min_i32 s4, s4, 0x200
	s_mul_i32 s4, s4, 0x804
	s_add_i32 s4, s4, s38
	buffer_load_dword v24, v28, s[20:23], s4 offen nt
	buffer_load_dwordx3 v[64:66], v27, s[24:27], s9 offen nt
	buffer_load_dword v56, v28, s[16:19], s7 offen nt
	buffer_load_dword v57, v28, s[16:19], s8 offen nt
	s_waitcnt vmcnt(8)
	s_add_i32 s4, s34, 6
	s_cmpk_lt_u32 s4, 0x201
	s_cselect_b64 s[12:13], s[40:41], 0
	v_cmp_eq_u32_e64 s[14:15], s37, v16
	s_and_b64 s[14:15], s[14:15], s[12:13]
	v_cndmask_b32_e64 v29, 0, 1, s[14:15]
	v_mul_f32_e64 v62, v32, v32
	v_mul_f32_e64 v63, v32, v33
	v_mul_f32_e64 v74, v32, v34
	v_mul_f32_e64 v75, v33, v33
	v_mul_f32_e64 v76, v33, v34
	v_mul_f32_e64 v77, v34, v34
	v_or_b32_dpp v31, v29, v29 wave_shr:1 row_mask:0xf bank_mask:0xf bound_ctrl:1
	s_nop 1
	v_or_b32_dpp v31, v29, v31 wave_shl:1 row_mask:0xf bank_mask:0xf bound_ctrl:1
	s_nop 1
	v_or_b32_dpp v68, v31, v31 wave_shr:1 row_mask:0xf bank_mask:0xf bound_ctrl:1
	s_nop 1
	v_or_b32_dpp v68, v31, v68 wave_shl:1 row_mask:0xf bank_mask:0xf bound_ctrl:1
	v_or3_b32 v29, v68, v69, v44
	v_or3_b32 v29, v29, v30, v45
	s_add_i32 s4, s34, 3
	s_cmpk_lt_u32 s4, 0x1ff
	s_cselect_b64 s[12:13], s[42:43], 0
	v_cmp_ne_u32_e64 s[30:31], 0, v29
	s_and_b64 s[30:31], s[30:31], s[12:13]
	v_cndmask_b32_e64 v29, 0, 1.0, s[30:31]
	v_add_f32_dpp v84, v32, v32 wave_shr:1 row_mask:0xf bank_mask:0xf bound_ctrl:1
	v_add_f32_dpp v85, v33, v33 wave_shr:1 row_mask:0xf bank_mask:0xf bound_ctrl:1
	v_add_f32_dpp v92, v34, v34 wave_shr:1 row_mask:0xf bank_mask:0xf bound_ctrl:1
	v_add_f32_dpp v93, v62, v62 wave_shr:1 row_mask:0xf bank_mask:0xf bound_ctrl:1
	v_add_f32_dpp v106, v63, v63 wave_shr:1 row_mask:0xf bank_mask:0xf bound_ctrl:1
	v_add_f32_dpp v107, v74, v74 wave_shr:1 row_mask:0xf bank_mask:0xf bound_ctrl:1
	v_add_f32_dpp v116, v75, v75 wave_shr:1 row_mask:0xf bank_mask:0xf bound_ctrl:1
	v_add_f32_dpp v117, v76, v76 wave_shr:1 row_mask:0xf bank_mask:0xf bound_ctrl:1
	v_add_f32_dpp v118, v77, v77 wave_shr:1 row_mask:0xf bank_mask:0xf bound_ctrl:1
	v_add_f32_dpp v119, v29, v29 wave_shr:1 row_mask:0xf bank_mask:0xf bound_ctrl:1
	v_add_f32_dpp v84, v32, v84 wave_shl:1 row_mask:0xf bank_mask:0xf bound_ctrl:1
	v_add_f32_dpp v85, v33, v85 wave_shl:1 row_mask:0xf bank_mask:0xf bound_ctrl:1
	v_add_f32_dpp v92, v34, v92 wave_shl:1 row_mask:0xf bank_mask:0xf bound_ctrl:1
	v_add_f32_dpp v93, v62, v93 wave_shl:1 row_mask:0xf bank_mask:0xf bound_ctrl:1
	v_add_f32_dpp v106, v63, v106 wave_shl:1 row_mask:0xf bank_mask:0xf bound_ctrl:1
	v_add_f32_dpp v107, v74, v107 wave_shl:1 row_mask:0xf bank_mask:0xf bound_ctrl:1
	v_add_f32_dpp v116, v75, v116 wave_shl:1 row_mask:0xf bank_mask:0xf bound_ctrl:1
	v_add_f32_dpp v117, v76, v117 wave_shl:1 row_mask:0xf bank_mask:0xf bound_ctrl:1
	v_add_f32_dpp v118, v77, v118 wave_shl:1 row_mask:0xf bank_mask:0xf bound_ctrl:1
	v_add_f32_dpp v119, v29, v119 wave_shl:1 row_mask:0xf bank_mask:0xf bound_ctrl:1
	v_pk_add_f32 v[62:63], v[38:39], v[84:85]
	v_pk_add_f32 v[38:39], v[48:49], v[92:93]
	v_pk_add_f32 v[48:49], v[82:83], v[106:107]
	v_pk_add_f32 v[74:75], v[90:91], v[116:117]
	v_pk_add_f32 v[76:77], v[96:97], v[118:119]
	v_mul_f32_e64 v120, v62, v22
	v_mul_f32_e64 v121, v63, v22
	v_mul_f32_e64 v122, v38, v22
	v_fma_f32 v29, v39, v22, v26
	v_mul_f32_e64 v31, v48, v22
	v_mul_f32_e64 v82, v49, v22
	v_fma_f32 v83, v74, v22, v26
	v_mul_f32_e64 v90, v75, v22
	v_fma_f32 v91, v76, v22, v26
	v_fma_f32 v29, -v120, v120, v29
	v_fma_f32 v31, -v120, v121, v31
	v_fma_f32 v82, -v120, v122, v82
	v_fma_f32 v83, -v121, v121, v83
	v_fma_f32 v90, -v121, v122, v90
	v_fma_f32 v91, -v122, v122, v91
	v_mul_f32_e64 v96, v90, v90
	v_mul_f32_e64 v97, v31, v91
	v_mul_f32_e64 v132, v82, v83
	v_mul_f32_e64 v133, v82, v82
	v_mul_f32_e64 v134, v29, v90
	v_mul_f32_e64 v135, v31, v31
	v_fma_f32 v96, v83, v91, -v96
	v_fma_f32 v97, v82, v90, -v97
	v_fma_f32 v132, v31, v90, -v132
	v_fma_f32 v133, v29, v91, -v133
	v_fma_f32 v134, v31, v82, -v134
	v_fma_f32 v135, v29, v83, -v135
	v_mul_f32_e64 v136, v29, v96
	v_fma_f32 v136, v31, v97, v136
	v_fma_f32 v136, v82, v132, v136
	v_rcp_f32_e32 v136, v136
	v_cmp_ne_u32_e64 vcc, s37, v17
	v_mul_f32_e64 v136, v136, v22
	v_cndmask_b32_e64 v136, 0, v136, s[30:31]
	v_cndmask_b32_e64 v29, 0, v18, vcc
	v_cndmask_b32_e64 v129, 0, v22, s[30:31]
	v_mul_f32_e64 v123, v96, v136
	v_mul_f32_e64 v124, v97, v136
	v_mul_f32_e64 v125, v132, v136
	v_mul_f32_e64 v126, v133, v136
	v_mul_f32_e64 v127, v134, v136
	v_mul_f32_e64 v128, v135, v136
	v_add_f32_e64 v130, v77, v29
	v_mov_b32_e32 v131, v17
	ds_write_b128 v23, v[120:123] offset:3072
	ds_write_b128 v23, v[124:127] offset:4096
	ds_write_b128 v23, v[128:131] offset:5120
	s_waitcnt lgkmcnt(0)
	s_barrier
	v_pk_mul_f32 v[38:39], v[20:21], v[32:33] op_sel_hi:[1,0]
	v_pk_mul_f32 v[48:49], v[20:21], v[32:33] op_sel:[0,1]
	v_pk_mul_f32 v[62:63], v[20:21], v[34:35] op_sel_hi:[1,0]
	v_add_f32_dpp v74, v20, v20 wave_shr:1 row_mask:0xf bank_mask:0xf bound_ctrl:1
	v_add_f32_dpp v75, v21, v21 wave_shr:1 row_mask:0xf bank_mask:0xf bound_ctrl:1
	v_add_f32_dpp v76, v38, v38 wave_shr:1 row_mask:0xf bank_mask:0xf bound_ctrl:1
	v_add_f32_dpp v77, v39, v39 wave_shr:1 row_mask:0xf bank_mask:0xf bound_ctrl:1
	v_add_f32_dpp v82, v48, v48 wave_shr:1 row_mask:0xf bank_mask:0xf bound_ctrl:1
	v_add_f32_dpp v83, v49, v49 wave_shr:1 row_mask:0xf bank_mask:0xf bound_ctrl:1
	v_add_f32_dpp v90, v62, v62 wave_shr:1 row_mask:0xf bank_mask:0xf bound_ctrl:1
	v_add_f32_dpp v91, v63, v63 wave_shr:1 row_mask:0xf bank_mask:0xf bound_ctrl:1
	v_add_f32_dpp v74, v20, v74 wave_shl:1 row_mask:0xf bank_mask:0xf bound_ctrl:1
	v_add_f32_dpp v75, v21, v75 wave_shl:1 row_mask:0xf bank_mask:0xf bound_ctrl:1
	v_add_f32_dpp v76, v38, v76 wave_shl:1 row_mask:0xf bank_mask:0xf bound_ctrl:1
	v_add_f32_dpp v77, v39, v77 wave_shl:1 row_mask:0xf bank_mask:0xf bound_ctrl:1
	v_add_f32_dpp v82, v48, v82 wave_shl:1 row_mask:0xf bank_mask:0xf bound_ctrl:1
	v_add_f32_dpp v83, v49, v83 wave_shl:1 row_mask:0xf bank_mask:0xf bound_ctrl:1
	v_add_f32_dpp v90, v62, v90 wave_shl:1 row_mask:0xf bank_mask:0xf bound_ctrl:1
	v_add_f32_dpp v91, v63, v91 wave_shl:1 row_mask:0xf bank_mask:0xf bound_ctrl:1
	v_pk_add_f32 v[38:39], v[46:47], v[74:75]
	v_pk_add_f32 v[46:47], v[70:71], v[76:77]
	v_pk_add_f32 v[48:49], v[72:73], v[82:83]
	v_pk_add_f32 v[62:63], v[94:95], v[90:91]
	v_pk_fma_f32 v[46:47], v[120:121], v[38:39], v[46:47] op_sel_hi:[0,1,1] neg_lo:[1,0,0] neg_hi:[1,0,0]
	v_pk_fma_f32 v[48:49], v[120:121], v[38:39], v[48:49] op_sel:[1,0,0] neg_lo:[1,0,0] neg_hi:[1,0,0]
	v_pk_fma_f32 v[62:63], v[122:123], v[38:39], v[62:63] op_sel_hi:[0,1,1] neg_lo:[1,0,0] neg_hi:[1,0,0]
	v_pk_mul_f32 v[70:71], v[122:123], v[46:47] op_sel:[1,0]
	v_pk_mul_f32 v[72:73], v[124:125], v[46:47] op_sel_hi:[0,1]
	v_pk_mul_f32 v[94:95], v[124:125], v[46:47] op_sel:[1,0]
	v_pk_fma_f32 v[70:71], v[124:125], v[48:49], v[70:71] op_sel_hi:[0,1,1]
	v_pk_fma_f32 v[72:73], v[126:127], v[48:49], v[72:73] op_sel_hi:[0,1,1]
	v_pk_fma_f32 v[94:95], v[126:127], v[48:49], v[94:95] op_sel:[1,0,0]
	v_pk_fma_f32 v[70:71], v[124:125], v[62:63], v[70:71] op_sel:[1,0,0]
	v_pk_fma_f32 v[72:73], v[126:127], v[62:63], v[72:73] op_sel:[1,0,0]
	v_pk_fma_f32 v[94:95], v[128:129], v[62:63], v[94:95] op_sel_hi:[0,1,1]
	v_pk_mul_f32 v[96:97], v[120:121], v[70:71] op_sel_hi:[0,1]
	v_pk_fma_f32 v[96:97], v[120:121], v[72:73], v[96:97] op_sel:[1,0,0]
	v_pk_fma_f32 v[96:97], v[122:123], v[94:95], v[96:97] op_sel_hi:[0,1,1]
	v_pk_fma_f32 v[96:97], v[128:129], v[38:39], v[96:97] op_sel:[1,0,0] neg_lo:[0,0,1] neg_hi:[0,0,1]
	v_cmp_eq_u32_e64 s[10:11], 6, v131
	v_cmp_eq_u32_e64 s[14:15], 7, v131
	v_add_f32_dpp v38, v70, v70 wave_shr:1 row_mask:0xf bank_mask:0xf bound_ctrl:1
	v_add_f32_dpp v39, v71, v71 wave_shr:1 row_mask:0xf bank_mask:0xf bound_ctrl:1
	v_add_f32_dpp v46, v72, v72 wave_shr:1 row_mask:0xf bank_mask:0xf bound_ctrl:1
	v_add_f32_dpp v47, v73, v73 wave_shr:1 row_mask:0xf bank_mask:0xf bound_ctrl:1
	v_add_f32_dpp v48, v94, v94 wave_shr:1 row_mask:0xf bank_mask:0xf bound_ctrl:1
	v_add_f32_dpp v49, v95, v95 wave_shr:1 row_mask:0xf bank_mask:0xf bound_ctrl:1
	v_add_f32_dpp v62, v96, v96 wave_shr:1 row_mask:0xf bank_mask:0xf bound_ctrl:1
	v_add_f32_dpp v63, v97, v97 wave_shr:1 row_mask:0xf bank_mask:0xf bound_ctrl:1
	v_add_f32_dpp v38, v70, v38 wave_shl:1 row_mask:0xf bank_mask:0xf bound_ctrl:1
	v_add_f32_dpp v39, v71, v39 wave_shl:1 row_mask:0xf bank_mask:0xf bound_ctrl:1
	v_add_f32_dpp v46, v72, v46 wave_shl:1 row_mask:0xf bank_mask:0xf bound_ctrl:1
	v_add_f32_dpp v47, v73, v47 wave_shl:1 row_mask:0xf bank_mask:0xf bound_ctrl:1
	v_add_f32_dpp v48, v94, v48 wave_shl:1 row_mask:0xf bank_mask:0xf bound_ctrl:1
	v_add_f32_dpp v49, v95, v49 wave_shl:1 row_mask:0xf bank_mask:0xf bound_ctrl:1
	v_add_f32_dpp v62, v96, v62 wave_shl:1 row_mask:0xf bank_mask:0xf bound_ctrl:1
	v_add_f32_dpp v63, v97, v63 wave_shl:1 row_mask:0xf bank_mask:0xf bound_ctrl:1
	v_pk_add_f32 v[70:71], v[98:99], v[38:39]
	v_pk_add_f32 v[72:73], v[50:51], v[46:47]
	v_pk_add_f32 v[50:51], v[52:53], v[48:49]
	v_pk_add_f32 v[52:53], v[54:55], v[62:63]
	v_pk_fma_f32 v[52:53], v[8:9], v[70:71], v[52:53] op_sel_hi:[0,1,1]
	v_pk_fma_f32 v[52:53], v[8:9], v[72:73], v[52:53] op_sel:[1,0,0]
	v_pk_fma_f32 v[52:53], v[10:11], v[50:51], v[52:53] op_sel_hi:[0,1,1]
	v_cndmask_b32_e64 v54, 0, v18, s[10:11]
	v_cndmask_b32_e64 v55, 0, v18, s[14:15]
	v_pk_fma_f32 v[52:53], v[4:5], v[130:131], v[52:53] op_sel_hi:[1,0,1] neg_lo:[0,0,1] neg_hi:[0,0,1]
	s_add_i32 s4, s34, 3
	s_cmpk_lt_i32 s4, 0x201
	s_cselect_b64 s[12:13], s[0:1], 0
	v_pk_add_f32 v[52:53], v[52:53], v[54:55] neg_lo:[0,1] neg_hi:[0,1]
	v_pk_mul_f32 v[94:95], v[52:53], v[52:53]
	v_add_f32_e32 v94, v94, v95
	v_cndmask_b32_e64 v95, 0, v94, s[12:13]
	v_add_f32_e32 v1, v1, v95
	s_add_i32 s5, s34, 8
	s_min_i32 s5, s5, 0x200
	s_mul_i32 s6, s5, 0x804
	s_add_i32 s6, s6, s35
	s_add_i32 s7, s6, 0x505014
	s_add_i32 s8, s6, 0x606018
	s_mul_i32 s9, s5, 0x180c
	s_add_i32 s9, s9, s33
	s_add_i32 s4, s34, 9
	s_min_i32 s4, s4, 0x200
	s_mul_i32 s4, s4, 0x804
	s_add_i32 s4, s4, s38
	buffer_load_dword v17, v28, s[20:23], s4 offen nt
	buffer_load_dwordx3 v[8:10], v27, s[24:27], s9 offen nt
	buffer_load_dword v4, v28, s[16:19], s7 offen nt
	buffer_load_dword v5, v28, s[16:19], s8 offen nt
	s_waitcnt vmcnt(8)
	s_add_i32 s4, s34, 7
	s_cmpk_lt_u32 s4, 0x201
	s_cselect_b64 s[12:13], s[40:41], 0
	v_cmp_eq_u32_e64 s[14:15], s37, v25
	s_and_b64 s[14:15], s[14:15], s[12:13]
	v_cndmask_b32_e64 v29, 0, 1, s[14:15]
	v_mul_f32_e64 v50, v40, v40
	v_mul_f32_e64 v51, v40, v41
	v_mul_f32_e64 v52, v40, v42
	v_mul_f32_e64 v53, v41, v41
	v_mul_f32_e64 v54, v41, v42
	v_mul_f32_e64 v55, v42, v42
	v_or_b32_dpp v31, v29, v29 wave_shr:1 row_mask:0xf bank_mask:0xf bound_ctrl:1
	s_nop 1
	v_or_b32_dpp v31, v29, v31 wave_shl:1 row_mask:0xf bank_mask:0xf bound_ctrl:1
	s_nop 1
	v_or_b32_dpp v45, v31, v31 wave_shr:1 row_mask:0xf bank_mask:0xf bound_ctrl:1
	s_nop 1
	v_or_b32_dpp v45, v31, v45 wave_shl:1 row_mask:0xf bank_mask:0xf bound_ctrl:1
	v_or3_b32 v29, v45, v68, v69
	v_or3_b32 v29, v29, v44, v30
	s_add_i32 s4, s34, 4
	s_cmpk_lt_u32 s4, 0x1ff
	s_cselect_b64 s[12:13], s[42:43], 0
	v_cmp_ne_u32_e64 s[30:31], 0, v29
	s_and_b64 s[30:31], s[30:31], s[12:13]
	v_cndmask_b32_e64 v29, 0, 1.0, s[30:31]
	v_add_f32_dpp v70, v40, v40 wave_shr:1 row_mask:0xf bank_mask:0xf bound_ctrl:1
	v_add_f32_dpp v71, v41, v41 wave_shr:1 row_mask:0xf bank_mask:0xf bound_ctrl:1
	v_add_f32_dpp v72, v42, v42 wave_shr:1 row_mask:0xf bank_mask:0xf bound_ctrl:1
	v_add_f32_dpp v73, v50, v50 wave_shr:1 row_mask:0xf bank_mask:0xf bound_ctrl:1
	v_add_f32_dpp v94, v51, v51 wave_shr:1 row_mask:0xf bank_mask:0xf bound_ctrl:1
	v_add_f32_dpp v95, v52, v52 wave_shr:1 row_mask:0xf bank_mask:0xf bound_ctrl:1
	v_add_f32_dpp v96, v53, v53 wave_shr:1 row_mask:0xf bank_mask:0xf bound_ctrl:1
	v_add_f32_dpp v97, v54, v54 wave_shr:1 row_mask:0xf bank_mask:0xf bound_ctrl:1
	v_add_f32_dpp v98, v55, v55 wave_shr:1 row_mask:0xf bank_mask:0xf bound_ctrl:1
	v_add_f32_dpp v99, v29, v29 wave_shr:1 row_mask:0xf bank_mask:0xf bound_ctrl:1
	v_add_f32_dpp v70, v40, v70 wave_shl:1 row_mask:0xf bank_mask:0xf bound_ctrl:1
	v_add_f32_dpp v71, v41, v71 wave_shl:1 row_mask:0xf bank_mask:0xf bound_ctrl:1
	v_add_f32_dpp v72, v42, v72 wave_shl:1 row_mask:0xf bank_mask:0xf bound_ctrl:1
	v_add_f32_dpp v73, v50, v73 wave_shl:1 row_mask:0xf bank_mask:0xf bound_ctrl:1
	v_add_f32_dpp v94, v51, v94 wave_shl:1 row_mask:0xf bank_mask:0xf bound_ctrl:1
	v_add_f32_dpp v95, v52, v95 wave_shl:1 row_mask:0xf bank_mask:0xf bound_ctrl:1
	v_add_f32_dpp v96, v53, v96 wave_shl:1 row_mask:0xf bank_mask:0xf bound_ctrl:1
	v_add_f32_dpp v97, v54, v97 wave_shl:1 row_mask:0xf bank_mask:0xf bound_ctrl:1
	v_add_f32_dpp v98, v55, v98 wave_shl:1 row_mask:0xf bank_mask:0xf bound_ctrl:1
	v_add_f32_dpp v99, v29, v99 wave_shl:1 row_mask:0xf bank_mask:0xf bound_ctrl:1
	v_pk_add_f32 v[50:51], v[84:85], v[70:71]
	v_pk_add_f32 v[52:53], v[58:59], v[50:51]
	v_pk_add_f32 v[54:55], v[92:93], v[72:73]
	v_pk_add_f32 v[58:59], v[60:61], v[54:55]
	v_pk_add_f32 v[60:61], v[106:107], v[94:95]
	v_pk_add_f32 v[84:85], v[78:79], v[60:61]
	v_pk_add_f32 v[78:79], v[116:117], v[96:97]
	v_pk_add_f32 v[92:93], v[86:87], v[78:79]
	v_pk_add_f32 v[86:87], v[118:119], v[98:99]
	v_pk_add_f32 v[106:107], v[100:101], v[86:87]
	v_mul_f32_e64 v116, v52, v22
	v_mul_f32_e64 v117, v53, v22
	v_mul_f32_e64 v118, v58, v22
	v_fma_f32 v29, v59, v22, v26
	v_mul_f32_e64 v31, v84, v22
	v_mul_f32_e64 v100, v85, v22
	v_fma_f32 v101, v92, v22, v26
	v_mul_f32_e64 v128, v93, v22
	v_fma_f32 v129, v106, v22, v26
	v_fma_f32 v29, -v116, v116, v29
	v_fma_f32 v31, -v116, v117, v31
	v_fma_f32 v100, -v116, v118, v100
	v_fma_f32 v101, -v117, v117, v101
	v_fma_f32 v128, -v117, v118, v128
	v_fma_f32 v129, -v118, v118, v129
	v_mul_f32_e64 v130, v128, v128
	v_mul_f32_e64 v131, v31, v129
	v_mul_f32_e64 v132, v100, v101
	v_mul_f32_e64 v133, v100, v100
	v_mul_f32_e64 v134, v29, v128
	v_mul_f32_e64 v135, v31, v31
	v_fma_f32 v130, v101, v129, -v130
	v_fma_f32 v131, v100, v128, -v131
	v_fma_f32 v132, v31, v128, -v132
	v_fma_f32 v133, v29, v129, -v133
	v_fma_f32 v134, v31, v100, -v134
	v_fma_f32 v135, v29, v101, -v135
	v_mul_f32_e64 v136, v29, v130
	v_fma_f32 v136, v31, v131, v136
	v_fma_f32 v136, v100, v132, v136
	v_rcp_f32_e32 v136, v136
	v_cmp_ne_u32_e64 vcc, s37, v2
	v_mul_f32_e64 v136, v136, v22
	v_cndmask_b32_e64 v136, 0, v136, s[30:31]
	v_cndmask_b32_e64 v29, 0, v18, vcc
	v_cndmask_b32_e64 v125, 0, v22, s[30:31]
	v_mul_f32_e64 v119, v130, v136
	v_mul_f32_e64 v120, v131, v136
	v_mul_f32_e64 v121, v132, v136
	v_mul_f32_e64 v122, v133, v136
	v_mul_f32_e64 v123, v134, v136
	v_mul_f32_e64 v124, v135, v136
	v_add_f32_e64 v126, v107, v29
	v_mov_b32_e32 v127, v2
	ds_write_b128 v23, v[116:119]
	ds_write_b128 v23, v[120:123] offset:1024
	ds_write_b128 v23, v[124:127] offset:2048
	s_waitcnt lgkmcnt(0)
	s_barrier
	v_pk_mul_f32 v[30:31], v[36:37], v[40:41] op_sel_hi:[1,0]
	v_pk_mul_f32 v[52:53], v[36:37], v[40:41] op_sel:[0,1]
	v_pk_mul_f32 v[58:59], v[36:37], v[42:43] op_sel_hi:[1,0]
	v_add_f32_dpp v84, v36, v36 wave_shr:1 row_mask:0xf bank_mask:0xf bound_ctrl:1
	v_add_f32_dpp v85, v37, v37 wave_shr:1 row_mask:0xf bank_mask:0xf bound_ctrl:1
	v_add_f32_dpp v92, v30, v30 wave_shr:1 row_mask:0xf bank_mask:0xf bound_ctrl:1
	v_add_f32_dpp v93, v31, v31 wave_shr:1 row_mask:0xf bank_mask:0xf bound_ctrl:1
	v_add_f32_dpp v100, v52, v52 wave_shr:1 row_mask:0xf bank_mask:0xf bound_ctrl:1
	v_add_f32_dpp v101, v53, v53 wave_shr:1 row_mask:0xf bank_mask:0xf bound_ctrl:1
	v_add_f32_dpp v106, v58, v58 wave_shr:1 row_mask:0xf bank_mask:0xf bound_ctrl:1
	v_add_f32_dpp v107, v59, v59 wave_shr:1 row_mask:0xf bank_mask:0xf bound_ctrl:1
	v_add_f32_dpp v84, v36, v84 wave_shl:1 row_mask:0xf bank_mask:0xf bound_ctrl:1
	v_add_f32_dpp v85, v37, v85 wave_shl:1 row_mask:0xf bank_mask:0xf bound_ctrl:1
	v_add_f32_dpp v92, v30, v92 wave_shl:1 row_mask:0xf bank_mask:0xf bound_ctrl:1
	v_add_f32_dpp v93, v31, v93 wave_shl:1 row_mask:0xf bank_mask:0xf bound_ctrl:1
	v_add_f32_dpp v100, v52, v100 wave_shl:1 row_mask:0xf bank_mask:0xf bound_ctrl:1
	v_add_f32_dpp v101, v53, v101 wave_shl:1 row_mask:0xf bank_mask:0xf bound_ctrl:1
	v_add_f32_dpp v106, v58, v106 wave_shl:1 row_mask:0xf bank_mask:0xf bound_ctrl:1
	v_add_f32_dpp v107, v59, v107 wave_shl:1 row_mask:0xf bank_mask:0xf bound_ctrl:1
	v_pk_add_f32 v[30:31], v[74:75], v[84:85]
	v_pk_add_f32 v[52:53], v[108:109], v[30:31]
	v_pk_add_f32 v[58:59], v[76:77], v[92:93]
	v_pk_add_f32 v[74:75], v[110:111], v[58:59]
	v_pk_add_f32 v[76:77], v[82:83], v[100:101]
	v_pk_add_f32 v[108:109], v[112:113], v[76:77]
	v_pk_add_f32 v[82:83], v[90:91], v[106:107]
	v_pk_add_f32 v[110:111], v[114:115], v[82:83]
	v_pk_fma_f32 v[74:75], v[116:117], v[52:53], v[74:75] op_sel_hi:[0,1,1] neg_lo:[1,0,0] neg_hi:[1,0,0]
	v_pk_fma_f32 v[108:109], v[116:117], v[52:53], v[108:109] op_sel:[1,0,0] neg_lo:[1,0,0] neg_hi:[1,0,0]
	v_pk_fma_f32 v[110:111], v[118:119], v[52:53], v[110:111] op_sel_hi:[0,1,1] neg_lo:[1,0,0] neg_hi:[1,0,0]
	v_pk_mul_f32 v[90:91], v[118:119], v[74:75] op_sel:[1,0]
	v_pk_mul_f32 v[112:113], v[120:121], v[74:75] op_sel_hi:[0,1]
	v_pk_mul_f32 v[114:115], v[120:121], v[74:75] op_sel:[1,0]
	v_pk_fma_f32 v[90:91], v[120:121], v[108:109], v[90:91] op_sel_hi:[0,1,1]
	v_pk_fma_f32 v[112:113], v[122:123], v[108:109], v[112:113] op_sel_hi:[0,1,1]
	v_pk_fma_f32 v[114:115], v[122:123], v[108:109], v[114:115] op_sel:[1,0,0]
	v_pk_fma_f32 v[90:91], v[120:121], v[110:111], v[90:91] op_sel:[1,0,0]
	v_pk_fma_f32 v[112:113], v[122:123], v[110:111], v[112:113] op_sel:[1,0,0]
	v_pk_fma_f32 v[114:115], v[124:125], v[110:111], v[114:115] op_sel_hi:[0,1,1]
	v_pk_mul_f32 v[128:129], v[116:117], v[90:91] op_sel_hi:[0,1]
	v_pk_fma_f32 v[128:129], v[116:117], v[112:113], v[128:129] op_sel:[1,0,0]
	v_pk_fma_f32 v[128:129], v[118:119], v[114:115], v[128:129] op_sel_hi:[0,1,1]
	v_pk_fma_f32 v[128:129], v[124:125], v[52:53], v[128:129] op_sel:[1,0,0] neg_lo:[0,0,1] neg_hi:[0,0,1]
	v_cmp_eq_u32_e64 s[10:11], 6, v127
	v_cmp_eq_u32_e64 s[14:15], 7, v127
	v_add_f32_dpp v52, v90, v90 wave_shr:1 row_mask:0xf bank_mask:0xf bound_ctrl:1
	v_add_f32_dpp v53, v91, v91 wave_shr:1 row_mask:0xf bank_mask:0xf bound_ctrl:1
	v_add_f32_dpp v74, v112, v112 wave_shr:1 row_mask:0xf bank_mask:0xf bound_ctrl:1
	v_add_f32_dpp v75, v113, v113 wave_shr:1 row_mask:0xf bank_mask:0xf bound_ctrl:1
	v_add_f32_dpp v108, v114, v114 wave_shr:1 row_mask:0xf bank_mask:0xf bound_ctrl:1
	v_add_f32_dpp v109, v115, v115 wave_shr:1 row_mask:0xf bank_mask:0xf bound_ctrl:1
	v_add_f32_dpp v110, v128, v128 wave_shr:1 row_mask:0xf bank_mask:0xf bound_ctrl:1
	v_add_f32_dpp v111, v129, v129 wave_shr:1 row_mask:0xf bank_mask:0xf bound_ctrl:1
	v_add_f32_dpp v52, v90, v52 wave_shl:1 row_mask:0xf bank_mask:0xf bound_ctrl:1
	v_add_f32_dpp v53, v91, v53 wave_shl:1 row_mask:0xf bank_mask:0xf bound_ctrl:1
	v_add_f32_dpp v74, v112, v74 wave_shl:1 row_mask:0xf bank_mask:0xf bound_ctrl:1
	v_add_f32_dpp v75, v113, v75 wave_shl:1 row_mask:0xf bank_mask:0xf bound_ctrl:1
	v_add_f32_dpp v108, v114, v108 wave_shl:1 row_mask:0xf bank_mask:0xf bound_ctrl:1
	v_add_f32_dpp v109, v115, v109 wave_shl:1 row_mask:0xf bank_mask:0xf bound_ctrl:1
	v_add_f32_dpp v110, v128, v110 wave_shl:1 row_mask:0xf bank_mask:0xf bound_ctrl:1
	v_add_f32_dpp v111, v129, v111 wave_shl:1 row_mask:0xf bank_mask:0xf bound_ctrl:1
	v_pk_add_f32 v[90:91], v[38:39], v[52:53]
	v_pk_add_f32 v[112:113], v[80:81], v[90:91]
	v_pk_add_f32 v[38:39], v[46:47], v[74:75]
	v_pk_add_f32 v[80:81], v[88:89], v[38:39]
	v_pk_add_f32 v[46:47], v[48:49], v[108:109]
	v_pk_add_f32 v[88:89], v[102:103], v[46:47]
	v_pk_add_f32 v[48:49], v[62:63], v[110:111]
	v_pk_add_f32 v[102:103], v[104:105], v[48:49]
	v_pk_fma_f32 v[102:103], v[12:13], v[112:113], v[102:103] op_sel_hi:[0,1,1]
	v_pk_fma_f32 v[102:103], v[12:13], v[80:81], v[102:103] op_sel:[1,0,0]
	v_pk_fma_f32 v[102:103], v[14:15], v[88:89], v[102:103] op_sel_hi:[0,1,1]
	v_cndmask_b32_e64 v62, 0, v18, s[10:11]
	v_cndmask_b32_e64 v63, 0, v18, s[14:15]
	v_pk_fma_f32 v[102:103], v[6:7], v[126:127], v[102:103] op_sel_hi:[1,0,1] neg_lo:[0,0,1] neg_hi:[0,0,1]
	s_add_i32 s4, s34, 4
	s_cmpk_lt_i32 s4, 0x201
	s_cselect_b64 s[12:13], s[0:1], 0
	v_pk_add_f32 v[102:103], v[102:103], v[62:63] neg_lo:[0,1] neg_hi:[0,1]
	v_pk_mul_f32 v[104:105], v[102:103], v[102:103]
	v_add_f32_e32 v104, v104, v105
	v_cndmask_b32_e64 v105, 0, v104, s[12:13]
	v_add_f32_e32 v1, v1, v105
	s_add_i32 s5, s34, 9
	s_min_i32 s5, s5, 0x200
	s_mul_i32 s6, s5, 0x804
	s_add_i32 s6, s6, s35
	s_add_i32 s7, s6, 0x505014
	s_add_i32 s8, s6, 0x606018
	s_mul_i32 s9, s5, 0x180c
	s_add_i32 s9, s9, s33
	s_add_i32 s4, s34, 10
	s_min_i32 s4, s4, 0x200
	s_mul_i32 s4, s4, 0x804
	s_add_i32 s4, s4, s38
	buffer_load_dword v2, v28, s[20:23], s4 offen nt
	buffer_load_dwordx3 v[12:14], v27, s[24:27], s9 offen nt
	buffer_load_dword v6, v28, s[16:19], s7 offen nt
	buffer_load_dword v7, v28, s[16:19], s8 offen nt
	s_waitcnt vmcnt(8)
	s_add_i32 s4, s34, 8
	s_cmpk_lt_u32 s4, 0x201
	s_cselect_b64 s[12:13], s[40:41], 0
	v_cmp_eq_u32_e64 s[14:15], s37, v24
	s_and_b64 s[14:15], s[14:15], s[12:13]
	v_cndmask_b32_e64 v29, 0, 1, s[14:15]
	v_mul_f32_e64 v62, v64, v64
	v_mul_f32_e64 v63, v64, v65
	v_mul_f32_e64 v80, v64, v66
	v_mul_f32_e64 v81, v65, v65
	v_mul_f32_e64 v88, v65, v66
	v_mul_f32_e64 v89, v66, v66
	v_or_b32_dpp v102, v29, v29 wave_shr:1 row_mask:0xf bank_mask:0xf bound_ctrl:1
	s_nop 1
	v_or_b32_dpp v102, v29, v102 wave_shl:1 row_mask:0xf bank_mask:0xf bound_ctrl:1
	s_nop 1
	v_or_b32_dpp v103, v102, v102 wave_shr:1 row_mask:0xf bank_mask:0xf bound_ctrl:1
	s_nop 1
	v_or_b32_dpp v103, v102, v103 wave_shl:1 row_mask:0xf bank_mask:0xf bound_ctrl:1
	v_or3_b32 v29, v103, v45, v68
	v_or3_b32 v29, v29, v69, v44
	s_add_i32 s4, s34, 5
	s_cmpk_lt_u32 s4, 0x1ff
	s_cselect_b64 s[12:13], s[42:43], 0
	v_cmp_ne_u32_e64 s[30:31], 0, v29
	s_and_b64 s[30:31], s[30:31], s[12:13]
	v_cndmask_b32_e64 v29, 0, 1.0, s[30:31]
	v_add_f32_dpp v104, v64, v64 wave_shr:1 row_mask:0xf bank_mask:0xf bound_ctrl:1
	v_add_f32_dpp v105, v65, v65 wave_shr:1 row_mask:0xf bank_mask:0xf bound_ctrl:1
	v_add_f32_dpp v112, v66, v66 wave_shr:1 row_mask:0xf bank_mask:0xf bound_ctrl:1
	v_add_f32_dpp v113, v62, v62 wave_shr:1 row_mask:0xf bank_mask:0xf bound_ctrl:1
	v_add_f32_dpp v114, v63, v63 wave_shr:1 row_mask:0xf bank_mask:0xf bound_ctrl:1
	v_add_f32_dpp v115, v80, v80 wave_shr:1 row_mask:0xf bank_mask:0xf bound_ctrl:1
	v_add_f32_dpp v116, v81, v81 wave_shr:1 row_mask:0xf bank_mask:0xf bound_ctrl:1
	v_add_f32_dpp v117, v88, v88 wave_shr:1 row_mask:0xf bank_mask:0xf bound_ctrl:1
	v_add_f32_dpp v118, v89, v89 wave_shr:1 row_mask:0xf bank_mask:0xf bound_ctrl:1
	v_add_f32_dpp v119, v29, v29 wave_shr:1 row_mask:0xf bank_mask:0xf bound_ctrl:1
	v_add_f32_dpp v104, v64, v104 wave_shl:1 row_mask:0xf bank_mask:0xf bound_ctrl:1
	v_add_f32_dpp v105, v65, v105 wave_shl:1 row_mask:0xf bank_mask:0xf bound_ctrl:1
	v_add_f32_dpp v112, v66, v112 wave_shl:1 row_mask:0xf bank_mask:0xf bound_ctrl:1
	v_add_f32_dpp v113, v62, v113 wave_shl:1 row_mask:0xf bank_mask:0xf bound_ctrl:1
	v_add_f32_dpp v114, v63, v114 wave_shl:1 row_mask:0xf bank_mask:0xf bound_ctrl:1
	v_add_f32_dpp v115, v80, v115 wave_shl:1 row_mask:0xf bank_mask:0xf bound_ctrl:1
	v_add_f32_dpp v116, v81, v116 wave_shl:1 row_mask:0xf bank_mask:0xf bound_ctrl:1
	v_add_f32_dpp v117, v88, v117 wave_shl:1 row_mask:0xf bank_mask:0xf bound_ctrl:1
	v_add_f32_dpp v118, v89, v118 wave_shl:1 row_mask:0xf bank_mask:0xf bound_ctrl:1
	v_add_f32_dpp v119, v29, v119 wave_shl:1 row_mask:0xf bank_mask:0xf bound_ctrl:1
	v_pk_add_f32 v[62:63], v[50:51], v[104:105]
	v_pk_add_f32 v[50:51], v[54:55], v[112:113]
	v_pk_add_f32 v[54:55], v[60:61], v[114:115]
	v_pk_add_f32 v[60:61], v[78:79], v[116:117]
	v_pk_add_f32 v[78:79], v[86:87], v[118:119]
	v_mul_f32_e64 v120, v62, v22
	v_mul_f32_e64 v121, v63, v22
	v_mul_f32_e64 v122, v50, v22
	v_fma_f32 v29, v51, v22, v26
	v_mul_f32_e64 v102, v54, v22
	v_mul_f32_e64 v80, v55, v22
	v_fma_f32 v81, v60, v22, v26
	v_mul_f32_e64 v86, v61, v22
	v_fma_f32 v87, v78, v22, v26
	v_fma_f32 v29, -v120, v120, v29
	v_fma_f32 v102, -v120, v121, v102
	v_fma_f32 v80, -v120, v122, v80
	v_fma_f32 v81, -v121, v121, v81
	v_fma_f32 v86, -v121, v122, v86
	v_fma_f32 v87, -v122, v122, v87
	v_mul_f32_e64 v88, v86, v86
	v_mul_f32_e64 v89, v102, v87
	v_mul_f32_e64 v132, v80, v81
	v_mul_f32_e64 v133, v80, v80
	v_mul_f32_e64 v134, v29, v86
	v_mul_f32_e64 v135, v102, v102
	v_fma_f32 v88, v81, v87, -v88
	v_fma_f32 v89, v80, v86, -v89
	v_fma_f32 v132, v102, v86, -v132
	v_fma_f32 v133, v29, v87, -v133
	v_fma_f32 v134, v102, v80, -v134
	v_fma_f32 v135, v29, v81, -v135
	v_mul_f32_e64 v136, v29, v88
	v_fma_f32 v136, v102, v89, v136
	v_fma_f32 v136, v80, v132, v136
	v_rcp_f32_e32 v136, v136
	v_cmp_ne_u32_e64 vcc, s37, v3
	v_mul_f32_e64 v136, v136, v22
	v_cndmask_b32_e64 v136, 0, v136, s[30:31]
	v_cndmask_b32_e64 v29, 0, v18, vcc
	v_cndmask_b32_e64 v129, 0, v22, s[30:31]
	v_mul_f32_e64 v123, v88, v136
	v_mul_f32_e64 v124, v89, v136
	v_mul_f32_e64 v125, v132, v136
	v_mul_f32_e64 v126, v133, v136
	v_mul_f32_e64 v127, v134, v136
	v_mul_f32_e64 v128, v135, v136
	v_add_f32_e64 v130, v79, v29
	v_mov_b32_e32 v131, v3
	ds_write_b128 v23, v[120:123] offset:3072
	ds_write_b128 v23, v[124:127] offset:4096
	ds_write_b128 v23, v[128:131] offset:5120
	s_waitcnt lgkmcnt(0)
	s_barrier
	v_pk_mul_f32 v[50:51], v[56:57], v[64:65] op_sel_hi:[1,0]
	v_pk_mul_f32 v[54:55], v[56:57], v[64:65] op_sel:[0,1]
	v_pk_mul_f32 v[60:61], v[56:57], v[66:67] op_sel_hi:[1,0]
	v_add_f32_dpp v62, v56, v56 wave_shr:1 row_mask:0xf bank_mask:0xf bound_ctrl:1
	v_add_f32_dpp v63, v57, v57 wave_shr:1 row_mask:0xf bank_mask:0xf bound_ctrl:1
	v_add_f32_dpp v78, v50, v50 wave_shr:1 row_mask:0xf bank_mask:0xf bound_ctrl:1
	v_add_f32_dpp v79, v51, v51 wave_shr:1 row_mask:0xf bank_mask:0xf bound_ctrl:1
	v_add_f32_dpp v80, v54, v54 wave_shr:1 row_mask:0xf bank_mask:0xf bound_ctrl:1
	v_add_f32_dpp v81, v55, v55 wave_shr:1 row_mask:0xf bank_mask:0xf bound_ctrl:1
	v_add_f32_dpp v86, v60, v60 wave_shr:1 row_mask:0xf bank_mask:0xf bound_ctrl:1
	v_add_f32_dpp v87, v61, v61 wave_shr:1 row_mask:0xf bank_mask:0xf bound_ctrl:1
	v_add_f32_dpp v62, v56, v62 wave_shl:1 row_mask:0xf bank_mask:0xf bound_ctrl:1
	v_add_f32_dpp v63, v57, v63 wave_shl:1 row_mask:0xf bank_mask:0xf bound_ctrl:1
	v_add_f32_dpp v78, v50, v78 wave_shl:1 row_mask:0xf bank_mask:0xf bound_ctrl:1
	v_add_f32_dpp v79, v51, v79 wave_shl:1 row_mask:0xf bank_mask:0xf bound_ctrl:1
	v_add_f32_dpp v80, v54, v80 wave_shl:1 row_mask:0xf bank_mask:0xf bound_ctrl:1
	v_add_f32_dpp v81, v55, v81 wave_shl:1 row_mask:0xf bank_mask:0xf bound_ctrl:1
	v_add_f32_dpp v86, v60, v86 wave_shl:1 row_mask:0xf bank_mask:0xf bound_ctrl:1
	v_add_f32_dpp v87, v61, v87 wave_shl:1 row_mask:0xf bank_mask:0xf bound_ctrl:1
	v_pk_add_f32 v[50:51], v[30:31], v[62:63]
	v_pk_add_f32 v[30:31], v[58:59], v[78:79]
	v_pk_add_f32 v[54:55], v[76:77], v[80:81]
	v_pk_add_f32 v[58:59], v[82:83], v[86:87]
	v_pk_fma_f32 v[30:31], v[120:121], v[50:51], v[30:31] op_sel_hi:[0,1,1] neg_lo:[1,0,0] neg_hi:[1,0,0]
	v_pk_fma_f32 v[54:55], v[120:121], v[50:51], v[54:55] op_sel:[1,0,0] neg_lo:[1,0,0] neg_hi:[1,0,0]
	v_pk_fma_f32 v[58:59], v[122:123], v[50:51], v[58:59] op_sel_hi:[0,1,1] neg_lo:[1,0,0] neg_hi:[1,0,0]
	v_pk_mul_f32 v[60:61], v[122:123], v[30:31] op_sel:[1,0]
	v_pk_mul_f32 v[76:77], v[124:125], v[30:31] op_sel_hi:[0,1]
	v_pk_mul_f32 v[82:83], v[124:125], v[30:31] op_sel:[1,0]
	v_pk_fma_f32 v[60:61], v[124:125], v[54:55], v[60:61] op_sel_hi:[0,1,1]
	v_pk_fma_f32 v[76:77], v[126:127], v[54:55], v[76:77] op_sel_hi:[0,1,1]
	v_pk_fma_f32 v[82:83], v[126:127], v[54:55], v[82:83] op_sel:[1,0,0]
	v_pk_fma_f32 v[60:61], v[124:125], v[58:59], v[60:61] op_sel:[1,0,0]
	v_pk_fma_f32 v[76:77], v[126:127], v[58:59], v[76:77] op_sel:[1,0,0]
	v_pk_fma_f32 v[82:83], v[128:129], v[58:59], v[82:83] op_sel_hi:[0,1,1]
	v_pk_mul_f32 v[88:89], v[120:121], v[60:61] op_sel_hi:[0,1]
	v_pk_fma_f32 v[88:89], v[120:121], v[76:77], v[88:89] op_sel:[1,0,0]
	v_pk_fma_f32 v[88:89], v[122:123], v[82:83], v[88:89] op_sel_hi:[0,1,1]
	v_pk_fma_f32 v[88:89], v[128:129], v[50:51], v[88:89] op_sel:[1,0,0] neg_lo:[0,0,1] neg_hi:[0,0,1]
	v_cmp_eq_u32_e64 s[10:11], 6, v131
	v_cmp_eq_u32_e64 s[14:15], 7, v131
	v_add_f32_dpp v30, v60, v60 wave_shr:1 row_mask:0xf bank_mask:0xf bound_ctrl:1
	v_add_f32_dpp v31, v61, v61 wave_shr:1 row_mask:0xf bank_mask:0xf bound_ctrl:1
	v_add_f32_dpp v50, v76, v76 wave_shr:1 row_mask:0xf bank_mask:0xf bound_ctrl:1
	v_add_f32_dpp v51, v77, v77 wave_shr:1 row_mask:0xf bank_mask:0xf bound_ctrl:1
	v_add_f32_dpp v54, v82, v82 wave_shr:1 row_mask:0xf bank_mask:0xf bound_ctrl:1
	v_add_f32_dpp v55, v83, v83 wave_shr:1 row_mask:0xf bank_mask:0xf bound_ctrl:1
	v_add_f32_dpp v58, v88, v88 wave_shr:1 row_mask:0xf bank_mask:0xf bound_ctrl:1
	v_add_f32_dpp v59, v89, v89 wave_shr:1 row_mask:0xf bank_mask:0xf bound_ctrl:1
	v_add_f32_dpp v30, v60, v30 wave_shl:1 row_mask:0xf bank_mask:0xf bound_ctrl:1
	v_add_f32_dpp v31, v61, v31 wave_shl:1 row_mask:0xf bank_mask:0xf bound_ctrl:1
	v_add_f32_dpp v50, v76, v50 wave_shl:1 row_mask:0xf bank_mask:0xf bound_ctrl:1
	v_add_f32_dpp v51, v77, v51 wave_shl:1 row_mask:0xf bank_mask:0xf bound_ctrl:1
	v_add_f32_dpp v54, v82, v54 wave_shl:1 row_mask:0xf bank_mask:0xf bound_ctrl:1
	v_add_f32_dpp v55, v83, v55 wave_shl:1 row_mask:0xf bank_mask:0xf bound_ctrl:1
	v_add_f32_dpp v58, v88, v58 wave_shl:1 row_mask:0xf bank_mask:0xf bound_ctrl:1
	v_add_f32_dpp v59, v89, v59 wave_shl:1 row_mask:0xf bank_mask:0xf bound_ctrl:1
	v_pk_add_f32 v[60:61], v[90:91], v[30:31]
	v_pk_add_f32 v[76:77], v[38:39], v[50:51]
	v_pk_add_f32 v[38:39], v[46:47], v[54:55]
	v_pk_add_f32 v[46:47], v[48:49], v[58:59]
	v_pk_fma_f32 v[46:47], v[32:33], v[60:61], v[46:47] op_sel_hi:[0,1,1]
	v_pk_fma_f32 v[46:47], v[32:33], v[76:77], v[46:47] op_sel:[1,0,0]
	v_pk_fma_f32 v[46:47], v[34:35], v[38:39], v[46:47] op_sel_hi:[0,1,1]
	v_cndmask_b32_e64 v48, 0, v18, s[10:11]
	v_cndmask_b32_e64 v49, 0, v18, s[14:15]
	v_pk_fma_f32 v[46:47], v[20:21], v[130:131], v[46:47] op_sel_hi:[1,0,1] neg_lo:[0,0,1] neg_hi:[0,0,1]
	s_add_i32 s4, s34, 5
	s_cmpk_lt_i32 s4, 0x201
	s_cselect_b64 s[12:13], s[0:1], 0
	v_pk_add_f32 v[46:47], v[46:47], v[48:49] neg_lo:[0,1] neg_hi:[0,1]
	v_pk_mul_f32 v[82:83], v[46:47], v[46:47]
	v_add_f32_e32 v82, v82, v83
	v_cndmask_b32_e64 v83, 0, v82, s[12:13]
	v_add_f32_e32 v1, v1, v83
	s_add_i32 s5, s34, 10
	s_min_i32 s5, s5, 0x200
	s_mul_i32 s6, s5, 0x804
	s_add_i32 s6, s6, s35
	s_add_i32 s7, s6, 0x505014
	s_add_i32 s8, s6, 0x606018
	s_mul_i32 s9, s5, 0x180c
	s_add_i32 s9, s9, s33
	s_add_i32 s4, s34, 11
	s_min_i32 s4, s4, 0x200
	s_mul_i32 s4, s4, 0x804
	s_add_i32 s4, s4, s38
	buffer_load_dword v3, v28, s[20:23], s4 offen nt
	buffer_load_dwordx3 v[32:34], v27, s[24:27], s9 offen nt
	buffer_load_dword v20, v28, s[16:19], s7 offen nt
	buffer_load_dword v21, v28, s[16:19], s8 offen nt
	s_waitcnt vmcnt(8)
	s_add_i32 s4, s34, 9
	s_cmpk_lt_u32 s4, 0x201
	s_cselect_b64 s[12:13], s[40:41], 0
	v_cmp_eq_u32_e64 s[14:15], s37, v17
	s_and_b64 s[14:15], s[14:15], s[12:13]
	v_cndmask_b32_e64 v29, 0, 1, s[14:15]
	v_mul_f32_e64 v38, v8, v8
	v_mul_f32_e64 v39, v8, v9
	v_mul_f32_e64 v46, v8, v10
	v_mul_f32_e64 v47, v9, v9
	v_mul_f32_e64 v48, v9, v10
	v_mul_f32_e64 v49, v10, v10
	v_or_b32_dpp v44, v29, v29 wave_shr:1 row_mask:0xf bank_mask:0xf bound_ctrl:1
	s_nop 1
	v_or_b32_dpp v44, v29, v44 wave_shl:1 row_mask:0xf bank_mask:0xf bound_ctrl:1
	s_nop 1
	v_or_b32_dpp v102, v44, v44 wave_shr:1 row_mask:0xf bank_mask:0xf bound_ctrl:1
	s_nop 1
	v_or_b32_dpp v102, v44, v102 wave_shl:1 row_mask:0xf bank_mask:0xf bound_ctrl:1
	v_or3_b32 v29, v102, v103, v45
	v_or3_b32 v29, v29, v68, v69
	s_add_i32 s4, s34, 6
	s_cmpk_lt_u32 s4, 0x1ff
	s_cselect_b64 s[12:13], s[42:43], 0
	v_cmp_ne_u32_e64 s[30:31], 0, v29
	s_and_b64 s[30:31], s[30:31], s[12:13]
	v_cndmask_b32_e64 v29, 0, 1.0, s[30:31]
	v_add_f32_dpp v60, v8, v8 wave_shr:1 row_mask:0xf bank_mask:0xf bound_ctrl:1
	v_add_f32_dpp v61, v9, v9 wave_shr:1 row_mask:0xf bank_mask:0xf bound_ctrl:1
	v_add_f32_dpp v76, v10, v10 wave_shr:1 row_mask:0xf bank_mask:0xf bound_ctrl:1
	v_add_f32_dpp v77, v38, v38 wave_shr:1 row_mask:0xf bank_mask:0xf bound_ctrl:1
	v_add_f32_dpp v82, v39, v39 wave_shr:1 row_mask:0xf bank_mask:0xf bound_ctrl:1
	v_add_f32_dpp v83, v46, v46 wave_shr:1 row_mask:0xf bank_mask:0xf bound_ctrl:1
	v_add_f32_dpp v88, v47, v47 wave_shr:1 row_mask:0xf bank_mask:0xf bound_ctrl:1
	v_add_f32_dpp v89, v48, v48 wave_shr:1 row_mask:0xf bank_mask:0xf bound_ctrl:1
	v_add_f32_dpp v90, v49, v49 wave_shr:1 row_mask:0xf bank_mask:0xf bound_ctrl:1
	v_add_f32_dpp v91, v29, v29 wave_shr:1 row_mask:0xf bank_mask:0xf bound_ctrl:1
	v_add_f32_dpp v60, v8, v60 wave_shl:1 row_mask:0xf bank_mask:0xf bound_ctrl:1
	v_add_f32_dpp v61, v9, v61 wave_shl:1 row_mask:0xf bank_mask:0xf bound_ctrl:1
	v_add_f32_dpp v76, v10, v76 wave_shl:1 row_mask:0xf bank_mask:0xf bound_ctrl:1
	v_add_f32_dpp v77, v38, v77 wave_shl:1 row_mask:0xf bank_mask:0xf bound_ctrl:1
	v_add_f32_dpp v82, v39, v82 wave_shl:1 row_mask:0xf bank_mask:0xf bound_ctrl:1
	v_add_f32_dpp v83, v46, v83 wave_shl:1 row_mask:0xf bank_mask:0xf bound_ctrl:1
	v_add_f32_dpp v88, v47, v88 wave_shl:1 row_mask:0xf bank_mask:0xf bound_ctrl:1
	v_add_f32_dpp v89, v48, v89 wave_shl:1 row_mask:0xf bank_mask:0xf bound_ctrl:1
	v_add_f32_dpp v90, v49, v90 wave_shl:1 row_mask:0xf bank_mask:0xf bound_ctrl:1
	v_add_f32_dpp v91, v29, v91 wave_shl:1 row_mask:0xf bank_mask:0xf bound_ctrl:1
	v_pk_add_f32 v[38:39], v[104:105], v[60:61]
	v_pk_add_f32 v[46:47], v[70:71], v[38:39]
	v_pk_add_f32 v[48:49], v[112:113], v[76:77]
	v_pk_add_f32 v[70:71], v[72:73], v[48:49]
	v_pk_add_f32 v[72:73], v[114:115], v[82:83]
	v_pk_add_f32 v[104:105], v[94:95], v[72:73]
	v_pk_add_f32 v[94:95], v[116:117], v[88:89]
	v_pk_add_f32 v[112:113], v[96:97], v[94:95]
	v_pk_add_f32 v[96:97], v[118:119], v[90:91]
	v_pk_add_f32 v[114:115], v[98:99], v[96:97]
	v_mul_f32_e64 v116, v46, v22
	v_mul_f32_e64 v117, v47, v22
	v_mul_f32_e64 v118, v70, v22
	v_fma_f32 v29, v71, v22, v26
	v_mul_f32_e64 v44, v104, v22
	v_mul_f32_e64 v98, v105, v22
	v_fma_f32 v99, v112, v22, v26
	v_mul_f32_e64 v128, v113, v22
	v_fma_f32 v129, v114, v22, v26
	v_fma_f32 v29, -v116, v116, v29
	v_fma_f32 v44, -v116, v117, v44
	v_fma_f32 v98, -v116, v118, v98
	v_fma_f32 v99, -v117, v117, v99
	v_fma_f32 v128, -v117, v118, v128
	v_fma_f32 v129, -v118, v118, v129
	v_mul_f32_e64 v130, v128, v128
	v_mul_f32_e64 v131, v44, v129
	v_mul_f32_e64 v132, v98, v99
	v_mul_f32_e64 v133, v98, v98
	v_mul_f32_e64 v134, v29, v128
	v_mul_f32_e64 v135, v44, v44
	v_fma_f32 v130, v99, v129, -v130
	v_fma_f32 v131, v98, v128, -v131
	v_fma_f32 v132, v44, v128, -v132
	v_fma_f32 v133, v29, v129, -v133
	v_fma_f32 v134, v44, v98, -v134
	v_fma_f32 v135, v29, v99, -v135
	v_mul_f32_e64 v136, v29, v130
	v_fma_f32 v136, v44, v131, v136
	v_fma_f32 v136, v98, v132, v136
	v_rcp_f32_e32 v136, v136
	v_cmp_ne_u32_e64 vcc, s37, v16
	v_mul_f32_e64 v136, v136, v22
	v_cndmask_b32_e64 v136, 0, v136, s[30:31]
	v_cndmask_b32_e64 v29, 0, v18, vcc
	v_cndmask_b32_e64 v125, 0, v22, s[30:31]
	v_mul_f32_e64 v119, v130, v136
	v_mul_f32_e64 v120, v131, v136
	v_mul_f32_e64 v121, v132, v136
	v_mul_f32_e64 v122, v133, v136
	v_mul_f32_e64 v123, v134, v136
	v_mul_f32_e64 v124, v135, v136
	v_add_f32_e64 v126, v115, v29
	v_mov_b32_e32 v127, v16
	ds_write_b128 v23, v[116:119]
	ds_write_b128 v23, v[120:123] offset:1024
	ds_write_b128 v23, v[124:127] offset:2048
	s_waitcnt lgkmcnt(0)
	s_barrier
	v_pk_mul_f32 v[46:47], v[4:5], v[8:9] op_sel_hi:[1,0]
	v_pk_mul_f32 v[70:71], v[4:5], v[8:9] op_sel:[0,1]
	v_pk_mul_f32 v[98:99], v[4:5], v[10:11] op_sel_hi:[1,0]
	v_add_f32_dpp v104, v4, v4 wave_shr:1 row_mask:0xf bank_mask:0xf bound_ctrl:1
	v_add_f32_dpp v105, v5, v5 wave_shr:1 row_mask:0xf bank_mask:0xf bound_ctrl:1
	v_add_f32_dpp v112, v46, v46 wave_shr:1 row_mask:0xf bank_mask:0xf bound_ctrl:1
	v_add_f32_dpp v113, v47, v47 wave_shr:1 row_mask:0xf bank_mask:0xf bound_ctrl:1
	v_add_f32_dpp v114, v70, v70 wave_shr:1 row_mask:0xf bank_mask:0xf bound_ctrl:1
	v_add_f32_dpp v115, v71, v71 wave_shr:1 row_mask:0xf bank_mask:0xf bound_ctrl:1
	v_add_f32_dpp v128, v98, v98 wave_shr:1 row_mask:0xf bank_mask:0xf bound_ctrl:1
	v_add_f32_dpp v129, v99, v99 wave_shr:1 row_mask:0xf bank_mask:0xf bound_ctrl:1
	v_add_f32_dpp v104, v4, v104 wave_shl:1 row_mask:0xf bank_mask:0xf bound_ctrl:1
	v_add_f32_dpp v105, v5, v105 wave_shl:1 row_mask:0xf bank_mask:0xf bound_ctrl:1
	v_add_f32_dpp v112, v46, v112 wave_shl:1 row_mask:0xf bank_mask:0xf bound_ctrl:1
	v_add_f32_dpp v113, v47, v113 wave_shl:1 row_mask:0xf bank_mask:0xf bound_ctrl:1
	v_add_f32_dpp v114, v70, v114 wave_shl:1 row_mask:0xf bank_mask:0xf bound_ctrl:1
	v_add_f32_dpp v115, v71, v115 wave_shl:1 row_mask:0xf bank_mask:0xf bound_ctrl:1
	v_add_f32_dpp v128, v98, v128 wave_shl:1 row_mask:0xf bank_mask:0xf bound_ctrl:1
	v_add_f32_dpp v129, v99, v129 wave_shl:1 row_mask:0xf bank_mask:0xf bound_ctrl:1
	v_pk_add_f32 v[46:47], v[62:63], v[104:105]
	v_pk_add_f32 v[70:71], v[84:85], v[46:47]
	v_pk_add_f32 v[62:63], v[78:79], v[112:113]
	v_pk_add_f32 v[84:85], v[92:93], v[62:63]
	v_pk_add_f32 v[78:79], v[80:81], v[114:115]
	v_pk_add_f32 v[92:93], v[100:101], v[78:79]
	v_pk_add_f32 v[80:81], v[86:87], v[128:129]
	v_pk_add_f32 v[98:99], v[106:107], v[80:81]
	v_pk_fma_f32 v[84:85], v[116:117], v[70:71], v[84:85] op_sel_hi:[0,1,1] neg_lo:[1,0,0] neg_hi:[1,0,0]
	v_pk_fma_f32 v[92:93], v[116:117], v[70:71], v[92:93] op_sel:[1,0,0] neg_lo:[1,0,0] neg_hi:[1,0,0]
	v_pk_fma_f32 v[98:99], v[118:119], v[70:71], v[98:99] op_sel_hi:[0,1,1] neg_lo:[1,0,0] neg_hi:[1,0,0]
	v_pk_mul_f32 v[86:87], v[118:119], v[84:85] op_sel:[1,0]
	v_pk_mul_f32 v[100:101], v[120:121], v[84:85] op_sel_hi:[0,1]
	v_pk_mul_f32 v[106:107], v[120:121], v[84:85] op_sel:[1,0]
	v_pk_fma_f32 v[86:87], v[120:121], v[92:93], v[86:87] op_sel_hi:[0,1,1]
	v_pk_fma_f32 v[100:101], v[122:123], v[92:93], v[100:101] op_sel_hi:[0,1,1]
	v_pk_fma_f32 v[106:107], v[122:123], v[92:93], v[106:107] op_sel:[1,0,0]
	v_pk_fma_f32 v[86:87], v[120:121], v[98:99], v[86:87] op_sel:[1,0,0]
	v_pk_fma_f32 v[100:101], v[122:123], v[98:99], v[100:101] op_sel:[1,0,0]
	v_pk_fma_f32 v[106:107], v[124:125], v[98:99], v[106:107] op_sel_hi:[0,1,1]
	v_pk_mul_f32 v[130:131], v[116:117], v[86:87] op_sel_hi:[0,1]
	v_pk_fma_f32 v[130:131], v[116:117], v[100:101], v[130:131] op_sel:[1,0,0]
	v_pk_fma_f32 v[130:131], v[118:119], v[106:107], v[130:131] op_sel_hi:[0,1,1]
	v_pk_fma_f32 v[130:131], v[124:125], v[70:71], v[130:131] op_sel:[1,0,0] neg_lo:[0,0,1] neg_hi:[0,0,1]
	v_cmp_eq_u32_e64 s[10:11], 6, v127
	v_cmp_eq_u32_e64 s[14:15], 7, v127
	v_add_f32_dpp v70, v86, v86 wave_shr:1 row_mask:0xf bank_mask:0xf bound_ctrl:1
	v_add_f32_dpp v71, v87, v87 wave_shr:1 row_mask:0xf bank_mask:0xf bound_ctrl:1
	v_add_f32_dpp v84, v100, v100 wave_shr:1 row_mask:0xf bank_mask:0xf bound_ctrl:1
	v_add_f32_dpp v85, v101, v101 wave_shr:1 row_mask:0xf bank_mask:0xf bound_ctrl:1
	v_add_f32_dpp v92, v106, v106 wave_shr:1 row_mask:0xf bank_mask:0xf bound_ctrl:1
	v_add_f32_dpp v93, v107, v107 wave_shr:1 row_mask:0xf bank_mask:0xf bound_ctrl:1
	v_add_f32_dpp v98, v130, v130 wave_shr:1 row_mask:0xf bank_mask:0xf bound_ctrl:1
	v_add_f32_dpp v99, v131, v131 wave_shr:1 row_mask:0xf bank_mask:0xf bound_ctrl:1
	v_add_f32_dpp v70, v86, v70 wave_shl:1 row_mask:0xf bank_mask:0xf bound_ctrl:1
	v_add_f32_dpp v71, v87, v71 wave_shl:1 row_mask:0xf bank_mask:0xf bound_ctrl:1
	v_add_f32_dpp v84, v100, v84 wave_shl:1 row_mask:0xf bank_mask:0xf bound_ctrl:1
	v_add_f32_dpp v85, v101, v85 wave_shl:1 row_mask:0xf bank_mask:0xf bound_ctrl:1
	v_add_f32_dpp v92, v106, v92 wave_shl:1 row_mask:0xf bank_mask:0xf bound_ctrl:1
	v_add_f32_dpp v93, v107, v93 wave_shl:1 row_mask:0xf bank_mask:0xf bound_ctrl:1
	v_add_f32_dpp v98, v130, v98 wave_shl:1 row_mask:0xf bank_mask:0xf bound_ctrl:1
	v_add_f32_dpp v99, v131, v99 wave_shl:1 row_mask:0xf bank_mask:0xf bound_ctrl:1
	v_pk_add_f32 v[86:87], v[30:31], v[70:71]
	v_pk_add_f32 v[100:101], v[52:53], v[86:87]
	v_pk_add_f32 v[30:31], v[50:51], v[84:85]
	v_pk_add_f32 v[52:53], v[74:75], v[30:31]
	v_pk_add_f32 v[50:51], v[54:55], v[92:93]
	v_pk_add_f32 v[74:75], v[108:109], v[50:51]
	v_pk_add_f32 v[54:55], v[58:59], v[98:99]
	v_pk_add_f32 v[106:107], v[110:111], v[54:55]
	v_pk_fma_f32 v[106:107], v[40:41], v[100:101], v[106:107] op_sel_hi:[0,1,1]
	v_pk_fma_f32 v[106:107], v[40:41], v[52:53], v[106:107] op_sel:[1,0,0]
	v_pk_fma_f32 v[106:107], v[42:43], v[74:75], v[106:107] op_sel_hi:[0,1,1]
	v_cndmask_b32_e64 v58, 0, v18, s[10:11]
	v_cndmask_b32_e64 v59, 0, v18, s[14:15]
	v_pk_fma_f32 v[106:107], v[36:37], v[126:127], v[106:107] op_sel_hi:[1,0,1] neg_lo:[0,0,1] neg_hi:[0,0,1]
	s_add_i32 s4, s34, 6
	s_cmpk_lt_i32 s4, 0x201
	s_cselect_b64 s[12:13], s[0:1], 0
	v_pk_add_f32 v[106:107], v[106:107], v[58:59] neg_lo:[0,1] neg_hi:[0,1]
	v_pk_mul_f32 v[108:109], v[106:107], v[106:107]
	v_add_f32_e32 v108, v108, v109
	v_cndmask_b32_e64 v109, 0, v108, s[12:13]
	v_add_f32_e32 v1, v1, v109
	s_add_i32 s5, s34, 11
	s_min_i32 s5, s5, 0x200
	s_mul_i32 s6, s5, 0x804
	s_add_i32 s6, s6, s35
	s_add_i32 s7, s6, 0x505014
	s_add_i32 s8, s6, 0x606018
	s_mul_i32 s9, s5, 0x180c
	s_add_i32 s9, s9, s33
	s_add_i32 s4, s34, 12
	s_min_i32 s4, s4, 0x200
	s_mul_i32 s4, s4, 0x804
	s_add_i32 s4, s4, s38
	buffer_load_dword v16, v28, s[20:23], s4 offen nt
	buffer_load_dwordx3 v[40:42], v27, s[24:27], s9 offen nt
	buffer_load_dword v36, v28, s[16:19], s7 offen nt
	buffer_load_dword v37, v28, s[16:19], s8 offen nt
	s_waitcnt vmcnt(8)
	s_add_i32 s4, s34, 10
	s_cmpk_lt_u32 s4, 0x201
	s_cselect_b64 s[12:13], s[40:41], 0
	v_cmp_eq_u32_e64 s[14:15], s37, v2
	s_and_b64 s[14:15], s[14:15], s[12:13]
	v_cndmask_b32_e64 v29, 0, 1, s[14:15]
	v_mul_f32_e64 v52, v12, v12
	v_mul_f32_e64 v53, v12, v13
	v_mul_f32_e64 v58, v12, v14
	v_mul_f32_e64 v59, v13, v13
	v_mul_f32_e64 v74, v13, v14
	v_mul_f32_e64 v75, v14, v14
	v_or_b32_dpp v44, v29, v29 wave_shr:1 row_mask:0xf bank_mask:0xf bound_ctrl:1
	s_nop 1
	v_or_b32_dpp v44, v29, v44 wave_shl:1 row_mask:0xf bank_mask:0xf bound_ctrl:1
	s_nop 1
	v_or_b32_dpp v69, v44, v44 wave_shr:1 row_mask:0xf bank_mask:0xf bound_ctrl:1
	s_nop 1
	v_or_b32_dpp v69, v44, v69 wave_shl:1 row_mask:0xf bank_mask:0xf bound_ctrl:1
	v_or3_b32 v29, v69, v102, v103
	v_or3_b32 v29, v29, v45, v68
	s_add_i32 s4, s34, 7
	s_cmpk_lt_u32 s4, 0x1ff
	s_cselect_b64 s[12:13], s[42:43], 0
	v_cmp_ne_u32_e64 s[30:31], 0, v29
	s_and_b64 s[30:31], s[30:31], s[12:13]
	v_cndmask_b32_e64 v29, 0, 1.0, s[30:31]
	v_add_f32_dpp v100, v12, v12 wave_shr:1 row_mask:0xf bank_mask:0xf bound_ctrl:1
	v_add_f32_dpp v101, v13, v13 wave_shr:1 row_mask:0xf bank_mask:0xf bound_ctrl:1
	v_add_f32_dpp v106, v14, v14 wave_shr:1 row_mask:0xf bank_mask:0xf bound_ctrl:1
	v_add_f32_dpp v107, v52, v52 wave_shr:1 row_mask:0xf bank_mask:0xf bound_ctrl:1
	v_add_f32_dpp v108, v53, v53 wave_shr:1 row_mask:0xf bank_mask:0xf bound_ctrl:1
	v_add_f32_dpp v109, v58, v58 wave_shr:1 row_mask:0xf bank_mask:0xf bound_ctrl:1
	v_add_f32_dpp v110, v59, v59 wave_shr:1 row_mask:0xf bank_mask:0xf bound_ctrl:1
	v_add_f32_dpp v111, v74, v74 wave_shr:1 row_mask:0xf bank_mask:0xf bound_ctrl:1
	v_add_f32_dpp v116, v75, v75 wave_shr:1 row_mask:0xf bank_mask:0xf bound_ctrl:1
	v_add_f32_dpp v117, v29, v29 wave_shr:1 row_mask:0xf bank_mask:0xf bound_ctrl:1
	v_add_f32_dpp v100, v12, v100 wave_shl:1 row_mask:0xf bank_mask:0xf bound_ctrl:1
	v_add_f32_dpp v101, v13, v101 wave_shl:1 row_mask:0xf bank_mask:0xf bound_ctrl:1
	v_add_f32_dpp v106, v14, v106 wave_shl:1 row_mask:0xf bank_mask:0xf bound_ctrl:1
	v_add_f32_dpp v107, v52, v107 wave_shl:1 row_mask:0xf bank_mask:0xf bound_ctrl:1
	v_add_f32_dpp v108, v53, v108 wave_shl:1 row_mask:0xf bank_mask:0xf bound_ctrl:1
	v_add_f32_dpp v109, v58, v109 wave_shl:1 row_mask:0xf bank_mask:0xf bound_ctrl:1
	v_add_f32_dpp v110, v59, v110 wave_shl:1 row_mask:0xf bank_mask:0xf bound_ctrl:1
	v_add_f32_dpp v111, v74, v111 wave_shl:1 row_mask:0xf bank_mask:0xf bound_ctrl:1
	v_add_f32_dpp v116, v75, v116 wave_shl:1 row_mask:0xf bank_mask:0xf bound_ctrl:1
	v_add_f32_dpp v117, v29, v117 wave_shl:1 row_mask:0xf bank_mask:0xf bound_ctrl:1
	v_pk_add_f32 v[52:53], v[38:39], v[100:101]
	v_pk_add_f32 v[38:39], v[48:49], v[106:107]
	v_pk_add_f32 v[48:49], v[72:73], v[108:109]
	v_pk_add_f32 v[58:59], v[94:95], v[110:111]
	v_pk_add_f32 v[72:73], v[96:97], v[116:117]
	v_mul_f32_e64 v120, v52, v22
	v_mul_f32_e64 v121, v53, v22
	v_mul_f32_e64 v122, v38, v22
	v_fma_f32 v29, v39, v22, v26
	v_mul_f32_e64 v44, v48, v22
	v_mul_f32_e64 v74, v49, v22
	v_fma_f32 v75, v58, v22, v26
	v_mul_f32_e64 v94, v59, v22
	v_fma_f32 v95, v72, v22, v26
	v_fma_f32 v29, -v120, v120, v29
	v_fma_f32 v44, -v120, v121, v44
	v_fma_f32 v74, -v120, v122, v74
	v_fma_f32 v75, -v121, v121, v75
	v_fma_f32 v94, -v121, v122, v94
	v_fma_f32 v95, -v122, v122, v95
	v_mul_f32_e64 v96, v94, v94
	v_mul_f32_e64 v97, v44, v95
	v_mul_f32_e64 v118, v74, v75
	v_mul_f32_e64 v119, v74, v74
	v_mul_f32_e64 v130, v29, v94
	v_mul_f32_e64 v131, v44, v44
	v_fma_f32 v96, v75, v95, -v96
	v_fma_f32 v97, v74, v94, -v97
	v_fma_f32 v118, v44, v94, -v118
	v_fma_f32 v119, v29, v95, -v119
	v_fma_f32 v130, v44, v74, -v130
	v_fma_f32 v131, v29, v75, -v131
	v_mul_f32_e64 v136, v29, v96
	v_fma_f32 v136, v44, v97, v136
	v_fma_f32 v136, v74, v118, v136
	v_rcp_f32_e32 v136, v136
	v_cmp_ne_u32_e64 vcc, s37, v25
	v_mul_f32_e64 v136, v136, v22
	v_cndmask_b32_e64 v136, 0, v136, s[30:31]
	v_cndmask_b32_e64 v29, 0, v18, vcc
	v_cndmask_b32_e64 v133, 0, v22, s[30:31]
	v_mul_f32_e64 v123, v96, v136
	v_mul_f32_e64 v124, v97, v136
	v_mul_f32_e64 v125, v118, v136
	v_mul_f32_e64 v126, v119, v136
	v_mul_f32_e64 v127, v130, v136
	v_mul_f32_e64 v132, v131, v136
	v_add_f32_e64 v134, v73, v29
	v_mov_b32_e32 v135, v25
	ds_write_b128 v23, v[120:123] offset:3072
	ds_write_b128 v23, v[124:127] offset:4096
	ds_write_b128 v23, v[132:135] offset:5120
	s_waitcnt lgkmcnt(0)
	s_barrier
	v_pk_mul_f32 v[38:39], v[6:7], v[12:13] op_sel_hi:[1,0]
	v_pk_mul_f32 v[48:49], v[6:7], v[12:13] op_sel:[0,1]
	v_pk_mul_f32 v[52:53], v[6:7], v[14:15] op_sel_hi:[1,0]
	v_add_f32_dpp v58, v6, v6 wave_shr:1 row_mask:0xf bank_mask:0xf bound_ctrl:1
	v_add_f32_dpp v59, v7, v7 wave_shr:1 row_mask:0xf bank_mask:0xf bound_ctrl:1
	v_add_f32_dpp v72, v38, v38 wave_shr:1 row_mask:0xf bank_mask:0xf bound_ctrl:1
	v_add_f32_dpp v73, v39, v39 wave_shr:1 row_mask:0xf bank_mask:0xf bound_ctrl:1
	v_add_f32_dpp v74, v48, v48 wave_shr:1 row_mask:0xf bank_mask:0xf bound_ctrl:1
	v_add_f32_dpp v75, v49, v49 wave_shr:1 row_mask:0xf bank_mask:0xf bound_ctrl:1
	v_add_f32_dpp v94, v52, v52 wave_shr:1 row_mask:0xf bank_mask:0xf bound_ctrl:1
	v_add_f32_dpp v95, v53, v53 wave_shr:1 row_mask:0xf bank_mask:0xf bound_ctrl:1
	v_add_f32_dpp v58, v6, v58 wave_shl:1 row_mask:0xf bank_mask:0xf bound_ctrl:1
	v_add_f32_dpp v59, v7, v59 wave_shl:1 row_mask:0xf bank_mask:0xf bound_ctrl:1
	v_add_f32_dpp v72, v38, v72 wave_shl:1 row_mask:0xf bank_mask:0xf bound_ctrl:1
	v_add_f32_dpp v73, v39, v73 wave_shl:1 row_mask:0xf bank_mask:0xf bound_ctrl:1
	v_add_f32_dpp v74, v48, v74 wave_shl:1 row_mask:0xf bank_mask:0xf bound_ctrl:1
	v_add_f32_dpp v75, v49, v75 wave_shl:1 row_mask:0xf bank_mask:0xf bound_ctrl:1
	v_add_f32_dpp v94, v52, v94 wave_shl:1 row_mask:0xf bank_mask:0xf bound_ctrl:1
	v_add_f32_dpp v95, v53, v95 wave_shl:1 row_mask:0xf bank_mask:0xf bound_ctrl:1
	v_pk_add_f32 v[38:39], v[46:47], v[58:59]
	v_pk_add_f32 v[46:47], v[62:63], v[72:73]
	v_pk_add_f32 v[48:49], v[78:79], v[74:75]
	v_pk_add_f32 v[52:53], v[80:81], v[94:95]
	v_pk_fma_f32 v[46:47], v[120:121], v[38:39], v[46:47] op_sel_hi:[0,1,1] neg_lo:[1,0,0] neg_hi:[1,0,0]
	v_pk_fma_f32 v[48:49], v[120:121], v[38:39], v[48:49] op_sel:[1,0,0] neg_lo:[1,0,0] neg_hi:[1,0,0]
	v_pk_fma_f32 v[52:53], v[122:123], v[38:39], v[52:53] op_sel_hi:[0,1,1] neg_lo:[1,0,0] neg_hi:[1,0,0]
	v_pk_mul_f32 v[62:63], v[122:123], v[46:47] op_sel:[1,0]
	v_pk_mul_f32 v[78:79], v[124:125], v[46:47] op_sel_hi:[0,1]
	v_pk_mul_f32 v[80:81], v[124:125], v[46:47] op_sel:[1,0]
	v_pk_fma_f32 v[62:63], v[124:125], v[48:49], v[62:63] op_sel_hi:[0,1,1]
	v_pk_fma_f32 v[78:79], v[126:127], v[48:49], v[78:79] op_sel_hi:[0,1,1]
	v_pk_fma_f32 v[80:81], v[126:127], v[48:49], v[80:81] op_sel:[1,0,0]
	v_pk_fma_f32 v[62:63], v[124:125], v[52:53], v[62:63] op_sel:[1,0,0]
	v_pk_fma_f32 v[78:79], v[126:127], v[52:53], v[78:79] op_sel:[1,0,0]
	v_pk_fma_f32 v[80:81], v[132:133], v[52:53], v[80:81] op_sel_hi:[0,1,1]
	v_pk_mul_f32 v[96:97], v[120:121], v[62:63] op_sel_hi:[0,1]
	v_pk_fma_f32 v[96:97], v[120:121], v[78:79], v[96:97] op_sel:[1,0,0]
	v_pk_fma_f32 v[96:97], v[122:123], v[80:81], v[96:97] op_sel_hi:[0,1,1]
	v_pk_fma_f32 v[96:97], v[132:133], v[38:39], v[96:97] op_sel:[1,0,0] neg_lo:[0,0,1] neg_hi:[0,0,1]
	v_cmp_eq_u32_e64 s[10:11], 6, v135
	v_cmp_eq_u32_e64 s[14:15], 7, v135
	v_add_f32_dpp v38, v62, v62 wave_shr:1 row_mask:0xf bank_mask:0xf bound_ctrl:1
	v_add_f32_dpp v39, v63, v63 wave_shr:1 row_mask:0xf bank_mask:0xf bound_ctrl:1
	v_add_f32_dpp v46, v78, v78 wave_shr:1 row_mask:0xf bank_mask:0xf bound_ctrl:1
	v_add_f32_dpp v47, v79, v79 wave_shr:1 row_mask:0xf bank_mask:0xf bound_ctrl:1
	v_add_f32_dpp v48, v80, v80 wave_shr:1 row_mask:0xf bank_mask:0xf bound_ctrl:1
	v_add_f32_dpp v49, v81, v81 wave_shr:1 row_mask:0xf bank_mask:0xf bound_ctrl:1
	v_add_f32_dpp v52, v96, v96 wave_shr:1 row_mask:0xf bank_mask:0xf bound_ctrl:1
	v_add_f32_dpp v53, v97, v97 wave_shr:1 row_mask:0xf bank_mask:0xf bound_ctrl:1
	v_add_f32_dpp v38, v62, v38 wave_shl:1 row_mask:0xf bank_mask:0xf bound_ctrl:1
	v_add_f32_dpp v39, v63, v39 wave_shl:1 row_mask:0xf bank_mask:0xf bound_ctrl:1
	v_add_f32_dpp v46, v78, v46 wave_shl:1 row_mask:0xf bank_mask:0xf bound_ctrl:1
	v_add_f32_dpp v47, v79, v47 wave_shl:1 row_mask:0xf bank_mask:0xf bound_ctrl:1
	v_add_f32_dpp v48, v80, v48 wave_shl:1 row_mask:0xf bank_mask:0xf bound_ctrl:1
	v_add_f32_dpp v49, v81, v49 wave_shl:1 row_mask:0xf bank_mask:0xf bound_ctrl:1
	v_add_f32_dpp v52, v96, v52 wave_shl:1 row_mask:0xf bank_mask:0xf bound_ctrl:1
	v_add_f32_dpp v53, v97, v53 wave_shl:1 row_mask:0xf bank_mask:0xf bound_ctrl:1
	v_pk_add_f32 v[62:63], v[86:87], v[38:39]
	v_pk_add_f32 v[78:79], v[30:31], v[46:47]
	v_pk_add_f32 v[30:31], v[50:51], v[48:49]
	v_pk_add_f32 v[50:51], v[54:55], v[52:53]
	v_pk_fma_f32 v[50:51], v[64:65], v[62:63], v[50:51] op_sel_hi:[0,1,1]
	v_pk_fma_f32 v[50:51], v[64:65], v[78:79], v[50:51] op_sel:[1,0,0]
	v_pk_fma_f32 v[50:51], v[66:67], v[30:31], v[50:51] op_sel_hi:[0,1,1]
	v_cndmask_b32_e64 v54, 0, v18, s[10:11]
	v_cndmask_b32_e64 v55, 0, v18, s[14:15]
	v_pk_fma_f32 v[50:51], v[56:57], v[134:135], v[50:51] op_sel_hi:[1,0,1] neg_lo:[0,0,1] neg_hi:[0,0,1]
	s_add_i32 s4, s34, 7
	s_cmpk_lt_i32 s4, 0x201
	s_cselect_b64 s[12:13], s[0:1], 0
	v_pk_add_f32 v[50:51], v[50:51], v[54:55] neg_lo:[0,1] neg_hi:[0,1]
	v_pk_mul_f32 v[80:81], v[50:51], v[50:51]
	v_add_f32_e32 v80, v80, v81
	v_cndmask_b32_e64 v81, 0, v80, s[12:13]
	v_add_f32_e32 v1, v1, v81
	s_waitcnt vmcnt(4)
	s_add_i32 s4, s34, 11
	s_cmpk_lt_u32 s4, 0x201
	s_cselect_b64 s[12:13], s[40:41], 0
	v_cmp_eq_u32_e64 s[14:15], s37, v3
	s_and_b64 s[14:15], s[14:15], s[12:13]
	v_cndmask_b32_e64 v25, 0, 1, s[14:15]
	v_mul_f32_e64 v30, v32, v32
	v_mul_f32_e64 v31, v32, v33
	v_mul_f32_e64 v50, v32, v34
	v_mul_f32_e64 v51, v33, v33
	v_mul_f32_e64 v54, v33, v34
	v_mul_f32_e64 v55, v34, v34
	v_or_b32_dpp v29, v25, v25 wave_shr:1 row_mask:0xf bank_mask:0xf bound_ctrl:1
	s_nop 1
	v_or_b32_dpp v29, v25, v29 wave_shl:1 row_mask:0xf bank_mask:0xf bound_ctrl:1
	s_nop 1
	v_or_b32_dpp v44, v29, v29 wave_shr:1 row_mask:0xf bank_mask:0xf bound_ctrl:1
	s_nop 1
	v_or_b32_dpp v44, v29, v44 wave_shl:1 row_mask:0xf bank_mask:0xf bound_ctrl:1
	v_or3_b32 v25, v44, v69, v102
	v_or3_b32 v25, v25, v103, v45
	s_add_i32 s4, s34, 8
	s_cmpk_lt_u32 s4, 0x1ff
	s_cselect_b64 s[12:13], s[42:43], 0
	v_cmp_ne_u32_e64 s[30:31], 0, v25
	s_and_b64 s[30:31], s[30:31], s[12:13]
	v_cndmask_b32_e64 v25, 0, 1.0, s[30:31]
	v_add_f32_dpp v56, v32, v32 wave_shr:1 row_mask:0xf bank_mask:0xf bound_ctrl:1
	v_add_f32_dpp v57, v33, v33 wave_shr:1 row_mask:0xf bank_mask:0xf bound_ctrl:1
	v_add_f32_dpp v62, v34, v34 wave_shr:1 row_mask:0xf bank_mask:0xf bound_ctrl:1
	v_add_f32_dpp v63, v30, v30 wave_shr:1 row_mask:0xf bank_mask:0xf bound_ctrl:1
	v_add_f32_dpp v64, v31, v31 wave_shr:1 row_mask:0xf bank_mask:0xf bound_ctrl:1
	v_add_f32_dpp v65, v50, v50 wave_shr:1 row_mask:0xf bank_mask:0xf bound_ctrl:1
	v_add_f32_dpp v66, v51, v51 wave_shr:1 row_mask:0xf bank_mask:0xf bound_ctrl:1
	v_add_f32_dpp v67, v54, v54 wave_shr:1 row_mask:0xf bank_mask:0xf bound_ctrl:1
	v_add_f32_dpp v78, v55, v55 wave_shr:1 row_mask:0xf bank_mask:0xf bound_ctrl:1
	v_add_f32_dpp v79, v25, v25 wave_shr:1 row_mask:0xf bank_mask:0xf bound_ctrl:1
	v_add_f32_dpp v56, v32, v56 wave_shl:1 row_mask:0xf bank_mask:0xf bound_ctrl:1
	v_add_f32_dpp v57, v33, v57 wave_shl:1 row_mask:0xf bank_mask:0xf bound_ctrl:1
	v_add_f32_dpp v62, v34, v62 wave_shl:1 row_mask:0xf bank_mask:0xf bound_ctrl:1
	v_add_f32_dpp v63, v30, v63 wave_shl:1 row_mask:0xf bank_mask:0xf bound_ctrl:1
	v_add_f32_dpp v64, v31, v64 wave_shl:1 row_mask:0xf bank_mask:0xf bound_ctrl:1
	v_add_f32_dpp v65, v50, v65 wave_shl:1 row_mask:0xf bank_mask:0xf bound_ctrl:1
	v_add_f32_dpp v66, v51, v66 wave_shl:1 row_mask:0xf bank_mask:0xf bound_ctrl:1
	v_add_f32_dpp v67, v54, v67 wave_shl:1 row_mask:0xf bank_mask:0xf bound_ctrl:1
	v_add_f32_dpp v78, v55, v78 wave_shl:1 row_mask:0xf bank_mask:0xf bound_ctrl:1
	v_add_f32_dpp v79, v25, v79 wave_shl:1 row_mask:0xf bank_mask:0xf bound_ctrl:1
	v_pk_add_f32 v[30:31], v[100:101], v[56:57]
	v_pk_add_f32 v[50:51], v[60:61], v[30:31]
	v_pk_add_f32 v[54:55], v[106:107], v[62:63]
	v_pk_add_f32 v[60:61], v[76:77], v[54:55]
	v_pk_add_f32 v[76:77], v[108:109], v[64:65]
	v_pk_add_f32 v[80:81], v[82:83], v[76:77]
	v_pk_add_f32 v[82:83], v[110:111], v[66:67]
	v_pk_add_f32 v[86:87], v[88:89], v[82:83]
	v_pk_add_f32 v[88:89], v[116:117], v[78:79]
	v_pk_add_f32 v[96:97], v[90:91], v[88:89]
	v_mul_f32_e64 v108, v50, v22
	v_mul_f32_e64 v109, v51, v22
	v_mul_f32_e64 v110, v60, v22
	v_fma_f32 v25, v61, v22, v26
	v_mul_f32_e64 v29, v80, v22
	v_mul_f32_e64 v68, v81, v22
	v_fma_f32 v90, v86, v22, v26
	v_mul_f32_e64 v91, v87, v22
	v_fma_f32 v100, v96, v22, v26
	v_fma_f32 v25, -v108, v108, v25
	v_fma_f32 v29, -v108, v109, v29
	v_fma_f32 v68, -v108, v110, v68
	v_fma_f32 v90, -v109, v109, v90
	v_fma_f32 v91, -v109, v110, v91
	v_fma_f32 v100, -v110, v110, v100
	v_mul_f32_e64 v101, v91, v91
	v_mul_f32_e64 v106, v29, v100
	v_mul_f32_e64 v107, v68, v90
	v_mul_f32_e64 v124, v68, v68
	v_mul_f32_e64 v125, v25, v91
	v_mul_f32_e64 v126, v29, v29
	v_fma_f32 v101, v90, v100, -v101
	v_fma_f32 v106, v68, v91, -v106
	v_fma_f32 v107, v29, v91, -v107
	v_fma_f32 v124, v25, v100, -v124
	v_fma_f32 v125, v29, v68, -v125
	v_fma_f32 v126, v25, v90, -v126
	v_mul_f32_e64 v127, v25, v101
	v_fma_f32 v127, v29, v106, v127
	v_fma_f32 v127, v68, v107, v127
	v_rcp_f32_e32 v127, v127
	v_cmp_ne_u32_e64 vcc, s37, v24
	v_mul_f32_e64 v127, v127, v22
	v_cndmask_b32_e64 v127, 0, v127, s[30:31]
	v_cndmask_b32_e64 v25, 0, v18, vcc
	v_cndmask_b32_e64 v121, 0, v22, s[30:31]
	v_mul_f32_e64 v111, v101, v127
	v_mul_f32_e64 v116, v106, v127
	v_mul_f32_e64 v117, v107, v127
	v_mul_f32_e64 v118, v124, v127
	v_mul_f32_e64 v119, v125, v127
	v_mul_f32_e64 v120, v126, v127
	v_add_f32_e64 v122, v97, v25
	v_mov_b32_e32 v123, v24
	ds_write_b128 v23, v[108:111]
	ds_write_b128 v23, v[116:119] offset:1024
	ds_write_b128 v23, v[120:123] offset:2048
	s_waitcnt lgkmcnt(0)
	s_barrier
	v_pk_mul_f32 v[24:25], v[20:21], v[32:33] op_sel_hi:[1,0]
	v_pk_mul_f32 v[50:51], v[20:21], v[32:33] op_sel:[0,1]
	v_pk_mul_f32 v[60:61], v[20:21], v[34:35] op_sel_hi:[1,0]
	v_add_f32_dpp v80, v20, v20 wave_shr:1 row_mask:0xf bank_mask:0xf bound_ctrl:1
	v_add_f32_dpp v81, v21, v21 wave_shr:1 row_mask:0xf bank_mask:0xf bound_ctrl:1
	v_add_f32_dpp v86, v24, v24 wave_shr:1 row_mask:0xf bank_mask:0xf bound_ctrl:1
	v_add_f32_dpp v87, v25, v25 wave_shr:1 row_mask:0xf bank_mask:0xf bound_ctrl:1
	v_add_f32_dpp v90, v50, v50 wave_shr:1 row_mask:0xf bank_mask:0xf bound_ctrl:1
	v_add_f32_dpp v91, v51, v51 wave_shr:1 row_mask:0xf bank_mask:0xf bound_ctrl:1
	v_add_f32_dpp v96, v60, v60 wave_shr:1 row_mask:0xf bank_mask:0xf bound_ctrl:1
	v_add_f32_dpp v97, v61, v61 wave_shr:1 row_mask:0xf bank_mask:0xf bound_ctrl:1
	v_add_f32_dpp v80, v20, v80 wave_shl:1 row_mask:0xf bank_mask:0xf bound_ctrl:1
	v_add_f32_dpp v81, v21, v81 wave_shl:1 row_mask:0xf bank_mask:0xf bound_ctrl:1
	v_add_f32_dpp v86, v24, v86 wave_shl:1 row_mask:0xf bank_mask:0xf bound_ctrl:1
	v_add_f32_dpp v87, v25, v87 wave_shl:1 row_mask:0xf bank_mask:0xf bound_ctrl:1
	v_add_f32_dpp v90, v50, v90 wave_shl:1 row_mask:0xf bank_mask:0xf bound_ctrl:1
	v_add_f32_dpp v91, v51, v91 wave_shl:1 row_mask:0xf bank_mask:0xf bound_ctrl:1
	v_add_f32_dpp v96, v60, v96 wave_shl:1 row_mask:0xf bank_mask:0xf bound_ctrl:1
	v_add_f32_dpp v97, v61, v97 wave_shl:1 row_mask:0xf bank_mask:0xf bound_ctrl:1
	v_pk_add_f32 v[24:25], v[58:59], v[80:81]
	v_pk_add_f32 v[50:51], v[104:105], v[24:25]
	v_pk_add_f32 v[58:59], v[72:73], v[86:87]
	v_pk_add_f32 v[60:61], v[112:113], v[58:59]
	v_pk_add_f32 v[72:73], v[74:75], v[90:91]
	v_pk_add_f32 v[100:101], v[114:115], v[72:73]
	v_pk_add_f32 v[74:75], v[94:95], v[96:97]
	v_pk_add_f32 v[104:105], v[128:129], v[74:75]
	v_pk_fma_f32 v[60:61], v[108:109], v[50:51], v[60:61] op_sel_hi:[0,1,1] neg_lo:[1,0,0] neg_hi:[1,0,0]
	v_pk_fma_f32 v[100:101], v[108:109], v[50:51], v[100:101] op_sel:[1,0,0] neg_lo:[1,0,0] neg_hi:[1,0,0]
	v_pk_fma_f32 v[104:105], v[110:111], v[50:51], v[104:105] op_sel_hi:[0,1,1] neg_lo:[1,0,0] neg_hi:[1,0,0]
	v_pk_mul_f32 v[94:95], v[110:111], v[60:61] op_sel:[1,0]
	v_pk_mul_f32 v[106:107], v[116:117], v[60:61] op_sel_hi:[0,1]
	v_pk_mul_f32 v[112:113], v[116:117], v[60:61] op_sel:[1,0]
	v_pk_fma_f32 v[94:95], v[116:117], v[100:101], v[94:95] op_sel_hi:[0,1,1]
	v_pk_fma_f32 v[106:107], v[118:119], v[100:101], v[106:107] op_sel_hi:[0,1,1]
	v_pk_fma_f32 v[112:113], v[118:119], v[100:101], v[112:113] op_sel:[1,0,0]
	v_pk_fma_f32 v[94:95], v[116:117], v[104:105], v[94:95] op_sel:[1,0,0]
	v_pk_fma_f32 v[106:107], v[118:119], v[104:105], v[106:107] op_sel:[1,0,0]
	v_pk_fma_f32 v[112:113], v[120:121], v[104:105], v[112:113] op_sel_hi:[0,1,1]
	v_pk_mul_f32 v[114:115], v[108:109], v[94:95] op_sel_hi:[0,1]
	v_pk_fma_f32 v[114:115], v[108:109], v[106:107], v[114:115] op_sel:[1,0,0]
	v_pk_fma_f32 v[114:115], v[110:111], v[112:113], v[114:115] op_sel_hi:[0,1,1]
	v_pk_fma_f32 v[114:115], v[120:121], v[50:51], v[114:115] op_sel:[1,0,0] neg_lo:[0,0,1] neg_hi:[0,0,1]
	v_cmp_eq_u32_e64 s[10:11], 6, v123
	v_cmp_eq_u32_e64 s[14:15], 7, v123
	v_add_f32_dpp v50, v94, v94 wave_shr:1 row_mask:0xf bank_mask:0xf bound_ctrl:1
	v_add_f32_dpp v51, v95, v95 wave_shr:1 row_mask:0xf bank_mask:0xf bound_ctrl:1
	v_add_f32_dpp v60, v106, v106 wave_shr:1 row_mask:0xf bank_mask:0xf bound_ctrl:1
	v_add_f32_dpp v61, v107, v107 wave_shr:1 row_mask:0xf bank_mask:0xf bound_ctrl:1
	v_add_f32_dpp v100, v112, v112 wave_shr:1 row_mask:0xf bank_mask:0xf bound_ctrl:1
	v_add_f32_dpp v101, v113, v113 wave_shr:1 row_mask:0xf bank_mask:0xf bound_ctrl:1
	v_add_f32_dpp v104, v114, v114 wave_shr:1 row_mask:0xf bank_mask:0xf bound_ctrl:1
	v_add_f32_dpp v105, v115, v115 wave_shr:1 row_mask:0xf bank_mask:0xf bound_ctrl:1
	v_add_f32_dpp v50, v94, v50 wave_shl:1 row_mask:0xf bank_mask:0xf bound_ctrl:1
	v_add_f32_dpp v51, v95, v51 wave_shl:1 row_mask:0xf bank_mask:0xf bound_ctrl:1
	v_add_f32_dpp v60, v106, v60 wave_shl:1 row_mask:0xf bank_mask:0xf bound_ctrl:1
	v_add_f32_dpp v61, v107, v61 wave_shl:1 row_mask:0xf bank_mask:0xf bound_ctrl:1
	v_add_f32_dpp v100, v112, v100 wave_shl:1 row_mask:0xf bank_mask:0xf bound_ctrl:1
	v_add_f32_dpp v101, v113, v101 wave_shl:1 row_mask:0xf bank_mask:0xf bound_ctrl:1
	v_add_f32_dpp v104, v114, v104 wave_shl:1 row_mask:0xf bank_mask:0xf bound_ctrl:1
	v_add_f32_dpp v105, v115, v105 wave_shl:1 row_mask:0xf bank_mask:0xf bound_ctrl:1
	v_pk_add_f32 v[94:95], v[38:39], v[50:51]
	v_pk_add_f32 v[106:107], v[70:71], v[94:95]
	v_pk_add_f32 v[38:39], v[46:47], v[60:61]
	v_pk_add_f32 v[70:71], v[84:85], v[38:39]
	v_pk_add_f32 v[46:47], v[48:49], v[100:101]
	v_pk_add_f32 v[84:85], v[92:93], v[46:47]
	v_pk_add_f32 v[48:49], v[52:53], v[104:105]
	v_pk_add_f32 v[92:93], v[98:99], v[48:49]
	v_pk_fma_f32 v[92:93], v[8:9], v[106:107], v[92:93] op_sel_hi:[0,1,1]
	v_pk_fma_f32 v[92:93], v[8:9], v[70:71], v[92:93] op_sel:[1,0,0]
	v_pk_fma_f32 v[92:93], v[10:11], v[84:85], v[92:93] op_sel_hi:[0,1,1]
	v_cndmask_b32_e64 v52, 0, v18, s[10:11]
	v_cndmask_b32_e64 v53, 0, v18, s[14:15]
	v_pk_fma_f32 v[92:93], v[4:5], v[122:123], v[92:93] op_sel_hi:[1,0,1] neg_lo:[0,0,1] neg_hi:[0,0,1]
	s_add_i32 s4, s34, 8
	s_cmpk_lt_i32 s4, 0x201
	s_cselect_b64 s[12:13], s[0:1], 0
	v_pk_add_f32 v[92:93], v[92:93], v[52:53] neg_lo:[0,1] neg_hi:[0,1]
	v_pk_mul_f32 v[98:99], v[92:93], v[92:93]
	v_add_f32_e32 v98, v98, v99
	v_cndmask_b32_e64 v99, 0, v98, s[12:13]
	v_add_f32_e32 v1, v1, v99
	s_waitcnt vmcnt(0)
	s_add_i32 s4, s34, 12
	s_cmpk_lt_u32 s4, 0x201
	s_cselect_b64 s[12:13], s[40:41], 0
	v_cmp_eq_u32_e64 s[14:15], s37, v16
	s_and_b64 s[14:15], s[14:15], s[12:13]
	v_cndmask_b32_e64 v29, 0, 1, s[14:15]
	v_mul_f32_e64 v4, v40, v40
	v_mul_f32_e64 v5, v40, v41
	v_mul_f32_e64 v8, v40, v42
	v_mul_f32_e64 v9, v41, v41
	v_mul_f32_e64 v10, v41, v42
	v_mul_f32_e64 v11, v42, v42
	v_or_b32_dpp v45, v29, v29 wave_shr:1 row_mask:0xf bank_mask:0xf bound_ctrl:1
	s_nop 1
	v_or_b32_dpp v45, v29, v45 wave_shl:1 row_mask:0xf bank_mask:0xf bound_ctrl:1
	s_nop 1
	v_or_b32_dpp v68, v45, v45 wave_shr:1 row_mask:0xf bank_mask:0xf bound_ctrl:1
	s_nop 1
	v_or_b32_dpp v68, v45, v68 wave_shl:1 row_mask:0xf bank_mask:0xf bound_ctrl:1
	v_or3_b32 v29, v68, v44, v69
	v_or3_b32 v29, v29, v102, v103
	s_add_i32 s4, s34, 9
	s_cmpk_lt_u32 s4, 0x1ff
	s_cselect_b64 s[12:13], s[42:43], 0
	v_cmp_ne_u32_e64 s[30:31], 0, v29
	s_and_b64 s[30:31], s[30:31], s[12:13]
	v_cndmask_b32_e64 v29, 0, 1.0, s[30:31]
	v_add_f32_dpp v52, v40, v40 wave_shr:1 row_mask:0xf bank_mask:0xf bound_ctrl:1
	v_add_f32_dpp v53, v41, v41 wave_shr:1 row_mask:0xf bank_mask:0xf bound_ctrl:1
	v_add_f32_dpp v70, v42, v42 wave_shr:1 row_mask:0xf bank_mask:0xf bound_ctrl:1
	v_add_f32_dpp v71, v4, v4 wave_shr:1 row_mask:0xf bank_mask:0xf bound_ctrl:1
	v_add_f32_dpp v84, v5, v5 wave_shr:1 row_mask:0xf bank_mask:0xf bound_ctrl:1
	v_add_f32_dpp v85, v8, v8 wave_shr:1 row_mask:0xf bank_mask:0xf bound_ctrl:1
	v_add_f32_dpp v92, v9, v9 wave_shr:1 row_mask:0xf bank_mask:0xf bound_ctrl:1
	v_add_f32_dpp v93, v10, v10 wave_shr:1 row_mask:0xf bank_mask:0xf bound_ctrl:1
	v_add_f32_dpp v98, v11, v11 wave_shr:1 row_mask:0xf bank_mask:0xf bound_ctrl:1
	v_add_f32_dpp v99, v29, v29 wave_shr:1 row_mask:0xf bank_mask:0xf bound_ctrl:1
	v_add_f32_dpp v52, v40, v52 wave_shl:1 row_mask:0xf bank_mask:0xf bound_ctrl:1
	v_add_f32_dpp v53, v41, v53 wave_shl:1 row_mask:0xf bank_mask:0xf bound_ctrl:1
	v_add_f32_dpp v70, v42, v70 wave_shl:1 row_mask:0xf bank_mask:0xf bound_ctrl:1
	v_add_f32_dpp v71, v4, v71 wave_shl:1 row_mask:0xf bank_mask:0xf bound_ctrl:1
	v_add_f32_dpp v84, v5, v84 wave_shl:1 row_mask:0xf bank_mask:0xf bound_ctrl:1
	v_add_f32_dpp v85, v8, v85 wave_shl:1 row_mask:0xf bank_mask:0xf bound_ctrl:1
	v_add_f32_dpp v92, v9, v92 wave_shl:1 row_mask:0xf bank_mask:0xf bound_ctrl:1
	v_add_f32_dpp v93, v10, v93 wave_shl:1 row_mask:0xf bank_mask:0xf bound_ctrl:1
	v_add_f32_dpp v98, v11, v98 wave_shl:1 row_mask:0xf bank_mask:0xf bound_ctrl:1
	v_add_f32_dpp v99, v29, v99 wave_shl:1 row_mask:0xf bank_mask:0xf bound_ctrl:1
	v_pk_add_f32 v[4:5], v[30:31], v[52:53]
	v_pk_add_f32 v[8:9], v[54:55], v[70:71]
	v_pk_add_f32 v[10:11], v[76:77], v[84:85]
	v_pk_add_f32 v[30:31], v[82:83], v[92:93]
	v_pk_add_f32 v[54:55], v[88:89], v[98:99]
	v_mul_f32_e64 v108, v4, v22
	v_mul_f32_e64 v109, v5, v22
	v_mul_f32_e64 v110, v8, v22
	v_fma_f32 v29, v9, v22, v26
	v_mul_f32_e64 v45, v10, v22
	v_mul_f32_e64 v76, v11, v22
	v_fma_f32 v77, v30, v22, v26
	v_mul_f32_e64 v82, v31, v22
	v_fma_f32 v83, v54, v22, v26
	v_fma_f32 v29, -v108, v108, v29
	v_fma_f32 v45, -v108, v109, v45
	v_fma_f32 v76, -v108, v110, v76
	v_fma_f32 v77, -v109, v109, v77
	v_fma_f32 v82, -v109, v110, v82
	v_fma_f32 v83, -v110, v110, v83
	v_mul_f32_e64 v88, v82, v82
	v_mul_f32_e64 v89, v45, v83
	v_mul_f32_e64 v106, v76, v77
	v_mul_f32_e64 v107, v76, v76
	v_mul_f32_e64 v120, v29, v82
	v_mul_f32_e64 v121, v45, v45
	v_fma_f32 v88, v77, v83, -v88
	v_fma_f32 v89, v76, v82, -v89
	v_fma_f32 v106, v45, v82, -v106
	v_fma_f32 v107, v29, v83, -v107
	v_fma_f32 v120, v45, v76, -v120
	v_fma_f32 v121, v29, v77, -v121
	v_mul_f32_e64 v122, v29, v88
	v_fma_f32 v122, v45, v89, v122
	v_fma_f32 v122, v76, v106, v122
	v_rcp_f32_e32 v122, v122
	v_cmp_ne_u32_e64 vcc, s37, v17
	v_mul_f32_e64 v122, v122, v22
	v_cndmask_b32_e64 v122, 0, v122, s[30:31]
	v_cndmask_b32_e64 v29, 0, v18, vcc
	v_cndmask_b32_e64 v117, 0, v22, s[30:31]
	v_mul_f32_e64 v111, v88, v122
	v_mul_f32_e64 v112, v89, v122
	v_mul_f32_e64 v113, v106, v122
	v_mul_f32_e64 v114, v107, v122
	v_mul_f32_e64 v115, v120, v122
	v_mul_f32_e64 v116, v121, v122
	v_add_f32_e64 v118, v55, v29
	v_mov_b32_e32 v119, v17
	ds_write_b128 v23, v[108:111] offset:3072
	ds_write_b128 v23, v[112:115] offset:4096
	ds_write_b128 v23, v[116:119] offset:5120
	s_waitcnt lgkmcnt(0)
	s_barrier
	v_pk_mul_f32 v[4:5], v[36:37], v[40:41] op_sel_hi:[1,0]
	v_pk_mul_f32 v[8:9], v[36:37], v[40:41] op_sel:[0,1]
	v_pk_mul_f32 v[10:11], v[36:37], v[42:43] op_sel_hi:[1,0]
	v_add_f32_dpp v30, v36, v36 wave_shr:1 row_mask:0xf bank_mask:0xf bound_ctrl:1
	v_add_f32_dpp v31, v37, v37 wave_shr:1 row_mask:0xf bank_mask:0xf bound_ctrl:1
	v_add_f32_dpp v54, v4, v4 wave_shr:1 row_mask:0xf bank_mask:0xf bound_ctrl:1
	v_add_f32_dpp v55, v5, v5 wave_shr:1 row_mask:0xf bank_mask:0xf bound_ctrl:1
	v_add_f32_dpp v76, v8, v8 wave_shr:1 row_mask:0xf bank_mask:0xf bound_ctrl:1
	v_add_f32_dpp v77, v9, v9 wave_shr:1 row_mask:0xf bank_mask:0xf bound_ctrl:1
	v_add_f32_dpp v82, v10, v10 wave_shr:1 row_mask:0xf bank_mask:0xf bound_ctrl:1
	v_add_f32_dpp v83, v11, v11 wave_shr:1 row_mask:0xf bank_mask:0xf bound_ctrl:1
	v_add_f32_dpp v30, v36, v30 wave_shl:1 row_mask:0xf bank_mask:0xf bound_ctrl:1
	v_add_f32_dpp v31, v37, v31 wave_shl:1 row_mask:0xf bank_mask:0xf bound_ctrl:1
	v_add_f32_dpp v54, v4, v54 wave_shl:1 row_mask:0xf bank_mask:0xf bound_ctrl:1
	v_add_f32_dpp v55, v5, v55 wave_shl:1 row_mask:0xf bank_mask:0xf bound_ctrl:1
	v_add_f32_dpp v76, v8, v76 wave_shl:1 row_mask:0xf bank_mask:0xf bound_ctrl:1
	v_add_f32_dpp v77, v9, v77 wave_shl:1 row_mask:0xf bank_mask:0xf bound_ctrl:1
	v_add_f32_dpp v82, v10, v82 wave_shl:1 row_mask:0xf bank_mask:0xf bound_ctrl:1
	v_add_f32_dpp v83, v11, v83 wave_shl:1 row_mask:0xf bank_mask:0xf bound_ctrl:1
	v_pk_add_f32 v[4:5], v[24:25], v[30:31]
	v_pk_add_f32 v[8:9], v[58:59], v[54:55]
	v_pk_add_f32 v[10:11], v[72:73], v[76:77]
	v_pk_add_f32 v[24:25], v[74:75], v[82:83]
	v_pk_fma_f32 v[8:9], v[108:109], v[4:5], v[8:9] op_sel_hi:[0,1,1] neg_lo:[1,0,0] neg_hi:[1,0,0]
	v_pk_fma_f32 v[10:11], v[108:109], v[4:5], v[10:11] op_sel:[1,0,0] neg_lo:[1,0,0] neg_hi:[1,0,0]
	v_pk_fma_f32 v[24:25], v[110:111], v[4:5], v[24:25] op_sel_hi:[0,1,1] neg_lo:[1,0,0] neg_hi:[1,0,0]
	v_pk_mul_f32 v[58:59], v[110:111], v[8:9] op_sel:[1,0]
	v_pk_mul_f32 v[72:73], v[112:113], v[8:9] op_sel_hi:[0,1]
	v_pk_mul_f32 v[74:75], v[112:113], v[8:9] op_sel:[1,0]
	v_pk_fma_f32 v[58:59], v[112:113], v[10:11], v[58:59] op_sel_hi:[0,1,1]
	v_pk_fma_f32 v[72:73], v[114:115], v[10:11], v[72:73] op_sel_hi:[0,1,1]
	v_pk_fma_f32 v[74:75], v[114:115], v[10:11], v[74:75] op_sel:[1,0,0]
	v_pk_fma_f32 v[58:59], v[112:113], v[24:25], v[58:59] op_sel:[1,0,0]
	v_pk_fma_f32 v[72:73], v[114:115], v[24:25], v[72:73] op_sel:[1,0,0]
	v_pk_fma_f32 v[74:75], v[116:117], v[24:25], v[74:75] op_sel_hi:[0,1,1]
	v_pk_mul_f32 v[88:89], v[108:109], v[58:59] op_sel_hi:[0,1]
	v_pk_fma_f32 v[88:89], v[108:109], v[72:73], v[88:89] op_sel:[1,0,0]
	v_pk_fma_f32 v[88:89], v[110:111], v[74:75], v[88:89] op_sel_hi:[0,1,1]
	v_pk_fma_f32 v[88:89], v[116:117], v[4:5], v[88:89] op_sel:[1,0,0] neg_lo:[0,0,1] neg_hi:[0,0,1]
	v_cmp_eq_u32_e64 s[10:11], 6, v119
	v_cmp_eq_u32_e64 s[14:15], 7, v119
	v_add_f32_dpp v4, v58, v58 wave_shr:1 row_mask:0xf bank_mask:0xf bound_ctrl:1
	v_add_f32_dpp v5, v59, v59 wave_shr:1 row_mask:0xf bank_mask:0xf bound_ctrl:1
	v_add_f32_dpp v8, v72, v72 wave_shr:1 row_mask:0xf bank_mask:0xf bound_ctrl:1
	v_add_f32_dpp v9, v73, v73 wave_shr:1 row_mask:0xf bank_mask:0xf bound_ctrl:1
	v_add_f32_dpp v10, v74, v74 wave_shr:1 row_mask:0xf bank_mask:0xf bound_ctrl:1
	v_add_f32_dpp v11, v75, v75 wave_shr:1 row_mask:0xf bank_mask:0xf bound_ctrl:1
	v_add_f32_dpp v24, v88, v88 wave_shr:1 row_mask:0xf bank_mask:0xf bound_ctrl:1
	v_add_f32_dpp v25, v89, v89 wave_shr:1 row_mask:0xf bank_mask:0xf bound_ctrl:1
	v_add_f32_dpp v4, v58, v4 wave_shl:1 row_mask:0xf bank_mask:0xf bound_ctrl:1
	v_add_f32_dpp v5, v59, v5 wave_shl:1 row_mask:0xf bank_mask:0xf bound_ctrl:1
	v_add_f32_dpp v8, v72, v8 wave_shl:1 row_mask:0xf bank_mask:0xf bound_ctrl:1
	v_add_f32_dpp v9, v73, v9 wave_shl:1 row_mask:0xf bank_mask:0xf bound_ctrl:1
	v_add_f32_dpp v10, v74, v10 wave_shl:1 row_mask:0xf bank_mask:0xf bound_ctrl:1
	v_add_f32_dpp v11, v75, v11 wave_shl:1 row_mask:0xf bank_mask:0xf bound_ctrl:1
	v_add_f32_dpp v24, v88, v24 wave_shl:1 row_mask:0xf bank_mask:0xf bound_ctrl:1
	v_add_f32_dpp v25, v89, v25 wave_shl:1 row_mask:0xf bank_mask:0xf bound_ctrl:1
	v_pk_add_f32 v[58:59], v[94:95], v[4:5]
	v_pk_add_f32 v[72:73], v[38:39], v[8:9]
	v_pk_add_f32 v[38:39], v[46:47], v[10:11]
	v_pk_add_f32 v[46:47], v[48:49], v[24:25]
	v_pk_fma_f32 v[46:47], v[12:13], v[58:59], v[46:47] op_sel_hi:[0,1,1]
	v_pk_fma_f32 v[46:47], v[12:13], v[72:73], v[46:47] op_sel:[1,0,0]
	v_pk_fma_f32 v[46:47], v[14:15], v[38:39], v[46:47] op_sel_hi:[0,1,1]
	v_cndmask_b32_e64 v48, 0, v18, s[10:11]
	v_cndmask_b32_e64 v49, 0, v18, s[14:15]
	v_pk_fma_f32 v[46:47], v[6:7], v[118:119], v[46:47] op_sel_hi:[1,0,1] neg_lo:[0,0,1] neg_hi:[0,0,1]
	s_add_i32 s4, s34, 9
	s_cmpk_lt_i32 s4, 0x201
	s_cselect_b64 s[12:13], s[0:1], 0
	v_pk_add_f32 v[46:47], v[46:47], v[48:49] neg_lo:[0,1] neg_hi:[0,1]
	v_pk_mul_f32 v[74:75], v[46:47], v[46:47]
	v_add_f32_e32 v74, v74, v75
	v_cndmask_b32_e64 v75, 0, v74, s[12:13]
	v_add_f32_e32 v1, v1, v75
	v_mov_b32_e32 v0, v1
	s_branch .LBB0_29
.LBB0_15:
.LBB0_16:
	s_mov_b32 s27, s19
	v_mov_b32_e32 v1, 0x42c80000
	v_mov_b32_e32 v0, 0
	s_add_i32 s4, s34, -2
	s_max_i32 s4, s4, 0
	s_mul_i32 s5, s4, 0x804
	s_add_i32 s5, s5, s35
	s_add_i32 s6, s5, 0x0
	s_add_i32 s7, s5, 0x101004
	s_add_i32 s8, s5, 0x202008
	s_add_i32 s11, s5, 0x30300c
	s_add_i32 s15, s5, 0x404010
	s_mul_i32 s9, s4, 0x180c
	s_add_i32 s9, s9, s33
	buffer_load_dword v2, v28, s[16:19], s6 offen nt
	buffer_load_dword v3, v28, s[16:19], s7 offen nt
	buffer_load_dword v4, v28, s[16:19], s8 offen nt
	buffer_load_dword v5, v28, s[16:19], s11 offen nt
	buffer_load_dword v6, v28, s[16:19], s15 offen nt
	buffer_load_dwordx3 v[8:10], v27, s[24:27], s9 offen nt
	s_add_i32 s4, s34, -1
	s_max_i32 s4, s4, 0
	s_mul_i32 s5, s4, 0x804
	s_add_i32 s5, s5, s35
	s_add_i32 s6, s5, 0x0
	s_add_i32 s7, s5, 0x101004
	s_add_i32 s8, s5, 0x202008
	s_add_i32 s11, s5, 0x30300c
	s_add_i32 s15, s5, 0x404010
	s_mul_i32 s9, s4, 0x180c
	s_add_i32 s9, s9, s33
	buffer_load_dword v12, v28, s[16:19], s6 offen nt
	buffer_load_dword v13, v28, s[16:19], s7 offen nt
	buffer_load_dword v14, v28, s[16:19], s8 offen nt
	buffer_load_dword v15, v28, s[16:19], s11 offen nt
	buffer_load_dword v16, v28, s[16:19], s15 offen nt
	buffer_load_dwordx3 v[32:34], v27, s[24:27], s9 offen nt
	s_add_i32 s4, s34, 0
	s_min_i32 s4, s4, 0x200
	s_mul_i32 s5, s4, 0x804
	s_add_i32 s5, s5, s35
	s_add_i32 s6, s5, 0x0
	s_add_i32 s7, s5, 0x101004
	s_add_i32 s8, s5, 0x202008
	s_add_i32 s11, s5, 0x30300c
	s_add_i32 s15, s5, 0x404010
	s_mul_i32 s9, s4, 0x180c
	s_add_i32 s9, s9, s33
	buffer_load_dword v20, v28, s[16:19], s6 offen nt
	buffer_load_dword v21, v28, s[16:19], s7 offen nt
	buffer_load_dword v24, v28, s[16:19], s8 offen nt
	buffer_load_dword v25, v28, s[16:19], s11 offen nt
	buffer_load_dword v30, v28, s[16:19], s15 offen nt
	buffer_load_dwordx3 v[36:38], v27, s[24:27], s9 offen nt
	s_waitcnt vmcnt(12)
	v_pk_mul_f32 v[40:41], v[2:3], v[8:9] op_sel_hi:[1,0]
	v_pk_mul_f32 v[42:43], v[4:5], v[8:9] op_sel_hi:[1,0]
	v_mul_f32_e64 v44, v6, v8
	v_pk_mul_f32 v[46:47], v[2:3], v[8:9] op_sel:[0,1]
	v_pk_mul_f32 v[48:49], v[4:5], v[8:9] op_sel:[0,1]
	v_mul_f32_e64 v50, v6, v9
	v_pk_mul_f32 v[52:53], v[2:3], v[10:11] op_sel_hi:[1,0]
	v_pk_mul_f32 v[54:55], v[4:5], v[10:11] op_sel_hi:[1,0]
	v_mul_f32_e64 v56, v6, v10
	v_add_f32_dpp v58, v2, v2 wave_shr:1 row_mask:0xf bank_mask:0xf bound_ctrl:1
	v_add_f32_dpp v59, v3, v3 wave_shr:1 row_mask:0xf bank_mask:0xf bound_ctrl:1
	v_add_f32_dpp v60, v4, v4 wave_shr:1 row_mask:0xf bank_mask:0xf bound_ctrl:1
	v_add_f32_dpp v61, v5, v5 wave_shr:1 row_mask:0xf bank_mask:0xf bound_ctrl:1
	v_add_f32_dpp v62, v6, v6 wave_shr:1 row_mask:0xf bank_mask:0xf bound_ctrl:1
	v_add_f32_dpp v64, v40, v40 wave_shr:1 row_mask:0xf bank_mask:0xf bound_ctrl:1
	v_add_f32_dpp v65, v41, v41 wave_shr:1 row_mask:0xf bank_mask:0xf bound_ctrl:1
	v_add_f32_dpp v66, v42, v42 wave_shr:1 row_mask:0xf bank_mask:0xf bound_ctrl:1
	v_add_f32_dpp v67, v43, v43 wave_shr:1 row_mask:0xf bank_mask:0xf bound_ctrl:1
	v_add_f32_dpp v68, v44, v44 wave_shr:1 row_mask:0xf bank_mask:0xf bound_ctrl:1
	v_add_f32_dpp v70, v46, v46 wave_shr:1 row_mask:0xf bank_mask:0xf bound_ctrl:1
	v_add_f32_dpp v71, v47, v47 wave_shr:1 row_mask:0xf bank_mask:0xf bound_ctrl:1
	v_add_f32_dpp v72, v48, v48 wave_shr:1 row_mask:0xf bank_mask:0xf bound_ctrl:1
	v_add_f32_dpp v73, v49, v49 wave_shr:1 row_mask:0xf bank_mask:0xf bound_ctrl:1
	v_add_f32_dpp v74, v50, v50 wave_shr:1 row_mask:0xf bank_mask:0xf bound_ctrl:1
	v_add_f32_dpp v76, v52, v52 wave_shr:1 row_mask:0xf bank_mask:0xf bound_ctrl:1
	v_add_f32_dpp v77, v53, v53 wave_shr:1 row_mask:0xf bank_mask:0xf bound_ctrl:1
	v_add_f32_dpp v78, v54, v54 wave_shr:1 row_mask:0xf bank_mask:0xf bound_ctrl:1
	v_add_f32_dpp v79, v55, v55 wave_shr:1 row_mask:0xf bank_mask:0xf bound_ctrl:1
	v_add_f32_dpp v80, v56, v56 wave_shr:1 row_mask:0xf bank_mask:0xf bound_ctrl:1
	v_add_f32_dpp v58, v2, v58 wave_shl:1 row_mask:0xf bank_mask:0xf bound_ctrl:1
	v_add_f32_dpp v59, v3, v59 wave_shl:1 row_mask:0xf bank_mask:0xf bound_ctrl:1
	v_add_f32_dpp v60, v4, v60 wave_shl:1 row_mask:0xf bank_mask:0xf bound_ctrl:1
	v_add_f32_dpp v61, v5, v61 wave_shl:1 row_mask:0xf bank_mask:0xf bound_ctrl:1
	v_add_f32_dpp v62, v6, v62 wave_shl:1 row_mask:0xf bank_mask:0xf bound_ctrl:1
	v_add_f32_dpp v64, v40, v64 wave_shl:1 row_mask:0xf bank_mask:0xf bound_ctrl:1
	v_add_f32_dpp v65, v41, v65 wave_shl:1 row_mask:0xf bank_mask:0xf bound_ctrl:1
	v_add_f32_dpp v66, v42, v66 wave_shl:1 row_mask:0xf bank_mask:0xf bound_ctrl:1
	v_add_f32_dpp v67, v43, v67 wave_shl:1 row_mask:0xf bank_mask:0xf bound_ctrl:1
	v_add_f32_dpp v68, v44, v68 wave_shl:1 row_mask:0xf bank_mask:0xf bound_ctrl:1
	v_add_f32_dpp v70, v46, v70 wave_shl:1 row_mask:0xf bank_mask:0xf bound_ctrl:1
	v_add_f32_dpp v71, v47, v71 wave_shl:1 row_mask:0xf bank_mask:0xf bound_ctrl:1
	v_add_f32_dpp v72, v48, v72 wave_shl:1 row_mask:0xf bank_mask:0xf bound_ctrl:1
	v_add_f32_dpp v73, v49, v73 wave_shl:1 row_mask:0xf bank_mask:0xf bound_ctrl:1
	v_add_f32_dpp v74, v50, v74 wave_shl:1 row_mask:0xf bank_mask:0xf bound_ctrl:1
	v_add_f32_dpp v76, v52, v76 wave_shl:1 row_mask:0xf bank_mask:0xf bound_ctrl:1
	v_add_f32_dpp v77, v53, v77 wave_shl:1 row_mask:0xf bank_mask:0xf bound_ctrl:1
	v_add_f32_dpp v78, v54, v78 wave_shl:1 row_mask:0xf bank_mask:0xf bound_ctrl:1
	v_add_f32_dpp v79, v55, v79 wave_shl:1 row_mask:0xf bank_mask:0xf bound_ctrl:1
	v_add_f32_dpp v80, v56, v80 wave_shl:1 row_mask:0xf bank_mask:0xf bound_ctrl:1
	s_barrier
	s_add_i32 s4, s34, 1
	s_min_i32 s4, s4, 0x200
	s_mul_i32 s5, s4, 0x804
	s_add_i32 s5, s5, s35
	s_add_i32 s6, s5, 0x0
	s_add_i32 s7, s5, 0x101004
	s_add_i32 s8, s5, 0x202008
	s_add_i32 s11, s5, 0x30300c
	s_add_i32 s15, s5, 0x404010
	s_mul_i32 s9, s4, 0x180c
	s_add_i32 s9, s9, s33
	buffer_load_dword v40, v28, s[16:19], s6 offen nt
	buffer_load_dword v41, v28, s[16:19], s7 offen nt
	buffer_load_dword v42, v28, s[16:19], s8 offen nt
	buffer_load_dword v43, v28, s[16:19], s11 offen nt
	buffer_load_dword v44, v28, s[16:19], s15 offen nt
	buffer_load_dwordx3 v[48:50], v27, s[24:27], s9 offen nt
	s_waitcnt vmcnt(12)
	v_pk_mul_f32 v[46:47], v[12:13], v[32:33] op_sel_hi:[1,0]
	v_pk_mul_f32 v[52:53], v[14:15], v[32:33] op_sel_hi:[1,0]
	v_mul_f32_e64 v54, v16, v32
	v_pk_mul_f32 v[56:57], v[12:13], v[32:33] op_sel:[0,1]
	v_pk_mul_f32 v[82:83], v[14:15], v[32:33] op_sel:[0,1]
	v_mul_f32_e64 v84, v16, v33
	v_pk_mul_f32 v[86:87], v[12:13], v[34:35] op_sel_hi:[1,0]
	v_pk_mul_f32 v[88:89], v[14:15], v[34:35] op_sel_hi:[1,0]
	v_mul_f32_e64 v90, v16, v34
	v_add_f32_dpp v92, v12, v12 wave_shr:1 row_mask:0xf bank_mask:0xf bound_ctrl:1
	v_add_f32_dpp v93, v13, v13 wave_shr:1 row_mask:0xf bank_mask:0xf bound_ctrl:1
	v_add_f32_dpp v94, v14, v14 wave_shr:1 row_mask:0xf bank_mask:0xf bound_ctrl:1
	v_add_f32_dpp v95, v15, v15 wave_shr:1 row_mask:0xf bank_mask:0xf bound_ctrl:1
	v_add_f32_dpp v96, v16, v16 wave_shr:1 row_mask:0xf bank_mask:0xf bound_ctrl:1
	v_add_f32_dpp v98, v46, v46 wave_shr:1 row_mask:0xf bank_mask:0xf bound_ctrl:1
	v_add_f32_dpp v99, v47, v47 wave_shr:1 row_mask:0xf bank_mask:0xf bound_ctrl:1
	v_add_f32_dpp v100, v52, v52 wave_shr:1 row_mask:0xf bank_mask:0xf bound_ctrl:1
	v_add_f32_dpp v101, v53, v53 wave_shr:1 row_mask:0xf bank_mask:0xf bound_ctrl:1
	v_add_f32_dpp v102, v54, v54 wave_shr:1 row_mask:0xf bank_mask:0xf bound_ctrl:1
	v_add_f32_dpp v104, v56, v56 wave_shr:1 row_mask:0xf bank_mask:0xf bound_ctrl:1
	v_add_f32_dpp v105, v57, v57 wave_shr:1 row_mask:0xf bank_mask:0xf bound_ctrl:1
	v_add_f32_dpp v106, v82, v82 wave_shr:1 row_mask:0xf bank_mask:0xf bound_ctrl:1
	v_add_f32_dpp v107, v83, v83 wave_shr:1 row_mask:0xf bank_mask:0xf bound_ctrl:1
	v_add_f32_dpp v108, v84, v84 wave_shr:1 row_mask:0xf bank_mask:0xf bound_ctrl:1
	v_add_f32_dpp v110, v86, v86 wave_shr:1 row_mask:0xf bank_mask:0xf bound_ctrl:1
	v_add_f32_dpp v111, v87, v87 wave_shr:1 row_mask:0xf bank_mask:0xf bound_ctrl:1
	v_add_f32_dpp v112, v88, v88 wave_shr:1 row_mask:0xf bank_mask:0xf bound_ctrl:1
	v_add_f32_dpp v113, v89, v89 wave_shr:1 row_mask:0xf bank_mask:0xf bound_ctrl:1
	v_add_f32_dpp v114, v90, v90 wave_shr:1 row_mask:0xf bank_mask:0xf bound_ctrl:1
	v_add_f32_dpp v92, v12, v92 wave_shl:1 row_mask:0xf bank_mask:0xf bound_ctrl:1
	v_add_f32_dpp v93, v13, v93 wave_shl:1 row_mask:0xf bank_mask:0xf bound_ctrl:1
	v_add_f32_dpp v94, v14, v94 wave_shl:1 row_mask:0xf bank_mask:0xf bound_ctrl:1
	v_add_f32_dpp v95, v15, v95 wave_shl:1 row_mask:0xf bank_mask:0xf bound_ctrl:1
	v_add_f32_dpp v96, v16, v96 wave_shl:1 row_mask:0xf bank_mask:0xf bound_ctrl:1
	v_add_f32_dpp v98, v46, v98 wave_shl:1 row_mask:0xf bank_mask:0xf bound_ctrl:1
	v_add_f32_dpp v99, v47, v99 wave_shl:1 row_mask:0xf bank_mask:0xf bound_ctrl:1
	v_add_f32_dpp v100, v52, v100 wave_shl:1 row_mask:0xf bank_mask:0xf bound_ctrl:1
	v_add_f32_dpp v101, v53, v101 wave_shl:1 row_mask:0xf bank_mask:0xf bound_ctrl:1
	v_add_f32_dpp v102, v54, v102 wave_shl:1 row_mask:0xf bank_mask:0xf bound_ctrl:1
	v_add_f32_dpp v104, v56, v104 wave_shl:1 row_mask:0xf bank_mask:0xf bound_ctrl:1
	v_add_f32_dpp v105, v57, v105 wave_shl:1 row_mask:0xf bank_mask:0xf bound_ctrl:1
	v_add_f32_dpp v106, v82, v106 wave_shl:1 row_mask:0xf bank_mask:0xf bound_ctrl:1
	v_add_f32_dpp v107, v83, v107 wave_shl:1 row_mask:0xf bank_mask:0xf bound_ctrl:1
	v_add_f32_dpp v108, v84, v108 wave_shl:1 row_mask:0xf bank_mask:0xf bound_ctrl:1
	v_add_f32_dpp v110, v86, v110 wave_shl:1 row_mask:0xf bank_mask:0xf bound_ctrl:1
	v_add_f32_dpp v111, v87, v111 wave_shl:1 row_mask:0xf bank_mask:0xf bound_ctrl:1
	v_add_f32_dpp v112, v88, v112 wave_shl:1 row_mask:0xf bank_mask:0xf bound_ctrl:1
	v_add_f32_dpp v113, v89, v113 wave_shl:1 row_mask:0xf bank_mask:0xf bound_ctrl:1
	v_add_f32_dpp v114, v90, v114 wave_shl:1 row_mask:0xf bank_mask:0xf bound_ctrl:1
	s_barrier
	s_add_i32 s4, s34, 2
	s_min_i32 s4, s4, 0x200
	s_mul_i32 s5, s4, 0x804
	s_add_i32 s5, s5, s35
	s_add_i32 s6, s5, 0x0
	s_add_i32 s7, s5, 0x101004
	s_add_i32 s8, s5, 0x202008
	s_add_i32 s11, s5, 0x30300c
	s_add_i32 s15, s5, 0x404010
	s_mul_i32 s9, s4, 0x180c
	s_add_i32 s9, s9, s33
	buffer_load_dword v46, v28, s[16:19], s6 offen nt
	buffer_load_dword v47, v28, s[16:19], s7 offen nt
	buffer_load_dword v52, v28, s[16:19], s8 offen nt
	buffer_load_dword v53, v28, s[16:19], s11 offen nt
	buffer_load_dword v54, v28, s[16:19], s15 offen nt
	buffer_load_dwordx3 v[84:86], v27, s[24:27], s9 offen nt
	s_waitcnt vmcnt(12)
	v_pk_mul_f32 v[56:57], v[20:21], v[36:37] op_sel_hi:[1,0]
	v_pk_mul_f32 v[82:83], v[24:25], v[36:37] op_sel_hi:[1,0]
	v_mul_f32_e64 v88, v30, v36
	v_pk_mul_f32 v[90:91], v[20:21], v[36:37] op_sel:[0,1]
	v_pk_mul_f32 v[116:117], v[24:25], v[36:37] op_sel:[0,1]
	v_mul_f32_e64 v118, v30, v37
	v_pk_mul_f32 v[120:121], v[20:21], v[38:39] op_sel_hi:[1,0]
	v_pk_mul_f32 v[122:123], v[24:25], v[38:39] op_sel_hi:[1,0]
	v_mul_f32_e64 v124, v30, v38
	v_add_f32_dpp v126, v20, v20 wave_shr:1 row_mask:0xf bank_mask:0xf bound_ctrl:1
	v_add_f32_dpp v127, v21, v21 wave_shr:1 row_mask:0xf bank_mask:0xf bound_ctrl:1
	v_add_f32_dpp v128, v24, v24 wave_shr:1 row_mask:0xf bank_mask:0xf bound_ctrl:1
	v_add_f32_dpp v129, v25, v25 wave_shr:1 row_mask:0xf bank_mask:0xf bound_ctrl:1
	v_add_f32_dpp v130, v30, v30 wave_shr:1 row_mask:0xf bank_mask:0xf bound_ctrl:1
	v_add_f32_dpp v132, v56, v56 wave_shr:1 row_mask:0xf bank_mask:0xf bound_ctrl:1
	v_add_f32_dpp v133, v57, v57 wave_shr:1 row_mask:0xf bank_mask:0xf bound_ctrl:1
	v_add_f32_dpp v134, v82, v82 wave_shr:1 row_mask:0xf bank_mask:0xf bound_ctrl:1
	v_add_f32_dpp v135, v83, v83 wave_shr:1 row_mask:0xf bank_mask:0xf bound_ctrl:1
	v_add_f32_dpp v136, v88, v88 wave_shr:1 row_mask:0xf bank_mask:0xf bound_ctrl:1
	v_add_f32_dpp v138, v90, v90 wave_shr:1 row_mask:0xf bank_mask:0xf bound_ctrl:1
	v_add_f32_dpp v139, v91, v91 wave_shr:1 row_mask:0xf bank_mask:0xf bound_ctrl:1
	v_add_f32_dpp v140, v116, v116 wave_shr:1 row_mask:0xf bank_mask:0xf bound_ctrl:1
	v_add_f32_dpp v141, v117, v117 wave_shr:1 row_mask:0xf bank_mask:0xf bound_ctrl:1
	v_add_f32_dpp v142, v118, v118 wave_shr:1 row_mask:0xf bank_mask:0xf bound_ctrl:1
	v_add_f32_dpp v144, v120, v120 wave_shr:1 row_mask:0xf bank_mask:0xf bound_ctrl:1
	v_add_f32_dpp v145, v121, v121 wave_shr:1 row_mask:0xf bank_mask:0xf bound_ctrl:1
	v_add_f32_dpp v146, v122, v122 wave_shr:1 row_mask:0xf bank_mask:0xf bound_ctrl:1
	v_add_f32_dpp v147, v123, v123 wave_shr:1 row_mask:0xf bank_mask:0xf bound_ctrl:1
	v_add_f32_dpp v148, v124, v124 wave_shr:1 row_mask:0xf bank_mask:0xf bound_ctrl:1
	v_add_f32_dpp v126, v20, v126 wave_shl:1 row_mask:0xf bank_mask:0xf bound_ctrl:1
	v_add_f32_dpp v127, v21, v127 wave_shl:1 row_mask:0xf bank_mask:0xf bound_ctrl:1
	v_add_f32_dpp v128, v24, v128 wave_shl:1 row_mask:0xf bank_mask:0xf bound_ctrl:1
	v_add_f32_dpp v129, v25, v129 wave_shl:1 row_mask:0xf bank_mask:0xf bound_ctrl:1
	v_add_f32_dpp v130, v30, v130 wave_shl:1 row_mask:0xf bank_mask:0xf bound_ctrl:1
	v_add_f32_dpp v132, v56, v132 wave_shl:1 row_mask:0xf bank_mask:0xf bound_ctrl:1
	v_add_f32_dpp v133, v57, v133 wave_shl:1 row_mask:0xf bank_mask:0xf bound_ctrl:1
	v_add_f32_dpp v134, v82, v134 wave_shl:1 row_mask:0xf bank_mask:0xf bound_ctrl:1
	v_add_f32_dpp v135, v83, v135 wave_shl:1 row_mask:0xf bank_mask:0xf bound_ctrl:1
	v_add_f32_dpp v136, v88, v136 wave_shl:1 row_mask:0xf bank_mask:0xf bound_ctrl:1
	v_add_f32_dpp v138, v90, v138 wave_shl:1 row_mask:0xf bank_mask:0xf bound_ctrl:1
	v_add_f32_dpp v139, v91, v139 wave_shl:1 row_mask:0xf bank_mask:0xf bound_ctrl:1
	v_add_f32_dpp v140, v116, v140 wave_shl:1 row_mask:0xf bank_mask:0xf bound_ctrl:1
	v_add_f32_dpp v141, v117, v141 wave_shl:1 row_mask:0xf bank_mask:0xf bound_ctrl:1
	v_add_f32_dpp v142, v118, v142 wave_shl:1 row_mask:0xf bank_mask:0xf bound_ctrl:1
	v_add_f32_dpp v144, v120, v144 wave_shl:1 row_mask:0xf bank_mask:0xf bound_ctrl:1
	v_add_f32_dpp v145, v121, v145 wave_shl:1 row_mask:0xf bank_mask:0xf bound_ctrl:1
	v_add_f32_dpp v146, v122, v146 wave_shl:1 row_mask:0xf bank_mask:0xf bound_ctrl:1
	v_add_f32_dpp v147, v123, v147 wave_shl:1 row_mask:0xf bank_mask:0xf bound_ctrl:1
	v_add_f32_dpp v148, v124, v148 wave_shl:1 row_mask:0xf bank_mask:0xf bound_ctrl:1
	s_barrier
	ds_read_b128 v[88:91], v23 offset:0
	ds_read_b128 v[116:119], v23 offset:1024
	ds_read_b128 v[120:123], v23 offset:2048
	v_pk_add_f32 v[56:57], v[92:93], v[126:127]
	v_pk_add_f32 v[82:83], v[58:59], v[56:57]
	v_pk_add_f32 v[58:59], v[94:95], v[128:129]
	v_pk_add_f32 v[92:93], v[60:61], v[58:59]
	v_add_f32_e64 v60, v96, v130
	v_add_f32_e64 v94, v62, v60
	v_pk_add_f32 v[62:63], v[98:99], v[132:133]
	v_pk_add_f32 v[96:97], v[64:65], v[62:63]
	v_pk_add_f32 v[64:65], v[100:101], v[134:135]
	v_pk_add_f32 v[98:99], v[66:67], v[64:65]
	v_add_f32_e64 v66, v102, v136
	v_add_f32_e64 v100, v68, v66
	v_pk_add_f32 v[68:69], v[104:105], v[138:139]
	v_pk_add_f32 v[102:103], v[70:71], v[68:69]
	v_pk_add_f32 v[70:71], v[106:107], v[140:141]
	v_pk_add_f32 v[104:105], v[72:73], v[70:71]
	v_add_f32_e64 v72, v108, v142
	v_add_f32_e64 v106, v74, v72
	v_pk_add_f32 v[74:75], v[110:111], v[144:145]
	v_pk_add_f32 v[108:109], v[76:77], v[74:75]
	v_pk_add_f32 v[76:77], v[112:113], v[146:147]
	v_pk_add_f32 v[110:111], v[78:79], v[76:77]
	v_add_f32_e64 v78, v114, v148
	v_add_f32_e64 v112, v80, v78
	s_waitcnt lgkmcnt(2)
	v_pk_fma_f32 v[96:97], v[88:89], v[82:83], v[96:97] op_sel_hi:[0,1,1] neg_lo:[1,0,0] neg_hi:[1,0,0]
	v_pk_fma_f32 v[98:99], v[88:89], v[92:93], v[98:99] op_sel_hi:[0,1,1] neg_lo:[1,0,0] neg_hi:[1,0,0]
	v_fma_f32 v100, -v88, v94, v100
	v_pk_fma_f32 v[102:103], v[88:89], v[82:83], v[102:103] op_sel:[1,0,0] neg_lo:[1,0,0] neg_hi:[1,0,0]
	v_pk_fma_f32 v[104:105], v[88:89], v[92:93], v[104:105] op_sel:[1,0,0] neg_lo:[1,0,0] neg_hi:[1,0,0]
	v_fma_f32 v106, -v89, v94, v106
	v_pk_fma_f32 v[108:109], v[90:91], v[82:83], v[108:109] op_sel_hi:[0,1,1] neg_lo:[1,0,0] neg_hi:[1,0,0]
	v_pk_fma_f32 v[110:111], v[90:91], v[92:93], v[110:111] op_sel_hi:[0,1,1] neg_lo:[1,0,0] neg_hi:[1,0,0]
	v_fma_f32 v112, -v90, v94, v112
	v_pk_mul_f32 v[80:81], v[90:91], v[96:97] op_sel:[1,0]
	v_pk_mul_f32 v[150:151], v[90:91], v[98:99] op_sel:[1,0]
	v_mul_f32_e64 v156, v91, v100
	s_waitcnt lgkmcnt(1)
	v_pk_mul_f32 v[114:115], v[116:117], v[96:97] op_sel_hi:[0,1]
	v_pk_mul_f32 v[152:153], v[116:117], v[98:99] op_sel_hi:[0,1]
	v_mul_f32_e64 v158, v116, v100
	v_pk_mul_f32 v[124:125], v[116:117], v[96:97] op_sel:[1,0]
	v_pk_mul_f32 v[154:155], v[116:117], v[98:99] op_sel:[1,0]
	v_mul_f32_e64 v160, v117, v100
	v_pk_fma_f32 v[80:81], v[116:117], v[102:103], v[80:81] op_sel_hi:[0,1,1]
	v_pk_fma_f32 v[150:151], v[116:117], v[104:105], v[150:151] op_sel_hi:[0,1,1]
	v_fma_f32 v156, v116, v106, v156
	v_pk_fma_f32 v[114:115], v[118:119], v[102:103], v[114:115] op_sel_hi:[0,1,1]
	v_pk_fma_f32 v[152:153], v[118:119], v[104:105], v[152:153] op_sel_hi:[0,1,1]
	v_fma_f32 v158, v118, v106, v158
	v_pk_fma_f32 v[124:125], v[118:119], v[102:103], v[124:125] op_sel:[1,0,0]
	v_pk_fma_f32 v[154:155], v[118:119], v[104:105], v[154:155] op_sel:[1,0,0]
	v_fma_f32 v160, v119, v106, v160
	v_pk_fma_f32 v[80:81], v[116:117], v[108:109], v[80:81] op_sel:[1,0,0]
	v_pk_fma_f32 v[150:151], v[116:117], v[110:111], v[150:151] op_sel:[1,0,0]
	v_fma_f32 v156, v117, v112, v156
	v_pk_fma_f32 v[114:115], v[118:119], v[108:109], v[114:115] op_sel:[1,0,0]
	v_pk_fma_f32 v[152:153], v[118:119], v[110:111], v[152:153] op_sel:[1,0,0]
	v_fma_f32 v158, v119, v112, v158
	s_waitcnt lgkmcnt(0)
	v_pk_fma_f32 v[124:125], v[120:121], v[108:109], v[124:125] op_sel_hi:[0,1,1]
	v_pk_fma_f32 v[154:155], v[120:121], v[110:111], v[154:155] op_sel_hi:[0,1,1]
	v_fma_f32 v160, v120, v112, v160
	v_pk_mul_f32 v[162:163], v[88:89], v[80:81] op_sel_hi:[0,1]
	v_pk_mul_f32 v[164:165], v[88:89], v[150:151] op_sel_hi:[0,1]
	v_mul_f32_e64 v166, v88, v156
	v_pk_fma_f32 v[162:163], v[88:89], v[114:115], v[162:163] op_sel:[1,0,0]
	v_pk_fma_f32 v[164:165], v[88:89], v[152:153], v[164:165] op_sel:[1,0,0]
	v_fma_f32 v166, v89, v158, v166
	v_pk_fma_f32 v[162:163], v[90:91], v[124:125], v[162:163] op_sel_hi:[0,1,1]
	v_pk_fma_f32 v[164:165], v[90:91], v[154:155], v[164:165] op_sel_hi:[0,1,1]
	v_fma_f32 v166, v90, v160, v166
	v_pk_fma_f32 v[162:163], v[120:121], v[82:83], v[162:163] op_sel:[1,0,0] neg_lo:[0,0,1] neg_hi:[0,0,1]
	v_pk_fma_f32 v[164:165], v[120:121], v[92:93], v[164:165] op_sel:[1,0,0] neg_lo:[0,0,1] neg_hi:[0,0,1]
	v_fma_f32 v166, v121, v94, -v166
	v_add_f32_dpp v82, v80, v80 wave_shr:1 row_mask:0xf bank_mask:0xf bound_ctrl:1
	v_add_f32_dpp v83, v81, v81 wave_shr:1 row_mask:0xf bank_mask:0xf bound_ctrl:1
	v_add_f32_dpp v92, v150, v150 wave_shr:1 row_mask:0xf bank_mask:0xf bound_ctrl:1
	v_add_f32_dpp v93, v151, v151 wave_shr:1 row_mask:0xf bank_mask:0xf bound_ctrl:1
	v_add_f32_dpp v94, v156, v156 wave_shr:1 row_mask:0xf bank_mask:0xf bound_ctrl:1
	v_add_f32_dpp v96, v114, v114 wave_shr:1 row_mask:0xf bank_mask:0xf bound_ctrl:1
	v_add_f32_dpp v97, v115, v115 wave_shr:1 row_mask:0xf bank_mask:0xf bound_ctrl:1
	v_add_f32_dpp v98, v152, v152 wave_shr:1 row_mask:0xf bank_mask:0xf bound_ctrl:1
	v_add_f32_dpp v99, v153, v153 wave_shr:1 row_mask:0xf bank_mask:0xf bound_ctrl:1
	v_add_f32_dpp v100, v158, v158 wave_shr:1 row_mask:0xf bank_mask:0xf bound_ctrl:1
	v_add_f32_dpp v102, v124, v124 wave_shr:1 row_mask:0xf bank_mask:0xf bound_ctrl:1
	v_add_f32_dpp v103, v125, v125 wave_shr:1 row_mask:0xf bank_mask:0xf bound_ctrl:1
	v_add_f32_dpp v104, v154, v154 wave_shr:1 row_mask:0xf bank_mask:0xf bound_ctrl:1
	v_add_f32_dpp v105, v155, v155 wave_shr:1 row_mask:0xf bank_mask:0xf bound_ctrl:1
	v_add_f32_dpp v106, v160, v160 wave_shr:1 row_mask:0xf bank_mask:0xf bound_ctrl:1
	v_add_f32_dpp v108, v162, v162 wave_shr:1 row_mask:0xf bank_mask:0xf bound_ctrl:1
	v_add_f32_dpp v109, v163, v163 wave_shr:1 row_mask:0xf bank_mask:0xf bound_ctrl:1
	v_add_f32_dpp v110, v164, v164 wave_shr:1 row_mask:0xf bank_mask:0xf bound_ctrl:1
	v_add_f32_dpp v111, v165, v165 wave_shr:1 row_mask:0xf bank_mask:0xf bound_ctrl:1
	v_add_f32_dpp v112, v166, v166 wave_shr:1 row_mask:0xf bank_mask:0xf bound_ctrl:1
	v_add_f32_dpp v82, v80, v82 wave_shl:1 row_mask:0xf bank_mask:0xf bound_ctrl:1
	v_add_f32_dpp v83, v81, v83 wave_shl:1 row_mask:0xf bank_mask:0xf bound_ctrl:1
	v_add_f32_dpp v92, v150, v92 wave_shl:1 row_mask:0xf bank_mask:0xf bound_ctrl:1
	v_add_f32_dpp v93, v151, v93 wave_shl:1 row_mask:0xf bank_mask:0xf bound_ctrl:1
	v_add_f32_dpp v94, v156, v94 wave_shl:1 row_mask:0xf bank_mask:0xf bound_ctrl:1
	v_add_f32_dpp v96, v114, v96 wave_shl:1 row_mask:0xf bank_mask:0xf bound_ctrl:1
	v_add_f32_dpp v97, v115, v97 wave_shl:1 row_mask:0xf bank_mask:0xf bound_ctrl:1
	v_add_f32_dpp v98, v152, v98 wave_shl:1 row_mask:0xf bank_mask:0xf bound_ctrl:1
	v_add_f32_dpp v99, v153, v99 wave_shl:1 row_mask:0xf bank_mask:0xf bound_ctrl:1
	v_add_f32_dpp v100, v158, v100 wave_shl:1 row_mask:0xf bank_mask:0xf bound_ctrl:1
	v_add_f32_dpp v102, v124, v102 wave_shl:1 row_mask:0xf bank_mask:0xf bound_ctrl:1
	v_add_f32_dpp v103, v125, v103 wave_shl:1 row_mask:0xf bank_mask:0xf bound_ctrl:1
	v_add_f32_dpp v104, v154, v104 wave_shl:1 row_mask:0xf bank_mask:0xf bound_ctrl:1
	v_add_f32_dpp v105, v155, v105 wave_shl:1 row_mask:0xf bank_mask:0xf bound_ctrl:1
	v_add_f32_dpp v106, v160, v106 wave_shl:1 row_mask:0xf bank_mask:0xf bound_ctrl:1
	v_add_f32_dpp v108, v162, v108 wave_shl:1 row_mask:0xf bank_mask:0xf bound_ctrl:1
	v_add_f32_dpp v109, v163, v109 wave_shl:1 row_mask:0xf bank_mask:0xf bound_ctrl:1
	v_add_f32_dpp v110, v164, v110 wave_shl:1 row_mask:0xf bank_mask:0xf bound_ctrl:1
	v_add_f32_dpp v111, v165, v111 wave_shl:1 row_mask:0xf bank_mask:0xf bound_ctrl:1
	v_add_f32_dpp v112, v166, v112 wave_shl:1 row_mask:0xf bank_mask:0xf bound_ctrl:1
	s_add_i32 s4, s34, 3
	s_min_i32 s4, s4, 0x200
	s_mul_i32 s5, s4, 0x804
	s_add_i32 s5, s5, s35
	s_add_i32 s6, s5, 0x0
	s_add_i32 s7, s5, 0x101004
	s_add_i32 s8, s5, 0x202008
	s_add_i32 s11, s5, 0x30300c
	s_add_i32 s15, s5, 0x404010
	s_mul_i32 s9, s4, 0x180c
	s_add_i32 s9, s9, s33
	buffer_load_dword v2, v28, s[16:19], s6 offen nt
	buffer_load_dword v3, v28, s[16:19], s7 offen nt
	buffer_load_dword v4, v28, s[16:19], s8 offen nt
	buffer_load_dword v5, v28, s[16:19], s11 offen nt
	buffer_load_dword v6, v28, s[16:19], s15 offen nt
	buffer_load_dwordx3 v[8:10], v27, s[24:27], s9 offen nt
	s_waitcnt vmcnt(12)
	v_pk_mul_f32 v[80:81], v[40:41], v[48:49] op_sel_hi:[1,0]
	v_pk_mul_f32 v[88:89], v[42:43], v[48:49] op_sel_hi:[1,0]
	v_mul_f32_e64 v90, v44, v48
	v_pk_mul_f32 v[114:115], v[40:41], v[48:49] op_sel:[0,1]
	v_pk_mul_f32 v[116:117], v[42:43], v[48:49] op_sel:[0,1]
	v_mul_f32_e64 v118, v44, v49
	v_pk_mul_f32 v[120:121], v[40:41], v[50:51] op_sel_hi:[1,0]
	v_pk_mul_f32 v[122:123], v[42:43], v[50:51] op_sel_hi:[1,0]
	v_mul_f32_e64 v124, v44, v50
	v_add_f32_dpp v150, v40, v40 wave_shr:1 row_mask:0xf bank_mask:0xf bound_ctrl:1
	v_add_f32_dpp v151, v41, v41 wave_shr:1 row_mask:0xf bank_mask:0xf bound_ctrl:1
	v_add_f32_dpp v152, v42, v42 wave_shr:1 row_mask:0xf bank_mask:0xf bound_ctrl:1
	v_add_f32_dpp v153, v43, v43 wave_shr:1 row_mask:0xf bank_mask:0xf bound_ctrl:1
	v_add_f32_dpp v154, v44, v44 wave_shr:1 row_mask:0xf bank_mask:0xf bound_ctrl:1
	v_add_f32_dpp v156, v80, v80 wave_shr:1 row_mask:0xf bank_mask:0xf bound_ctrl:1
	v_add_f32_dpp v157, v81, v81 wave_shr:1 row_mask:0xf bank_mask:0xf bound_ctrl:1
	v_add_f32_dpp v158, v88, v88 wave_shr:1 row_mask:0xf bank_mask:0xf bound_ctrl:1
	v_add_f32_dpp v159, v89, v89 wave_shr:1 row_mask:0xf bank_mask:0xf bound_ctrl:1
	v_add_f32_dpp v160, v90, v90 wave_shr:1 row_mask:0xf bank_mask:0xf bound_ctrl:1
	v_add_f32_dpp v162, v114, v114 wave_shr:1 row_mask:0xf bank_mask:0xf bound_ctrl:1
	v_add_f32_dpp v163, v115, v115 wave_shr:1 row_mask:0xf bank_mask:0xf bound_ctrl:1
	v_add_f32_dpp v164, v116, v116 wave_shr:1 row_mask:0xf bank_mask:0xf bound_ctrl:1
	v_add_f32_dpp v165, v117, v117 wave_shr:1 row_mask:0xf bank_mask:0xf bound_ctrl:1
	v_add_f32_dpp v166, v118, v118 wave_shr:1 row_mask:0xf bank_mask:0xf bound_ctrl:1
	v_add_f32_dpp v168, v120, v120 wave_shr:1 row_mask:0xf bank_mask:0xf bound_ctrl:1
	v_add_f32_dpp v169, v121, v121 wave_shr:1 row_mask:0xf bank_mask:0xf bound_ctrl:1
	v_add_f32_dpp v170, v122, v122 wave_shr:1 row_mask:0xf bank_mask:0xf bound_ctrl:1
	v_add_f32_dpp v171, v123, v123 wave_shr:1 row_mask:0xf bank_mask:0xf bound_ctrl:1
	v_add_f32_dpp v172, v124, v124 wave_shr:1 row_mask:0xf bank_mask:0xf bound_ctrl:1
	v_add_f32_dpp v150, v40, v150 wave_shl:1 row_mask:0xf bank_mask:0xf bound_ctrl:1
	v_add_f32_dpp v151, v41, v151 wave_shl:1 row_mask:0xf bank_mask:0xf bound_ctrl:1
	v_add_f32_dpp v152, v42, v152 wave_shl:1 row_mask:0xf bank_mask:0xf bound_ctrl:1
	v_add_f32_dpp v153, v43, v153 wave_shl:1 row_mask:0xf bank_mask:0xf bound_ctrl:1
	v_add_f32_dpp v154, v44, v154 wave_shl:1 row_mask:0xf bank_mask:0xf bound_ctrl:1
	v_add_f32_dpp v156, v80, v156 wave_shl:1 row_mask:0xf bank_mask:0xf bound_ctrl:1
	v_add_f32_dpp v157, v81, v157 wave_shl:1 row_mask:0xf bank_mask:0xf bound_ctrl:1
	v_add_f32_dpp v158, v88, v158 wave_shl:1 row_mask:0xf bank_mask:0xf bound_ctrl:1
	v_add_f32_dpp v159, v89, v159 wave_shl:1 row_mask:0xf bank_mask:0xf bound_ctrl:1
	v_add_f32_dpp v160, v90, v160 wave_shl:1 row_mask:0xf bank_mask:0xf bound_ctrl:1
	v_add_f32_dpp v162, v114, v162 wave_shl:1 row_mask:0xf bank_mask:0xf bound_ctrl:1
	v_add_f32_dpp v163, v115, v163 wave_shl:1 row_mask:0xf bank_mask:0xf bound_ctrl:1
	v_add_f32_dpp v164, v116, v164 wave_shl:1 row_mask:0xf bank_mask:0xf bound_ctrl:1
	v_add_f32_dpp v165, v117, v165 wave_shl:1 row_mask:0xf bank_mask:0xf bound_ctrl:1
	v_add_f32_dpp v166, v118, v166 wave_shl:1 row_mask:0xf bank_mask:0xf bound_ctrl:1
	v_add_f32_dpp v168, v120, v168 wave_shl:1 row_mask:0xf bank_mask:0xf bound_ctrl:1
	v_add_f32_dpp v169, v121, v169 wave_shl:1 row_mask:0xf bank_mask:0xf bound_ctrl:1
	v_add_f32_dpp v170, v122, v170 wave_shl:1 row_mask:0xf bank_mask:0xf bound_ctrl:1
	v_add_f32_dpp v171, v123, v171 wave_shl:1 row_mask:0xf bank_mask:0xf bound_ctrl:1
	v_add_f32_dpp v172, v124, v172 wave_shl:1 row_mask:0xf bank_mask:0xf bound_ctrl:1
	s_barrier
	ds_read_b128 v[88:91], v23 offset:3072
	ds_read_b128 v[116:119], v23 offset:4096
	ds_read_b128 v[120:123], v23 offset:5120
	v_pk_add_f32 v[80:81], v[56:57], v[150:151]
	v_pk_add_f32 v[56:57], v[58:59], v[152:153]
	v_add_f32_e64 v58, v60, v154
	v_pk_add_f32 v[60:61], v[62:63], v[156:157]
	v_pk_add_f32 v[62:63], v[64:65], v[158:159]
	v_add_f32_e64 v64, v66, v160
	v_pk_add_f32 v[66:67], v[68:69], v[162:163]
	v_pk_add_f32 v[68:69], v[70:71], v[164:165]
	v_add_f32_e64 v70, v72, v166
	v_pk_add_f32 v[72:73], v[74:75], v[168:169]
	v_pk_add_f32 v[74:75], v[76:77], v[170:171]
	v_add_f32_e64 v76, v78, v172
	s_waitcnt lgkmcnt(2)
	v_pk_fma_f32 v[60:61], v[88:89], v[80:81], v[60:61] op_sel_hi:[0,1,1] neg_lo:[1,0,0] neg_hi:[1,0,0]
	v_pk_fma_f32 v[62:63], v[88:89], v[56:57], v[62:63] op_sel_hi:[0,1,1] neg_lo:[1,0,0] neg_hi:[1,0,0]
	v_fma_f32 v64, -v88, v58, v64
	v_pk_fma_f32 v[66:67], v[88:89], v[80:81], v[66:67] op_sel:[1,0,0] neg_lo:[1,0,0] neg_hi:[1,0,0]
	v_pk_fma_f32 v[68:69], v[88:89], v[56:57], v[68:69] op_sel:[1,0,0] neg_lo:[1,0,0] neg_hi:[1,0,0]
	v_fma_f32 v70, -v89, v58, v70
	v_pk_fma_f32 v[72:73], v[90:91], v[80:81], v[72:73] op_sel_hi:[0,1,1] neg_lo:[1,0,0] neg_hi:[1,0,0]
	v_pk_fma_f32 v[74:75], v[90:91], v[56:57], v[74:75] op_sel_hi:[0,1,1] neg_lo:[1,0,0] neg_hi:[1,0,0]
	v_fma_f32 v76, -v90, v58, v76
	v_pk_mul_f32 v[78:79], v[90:91], v[60:61] op_sel:[1,0]
	v_pk_mul_f32 v[174:175], v[90:91], v[62:63] op_sel:[1,0]
	v_mul_f32_e64 v180, v91, v64
	s_waitcnt lgkmcnt(1)
	v_pk_mul_f32 v[114:115], v[116:117], v[60:61] op_sel_hi:[0,1]
	v_pk_mul_f32 v[176:177], v[116:117], v[62:63] op_sel_hi:[0,1]
	v_mul_f32_e64 v182, v116, v64
	v_pk_mul_f32 v[124:125], v[116:117], v[60:61] op_sel:[1,0]
	v_pk_mul_f32 v[178:179], v[116:117], v[62:63] op_sel:[1,0]
	v_mul_f32_e64 v184, v117, v64
	v_pk_fma_f32 v[78:79], v[116:117], v[66:67], v[78:79] op_sel_hi:[0,1,1]
	v_pk_fma_f32 v[174:175], v[116:117], v[68:69], v[174:175] op_sel_hi:[0,1,1]
	v_fma_f32 v180, v116, v70, v180
	v_pk_fma_f32 v[114:115], v[118:119], v[66:67], v[114:115] op_sel_hi:[0,1,1]
	v_pk_fma_f32 v[176:177], v[118:119], v[68:69], v[176:177] op_sel_hi:[0,1,1]
	v_fma_f32 v182, v118, v70, v182
	v_pk_fma_f32 v[124:125], v[118:119], v[66:67], v[124:125] op_sel:[1,0,0]
	v_pk_fma_f32 v[178:179], v[118:119], v[68:69], v[178:179] op_sel:[1,0,0]
	v_fma_f32 v184, v119, v70, v184
	v_pk_fma_f32 v[78:79], v[116:117], v[72:73], v[78:79] op_sel:[1,0,0]
	v_pk_fma_f32 v[174:175], v[116:117], v[74:75], v[174:175] op_sel:[1,0,0]
	v_fma_f32 v180, v117, v76, v180
	v_pk_fma_f32 v[114:115], v[118:119], v[72:73], v[114:115] op_sel:[1,0,0]
	v_pk_fma_f32 v[176:177], v[118:119], v[74:75], v[176:177] op_sel:[1,0,0]
	v_fma_f32 v182, v119, v76, v182
	s_waitcnt lgkmcnt(0)
	v_pk_fma_f32 v[124:125], v[120:121], v[72:73], v[124:125] op_sel_hi:[0,1,1]
	v_pk_fma_f32 v[178:179], v[120:121], v[74:75], v[178:179] op_sel_hi:[0,1,1]
	v_fma_f32 v184, v120, v76, v184
	v_pk_mul_f32 v[186:187], v[88:89], v[78:79] op_sel_hi:[0,1]
	v_pk_mul_f32 v[188:189], v[88:89], v[174:175] op_sel_hi:[0,1]
	v_mul_f32_e64 v190, v88, v180
	v_pk_fma_f32 v[186:187], v[88:89], v[114:115], v[186:187] op_sel:[1,0,0]
	v_pk_fma_f32 v[188:189], v[88:89], v[176:177], v[188:189] op_sel:[1,0,0]
	v_fma_f32 v190, v89, v182, v190
	v_pk_fma_f32 v[186:187], v[90:91], v[124:125], v[186:187] op_sel_hi:[0,1,1]
	v_pk_fma_f32 v[188:189], v[90:91], v[178:179], v[188:189] op_sel_hi:[0,1,1]
	v_fma_f32 v190, v90, v184, v190
	v_pk_fma_f32 v[186:187], v[120:121], v[80:81], v[186:187] op_sel:[1,0,0] neg_lo:[0,0,1] neg_hi:[0,0,1]
	v_pk_fma_f32 v[188:189], v[120:121], v[56:57], v[188:189] op_sel:[1,0,0] neg_lo:[0,0,1] neg_hi:[0,0,1]
	v_fma_f32 v190, v121, v58, -v190
	v_add_f32_dpp v56, v78, v78 wave_shr:1 row_mask:0xf bank_mask:0xf bound_ctrl:1
	v_add_f32_dpp v57, v79, v79 wave_shr:1 row_mask:0xf bank_mask:0xf bound_ctrl:1
	v_add_f32_dpp v58, v174, v174 wave_shr:1 row_mask:0xf bank_mask:0xf bound_ctrl:1
	v_add_f32_dpp v59, v175, v175 wave_shr:1 row_mask:0xf bank_mask:0xf bound_ctrl:1
	v_add_f32_dpp v60, v180, v180 wave_shr:1 row_mask:0xf bank_mask:0xf bound_ctrl:1
	v_add_f32_dpp v62, v114, v114 wave_shr:1 row_mask:0xf bank_mask:0xf bound_ctrl:1
	v_add_f32_dpp v63, v115, v115 wave_shr:1 row_mask:0xf bank_mask:0xf bound_ctrl:1
	v_add_f32_dpp v64, v176, v176 wave_shr:1 row_mask:0xf bank_mask:0xf bound_ctrl:1
	v_add_f32_dpp v65, v177, v177 wave_shr:1 row_mask:0xf bank_mask:0xf bound_ctrl:1
	v_add_f32_dpp v66, v182, v182 wave_shr:1 row_mask:0xf bank_mask:0xf bound_ctrl:1
	v_add_f32_dpp v68, v124, v124 wave_shr:1 row_mask:0xf bank_mask:0xf bound_ctrl:1
	v_add_f32_dpp v69, v125, v125 wave_shr:1 row_mask:0xf bank_mask:0xf bound_ctrl:1
	v_add_f32_dpp v70, v178, v178 wave_shr:1 row_mask:0xf bank_mask:0xf bound_ctrl:1
	v_add_f32_dpp v71, v179, v179 wave_shr:1 row_mask:0xf bank_mask:0xf bound_ctrl:1
	v_add_f32_dpp v72, v184, v184 wave_shr:1 row_mask:0xf bank_mask:0xf bound_ctrl:1
	v_add_f32_dpp v74, v186, v186 wave_shr:1 row_mask:0xf bank_mask:0xf bound_ctrl:1
	v_add_f32_dpp v75, v187, v187 wave_shr:1 row_mask:0xf bank_mask:0xf bound_ctrl:1
	v_add_f32_dpp v76, v188, v188 wave_shr:1 row_mask:0xf bank_mask:0xf bound_ctrl:1
	v_add_f32_dpp v77, v189, v189 wave_shr:1 row_mask:0xf bank_mask:0xf bound_ctrl:1
	v_add_f32_dpp v80, v190, v190 wave_shr:1 row_mask:0xf bank_mask:0xf bound_ctrl:1
	v_add_f32_dpp v56, v78, v56 wave_shl:1 row_mask:0xf bank_mask:0xf bound_ctrl:1
	v_add_f32_dpp v57, v79, v57 wave_shl:1 row_mask:0xf bank_mask:0xf bound_ctrl:1
	v_add_f32_dpp v58, v174, v58 wave_shl:1 row_mask:0xf bank_mask:0xf bound_ctrl:1
	v_add_f32_dpp v59, v175, v59 wave_shl:1 row_mask:0xf bank_mask:0xf bound_ctrl:1
	v_add_f32_dpp v60, v180, v60 wave_shl:1 row_mask:0xf bank_mask:0xf bound_ctrl:1
	v_add_f32_dpp v62, v114, v62 wave_shl:1 row_mask:0xf bank_mask:0xf bound_ctrl:1
	v_add_f32_dpp v63, v115, v63 wave_shl:1 row_mask:0xf bank_mask:0xf bound_ctrl:1
	v_add_f32_dpp v64, v176, v64 wave_shl:1 row_mask:0xf bank_mask:0xf bound_ctrl:1
	v_add_f32_dpp v65, v177, v65 wave_shl:1 row_mask:0xf bank_mask:0xf bound_ctrl:1
	v_add_f32_dpp v66, v182, v66 wave_shl:1 row_mask:0xf bank_mask:0xf bound_ctrl:1
	v_add_f32_dpp v68, v124, v68 wave_shl:1 row_mask:0xf bank_mask:0xf bound_ctrl:1
	v_add_f32_dpp v69, v125, v69 wave_shl:1 row_mask:0xf bank_mask:0xf bound_ctrl:1
	v_add_f32_dpp v70, v178, v70 wave_shl:1 row_mask:0xf bank_mask:0xf bound_ctrl:1
	v_add_f32_dpp v71, v179, v71 wave_shl:1 row_mask:0xf bank_mask:0xf bound_ctrl:1
	v_add_f32_dpp v72, v184, v72 wave_shl:1 row_mask:0xf bank_mask:0xf bound_ctrl:1
	v_add_f32_dpp v74, v186, v74 wave_shl:1 row_mask:0xf bank_mask:0xf bound_ctrl:1
	v_add_f32_dpp v75, v187, v75 wave_shl:1 row_mask:0xf bank_mask:0xf bound_ctrl:1
	v_add_f32_dpp v76, v188, v76 wave_shl:1 row_mask:0xf bank_mask:0xf bound_ctrl:1
	v_add_f32_dpp v77, v189, v77 wave_shl:1 row_mask:0xf bank_mask:0xf bound_ctrl:1
	v_add_f32_dpp v80, v190, v80 wave_shl:1 row_mask:0xf bank_mask:0xf bound_ctrl:1
	s_add_i32 s4, s34, 4
	s_min_i32 s4, s4, 0x200
	s_mul_i32 s5, s4, 0x804
	s_add_i32 s5, s5, s35
	s_add_i32 s6, s5, 0x0
	s_add_i32 s7, s5, 0x101004
	s_add_i32 s8, s5, 0x202008
	s_add_i32 s11, s5, 0x30300c
	s_add_i32 s15, s5, 0x404010
	s_mul_i32 s9, s4, 0x180c
	s_add_i32 s9, s9, s33
	buffer_load_dword v12, v28, s[16:19], s6 offen nt
	buffer_load_dword v13, v28, s[16:19], s7 offen nt
	buffer_load_dword v14, v28, s[16:19], s8 offen nt
	buffer_load_dword v15, v28, s[16:19], s11 offen nt
	buffer_load_dword v16, v28, s[16:19], s15 offen nt
	buffer_load_dwordx3 v[32:34], v27, s[24:27], s9 offen nt
	s_waitcnt vmcnt(12)
	v_pk_mul_f32 v[78:79], v[46:47], v[84:85] op_sel_hi:[1,0]
	v_pk_mul_f32 v[88:89], v[52:53], v[84:85] op_sel_hi:[1,0]
	v_mul_f32_e64 v90, v54, v84
	v_pk_mul_f32 v[114:115], v[46:47], v[84:85] op_sel:[0,1]
	v_pk_mul_f32 v[116:117], v[52:53], v[84:85] op_sel:[0,1]
	v_mul_f32_e64 v118, v54, v85
	v_pk_mul_f32 v[120:121], v[46:47], v[86:87] op_sel_hi:[1,0]
	v_pk_mul_f32 v[122:123], v[52:53], v[86:87] op_sel_hi:[1,0]
	v_mul_f32_e64 v124, v54, v86
	v_add_f32_dpp v174, v46, v46 wave_shr:1 row_mask:0xf bank_mask:0xf bound_ctrl:1
	v_add_f32_dpp v175, v47, v47 wave_shr:1 row_mask:0xf bank_mask:0xf bound_ctrl:1
	v_add_f32_dpp v176, v52, v52 wave_shr:1 row_mask:0xf bank_mask:0xf bound_ctrl:1
	v_add_f32_dpp v177, v53, v53 wave_shr:1 row_mask:0xf bank_mask:0xf bound_ctrl:1
	v_add_f32_dpp v178, v54, v54 wave_shr:1 row_mask:0xf bank_mask:0xf bound_ctrl:1
	v_add_f32_dpp v180, v78, v78 wave_shr:1 row_mask:0xf bank_mask:0xf bound_ctrl:1
	v_add_f32_dpp v181, v79, v79 wave_shr:1 row_mask:0xf bank_mask:0xf bound_ctrl:1
	v_add_f32_dpp v182, v88, v88 wave_shr:1 row_mask:0xf bank_mask:0xf bound_ctrl:1
	v_add_f32_dpp v183, v89, v89 wave_shr:1 row_mask:0xf bank_mask:0xf bound_ctrl:1
	v_add_f32_dpp v184, v90, v90 wave_shr:1 row_mask:0xf bank_mask:0xf bound_ctrl:1
	v_add_f32_dpp v186, v114, v114 wave_shr:1 row_mask:0xf bank_mask:0xf bound_ctrl:1
	v_add_f32_dpp v187, v115, v115 wave_shr:1 row_mask:0xf bank_mask:0xf bound_ctrl:1
	v_add_f32_dpp v188, v116, v116 wave_shr:1 row_mask:0xf bank_mask:0xf bound_ctrl:1
	v_add_f32_dpp v189, v117, v117 wave_shr:1 row_mask:0xf bank_mask:0xf bound_ctrl:1
	v_add_f32_dpp v190, v118, v118 wave_shr:1 row_mask:0xf bank_mask:0xf bound_ctrl:1
	v_add_f32_dpp v192, v120, v120 wave_shr:1 row_mask:0xf bank_mask:0xf bound_ctrl:1
	v_add_f32_dpp v193, v121, v121 wave_shr:1 row_mask:0xf bank_mask:0xf bound_ctrl:1
	v_add_f32_dpp v194, v122, v122 wave_shr:1 row_mask:0xf bank_mask:0xf bound_ctrl:1
	v_add_f32_dpp v195, v123, v123 wave_shr:1 row_mask:0xf bank_mask:0xf bound_ctrl:1
	v_add_f32_dpp v196, v124, v124 wave_shr:1 row_mask:0xf bank_mask:0xf bound_ctrl:1
	v_add_f32_dpp v174, v46, v174 wave_shl:1 row_mask:0xf bank_mask:0xf bound_ctrl:1
	v_add_f32_dpp v175, v47, v175 wave_shl:1 row_mask:0xf bank_mask:0xf bound_ctrl:1
	v_add_f32_dpp v176, v52, v176 wave_shl:1 row_mask:0xf bank_mask:0xf bound_ctrl:1
	v_add_f32_dpp v177, v53, v177 wave_shl:1 row_mask:0xf bank_mask:0xf bound_ctrl:1
	v_add_f32_dpp v178, v54, v178 wave_shl:1 row_mask:0xf bank_mask:0xf bound_ctrl:1
	v_add_f32_dpp v180, v78, v180 wave_shl:1 row_mask:0xf bank_mask:0xf bound_ctrl:1
	v_add_f32_dpp v181, v79, v181 wave_shl:1 row_mask:0xf bank_mask:0xf bound_ctrl:1
	v_add_f32_dpp v182, v88, v182 wave_shl:1 row_mask:0xf bank_mask:0xf bound_ctrl:1
	v_add_f32_dpp v183, v89, v183 wave_shl:1 row_mask:0xf bank_mask:0xf bound_ctrl:1
	v_add_f32_dpp v184, v90, v184 wave_shl:1 row_mask:0xf bank_mask:0xf bound_ctrl:1
	v_add_f32_dpp v186, v114, v186 wave_shl:1 row_mask:0xf bank_mask:0xf bound_ctrl:1
	v_add_f32_dpp v187, v115, v187 wave_shl:1 row_mask:0xf bank_mask:0xf bound_ctrl:1
	v_add_f32_dpp v188, v116, v188 wave_shl:1 row_mask:0xf bank_mask:0xf bound_ctrl:1
	v_add_f32_dpp v189, v117, v189 wave_shl:1 row_mask:0xf bank_mask:0xf bound_ctrl:1
	v_add_f32_dpp v190, v118, v190 wave_shl:1 row_mask:0xf bank_mask:0xf bound_ctrl:1
	v_add_f32_dpp v192, v120, v192 wave_shl:1 row_mask:0xf bank_mask:0xf bound_ctrl:1
	v_add_f32_dpp v193, v121, v193 wave_shl:1 row_mask:0xf bank_mask:0xf bound_ctrl:1
	v_add_f32_dpp v194, v122, v194 wave_shl:1 row_mask:0xf bank_mask:0xf bound_ctrl:1
	v_add_f32_dpp v195, v123, v195 wave_shl:1 row_mask:0xf bank_mask:0xf bound_ctrl:1
	v_add_f32_dpp v196, v124, v196 wave_shl:1 row_mask:0xf bank_mask:0xf bound_ctrl:1
	s_barrier
	ds_read_b128 v[88:91], v23 offset:0
	ds_read_b128 v[116:119], v23 offset:1024
	ds_read_b128 v[120:123], v23 offset:2048
	v_pk_add_f32 v[78:79], v[150:151], v[174:175]
	v_pk_add_f32 v[114:115], v[126:127], v[78:79]
	v_pk_add_f32 v[124:125], v[152:153], v[176:177]
	v_pk_add_f32 v[126:127], v[128:129], v[124:125]
	v_add_f32_e64 v128, v154, v178
	v_add_f32_e64 v150, v130, v128
	v_pk_add_f32 v[130:131], v[156:157], v[180:181]
	v_pk_add_f32 v[152:153], v[132:133], v[130:131]
	v_pk_add_f32 v[132:133], v[158:159], v[182:183]
	v_pk_add_f32 v[154:155], v[134:135], v[132:133]
	v_add_f32_e64 v134, v160, v184
	v_add_f32_e64 v156, v136, v134
	v_pk_add_f32 v[136:137], v[162:163], v[186:187]
	v_pk_add_f32 v[158:159], v[138:139], v[136:137]
	v_pk_add_f32 v[138:139], v[164:165], v[188:189]
	v_pk_add_f32 v[160:161], v[140:141], v[138:139]
	v_add_f32_e64 v140, v166, v190
	v_add_f32_e64 v162, v142, v140
	v_pk_add_f32 v[142:143], v[168:169], v[192:193]
	v_pk_add_f32 v[164:165], v[144:145], v[142:143]
	v_pk_add_f32 v[144:145], v[170:171], v[194:195]
	v_pk_add_f32 v[166:167], v[146:147], v[144:145]
	v_add_f32_e64 v146, v172, v196
	v_add_f32_e64 v168, v148, v146
	s_waitcnt lgkmcnt(2)
	v_pk_fma_f32 v[152:153], v[88:89], v[114:115], v[152:153] op_sel_hi:[0,1,1] neg_lo:[1,0,0] neg_hi:[1,0,0]
	v_pk_fma_f32 v[154:155], v[88:89], v[126:127], v[154:155] op_sel_hi:[0,1,1] neg_lo:[1,0,0] neg_hi:[1,0,0]
	v_fma_f32 v156, -v88, v150, v156
	v_pk_fma_f32 v[158:159], v[88:89], v[114:115], v[158:159] op_sel:[1,0,0] neg_lo:[1,0,0] neg_hi:[1,0,0]
	v_pk_fma_f32 v[160:161], v[88:89], v[126:127], v[160:161] op_sel:[1,0,0] neg_lo:[1,0,0] neg_hi:[1,0,0]
	v_fma_f32 v162, -v89, v150, v162
	v_pk_fma_f32 v[164:165], v[90:91], v[114:115], v[164:165] op_sel_hi:[0,1,1] neg_lo:[1,0,0] neg_hi:[1,0,0]
	v_pk_fma_f32 v[166:167], v[90:91], v[126:127], v[166:167] op_sel_hi:[0,1,1] neg_lo:[1,0,0] neg_hi:[1,0,0]
	v_fma_f32 v168, -v90, v150, v168
	v_pk_mul_f32 v[148:149], v[90:91], v[152:153] op_sel:[1,0]
	v_pk_mul_f32 v[198:199], v[90:91], v[154:155] op_sel:[1,0]
	v_mul_f32_e64 v204, v91, v156
	s_waitcnt lgkmcnt(1)
	v_pk_mul_f32 v[170:171], v[116:117], v[152:153] op_sel_hi:[0,1]
	v_pk_mul_f32 v[200:201], v[116:117], v[154:155] op_sel_hi:[0,1]
	v_mul_f32_e64 v206, v116, v156
	v_pk_mul_f32 v[172:173], v[116:117], v[152:153] op_sel:[1,0]
	v_pk_mul_f32 v[202:203], v[116:117], v[154:155] op_sel:[1,0]
	v_mul_f32_e64 v208, v117, v156
	v_pk_fma_f32 v[148:149], v[116:117], v[158:159], v[148:149] op_sel_hi:[0,1,1]
	v_pk_fma_f32 v[198:199], v[116:117], v[160:161], v[198:199] op_sel_hi:[0,1,1]
	v_fma_f32 v204, v116, v162, v204
	v_pk_fma_f32 v[170:171], v[118:119], v[158:159], v[170:171] op_sel_hi:[0,1,1]
	v_pk_fma_f32 v[200:201], v[118:119], v[160:161], v[200:201] op_sel_hi:[0,1,1]
	v_fma_f32 v206, v118, v162, v206
	v_pk_fma_f32 v[172:173], v[118:119], v[158:159], v[172:173] op_sel:[1,0,0]
	v_pk_fma_f32 v[202:203], v[118:119], v[160:161], v[202:203] op_sel:[1,0,0]
	v_fma_f32 v208, v119, v162, v208
	v_pk_fma_f32 v[148:149], v[116:117], v[164:165], v[148:149] op_sel:[1,0,0]
	v_pk_fma_f32 v[198:199], v[116:117], v[166:167], v[198:199] op_sel:[1,0,0]
	v_fma_f32 v204, v117, v168, v204
	v_pk_fma_f32 v[170:171], v[118:119], v[164:165], v[170:171] op_sel:[1,0,0]
	v_pk_fma_f32 v[200:201], v[118:119], v[166:167], v[200:201] op_sel:[1,0,0]
	v_fma_f32 v206, v119, v168, v206
	s_waitcnt lgkmcnt(0)
	v_pk_fma_f32 v[172:173], v[120:121], v[164:165], v[172:173] op_sel_hi:[0,1,1]
	v_pk_fma_f32 v[202:203], v[120:121], v[166:167], v[202:203] op_sel_hi:[0,1,1]
	v_fma_f32 v208, v120, v168, v208
	v_pk_mul_f32 v[210:211], v[88:89], v[148:149] op_sel_hi:[0,1]
	v_pk_mul_f32 v[212:213], v[88:89], v[198:199] op_sel_hi:[0,1]
	v_mul_f32_e64 v214, v88, v204
	v_pk_fma_f32 v[210:211], v[88:89], v[170:171], v[210:211] op_sel:[1,0,0]
	v_pk_fma_f32 v[212:213], v[88:89], v[200:201], v[212:213] op_sel:[1,0,0]
	v_fma_f32 v214, v89, v206, v214
	v_pk_fma_f32 v[210:211], v[90:91], v[172:173], v[210:211] op_sel_hi:[0,1,1]
	v_pk_fma_f32 v[212:213], v[90:91], v[202:203], v[212:213] op_sel_hi:[0,1,1]
	v_fma_f32 v214, v90, v208, v214
	v_pk_fma_f32 v[210:211], v[120:121], v[114:115], v[210:211] op_sel:[1,0,0] neg_lo:[0,0,1] neg_hi:[0,0,1]
	v_pk_fma_f32 v[212:213], v[120:121], v[126:127], v[212:213] op_sel:[1,0,0] neg_lo:[0,0,1] neg_hi:[0,0,1]
	v_fma_f32 v214, v121, v150, -v214
	v_cmp_eq_u32_e64 s[10:11], 1, v123
	v_cmp_eq_u32_e64 s[14:15], 2, v123
	v_cmp_eq_u32_e64 s[20:21], 3, v123
	v_cmp_eq_u32_e64 s[22:23], 4, v123
	v_cmp_eq_u32_e64 s[30:31], 5, v123
	v_add_f32_dpp v114, v148, v148 wave_shr:1 row_mask:0xf bank_mask:0xf bound_ctrl:1
	v_add_f32_dpp v115, v149, v149 wave_shr:1 row_mask:0xf bank_mask:0xf bound_ctrl:1
	v_add_f32_dpp v126, v198, v198 wave_shr:1 row_mask:0xf bank_mask:0xf bound_ctrl:1
	v_add_f32_dpp v127, v199, v199 wave_shr:1 row_mask:0xf bank_mask:0xf bound_ctrl:1
	v_add_f32_dpp v150, v204, v204 wave_shr:1 row_mask:0xf bank_mask:0xf bound_ctrl:1
	v_add_f32_dpp v152, v170, v170 wave_shr:1 row_mask:0xf bank_mask:0xf bound_ctrl:1
	v_add_f32_dpp v153, v171, v171 wave_shr:1 row_mask:0xf bank_mask:0xf bound_ctrl:1
	v_add_f32_dpp v154, v200, v200 wave_shr:1 row_mask:0xf bank_mask:0xf bound_ctrl:1
	v_add_f32_dpp v155, v201, v201 wave_shr:1 row_mask:0xf bank_mask:0xf bound_ctrl:1
	v_add_f32_dpp v156, v206, v206 wave_shr:1 row_mask:0xf bank_mask:0xf bound_ctrl:1
	v_add_f32_dpp v158, v172, v172 wave_shr:1 row_mask:0xf bank_mask:0xf bound_ctrl:1
	v_add_f32_dpp v159, v173, v173 wave_shr:1 row_mask:0xf bank_mask:0xf bound_ctrl:1
	v_add_f32_dpp v160, v202, v202 wave_shr:1 row_mask:0xf bank_mask:0xf bound_ctrl:1
	v_add_f32_dpp v161, v203, v203 wave_shr:1 row_mask:0xf bank_mask:0xf bound_ctrl:1
	v_add_f32_dpp v162, v208, v208 wave_shr:1 row_mask:0xf bank_mask:0xf bound_ctrl:1
	v_add_f32_dpp v164, v210, v210 wave_shr:1 row_mask:0xf bank_mask:0xf bound_ctrl:1
	v_add_f32_dpp v165, v211, v211 wave_shr:1 row_mask:0xf bank_mask:0xf bound_ctrl:1
	v_add_f32_dpp v166, v212, v212 wave_shr:1 row_mask:0xf bank_mask:0xf bound_ctrl:1
	v_add_f32_dpp v167, v213, v213 wave_shr:1 row_mask:0xf bank_mask:0xf bound_ctrl:1
	v_add_f32_dpp v168, v214, v214 wave_shr:1 row_mask:0xf bank_mask:0xf bound_ctrl:1
	v_add_f32_dpp v114, v148, v114 wave_shl:1 row_mask:0xf bank_mask:0xf bound_ctrl:1
	v_add_f32_dpp v115, v149, v115 wave_shl:1 row_mask:0xf bank_mask:0xf bound_ctrl:1
	v_add_f32_dpp v126, v198, v126 wave_shl:1 row_mask:0xf bank_mask:0xf bound_ctrl:1
	v_add_f32_dpp v127, v199, v127 wave_shl:1 row_mask:0xf bank_mask:0xf bound_ctrl:1
	v_add_f32_dpp v150, v204, v150 wave_shl:1 row_mask:0xf bank_mask:0xf bound_ctrl:1
	v_add_f32_dpp v152, v170, v152 wave_shl:1 row_mask:0xf bank_mask:0xf bound_ctrl:1
	v_add_f32_dpp v153, v171, v153 wave_shl:1 row_mask:0xf bank_mask:0xf bound_ctrl:1
	v_add_f32_dpp v154, v200, v154 wave_shl:1 row_mask:0xf bank_mask:0xf bound_ctrl:1
	v_add_f32_dpp v155, v201, v155 wave_shl:1 row_mask:0xf bank_mask:0xf bound_ctrl:1
	v_add_f32_dpp v156, v206, v156 wave_shl:1 row_mask:0xf bank_mask:0xf bound_ctrl:1
	v_add_f32_dpp v158, v172, v158 wave_shl:1 row_mask:0xf bank_mask:0xf bound_ctrl:1
	v_add_f32_dpp v159, v173, v159 wave_shl:1 row_mask:0xf bank_mask:0xf bound_ctrl:1
	v_add_f32_dpp v160, v202, v160 wave_shl:1 row_mask:0xf bank_mask:0xf bound_ctrl:1
	v_add_f32_dpp v161, v203, v161 wave_shl:1 row_mask:0xf bank_mask:0xf bound_ctrl:1
	v_add_f32_dpp v162, v208, v162 wave_shl:1 row_mask:0xf bank_mask:0xf bound_ctrl:1
	v_add_f32_dpp v164, v210, v164 wave_shl:1 row_mask:0xf bank_mask:0xf bound_ctrl:1
	v_add_f32_dpp v165, v211, v165 wave_shl:1 row_mask:0xf bank_mask:0xf bound_ctrl:1
	v_add_f32_dpp v166, v212, v166 wave_shl:1 row_mask:0xf bank_mask:0xf bound_ctrl:1
	v_add_f32_dpp v167, v213, v167 wave_shl:1 row_mask:0xf bank_mask:0xf bound_ctrl:1
	v_add_f32_dpp v168, v214, v168 wave_shl:1 row_mask:0xf bank_mask:0xf bound_ctrl:1
	v_pk_add_f32 v[148:149], v[56:57], v[114:115]
	v_pk_add_f32 v[170:171], v[82:83], v[148:149]
	v_pk_add_f32 v[56:57], v[58:59], v[126:127]
	v_pk_add_f32 v[82:83], v[92:93], v[56:57]
	v_add_f32_e64 v58, v60, v150
	v_add_f32_e64 v92, v94, v58
	v_pk_add_f32 v[60:61], v[62:63], v[152:153]
	v_pk_add_f32 v[94:95], v[96:97], v[60:61]
	v_pk_add_f32 v[62:63], v[64:65], v[154:155]
	v_pk_add_f32 v[96:97], v[98:99], v[62:63]
	v_add_f32_e64 v64, v66, v156
	v_add_f32_e64 v98, v100, v64
	v_pk_add_f32 v[66:67], v[68:69], v[158:159]
	v_pk_add_f32 v[100:101], v[102:103], v[66:67]
	v_pk_add_f32 v[68:69], v[70:71], v[160:161]
	v_pk_add_f32 v[102:103], v[104:105], v[68:69]
	v_add_f32_e64 v70, v72, v162
	v_add_f32_e64 v104, v106, v70
	v_pk_add_f32 v[72:73], v[74:75], v[164:165]
	v_pk_add_f32 v[106:107], v[108:109], v[72:73]
	v_pk_add_f32 v[74:75], v[76:77], v[166:167]
	v_pk_add_f32 v[108:109], v[110:111], v[74:75]
	v_add_f32_e64 v76, v80, v168
	v_add_f32_e64 v110, v112, v76
	v_pk_fma_f32 v[106:107], v[36:37], v[170:171], v[106:107] op_sel_hi:[0,1,1]
	v_pk_fma_f32 v[108:109], v[36:37], v[82:83], v[108:109] op_sel_hi:[0,1,1]
	v_fma_f32 v110, v36, v92, v110
	v_pk_fma_f32 v[106:107], v[36:37], v[94:95], v[106:107] op_sel:[1,0,0]
	v_pk_fma_f32 v[108:109], v[36:37], v[96:97], v[108:109] op_sel:[1,0,0]
	v_fma_f32 v110, v37, v98, v110
	v_pk_fma_f32 v[106:107], v[38:39], v[100:101], v[106:107] op_sel_hi:[0,1,1]
	v_pk_fma_f32 v[108:109], v[38:39], v[102:103], v[108:109] op_sel_hi:[0,1,1]
	v_fma_f32 v110, v38, v104, v110
	v_cndmask_b32_e64 v80, 0, v1, s[10:11]
	v_cndmask_b32_e64 v81, 0, v1, s[14:15]
	v_cndmask_b32_e64 v112, 0, v1, s[20:21]
	v_cndmask_b32_e64 v113, 0, v1, s[22:23]
	v_cndmask_b32_e64 v172, 0, v1, s[30:31]
	v_pk_fma_f32 v[106:107], v[20:21], v[122:123], v[106:107] op_sel_hi:[1,0,1] neg_lo:[0,0,1] neg_hi:[0,0,1]
	v_pk_fma_f32 v[108:109], v[24:25], v[122:123], v[108:109] op_sel_hi:[1,0,1] neg_lo:[0,0,1] neg_hi:[0,0,1]
	v_fma_f32 v110, v30, v122, -v110
	s_add_i32 s4, s34, 0
	s_cmpk_lt_i32 s4, 0x201
	s_cselect_b64 s[12:13], s[0:1], 0
	v_pk_add_f32 v[106:107], v[106:107], v[80:81] neg_lo:[0,1] neg_hi:[0,1]
	v_pk_add_f32 v[108:109], v[108:109], v[112:113] neg_lo:[0,1] neg_hi:[0,1]
	v_add_f32_e64 v110, v110, -v172
	v_pk_mul_f32 v[198:199], v[106:107], v[106:107]
	v_pk_fma_f32 v[198:199], v[108:109], v[108:109], v[198:199]
	v_add_f32_e32 v198, v198, v199
	v_fma_f32 v198, v110, v110, v198
	v_cndmask_b32_e64 v199, 0, v198, s[12:13]
	v_add_f32_e32 v0, v0, v199
	s_add_i32 s4, s34, 5
	s_min_i32 s4, s4, 0x200
	s_mul_i32 s5, s4, 0x804
	s_add_i32 s5, s5, s35
	s_add_i32 s6, s5, 0x0
	s_add_i32 s7, s5, 0x101004
	s_add_i32 s8, s5, 0x202008
	s_add_i32 s11, s5, 0x30300c
	s_add_i32 s15, s5, 0x404010
	s_mul_i32 s9, s4, 0x180c
	s_add_i32 s9, s9, s33
	buffer_load_dword v20, v28, s[16:19], s6 offen nt
	buffer_load_dword v21, v28, s[16:19], s7 offen nt
	buffer_load_dword v24, v28, s[16:19], s8 offen nt
	buffer_load_dword v25, v28, s[16:19], s11 offen nt
	buffer_load_dword v30, v28, s[16:19], s15 offen nt
	buffer_load_dwordx3 v[36:38], v27, s[24:27], s9 offen nt
	s_waitcnt vmcnt(12)
	v_pk_mul_f32 v[80:81], v[2:3], v[8:9] op_sel_hi:[1,0]
	v_pk_mul_f32 v[82:83], v[4:5], v[8:9] op_sel_hi:[1,0]
	v_mul_f32_e64 v88, v6, v8
	v_pk_mul_f32 v[90:91], v[2:3], v[8:9] op_sel:[0,1]
	v_pk_mul_f32 v[92:93], v[4:5], v[8:9] op_sel:[0,1]
	v_mul_f32_e64 v94, v6, v9
	v_pk_mul_f32 v[96:97], v[2:3], v[10:11] op_sel_hi:[1,0]
	v_pk_mul_f32 v[98:99], v[4:5], v[10:11] op_sel_hi:[1,0]
	v_mul_f32_e64 v100, v6, v10
	v_add_f32_dpp v102, v2, v2 wave_shr:1 row_mask:0xf bank_mask:0xf bound_ctrl:1
	v_add_f32_dpp v103, v3, v3 wave_shr:1 row_mask:0xf bank_mask:0xf bound_ctrl:1
	v_add_f32_dpp v104, v4, v4 wave_shr:1 row_mask:0xf bank_mask:0xf bound_ctrl:1
	v_add_f32_dpp v105, v5, v5 wave_shr:1 row_mask:0xf bank_mask:0xf bound_ctrl:1
	v_add_f32_dpp v106, v6, v6 wave_shr:1 row_mask:0xf bank_mask:0xf bound_ctrl:1
	v_add_f32_dpp v108, v80, v80 wave_shr:1 row_mask:0xf bank_mask:0xf bound_ctrl:1
	v_add_f32_dpp v109, v81, v81 wave_shr:1 row_mask:0xf bank_mask:0xf bound_ctrl:1
	v_add_f32_dpp v110, v82, v82 wave_shr:1 row_mask:0xf bank_mask:0xf bound_ctrl:1
	v_add_f32_dpp v111, v83, v83 wave_shr:1 row_mask:0xf bank_mask:0xf bound_ctrl:1
	v_add_f32_dpp v112, v88, v88 wave_shr:1 row_mask:0xf bank_mask:0xf bound_ctrl:1
	v_add_f32_dpp v116, v90, v90 wave_shr:1 row_mask:0xf bank_mask:0xf bound_ctrl:1
	v_add_f32_dpp v117, v91, v91 wave_shr:1 row_mask:0xf bank_mask:0xf bound_ctrl:1
	v_add_f32_dpp v118, v92, v92 wave_shr:1 row_mask:0xf bank_mask:0xf bound_ctrl:1
	v_add_f32_dpp v119, v93, v93 wave_shr:1 row_mask:0xf bank_mask:0xf bound_ctrl:1
	v_add_f32_dpp v120, v94, v94 wave_shr:1 row_mask:0xf bank_mask:0xf bound_ctrl:1
	v_add_f32_dpp v122, v96, v96 wave_shr:1 row_mask:0xf bank_mask:0xf bound_ctrl:1
	v_add_f32_dpp v123, v97, v97 wave_shr:1 row_mask:0xf bank_mask:0xf bound_ctrl:1
	v_add_f32_dpp v170, v98, v98 wave_shr:1 row_mask:0xf bank_mask:0xf bound_ctrl:1
	v_add_f32_dpp v171, v99, v99 wave_shr:1 row_mask:0xf bank_mask:0xf bound_ctrl:1
	v_add_f32_dpp v172, v100, v100 wave_shr:1 row_mask:0xf bank_mask:0xf bound_ctrl:1
	v_add_f32_dpp v102, v2, v102 wave_shl:1 row_mask:0xf bank_mask:0xf bound_ctrl:1
	v_add_f32_dpp v103, v3, v103 wave_shl:1 row_mask:0xf bank_mask:0xf bound_ctrl:1
	v_add_f32_dpp v104, v4, v104 wave_shl:1 row_mask:0xf bank_mask:0xf bound_ctrl:1
	v_add_f32_dpp v105, v5, v105 wave_shl:1 row_mask:0xf bank_mask:0xf bound_ctrl:1
	v_add_f32_dpp v106, v6, v106 wave_shl:1 row_mask:0xf bank_mask:0xf bound_ctrl:1
	v_add_f32_dpp v108, v80, v108 wave_shl:1 row_mask:0xf bank_mask:0xf bound_ctrl:1
	v_add_f32_dpp v109, v81, v109 wave_shl:1 row_mask:0xf bank_mask:0xf bound_ctrl:1
	v_add_f32_dpp v110, v82, v110 wave_shl:1 row_mask:0xf bank_mask:0xf bound_ctrl:1
	v_add_f32_dpp v111, v83, v111 wave_shl:1 row_mask:0xf bank_mask:0xf bound_ctrl:1
	v_add_f32_dpp v112, v88, v112 wave_shl:1 row_mask:0xf bank_mask:0xf bound_ctrl:1
	v_add_f32_dpp v116, v90, v116 wave_shl:1 row_mask:0xf bank_mask:0xf bound_ctrl:1
	v_add_f32_dpp v117, v91, v117 wave_shl:1 row_mask:0xf bank_mask:0xf bound_ctrl:1
	v_add_f32_dpp v118, v92, v118 wave_shl:1 row_mask:0xf bank_mask:0xf bound_ctrl:1
	v_add_f32_dpp v119, v93, v119 wave_shl:1 row_mask:0xf bank_mask:0xf bound_ctrl:1
	v_add_f32_dpp v120, v94, v120 wave_shl:1 row_mask:0xf bank_mask:0xf bound_ctrl:1
	v_add_f32_dpp v122, v96, v122 wave_shl:1 row_mask:0xf bank_mask:0xf bound_ctrl:1
	v_add_f32_dpp v123, v97, v123 wave_shl:1 row_mask:0xf bank_mask:0xf bound_ctrl:1
	v_add_f32_dpp v170, v98, v170 wave_shl:1 row_mask:0xf bank_mask:0xf bound_ctrl:1
	v_add_f32_dpp v171, v99, v171 wave_shl:1 row_mask:0xf bank_mask:0xf bound_ctrl:1
	v_add_f32_dpp v172, v100, v172 wave_shl:1 row_mask:0xf bank_mask:0xf bound_ctrl:1
	s_barrier
	ds_read_b128 v[80:83], v23 offset:3072
	ds_read_b128 v[88:91], v23 offset:4096
	ds_read_b128 v[92:95], v23 offset:5120
	v_pk_add_f32 v[96:97], v[78:79], v[102:103]
	v_pk_add_f32 v[78:79], v[124:125], v[104:105]
	v_add_f32_e64 v98, v128, v106
	v_pk_add_f32 v[100:101], v[130:131], v[108:109]
	v_pk_add_f32 v[124:125], v[132:133], v[110:111]
	v_add_f32_e64 v128, v134, v112
	v_pk_add_f32 v[130:131], v[136:137], v[116:117]
	v_pk_add_f32 v[132:133], v[138:139], v[118:119]
	v_add_f32_e64 v134, v140, v120
	v_pk_add_f32 v[136:137], v[142:143], v[122:123]
	v_pk_add_f32 v[138:139], v[144:145], v[170:171]
	v_add_f32_e64 v140, v146, v172
	s_waitcnt lgkmcnt(2)
	v_pk_fma_f32 v[100:101], v[80:81], v[96:97], v[100:101] op_sel_hi:[0,1,1] neg_lo:[1,0,0] neg_hi:[1,0,0]
	v_pk_fma_f32 v[124:125], v[80:81], v[78:79], v[124:125] op_sel_hi:[0,1,1] neg_lo:[1,0,0] neg_hi:[1,0,0]
	v_fma_f32 v128, -v80, v98, v128
	v_pk_fma_f32 v[130:131], v[80:81], v[96:97], v[130:131] op_sel:[1,0,0] neg_lo:[1,0,0] neg_hi:[1,0,0]
	v_pk_fma_f32 v[132:133], v[80:81], v[78:79], v[132:133] op_sel:[1,0,0] neg_lo:[1,0,0] neg_hi:[1,0,0]
	v_fma_f32 v134, -v81, v98, v134
	v_pk_fma_f32 v[136:137], v[82:83], v[96:97], v[136:137] op_sel_hi:[0,1,1] neg_lo:[1,0,0] neg_hi:[1,0,0]
	v_pk_fma_f32 v[138:139], v[82:83], v[78:79], v[138:139] op_sel_hi:[0,1,1] neg_lo:[1,0,0] neg_hi:[1,0,0]
	v_fma_f32 v140, -v82, v98, v140
	v_pk_mul_f32 v[142:143], v[82:83], v[100:101] op_sel:[1,0]
	v_pk_mul_f32 v[198:199], v[82:83], v[124:125] op_sel:[1,0]
	v_mul_f32_e64 v204, v83, v128
	s_waitcnt lgkmcnt(1)
	v_pk_mul_f32 v[144:145], v[88:89], v[100:101] op_sel_hi:[0,1]
	v_pk_mul_f32 v[200:201], v[88:89], v[124:125] op_sel_hi:[0,1]
	v_mul_f32_e64 v206, v88, v128
	v_pk_mul_f32 v[146:147], v[88:89], v[100:101] op_sel:[1,0]
	v_pk_mul_f32 v[202:203], v[88:89], v[124:125] op_sel:[1,0]
	v_mul_f32_e64 v208, v89, v128
	v_pk_fma_f32 v[142:143], v[88:89], v[130:131], v[142:143] op_sel_hi:[0,1,1]
	v_pk_fma_f32 v[198:199], v[88:89], v[132:133], v[198:199] op_sel_hi:[0,1,1]
	v_fma_f32 v204, v88, v134, v204
	v_pk_fma_f32 v[144:145], v[90:91], v[130:131], v[144:145] op_sel_hi:[0,1,1]
	v_pk_fma_f32 v[200:201], v[90:91], v[132:133], v[200:201] op_sel_hi:[0,1,1]
	v_fma_f32 v206, v90, v134, v206
	v_pk_fma_f32 v[146:147], v[90:91], v[130:131], v[146:147] op_sel:[1,0,0]
	v_pk_fma_f32 v[202:203], v[90:91], v[132:133], v[202:203] op_sel:[1,0,0]
	v_fma_f32 v208, v91, v134, v208
	v_pk_fma_f32 v[142:143], v[88:89], v[136:137], v[142:143] op_sel:[1,0,0]
	v_pk_fma_f32 v[198:199], v[88:89], v[138:139], v[198:199] op_sel:[1,0,0]
	v_fma_f32 v204, v89, v140, v204
	v_pk_fma_f32 v[144:145], v[90:91], v[136:137], v[144:145] op_sel:[1,0,0]
	v_pk_fma_f32 v[200:201], v[90:91], v[138:139], v[200:201] op_sel:[1,0,0]
	v_fma_f32 v206, v91, v140, v206
	s_waitcnt lgkmcnt(0)
	v_pk_fma_f32 v[146:147], v[92:93], v[136:137], v[146:147] op_sel_hi:[0,1,1]
	v_pk_fma_f32 v[202:203], v[92:93], v[138:139], v[202:203] op_sel_hi:[0,1,1]
	v_fma_f32 v208, v92, v140, v208
	v_pk_mul_f32 v[210:211], v[80:81], v[142:143] op_sel_hi:[0,1]
	v_pk_mul_f32 v[212:213], v[80:81], v[198:199] op_sel_hi:[0,1]
	v_mul_f32_e64 v214, v80, v204
	v_pk_fma_f32 v[210:211], v[80:81], v[144:145], v[210:211] op_sel:[1,0,0]
	v_pk_fma_f32 v[212:213], v[80:81], v[200:201], v[212:213] op_sel:[1,0,0]
	v_fma_f32 v214, v81, v206, v214
	v_pk_fma_f32 v[210:211], v[82:83], v[146:147], v[210:211] op_sel_hi:[0,1,1]
	v_pk_fma_f32 v[212:213], v[82:83], v[202:203], v[212:213] op_sel_hi:[0,1,1]
	v_fma_f32 v214, v82, v208, v214
	v_pk_fma_f32 v[210:211], v[92:93], v[96:97], v[210:211] op_sel:[1,0,0] neg_lo:[0,0,1] neg_hi:[0,0,1]
	v_pk_fma_f32 v[212:213], v[92:93], v[78:79], v[212:213] op_sel:[1,0,0] neg_lo:[0,0,1] neg_hi:[0,0,1]
	v_fma_f32 v214, v93, v98, -v214
	v_cmp_eq_u32_e64 s[10:11], 1, v95
	v_cmp_eq_u32_e64 s[14:15], 2, v95
	v_cmp_eq_u32_e64 s[20:21], 3, v95
	v_cmp_eq_u32_e64 s[22:23], 4, v95
	v_cmp_eq_u32_e64 s[30:31], 5, v95
	v_add_f32_dpp v78, v142, v142 wave_shr:1 row_mask:0xf bank_mask:0xf bound_ctrl:1
	v_add_f32_dpp v79, v143, v143 wave_shr:1 row_mask:0xf bank_mask:0xf bound_ctrl:1
	v_add_f32_dpp v96, v198, v198 wave_shr:1 row_mask:0xf bank_mask:0xf bound_ctrl:1
	v_add_f32_dpp v97, v199, v199 wave_shr:1 row_mask:0xf bank_mask:0xf bound_ctrl:1
	v_add_f32_dpp v98, v204, v204 wave_shr:1 row_mask:0xf bank_mask:0xf bound_ctrl:1
	v_add_f32_dpp v100, v144, v144 wave_shr:1 row_mask:0xf bank_mask:0xf bound_ctrl:1
	v_add_f32_dpp v101, v145, v145 wave_shr:1 row_mask:0xf bank_mask:0xf bound_ctrl:1
	v_add_f32_dpp v124, v200, v200 wave_shr:1 row_mask:0xf bank_mask:0xf bound_ctrl:1
	v_add_f32_dpp v125, v201, v201 wave_shr:1 row_mask:0xf bank_mask:0xf bound_ctrl:1
	v_add_f32_dpp v128, v206, v206 wave_shr:1 row_mask:0xf bank_mask:0xf bound_ctrl:1
	v_add_f32_dpp v130, v146, v146 wave_shr:1 row_mask:0xf bank_mask:0xf bound_ctrl:1
	v_add_f32_dpp v131, v147, v147 wave_shr:1 row_mask:0xf bank_mask:0xf bound_ctrl:1
	v_add_f32_dpp v132, v202, v202 wave_shr:1 row_mask:0xf bank_mask:0xf bound_ctrl:1
	v_add_f32_dpp v133, v203, v203 wave_shr:1 row_mask:0xf bank_mask:0xf bound_ctrl:1
	v_add_f32_dpp v134, v208, v208 wave_shr:1 row_mask:0xf bank_mask:0xf bound_ctrl:1
	v_add_f32_dpp v136, v210, v210 wave_shr:1 row_mask:0xf bank_mask:0xf bound_ctrl:1
	v_add_f32_dpp v137, v211, v211 wave_shr:1 row_mask:0xf bank_mask:0xf bound_ctrl:1
	v_add_f32_dpp v138, v212, v212 wave_shr:1 row_mask:0xf bank_mask:0xf bound_ctrl:1
	v_add_f32_dpp v139, v213, v213 wave_shr:1 row_mask:0xf bank_mask:0xf bound_ctrl:1
	v_add_f32_dpp v140, v214, v214 wave_shr:1 row_mask:0xf bank_mask:0xf bound_ctrl:1
	v_add_f32_dpp v78, v142, v78 wave_shl:1 row_mask:0xf bank_mask:0xf bound_ctrl:1
	v_add_f32_dpp v79, v143, v79 wave_shl:1 row_mask:0xf bank_mask:0xf bound_ctrl:1
	v_add_f32_dpp v96, v198, v96 wave_shl:1 row_mask:0xf bank_mask:0xf bound_ctrl:1
	v_add_f32_dpp v97, v199, v97 wave_shl:1 row_mask:0xf bank_mask:0xf bound_ctrl:1
	v_add_f32_dpp v98, v204, v98 wave_shl:1 row_mask:0xf bank_mask:0xf bound_ctrl:1
	v_add_f32_dpp v100, v144, v100 wave_shl:1 row_mask:0xf bank_mask:0xf bound_ctrl:1
	v_add_f32_dpp v101, v145, v101 wave_shl:1 row_mask:0xf bank_mask:0xf bound_ctrl:1
	v_add_f32_dpp v124, v200, v124 wave_shl:1 row_mask:0xf bank_mask:0xf bound_ctrl:1
	v_add_f32_dpp v125, v201, v125 wave_shl:1 row_mask:0xf bank_mask:0xf bound_ctrl:1
	v_add_f32_dpp v128, v206, v128 wave_shl:1 row_mask:0xf bank_mask:0xf bound_ctrl:1
	v_add_f32_dpp v130, v146, v130 wave_shl:1 row_mask:0xf bank_mask:0xf bound_ctrl:1
	v_add_f32_dpp v131, v147, v131 wave_shl:1 row_mask:0xf bank_mask:0xf bound_ctrl:1
	v_add_f32_dpp v132, v202, v132 wave_shl:1 row_mask:0xf bank_mask:0xf bound_ctrl:1
	v_add_f32_dpp v133, v203, v133 wave_shl:1 row_mask:0xf bank_mask:0xf bound_ctrl:1
	v_add_f32_dpp v134, v208, v134 wave_shl:1 row_mask:0xf bank_mask:0xf bound_ctrl:1
	v_add_f32_dpp v136, v210, v136 wave_shl:1 row_mask:0xf bank_mask:0xf bound_ctrl:1
	v_add_f32_dpp v137, v211, v137 wave_shl:1 row_mask:0xf bank_mask:0xf bound_ctrl:1
	v_add_f32_dpp v138, v212, v138 wave_shl:1 row_mask:0xf bank_mask:0xf bound_ctrl:1
	v_add_f32_dpp v139, v213, v139 wave_shl:1 row_mask:0xf bank_mask:0xf bound_ctrl:1
	v_add_f32_dpp v140, v214, v140 wave_shl:1 row_mask:0xf bank_mask:0xf bound_ctrl:1
	v_pk_add_f32 v[142:143], v[148:149], v[78:79]
	v_pk_add_f32 v[144:145], v[56:57], v[96:97]
	v_add_f32_e64 v56, v58, v98
	v_pk_add_f32 v[58:59], v[60:61], v[100:101]
	v_pk_add_f32 v[60:61], v[62:63], v[124:125]
	v_add_f32_e64 v62, v64, v128
	v_pk_add_f32 v[64:65], v[66:67], v[130:131]
	v_pk_add_f32 v[66:67], v[68:69], v[132:133]
	v_add_f32_e64 v68, v70, v134
	v_pk_add_f32 v[70:71], v[72:73], v[136:137]
	v_pk_add_f32 v[72:73], v[74:75], v[138:139]
	v_add_f32_e64 v74, v76, v140
	v_pk_fma_f32 v[70:71], v[48:49], v[142:143], v[70:71] op_sel_hi:[0,1,1]
	v_pk_fma_f32 v[72:73], v[48:49], v[144:145], v[72:73] op_sel_hi:[0,1,1]
	v_fma_f32 v74, v48, v56, v74
	v_pk_fma_f32 v[70:71], v[48:49], v[58:59], v[70:71] op_sel:[1,0,0]
	v_pk_fma_f32 v[72:73], v[48:49], v[60:61], v[72:73] op_sel:[1,0,0]
	v_fma_f32 v74, v49, v62, v74
	v_pk_fma_f32 v[70:71], v[50:51], v[64:65], v[70:71] op_sel_hi:[0,1,1]
	v_pk_fma_f32 v[72:73], v[50:51], v[66:67], v[72:73] op_sel_hi:[0,1,1]
	v_fma_f32 v74, v50, v68, v74
	v_cndmask_b32_e64 v76, 0, v1, s[10:11]
	v_cndmask_b32_e64 v77, 0, v1, s[14:15]
	v_cndmask_b32_e64 v146, 0, v1, s[20:21]
	v_cndmask_b32_e64 v147, 0, v1, s[22:23]
	v_cndmask_b32_e64 v148, 0, v1, s[30:31]
	v_pk_fma_f32 v[70:71], v[40:41], v[94:95], v[70:71] op_sel_hi:[1,0,1] neg_lo:[0,0,1] neg_hi:[0,0,1]
	v_pk_fma_f32 v[72:73], v[42:43], v[94:95], v[72:73] op_sel_hi:[1,0,1] neg_lo:[0,0,1] neg_hi:[0,0,1]
	v_fma_f32 v74, v44, v94, -v74
	s_add_i32 s4, s34, 1
	s_cmpk_lt_i32 s4, 0x201
	s_cselect_b64 s[12:13], s[0:1], 0
	v_pk_add_f32 v[70:71], v[70:71], v[76:77] neg_lo:[0,1] neg_hi:[0,1]
	v_pk_add_f32 v[72:73], v[72:73], v[146:147] neg_lo:[0,1] neg_hi:[0,1]
	v_add_f32_e64 v74, v74, -v148
	v_pk_mul_f32 v[198:199], v[70:71], v[70:71]
	v_pk_fma_f32 v[198:199], v[72:73], v[72:73], v[198:199]
	v_add_f32_e32 v198, v198, v199
	v_fma_f32 v198, v74, v74, v198
	v_cndmask_b32_e64 v199, 0, v198, s[12:13]
	v_add_f32_e32 v0, v0, v199
	s_add_i32 s4, s34, 6
	s_min_i32 s4, s4, 0x200
	s_mul_i32 s5, s4, 0x804
	s_add_i32 s5, s5, s35
	s_add_i32 s6, s5, 0x0
	s_add_i32 s7, s5, 0x101004
	s_add_i32 s8, s5, 0x202008
	s_add_i32 s11, s5, 0x30300c
	s_add_i32 s15, s5, 0x404010
	s_mul_i32 s9, s4, 0x180c
	s_add_i32 s9, s9, s33
	buffer_load_dword v40, v28, s[16:19], s6 offen nt
	buffer_load_dword v41, v28, s[16:19], s7 offen nt
	buffer_load_dword v42, v28, s[16:19], s8 offen nt
	buffer_load_dword v43, v28, s[16:19], s11 offen nt
	buffer_load_dword v44, v28, s[16:19], s15 offen nt
	buffer_load_dwordx3 v[48:50], v27, s[24:27], s9 offen nt
	s_waitcnt vmcnt(12)
	v_pk_mul_f32 v[56:57], v[12:13], v[32:33] op_sel_hi:[1,0]
	v_pk_mul_f32 v[58:59], v[14:15], v[32:33] op_sel_hi:[1,0]
	v_mul_f32_e64 v60, v16, v32
	v_pk_mul_f32 v[62:63], v[12:13], v[32:33] op_sel:[0,1]
	v_pk_mul_f32 v[64:65], v[14:15], v[32:33] op_sel:[0,1]
	v_mul_f32_e64 v66, v16, v33
	v_pk_mul_f32 v[68:69], v[12:13], v[34:35] op_sel_hi:[1,0]
	v_pk_mul_f32 v[70:71], v[14:15], v[34:35] op_sel_hi:[1,0]
	v_mul_f32_e64 v72, v16, v34
	v_add_f32_dpp v74, v12, v12 wave_shr:1 row_mask:0xf bank_mask:0xf bound_ctrl:1
	v_add_f32_dpp v75, v13, v13 wave_shr:1 row_mask:0xf bank_mask:0xf bound_ctrl:1
	v_add_f32_dpp v76, v14, v14 wave_shr:1 row_mask:0xf bank_mask:0xf bound_ctrl:1
	v_add_f32_dpp v77, v15, v15 wave_shr:1 row_mask:0xf bank_mask:0xf bound_ctrl:1
	v_add_f32_dpp v80, v16, v16 wave_shr:1 row_mask:0xf bank_mask:0xf bound_ctrl:1
	v_add_f32_dpp v82, v56, v56 wave_shr:1 row_mask:0xf bank_mask:0xf bound_ctrl:1
	v_add_f32_dpp v83, v57, v57 wave_shr:1 row_mask:0xf bank_mask:0xf bound_ctrl:1
	v_add_f32_dpp v88, v58, v58 wave_shr:1 row_mask:0xf bank_mask:0xf bound_ctrl:1
	v_add_f32_dpp v89, v59, v59 wave_shr:1 row_mask:0xf bank_mask:0xf bound_ctrl:1
	v_add_f32_dpp v90, v60, v60 wave_shr:1 row_mask:0xf bank_mask:0xf bound_ctrl:1
	v_add_f32_dpp v92, v62, v62 wave_shr:1 row_mask:0xf bank_mask:0xf bound_ctrl:1
	v_add_f32_dpp v93, v63, v63 wave_shr:1 row_mask:0xf bank_mask:0xf bound_ctrl:1
	v_add_f32_dpp v94, v64, v64 wave_shr:1 row_mask:0xf bank_mask:0xf bound_ctrl:1
	v_add_f32_dpp v95, v65, v65 wave_shr:1 row_mask:0xf bank_mask:0xf bound_ctrl:1
	v_add_f32_dpp v142, v66, v66 wave_shr:1 row_mask:0xf bank_mask:0xf bound_ctrl:1
	v_add_f32_dpp v144, v68, v68 wave_shr:1 row_mask:0xf bank_mask:0xf bound_ctrl:1
	v_add_f32_dpp v145, v69, v69 wave_shr:1 row_mask:0xf bank_mask:0xf bound_ctrl:1
	v_add_f32_dpp v146, v70, v70 wave_shr:1 row_mask:0xf bank_mask:0xf bound_ctrl:1
	v_add_f32_dpp v147, v71, v71 wave_shr:1 row_mask:0xf bank_mask:0xf bound_ctrl:1
	v_add_f32_dpp v148, v72, v72 wave_shr:1 row_mask:0xf bank_mask:0xf bound_ctrl:1
	v_add_f32_dpp v74, v12, v74 wave_shl:1 row_mask:0xf bank_mask:0xf bound_ctrl:1
	v_add_f32_dpp v75, v13, v75 wave_shl:1 row_mask:0xf bank_mask:0xf bound_ctrl:1
	v_add_f32_dpp v76, v14, v76 wave_shl:1 row_mask:0xf bank_mask:0xf bound_ctrl:1
	v_add_f32_dpp v77, v15, v77 wave_shl:1 row_mask:0xf bank_mask:0xf bound_ctrl:1
	v_add_f32_dpp v80, v16, v80 wave_shl:1 row_mask:0xf bank_mask:0xf bound_ctrl:1
	v_add_f32_dpp v82, v56, v82 wave_shl:1 row_mask:0xf bank_mask:0xf bound_ctrl:1
	v_add_f32_dpp v83, v57, v83 wave_shl:1 row_mask:0xf bank_mask:0xf bound_ctrl:1
	v_add_f32_dpp v88, v58, v88 wave_shl:1 row_mask:0xf bank_mask:0xf bound_ctrl:1
	v_add_f32_dpp v89, v59, v89 wave_shl:1 row_mask:0xf bank_mask:0xf bound_ctrl:1
	v_add_f32_dpp v90, v60, v90 wave_shl:1 row_mask:0xf bank_mask:0xf bound_ctrl:1
	v_add_f32_dpp v92, v62, v92 wave_shl:1 row_mask:0xf bank_mask:0xf bound_ctrl:1
	v_add_f32_dpp v93, v63, v93 wave_shl:1 row_mask:0xf bank_mask:0xf bound_ctrl:1
	v_add_f32_dpp v94, v64, v94 wave_shl:1 row_mask:0xf bank_mask:0xf bound_ctrl:1
	v_add_f32_dpp v95, v65, v95 wave_shl:1 row_mask:0xf bank_mask:0xf bound_ctrl:1
	v_add_f32_dpp v142, v66, v142 wave_shl:1 row_mask:0xf bank_mask:0xf bound_ctrl:1
	v_add_f32_dpp v144, v68, v144 wave_shl:1 row_mask:0xf bank_mask:0xf bound_ctrl:1
	v_add_f32_dpp v145, v69, v145 wave_shl:1 row_mask:0xf bank_mask:0xf bound_ctrl:1
	v_add_f32_dpp v146, v70, v146 wave_shl:1 row_mask:0xf bank_mask:0xf bound_ctrl:1
	v_add_f32_dpp v147, v71, v147 wave_shl:1 row_mask:0xf bank_mask:0xf bound_ctrl:1
	v_add_f32_dpp v148, v72, v148 wave_shl:1 row_mask:0xf bank_mask:0xf bound_ctrl:1
	s_barrier
	ds_read_b128 v[56:59], v23 offset:0
	ds_read_b128 v[60:63], v23 offset:1024
	ds_read_b128 v[64:67], v23 offset:2048
	v_pk_add_f32 v[68:69], v[102:103], v[74:75]
	v_pk_add_f32 v[70:71], v[174:175], v[68:69]
	v_pk_add_f32 v[72:73], v[104:105], v[76:77]
	v_pk_add_f32 v[102:103], v[176:177], v[72:73]
	v_add_f32_e64 v104, v106, v80
	v_add_f32_e64 v174, v178, v104
	v_pk_add_f32 v[106:107], v[108:109], v[82:83]
	v_pk_add_f32 v[176:177], v[180:181], v[106:107]
	v_pk_add_f32 v[108:109], v[110:111], v[88:89]
	v_pk_add_f32 v[178:179], v[182:183], v[108:109]
	v_add_f32_e64 v110, v112, v90
	v_add_f32_e64 v180, v184, v110
	v_pk_add_f32 v[112:113], v[116:117], v[92:93]
	v_pk_add_f32 v[182:183], v[186:187], v[112:113]
	v_pk_add_f32 v[116:117], v[118:119], v[94:95]
	v_pk_add_f32 v[184:185], v[188:189], v[116:117]
	v_add_f32_e64 v118, v120, v142
	v_add_f32_e64 v186, v190, v118
	v_pk_add_f32 v[120:121], v[122:123], v[144:145]
	v_pk_add_f32 v[188:189], v[192:193], v[120:121]
	v_pk_add_f32 v[122:123], v[170:171], v[146:147]
	v_pk_add_f32 v[190:191], v[194:195], v[122:123]
	v_add_f32_e64 v170, v172, v148
	v_add_f32_e64 v192, v196, v170
	s_waitcnt lgkmcnt(2)
	v_pk_fma_f32 v[176:177], v[56:57], v[70:71], v[176:177] op_sel_hi:[0,1,1] neg_lo:[1,0,0] neg_hi:[1,0,0]
	v_pk_fma_f32 v[178:179], v[56:57], v[102:103], v[178:179] op_sel_hi:[0,1,1] neg_lo:[1,0,0] neg_hi:[1,0,0]
	v_fma_f32 v180, -v56, v174, v180
	v_pk_fma_f32 v[182:183], v[56:57], v[70:71], v[182:183] op_sel:[1,0,0] neg_lo:[1,0,0] neg_hi:[1,0,0]
	v_pk_fma_f32 v[184:185], v[56:57], v[102:103], v[184:185] op_sel:[1,0,0] neg_lo:[1,0,0] neg_hi:[1,0,0]
	v_fma_f32 v186, -v57, v174, v186
	v_pk_fma_f32 v[188:189], v[58:59], v[70:71], v[188:189] op_sel_hi:[0,1,1] neg_lo:[1,0,0] neg_hi:[1,0,0]
	v_pk_fma_f32 v[190:191], v[58:59], v[102:103], v[190:191] op_sel_hi:[0,1,1] neg_lo:[1,0,0] neg_hi:[1,0,0]
	v_fma_f32 v192, -v58, v174, v192
	v_pk_mul_f32 v[172:173], v[58:59], v[176:177] op_sel:[1,0]
	v_pk_mul_f32 v[198:199], v[58:59], v[178:179] op_sel:[1,0]
	v_mul_f32_e64 v204, v59, v180
	s_waitcnt lgkmcnt(1)
	v_pk_mul_f32 v[194:195], v[60:61], v[176:177] op_sel_hi:[0,1]
	v_pk_mul_f32 v[200:201], v[60:61], v[178:179] op_sel_hi:[0,1]
	v_mul_f32_e64 v206, v60, v180
	v_pk_mul_f32 v[196:197], v[60:61], v[176:177] op_sel:[1,0]
	v_pk_mul_f32 v[202:203], v[60:61], v[178:179] op_sel:[1,0]
	v_mul_f32_e64 v208, v61, v180
	v_pk_fma_f32 v[172:173], v[60:61], v[182:183], v[172:173] op_sel_hi:[0,1,1]
	v_pk_fma_f32 v[198:199], v[60:61], v[184:185], v[198:199] op_sel_hi:[0,1,1]
	v_fma_f32 v204, v60, v186, v204
	v_pk_fma_f32 v[194:195], v[62:63], v[182:183], v[194:195] op_sel_hi:[0,1,1]
	v_pk_fma_f32 v[200:201], v[62:63], v[184:185], v[200:201] op_sel_hi:[0,1,1]
	v_fma_f32 v206, v62, v186, v206
	v_pk_fma_f32 v[196:197], v[62:63], v[182:183], v[196:197] op_sel:[1,0,0]
	v_pk_fma_f32 v[202:203], v[62:63], v[184:185], v[202:203] op_sel:[1,0,0]
	v_fma_f32 v208, v63, v186, v208
	v_pk_fma_f32 v[172:173], v[60:61], v[188:189], v[172:173] op_sel:[1,0,0]
	v_pk_fma_f32 v[198:199], v[60:61], v[190:191], v[198:199] op_sel:[1,0,0]
	v_fma_f32 v204, v61, v192, v204
	v_pk_fma_f32 v[194:195], v[62:63], v[188:189], v[194:195] op_sel:[1,0,0]
	v_pk_fma_f32 v[200:201], v[62:63], v[190:191], v[200:201] op_sel:[1,0,0]
	v_fma_f32 v206, v63, v192, v206
	s_waitcnt lgkmcnt(0)
	v_pk_fma_f32 v[196:197], v[64:65], v[188:189], v[196:197] op_sel_hi:[0,1,1]
	v_pk_fma_f32 v[202:203], v[64:65], v[190:191], v[202:203] op_sel_hi:[0,1,1]
	v_fma_f32 v208, v64, v192, v208
	v_pk_mul_f32 v[210:211], v[56:57], v[172:173] op_sel_hi:[0,1]
	v_pk_mul_f32 v[212:213], v[56:57], v[198:199] op_sel_hi:[0,1]
	v_mul_f32_e64 v214, v56, v204
	v_pk_fma_f32 v[210:211], v[56:57], v[194:195], v[210:211] op_sel:[1,0,0]
	v_pk_fma_f32 v[212:213], v[56:57], v[200:201], v[212:213] op_sel:[1,0,0]
	v_fma_f32 v214, v57, v206, v214
	v_pk_fma_f32 v[210:211], v[58:59], v[196:197], v[210:211] op_sel_hi:[0,1,1]
	v_pk_fma_f32 v[212:213], v[58:59], v[202:203], v[212:213] op_sel_hi:[0,1,1]
	v_fma_f32 v214, v58, v208, v214
	v_pk_fma_f32 v[210:211], v[64:65], v[70:71], v[210:211] op_sel:[1,0,0] neg_lo:[0,0,1] neg_hi:[0,0,1]
	v_pk_fma_f32 v[212:213], v[64:65], v[102:103], v[212:213] op_sel:[1,0,0] neg_lo:[0,0,1] neg_hi:[0,0,1]
	v_fma_f32 v214, v65, v174, -v214
	v_cmp_eq_u32_e64 s[10:11], 1, v67
	v_cmp_eq_u32_e64 s[14:15], 2, v67
	v_cmp_eq_u32_e64 s[20:21], 3, v67
	v_cmp_eq_u32_e64 s[22:23], 4, v67
	v_cmp_eq_u32_e64 s[30:31], 5, v67
	v_add_f32_dpp v70, v172, v172 wave_shr:1 row_mask:0xf bank_mask:0xf bound_ctrl:1
	v_add_f32_dpp v71, v173, v173 wave_shr:1 row_mask:0xf bank_mask:0xf bound_ctrl:1
	v_add_f32_dpp v102, v198, v198 wave_shr:1 row_mask:0xf bank_mask:0xf bound_ctrl:1
	v_add_f32_dpp v103, v199, v199 wave_shr:1 row_mask:0xf bank_mask:0xf bound_ctrl:1
	v_add_f32_dpp v174, v204, v204 wave_shr:1 row_mask:0xf bank_mask:0xf bound_ctrl:1
	v_add_f32_dpp v176, v194, v194 wave_shr:1 row_mask:0xf bank_mask:0xf bound_ctrl:1
	v_add_f32_dpp v177, v195, v195 wave_shr:1 row_mask:0xf bank_mask:0xf bound_ctrl:1
	v_add_f32_dpp v178, v200, v200 wave_shr:1 row_mask:0xf bank_mask:0xf bound_ctrl:1
	v_add_f32_dpp v179, v201, v201 wave_shr:1 row_mask:0xf bank_mask:0xf bound_ctrl:1
	v_add_f32_dpp v180, v206, v206 wave_shr:1 row_mask:0xf bank_mask:0xf bound_ctrl:1
	v_add_f32_dpp v182, v196, v196 wave_shr:1 row_mask:0xf bank_mask:0xf bound_ctrl:1
	v_add_f32_dpp v183, v197, v197 wave_shr:1 row_mask:0xf bank_mask:0xf bound_ctrl:1
	v_add_f32_dpp v184, v202, v202 wave_shr:1 row_mask:0xf bank_mask:0xf bound_ctrl:1
	v_add_f32_dpp v185, v203, v203 wave_shr:1 row_mask:0xf bank_mask:0xf bound_ctrl:1
	v_add_f32_dpp v186, v208, v208 wave_shr:1 row_mask:0xf bank_mask:0xf bound_ctrl:1
	v_add_f32_dpp v188, v210, v210 wave_shr:1 row_mask:0xf bank_mask:0xf bound_ctrl:1
	v_add_f32_dpp v189, v211, v211 wave_shr:1 row_mask:0xf bank_mask:0xf bound_ctrl:1
	v_add_f32_dpp v190, v212, v212 wave_shr:1 row_mask:0xf bank_mask:0xf bound_ctrl:1
	v_add_f32_dpp v191, v213, v213 wave_shr:1 row_mask:0xf bank_mask:0xf bound_ctrl:1
	v_add_f32_dpp v192, v214, v214 wave_shr:1 row_mask:0xf bank_mask:0xf bound_ctrl:1
	v_add_f32_dpp v70, v172, v70 wave_shl:1 row_mask:0xf bank_mask:0xf bound_ctrl:1
	v_add_f32_dpp v71, v173, v71 wave_shl:1 row_mask:0xf bank_mask:0xf bound_ctrl:1
	v_add_f32_dpp v102, v198, v102 wave_shl:1 row_mask:0xf bank_mask:0xf bound_ctrl:1
	v_add_f32_dpp v103, v199, v103 wave_shl:1 row_mask:0xf bank_mask:0xf bound_ctrl:1
	v_add_f32_dpp v174, v204, v174 wave_shl:1 row_mask:0xf bank_mask:0xf bound_ctrl:1
	v_add_f32_dpp v176, v194, v176 wave_shl:1 row_mask:0xf bank_mask:0xf bound_ctrl:1
	v_add_f32_dpp v177, v195, v177 wave_shl:1 row_mask:0xf bank_mask:0xf bound_ctrl:1
	v_add_f32_dpp v178, v200, v178 wave_shl:1 row_mask:0xf bank_mask:0xf bound_ctrl:1
	v_add_f32_dpp v179, v201, v179 wave_shl:1 row_mask:0xf bank_mask:0xf bound_ctrl:1
	v_add_f32_dpp v180, v206, v180 wave_shl:1 row_mask:0xf bank_mask:0xf bound_ctrl:1
	v_add_f32_dpp v182, v196, v182 wave_shl:1 row_mask:0xf bank_mask:0xf bound_ctrl:1
	v_add_f32_dpp v183, v197, v183 wave_shl:1 row_mask:0xf bank_mask:0xf bound_ctrl:1
	v_add_f32_dpp v184, v202, v184 wave_shl:1 row_mask:0xf bank_mask:0xf bound_ctrl:1
	v_add_f32_dpp v185, v203, v185 wave_shl:1 row_mask:0xf bank_mask:0xf bound_ctrl:1
	v_add_f32_dpp v186, v208, v186 wave_shl:1 row_mask:0xf bank_mask:0xf bound_ctrl:1
	v_add_f32_dpp v188, v210, v188 wave_shl:1 row_mask:0xf bank_mask:0xf bound_ctrl:1
	v_add_f32_dpp v189, v211, v189 wave_shl:1 row_mask:0xf bank_mask:0xf bound_ctrl:1
	v_add_f32_dpp v190, v212, v190 wave_shl:1 row_mask:0xf bank_mask:0xf bound_ctrl:1
	v_add_f32_dpp v191, v213, v191 wave_shl:1 row_mask:0xf bank_mask:0xf bound_ctrl:1
	v_add_f32_dpp v192, v214, v192 wave_shl:1 row_mask:0xf bank_mask:0xf bound_ctrl:1
	v_pk_add_f32 v[172:173], v[78:79], v[70:71]
	v_pk_add_f32 v[194:195], v[114:115], v[172:173]
	v_pk_add_f32 v[78:79], v[96:97], v[102:103]
	v_pk_add_f32 v[114:115], v[126:127], v[78:79]
	v_add_f32_e64 v96, v98, v174
	v_add_f32_e64 v126, v150, v96
	v_pk_add_f32 v[98:99], v[100:101], v[176:177]
	v_pk_add_f32 v[150:151], v[152:153], v[98:99]
	v_pk_add_f32 v[100:101], v[124:125], v[178:179]
	v_pk_add_f32 v[152:153], v[154:155], v[100:101]
	v_add_f32_e64 v124, v128, v180
	v_add_f32_e64 v154, v156, v124
	v_pk_add_f32 v[128:129], v[130:131], v[182:183]
	v_pk_add_f32 v[156:157], v[158:159], v[128:129]
	v_pk_add_f32 v[130:131], v[132:133], v[184:185]
	v_pk_add_f32 v[158:159], v[160:161], v[130:131]
	v_add_f32_e64 v132, v134, v186
	v_add_f32_e64 v160, v162, v132
	v_pk_add_f32 v[134:135], v[136:137], v[188:189]
	v_pk_add_f32 v[162:163], v[164:165], v[134:135]
	v_pk_add_f32 v[136:137], v[138:139], v[190:191]
	v_pk_add_f32 v[164:165], v[166:167], v[136:137]
	v_add_f32_e64 v138, v140, v192
	v_add_f32_e64 v166, v168, v138
	v_pk_fma_f32 v[162:163], v[84:85], v[194:195], v[162:163] op_sel_hi:[0,1,1]
	v_pk_fma_f32 v[164:165], v[84:85], v[114:115], v[164:165] op_sel_hi:[0,1,1]
	v_fma_f32 v166, v84, v126, v166
	v_pk_fma_f32 v[162:163], v[84:85], v[150:151], v[162:163] op_sel:[1,0,0]
	v_pk_fma_f32 v[164:165], v[84:85], v[152:153], v[164:165] op_sel:[1,0,0]
	v_fma_f32 v166, v85, v154, v166
	v_pk_fma_f32 v[162:163], v[86:87], v[156:157], v[162:163] op_sel_hi:[0,1,1]
	v_pk_fma_f32 v[164:165], v[86:87], v[158:159], v[164:165] op_sel_hi:[0,1,1]
	v_fma_f32 v166, v86, v160, v166
	v_cndmask_b32_e64 v140, 0, v1, s[10:11]
	v_cndmask_b32_e64 v141, 0, v1, s[14:15]
	v_cndmask_b32_e64 v168, 0, v1, s[20:21]
	v_cndmask_b32_e64 v169, 0, v1, s[22:23]
	v_cndmask_b32_e64 v196, 0, v1, s[30:31]
	v_pk_fma_f32 v[162:163], v[46:47], v[66:67], v[162:163] op_sel_hi:[1,0,1] neg_lo:[0,0,1] neg_hi:[0,0,1]
	v_pk_fma_f32 v[164:165], v[52:53], v[66:67], v[164:165] op_sel_hi:[1,0,1] neg_lo:[0,0,1] neg_hi:[0,0,1]
	v_fma_f32 v166, v54, v66, -v166
	s_add_i32 s4, s34, 2
	s_cmpk_lt_i32 s4, 0x201
	s_cselect_b64 s[12:13], s[0:1], 0
	v_pk_add_f32 v[162:163], v[162:163], v[140:141] neg_lo:[0,1] neg_hi:[0,1]
	v_pk_add_f32 v[164:165], v[164:165], v[168:169] neg_lo:[0,1] neg_hi:[0,1]
	v_add_f32_e64 v166, v166, -v196
	v_pk_mul_f32 v[198:199], v[162:163], v[162:163]
	v_pk_fma_f32 v[198:199], v[164:165], v[164:165], v[198:199]
	v_add_f32_e32 v198, v198, v199
	v_fma_f32 v198, v166, v166, v198
	v_cndmask_b32_e64 v199, 0, v198, s[12:13]
	v_add_f32_e32 v0, v0, v199
	s_add_i32 s4, s34, 7
	s_min_i32 s4, s4, 0x200
	s_mul_i32 s5, s4, 0x804
	s_add_i32 s5, s5, s35
	s_add_i32 s6, s5, 0x0
	s_add_i32 s7, s5, 0x101004
	s_add_i32 s8, s5, 0x202008
	s_add_i32 s11, s5, 0x30300c
	s_add_i32 s15, s5, 0x404010
	s_mul_i32 s9, s4, 0x180c
	s_add_i32 s9, s9, s33
	buffer_load_dword v46, v28, s[16:19], s6 offen nt
	buffer_load_dword v47, v28, s[16:19], s7 offen nt
	buffer_load_dword v52, v28, s[16:19], s8 offen nt
	buffer_load_dword v53, v28, s[16:19], s11 offen nt
	buffer_load_dword v54, v28, s[16:19], s15 offen nt
	buffer_load_dwordx3 v[56:58], v27, s[24:27], s9 offen nt
	s_waitcnt vmcnt(12)
	v_pk_mul_f32 v[60:61], v[20:21], v[36:37] op_sel_hi:[1,0]
	v_pk_mul_f32 v[62:63], v[24:25], v[36:37] op_sel_hi:[1,0]
	v_mul_f32_e64 v64, v30, v36
	v_pk_mul_f32 v[66:67], v[20:21], v[36:37] op_sel:[0,1]
	v_pk_mul_f32 v[84:85], v[24:25], v[36:37] op_sel:[0,1]
	v_mul_f32_e64 v86, v30, v37
	v_pk_mul_f32 v[114:115], v[20:21], v[38:39] op_sel_hi:[1,0]
	v_pk_mul_f32 v[126:127], v[24:25], v[38:39] op_sel_hi:[1,0]
	v_mul_f32_e64 v140, v30, v38
	v_add_f32_dpp v150, v20, v20 wave_shr:1 row_mask:0xf bank_mask:0xf bound_ctrl:1
	v_add_f32_dpp v151, v21, v21 wave_shr:1 row_mask:0xf bank_mask:0xf bound_ctrl:1
	v_add_f32_dpp v152, v24, v24 wave_shr:1 row_mask:0xf bank_mask:0xf bound_ctrl:1
	v_add_f32_dpp v153, v25, v25 wave_shr:1 row_mask:0xf bank_mask:0xf bound_ctrl:1
	v_add_f32_dpp v154, v30, v30 wave_shr:1 row_mask:0xf bank_mask:0xf bound_ctrl:1
	v_add_f32_dpp v156, v60, v60 wave_shr:1 row_mask:0xf bank_mask:0xf bound_ctrl:1
	v_add_f32_dpp v157, v61, v61 wave_shr:1 row_mask:0xf bank_mask:0xf bound_ctrl:1
	v_add_f32_dpp v158, v62, v62 wave_shr:1 row_mask:0xf bank_mask:0xf bound_ctrl:1
	v_add_f32_dpp v159, v63, v63 wave_shr:1 row_mask:0xf bank_mask:0xf bound_ctrl:1
	v_add_f32_dpp v160, v64, v64 wave_shr:1 row_mask:0xf bank_mask:0xf bound_ctrl:1
	v_add_f32_dpp v162, v66, v66 wave_shr:1 row_mask:0xf bank_mask:0xf bound_ctrl:1
	v_add_f32_dpp v163, v67, v67 wave_shr:1 row_mask:0xf bank_mask:0xf bound_ctrl:1
	v_add_f32_dpp v164, v84, v84 wave_shr:1 row_mask:0xf bank_mask:0xf bound_ctrl:1
	v_add_f32_dpp v165, v85, v85 wave_shr:1 row_mask:0xf bank_mask:0xf bound_ctrl:1
	v_add_f32_dpp v166, v86, v86 wave_shr:1 row_mask:0xf bank_mask:0xf bound_ctrl:1
	v_add_f32_dpp v168, v114, v114 wave_shr:1 row_mask:0xf bank_mask:0xf bound_ctrl:1
	v_add_f32_dpp v169, v115, v115 wave_shr:1 row_mask:0xf bank_mask:0xf bound_ctrl:1
	v_add_f32_dpp v194, v126, v126 wave_shr:1 row_mask:0xf bank_mask:0xf bound_ctrl:1
	v_add_f32_dpp v195, v127, v127 wave_shr:1 row_mask:0xf bank_mask:0xf bound_ctrl:1
	v_add_f32_dpp v196, v140, v140 wave_shr:1 row_mask:0xf bank_mask:0xf bound_ctrl:1
	v_add_f32_dpp v150, v20, v150 wave_shl:1 row_mask:0xf bank_mask:0xf bound_ctrl:1
	v_add_f32_dpp v151, v21, v151 wave_shl:1 row_mask:0xf bank_mask:0xf bound_ctrl:1
	v_add_f32_dpp v152, v24, v152 wave_shl:1 row_mask:0xf bank_mask:0xf bound_ctrl:1
	v_add_f32_dpp v153, v25, v153 wave_shl:1 row_mask:0xf bank_mask:0xf bound_ctrl:1
	v_add_f32_dpp v154, v30, v154 wave_shl:1 row_mask:0xf bank_mask:0xf bound_ctrl:1
	v_add_f32_dpp v156, v60, v156 wave_shl:1 row_mask:0xf bank_mask:0xf bound_ctrl:1
	v_add_f32_dpp v157, v61, v157 wave_shl:1 row_mask:0xf bank_mask:0xf bound_ctrl:1
	v_add_f32_dpp v158, v62, v158 wave_shl:1 row_mask:0xf bank_mask:0xf bound_ctrl:1
	v_add_f32_dpp v159, v63, v159 wave_shl:1 row_mask:0xf bank_mask:0xf bound_ctrl:1
	v_add_f32_dpp v160, v64, v160 wave_shl:1 row_mask:0xf bank_mask:0xf bound_ctrl:1
	v_add_f32_dpp v162, v66, v162 wave_shl:1 row_mask:0xf bank_mask:0xf bound_ctrl:1
	v_add_f32_dpp v163, v67, v163 wave_shl:1 row_mask:0xf bank_mask:0xf bound_ctrl:1
	v_add_f32_dpp v164, v84, v164 wave_shl:1 row_mask:0xf bank_mask:0xf bound_ctrl:1
	v_add_f32_dpp v165, v85, v165 wave_shl:1 row_mask:0xf bank_mask:0xf bound_ctrl:1
	v_add_f32_dpp v166, v86, v166 wave_shl:1 row_mask:0xf bank_mask:0xf bound_ctrl:1
	v_add_f32_dpp v168, v114, v168 wave_shl:1 row_mask:0xf bank_mask:0xf bound_ctrl:1
	v_add_f32_dpp v169, v115, v169 wave_shl:1 row_mask:0xf bank_mask:0xf bound_ctrl:1
	v_add_f32_dpp v194, v126, v194 wave_shl:1 row_mask:0xf bank_mask:0xf bound_ctrl:1
	v_add_f32_dpp v195, v127, v195 wave_shl:1 row_mask:0xf bank_mask:0xf bound_ctrl:1
	v_add_f32_dpp v196, v140, v196 wave_shl:1 row_mask:0xf bank_mask:0xf bound_ctrl:1
	s_barrier
	ds_read_b128 v[60:63], v23 offset:3072
	ds_read_b128 v[64:67], v23 offset:4096
	ds_read_b128 v[84:87], v23 offset:5120
	v_pk_add_f32 v[114:115], v[68:69], v[150:151]
	v_pk_add_f32 v[68:69], v[72:73], v[152:153]
	v_add_f32_e64 v72, v104, v154
	v_pk_add_f32 v[104:105], v[106:107], v[156:157]
	v_pk_add_f32 v[106:107], v[108:109], v[158:159]
	v_add_f32_e64 v108, v110, v160
	v_pk_add_f32 v[110:111], v[112:113], v[162:163]
	v_pk_add_f32 v[112:113], v[116:117], v[164:165]
	v_add_f32_e64 v116, v118, v166
	v_pk_add_f32 v[118:119], v[120:121], v[168:169]
	v_pk_add_f32 v[120:121], v[122:123], v[194:195]
	v_add_f32_e64 v122, v170, v196
	s_waitcnt lgkmcnt(2)
	v_pk_fma_f32 v[104:105], v[60:61], v[114:115], v[104:105] op_sel_hi:[0,1,1] neg_lo:[1,0,0] neg_hi:[1,0,0]
	v_pk_fma_f32 v[106:107], v[60:61], v[68:69], v[106:107] op_sel_hi:[0,1,1] neg_lo:[1,0,0] neg_hi:[1,0,0]
	v_fma_f32 v108, -v60, v72, v108
	v_pk_fma_f32 v[110:111], v[60:61], v[114:115], v[110:111] op_sel:[1,0,0] neg_lo:[1,0,0] neg_hi:[1,0,0]
	v_pk_fma_f32 v[112:113], v[60:61], v[68:69], v[112:113] op_sel:[1,0,0] neg_lo:[1,0,0] neg_hi:[1,0,0]
	v_fma_f32 v116, -v61, v72, v116
	v_pk_fma_f32 v[118:119], v[62:63], v[114:115], v[118:119] op_sel_hi:[0,1,1] neg_lo:[1,0,0] neg_hi:[1,0,0]
	v_pk_fma_f32 v[120:121], v[62:63], v[68:69], v[120:121] op_sel_hi:[0,1,1] neg_lo:[1,0,0] neg_hi:[1,0,0]
	v_fma_f32 v122, -v62, v72, v122
	v_pk_mul_f32 v[126:127], v[62:63], v[104:105] op_sel:[1,0]
	v_pk_mul_f32 v[198:199], v[62:63], v[106:107] op_sel:[1,0]
	v_mul_f32_e64 v204, v63, v108
	s_waitcnt lgkmcnt(1)
	v_pk_mul_f32 v[140:141], v[64:65], v[104:105] op_sel_hi:[0,1]
	v_pk_mul_f32 v[200:201], v[64:65], v[106:107] op_sel_hi:[0,1]
	v_mul_f32_e64 v206, v64, v108
	v_pk_mul_f32 v[170:171], v[64:65], v[104:105] op_sel:[1,0]
	v_pk_mul_f32 v[202:203], v[64:65], v[106:107] op_sel:[1,0]
	v_mul_f32_e64 v208, v65, v108
	v_pk_fma_f32 v[126:127], v[64:65], v[110:111], v[126:127] op_sel_hi:[0,1,1]
	v_pk_fma_f32 v[198:199], v[64:65], v[112:113], v[198:199] op_sel_hi:[0,1,1]
	v_fma_f32 v204, v64, v116, v204
	v_pk_fma_f32 v[140:141], v[66:67], v[110:111], v[140:141] op_sel_hi:[0,1,1]
	v_pk_fma_f32 v[200:201], v[66:67], v[112:113], v[200:201] op_sel_hi:[0,1,1]
	v_fma_f32 v206, v66, v116, v206
	v_pk_fma_f32 v[170:171], v[66:67], v[110:111], v[170:171] op_sel:[1,0,0]
	v_pk_fma_f32 v[202:203], v[66:67], v[112:113], v[202:203] op_sel:[1,0,0]
	v_fma_f32 v208, v67, v116, v208
	v_pk_fma_f32 v[126:127], v[64:65], v[118:119], v[126:127] op_sel:[1,0,0]
	v_pk_fma_f32 v[198:199], v[64:65], v[120:121], v[198:199] op_sel:[1,0,0]
	v_fma_f32 v204, v65, v122, v204
	v_pk_fma_f32 v[140:141], v[66:67], v[118:119], v[140:141] op_sel:[1,0,0]
	v_pk_fma_f32 v[200:201], v[66:67], v[120:121], v[200:201] op_sel:[1,0,0]
	v_fma_f32 v206, v67, v122, v206
	s_waitcnt lgkmcnt(0)
	v_pk_fma_f32 v[170:171], v[84:85], v[118:119], v[170:171] op_sel_hi:[0,1,1]
	v_pk_fma_f32 v[202:203], v[84:85], v[120:121], v[202:203] op_sel_hi:[0,1,1]
	v_fma_f32 v208, v84, v122, v208
	v_pk_mul_f32 v[210:211], v[60:61], v[126:127] op_sel_hi:[0,1]
	v_pk_mul_f32 v[212:213], v[60:61], v[198:199] op_sel_hi:[0,1]
	v_mul_f32_e64 v214, v60, v204
	v_pk_fma_f32 v[210:211], v[60:61], v[140:141], v[210:211] op_sel:[1,0,0]
	v_pk_fma_f32 v[212:213], v[60:61], v[200:201], v[212:213] op_sel:[1,0,0]
	v_fma_f32 v214, v61, v206, v214
	v_pk_fma_f32 v[210:211], v[62:63], v[170:171], v[210:211] op_sel_hi:[0,1,1]
	v_pk_fma_f32 v[212:213], v[62:63], v[202:203], v[212:213] op_sel_hi:[0,1,1]
	v_fma_f32 v214, v62, v208, v214
	v_pk_fma_f32 v[210:211], v[84:85], v[114:115], v[210:211] op_sel:[1,0,0] neg_lo:[0,0,1] neg_hi:[0,0,1]
	v_pk_fma_f32 v[212:213], v[84:85], v[68:69], v[212:213] op_sel:[1,0,0] neg_lo:[0,0,1] neg_hi:[0,0,1]
	v_fma_f32 v214, v85, v72, -v214
	v_cmp_eq_u32_e64 s[10:11], 1, v87
	v_cmp_eq_u32_e64 s[14:15], 2, v87
	v_cmp_eq_u32_e64 s[20:21], 3, v87
	v_cmp_eq_u32_e64 s[22:23], 4, v87
	v_cmp_eq_u32_e64 s[30:31], 5, v87
	v_add_f32_dpp v68, v126, v126 wave_shr:1 row_mask:0xf bank_mask:0xf bound_ctrl:1
	v_add_f32_dpp v69, v127, v127 wave_shr:1 row_mask:0xf bank_mask:0xf bound_ctrl:1
	v_add_f32_dpp v72, v198, v198 wave_shr:1 row_mask:0xf bank_mask:0xf bound_ctrl:1
	v_add_f32_dpp v73, v199, v199 wave_shr:1 row_mask:0xf bank_mask:0xf bound_ctrl:1
	v_add_f32_dpp v104, v204, v204 wave_shr:1 row_mask:0xf bank_mask:0xf bound_ctrl:1
	v_add_f32_dpp v106, v140, v140 wave_shr:1 row_mask:0xf bank_mask:0xf bound_ctrl:1
	v_add_f32_dpp v107, v141, v141 wave_shr:1 row_mask:0xf bank_mask:0xf bound_ctrl:1
	v_add_f32_dpp v108, v200, v200 wave_shr:1 row_mask:0xf bank_mask:0xf bound_ctrl:1
	v_add_f32_dpp v109, v201, v201 wave_shr:1 row_mask:0xf bank_mask:0xf bound_ctrl:1
	v_add_f32_dpp v110, v206, v206 wave_shr:1 row_mask:0xf bank_mask:0xf bound_ctrl:1
	v_add_f32_dpp v112, v170, v170 wave_shr:1 row_mask:0xf bank_mask:0xf bound_ctrl:1
	v_add_f32_dpp v113, v171, v171 wave_shr:1 row_mask:0xf bank_mask:0xf bound_ctrl:1
	v_add_f32_dpp v114, v202, v202 wave_shr:1 row_mask:0xf bank_mask:0xf bound_ctrl:1
	v_add_f32_dpp v115, v203, v203 wave_shr:1 row_mask:0xf bank_mask:0xf bound_ctrl:1
	v_add_f32_dpp v116, v208, v208 wave_shr:1 row_mask:0xf bank_mask:0xf bound_ctrl:1
	v_add_f32_dpp v118, v210, v210 wave_shr:1 row_mask:0xf bank_mask:0xf bound_ctrl:1
	v_add_f32_dpp v119, v211, v211 wave_shr:1 row_mask:0xf bank_mask:0xf bound_ctrl:1
	v_add_f32_dpp v120, v212, v212 wave_shr:1 row_mask:0xf bank_mask:0xf bound_ctrl:1
	v_add_f32_dpp v121, v213, v213 wave_shr:1 row_mask:0xf bank_mask:0xf bound_ctrl:1
	v_add_f32_dpp v122, v214, v214 wave_shr:1 row_mask:0xf bank_mask:0xf bound_ctrl:1
	v_add_f32_dpp v68, v126, v68 wave_shl:1 row_mask:0xf bank_mask:0xf bound_ctrl:1
	v_add_f32_dpp v69, v127, v69 wave_shl:1 row_mask:0xf bank_mask:0xf bound_ctrl:1
	v_add_f32_dpp v72, v198, v72 wave_shl:1 row_mask:0xf bank_mask:0xf bound_ctrl:1
	v_add_f32_dpp v73, v199, v73 wave_shl:1 row_mask:0xf bank_mask:0xf bound_ctrl:1
	v_add_f32_dpp v104, v204, v104 wave_shl:1 row_mask:0xf bank_mask:0xf bound_ctrl:1
	v_add_f32_dpp v106, v140, v106 wave_shl:1 row_mask:0xf bank_mask:0xf bound_ctrl:1
	v_add_f32_dpp v107, v141, v107 wave_shl:1 row_mask:0xf bank_mask:0xf bound_ctrl:1
	v_add_f32_dpp v108, v200, v108 wave_shl:1 row_mask:0xf bank_mask:0xf bound_ctrl:1
	v_add_f32_dpp v109, v201, v109 wave_shl:1 row_mask:0xf bank_mask:0xf bound_ctrl:1
	v_add_f32_dpp v110, v206, v110 wave_shl:1 row_mask:0xf bank_mask:0xf bound_ctrl:1
	v_add_f32_dpp v112, v170, v112 wave_shl:1 row_mask:0xf bank_mask:0xf bound_ctrl:1
	v_add_f32_dpp v113, v171, v113 wave_shl:1 row_mask:0xf bank_mask:0xf bound_ctrl:1
	v_add_f32_dpp v114, v202, v114 wave_shl:1 row_mask:0xf bank_mask:0xf bound_ctrl:1
	v_add_f32_dpp v115, v203, v115 wave_shl:1 row_mask:0xf bank_mask:0xf bound_ctrl:1
	v_add_f32_dpp v116, v208, v116 wave_shl:1 row_mask:0xf bank_mask:0xf bound_ctrl:1
	v_add_f32_dpp v118, v210, v118 wave_shl:1 row_mask:0xf bank_mask:0xf bound_ctrl:1
	v_add_f32_dpp v119, v211, v119 wave_shl:1 row_mask:0xf bank_mask:0xf bound_ctrl:1
	v_add_f32_dpp v120, v212, v120 wave_shl:1 row_mask:0xf bank_mask:0xf bound_ctrl:1
	v_add_f32_dpp v121, v213, v121 wave_shl:1 row_mask:0xf bank_mask:0xf bound_ctrl:1
	v_add_f32_dpp v122, v214, v122 wave_shl:1 row_mask:0xf bank_mask:0xf bound_ctrl:1
	v_pk_add_f32 v[126:127], v[172:173], v[68:69]
	v_pk_add_f32 v[140:141], v[78:79], v[72:73]
	v_add_f32_e64 v78, v96, v104
	v_pk_add_f32 v[96:97], v[98:99], v[106:107]
	v_pk_add_f32 v[98:99], v[100:101], v[108:109]
	v_add_f32_e64 v100, v124, v110
	v_pk_add_f32 v[124:125], v[128:129], v[112:113]
	v_pk_add_f32 v[128:129], v[130:131], v[114:115]
	v_add_f32_e64 v130, v132, v116
	v_pk_add_f32 v[132:133], v[134:135], v[118:119]
	v_pk_add_f32 v[134:135], v[136:137], v[120:121]
	v_add_f32_e64 v136, v138, v122
	v_pk_fma_f32 v[132:133], v[8:9], v[126:127], v[132:133] op_sel_hi:[0,1,1]
	v_pk_fma_f32 v[134:135], v[8:9], v[140:141], v[134:135] op_sel_hi:[0,1,1]
	v_fma_f32 v136, v8, v78, v136
	v_pk_fma_f32 v[132:133], v[8:9], v[96:97], v[132:133] op_sel:[1,0,0]
	v_pk_fma_f32 v[134:135], v[8:9], v[98:99], v[134:135] op_sel:[1,0,0]
	v_fma_f32 v136, v9, v100, v136
	v_pk_fma_f32 v[132:133], v[10:11], v[124:125], v[132:133] op_sel_hi:[0,1,1]
	v_pk_fma_f32 v[134:135], v[10:11], v[128:129], v[134:135] op_sel_hi:[0,1,1]
	v_fma_f32 v136, v10, v130, v136
	v_cndmask_b32_e64 v138, 0, v1, s[10:11]
	v_cndmask_b32_e64 v139, 0, v1, s[14:15]
	v_cndmask_b32_e64 v170, 0, v1, s[20:21]
	v_cndmask_b32_e64 v171, 0, v1, s[22:23]
	v_cndmask_b32_e64 v172, 0, v1, s[30:31]
	v_pk_fma_f32 v[132:133], v[2:3], v[86:87], v[132:133] op_sel_hi:[1,0,1] neg_lo:[0,0,1] neg_hi:[0,0,1]
	v_pk_fma_f32 v[134:135], v[4:5], v[86:87], v[134:135] op_sel_hi:[1,0,1] neg_lo:[0,0,1] neg_hi:[0,0,1]
	v_fma_f32 v136, v6, v86, -v136
	s_add_i32 s4, s34, 3
	s_cmpk_lt_i32 s4, 0x201
	s_cselect_b64 s[12:13], s[0:1], 0
	v_pk_add_f32 v[132:133], v[132:133], v[138:139] neg_lo:[0,1] neg_hi:[0,1]
	v_pk_add_f32 v[134:135], v[134:135], v[170:171] neg_lo:[0,1] neg_hi:[0,1]
	v_add_f32_e64 v136, v136, -v172
	v_pk_mul_f32 v[198:199], v[132:133], v[132:133]
	v_pk_fma_f32 v[198:199], v[134:135], v[134:135], v[198:199]
	v_add_f32_e32 v198, v198, v199
	v_fma_f32 v198, v136, v136, v198
	v_cndmask_b32_e64 v199, 0, v198, s[12:13]
	v_add_f32_e32 v0, v0, v199
	s_add_i32 s4, s34, 8
	s_min_i32 s4, s4, 0x200
	s_mul_i32 s5, s4, 0x804
	s_add_i32 s5, s5, s35
	s_add_i32 s6, s5, 0x0
	s_add_i32 s7, s5, 0x101004
	s_add_i32 s8, s5, 0x202008
	s_add_i32 s11, s5, 0x30300c
	s_add_i32 s15, s5, 0x404010
	s_mul_i32 s9, s4, 0x180c
	s_add_i32 s9, s9, s33
	buffer_load_dword v2, v28, s[16:19], s6 offen nt
	buffer_load_dword v3, v28, s[16:19], s7 offen nt
	buffer_load_dword v4, v28, s[16:19], s8 offen nt
	buffer_load_dword v5, v28, s[16:19], s11 offen nt
	buffer_load_dword v6, v28, s[16:19], s15 offen nt
	buffer_load_dwordx3 v[8:10], v27, s[24:27], s9 offen nt
	s_waitcnt vmcnt(12)
	v_pk_mul_f32 v[60:61], v[40:41], v[48:49] op_sel_hi:[1,0]
	v_pk_mul_f32 v[62:63], v[42:43], v[48:49] op_sel_hi:[1,0]
	v_mul_f32_e64 v64, v44, v48
	v_pk_mul_f32 v[66:67], v[40:41], v[48:49] op_sel:[0,1]
	v_pk_mul_f32 v[78:79], v[42:43], v[48:49] op_sel:[0,1]
	v_mul_f32_e64 v84, v44, v49
	v_pk_mul_f32 v[86:87], v[40:41], v[50:51] op_sel_hi:[1,0]
	v_pk_mul_f32 v[96:97], v[42:43], v[50:51] op_sel_hi:[1,0]
	v_mul_f32_e64 v98, v44, v50
	v_add_f32_dpp v100, v40, v40 wave_shr:1 row_mask:0xf bank_mask:0xf bound_ctrl:1
	v_add_f32_dpp v101, v41, v41 wave_shr:1 row_mask:0xf bank_mask:0xf bound_ctrl:1
	v_add_f32_dpp v124, v42, v42 wave_shr:1 row_mask:0xf bank_mask:0xf bound_ctrl:1
	v_add_f32_dpp v125, v43, v43 wave_shr:1 row_mask:0xf bank_mask:0xf bound_ctrl:1
	v_add_f32_dpp v126, v44, v44 wave_shr:1 row_mask:0xf bank_mask:0xf bound_ctrl:1
	v_add_f32_dpp v128, v60, v60 wave_shr:1 row_mask:0xf bank_mask:0xf bound_ctrl:1
	v_add_f32_dpp v129, v61, v61 wave_shr:1 row_mask:0xf bank_mask:0xf bound_ctrl:1
	v_add_f32_dpp v130, v62, v62 wave_shr:1 row_mask:0xf bank_mask:0xf bound_ctrl:1
	v_add_f32_dpp v131, v63, v63 wave_shr:1 row_mask:0xf bank_mask:0xf bound_ctrl:1
	v_add_f32_dpp v132, v64, v64 wave_shr:1 row_mask:0xf bank_mask:0xf bound_ctrl:1
	v_add_f32_dpp v134, v66, v66 wave_shr:1 row_mask:0xf bank_mask:0xf bound_ctrl:1
	v_add_f32_dpp v135, v67, v67 wave_shr:1 row_mask:0xf bank_mask:0xf bound_ctrl:1
	v_add_f32_dpp v136, v78, v78 wave_shr:1 row_mask:0xf bank_mask:0xf bound_ctrl:1
	v_add_f32_dpp v137, v79, v79 wave_shr:1 row_mask:0xf bank_mask:0xf bound_ctrl:1
	v_add_f32_dpp v138, v84, v84 wave_shr:1 row_mask:0xf bank_mask:0xf bound_ctrl:1
	v_add_f32_dpp v140, v86, v86 wave_shr:1 row_mask:0xf bank_mask:0xf bound_ctrl:1
	v_add_f32_dpp v141, v87, v87 wave_shr:1 row_mask:0xf bank_mask:0xf bound_ctrl:1
	v_add_f32_dpp v170, v96, v96 wave_shr:1 row_mask:0xf bank_mask:0xf bound_ctrl:1
	v_add_f32_dpp v171, v97, v97 wave_shr:1 row_mask:0xf bank_mask:0xf bound_ctrl:1
	v_add_f32_dpp v172, v98, v98 wave_shr:1 row_mask:0xf bank_mask:0xf bound_ctrl:1
	v_add_f32_dpp v100, v40, v100 wave_shl:1 row_mask:0xf bank_mask:0xf bound_ctrl:1
	v_add_f32_dpp v101, v41, v101 wave_shl:1 row_mask:0xf bank_mask:0xf bound_ctrl:1
	v_add_f32_dpp v124, v42, v124 wave_shl:1 row_mask:0xf bank_mask:0xf bound_ctrl:1
	v_add_f32_dpp v125, v43, v125 wave_shl:1 row_mask:0xf bank_mask:0xf bound_ctrl:1
	v_add_f32_dpp v126, v44, v126 wave_shl:1 row_mask:0xf bank_mask:0xf bound_ctrl:1
	v_add_f32_dpp v128, v60, v128 wave_shl:1 row_mask:0xf bank_mask:0xf bound_ctrl:1
	v_add_f32_dpp v129, v61, v129 wave_shl:1 row_mask:0xf bank_mask:0xf bound_ctrl:1
	v_add_f32_dpp v130, v62, v130 wave_shl:1 row_mask:0xf bank_mask:0xf bound_ctrl:1
	v_add_f32_dpp v131, v63, v131 wave_shl:1 row_mask:0xf bank_mask:0xf bound_ctrl:1
	v_add_f32_dpp v132, v64, v132 wave_shl:1 row_mask:0xf bank_mask:0xf bound_ctrl:1
	v_add_f32_dpp v134, v66, v134 wave_shl:1 row_mask:0xf bank_mask:0xf bound_ctrl:1
	v_add_f32_dpp v135, v67, v135 wave_shl:1 row_mask:0xf bank_mask:0xf bound_ctrl:1
	v_add_f32_dpp v136, v78, v136 wave_shl:1 row_mask:0xf bank_mask:0xf bound_ctrl:1
	v_add_f32_dpp v137, v79, v137 wave_shl:1 row_mask:0xf bank_mask:0xf bound_ctrl:1
	v_add_f32_dpp v138, v84, v138 wave_shl:1 row_mask:0xf bank_mask:0xf bound_ctrl:1
	v_add_f32_dpp v140, v86, v140 wave_shl:1 row_mask:0xf bank_mask:0xf bound_ctrl:1
	v_add_f32_dpp v141, v87, v141 wave_shl:1 row_mask:0xf bank_mask:0xf bound_ctrl:1
	v_add_f32_dpp v170, v96, v170 wave_shl:1 row_mask:0xf bank_mask:0xf bound_ctrl:1
	v_add_f32_dpp v171, v97, v171 wave_shl:1 row_mask:0xf bank_mask:0xf bound_ctrl:1
	v_add_f32_dpp v172, v98, v172 wave_shl:1 row_mask:0xf bank_mask:0xf bound_ctrl:1
	s_barrier
	ds_read_b128 v[60:63], v23 offset:0
	ds_read_b128 v[64:67], v23 offset:1024
	ds_read_b128 v[84:87], v23 offset:2048
	v_pk_add_f32 v[78:79], v[150:151], v[100:101]
	v_pk_add_f32 v[96:97], v[74:75], v[78:79]
	v_pk_add_f32 v[74:75], v[152:153], v[124:125]
	v_pk_add_f32 v[98:99], v[76:77], v[74:75]
	v_add_f32_e64 v76, v154, v126
	v_add_f32_e64 v150, v80, v76
	v_pk_add_f32 v[80:81], v[156:157], v[128:129]
	v_pk_add_f32 v[152:153], v[82:83], v[80:81]
	v_pk_add_f32 v[82:83], v[158:159], v[130:131]
	v_pk_add_f32 v[154:155], v[88:89], v[82:83]
	v_add_f32_e64 v88, v160, v132
	v_add_f32_e64 v156, v90, v88
	v_pk_add_f32 v[90:91], v[162:163], v[134:135]
	v_pk_add_f32 v[158:159], v[92:93], v[90:91]
	v_pk_add_f32 v[92:93], v[164:165], v[136:137]
	v_pk_add_f32 v[160:161], v[94:95], v[92:93]
	v_add_f32_e64 v94, v166, v138
	v_add_f32_e64 v162, v142, v94
	v_pk_add_f32 v[142:143], v[168:169], v[140:141]
	v_pk_add_f32 v[164:165], v[144:145], v[142:143]
	v_pk_add_f32 v[144:145], v[194:195], v[170:171]
	v_pk_add_f32 v[166:167], v[146:147], v[144:145]
	v_add_f32_e64 v146, v196, v172
	v_add_f32_e64 v168, v148, v146
	s_waitcnt lgkmcnt(2)
	v_pk_fma_f32 v[152:153], v[60:61], v[96:97], v[152:153] op_sel_hi:[0,1,1] neg_lo:[1,0,0] neg_hi:[1,0,0]
	v_pk_fma_f32 v[154:155], v[60:61], v[98:99], v[154:155] op_sel_hi:[0,1,1] neg_lo:[1,0,0] neg_hi:[1,0,0]
	v_fma_f32 v156, -v60, v150, v156
	v_pk_fma_f32 v[158:159], v[60:61], v[96:97], v[158:159] op_sel:[1,0,0] neg_lo:[1,0,0] neg_hi:[1,0,0]
	v_pk_fma_f32 v[160:161], v[60:61], v[98:99], v[160:161] op_sel:[1,0,0] neg_lo:[1,0,0] neg_hi:[1,0,0]
	v_fma_f32 v162, -v61, v150, v162
	v_pk_fma_f32 v[164:165], v[62:63], v[96:97], v[164:165] op_sel_hi:[0,1,1] neg_lo:[1,0,0] neg_hi:[1,0,0]
	v_pk_fma_f32 v[166:167], v[62:63], v[98:99], v[166:167] op_sel_hi:[0,1,1] neg_lo:[1,0,0] neg_hi:[1,0,0]
	v_fma_f32 v168, -v62, v150, v168
	v_pk_mul_f32 v[148:149], v[62:63], v[152:153] op_sel:[1,0]
	v_pk_mul_f32 v[198:199], v[62:63], v[154:155] op_sel:[1,0]
	v_mul_f32_e64 v204, v63, v156
	s_waitcnt lgkmcnt(1)
	v_pk_mul_f32 v[194:195], v[64:65], v[152:153] op_sel_hi:[0,1]
	v_pk_mul_f32 v[200:201], v[64:65], v[154:155] op_sel_hi:[0,1]
	v_mul_f32_e64 v206, v64, v156
	v_pk_mul_f32 v[196:197], v[64:65], v[152:153] op_sel:[1,0]
	v_pk_mul_f32 v[202:203], v[64:65], v[154:155] op_sel:[1,0]
	v_mul_f32_e64 v208, v65, v156
	v_pk_fma_f32 v[148:149], v[64:65], v[158:159], v[148:149] op_sel_hi:[0,1,1]
	v_pk_fma_f32 v[198:199], v[64:65], v[160:161], v[198:199] op_sel_hi:[0,1,1]
	v_fma_f32 v204, v64, v162, v204
	v_pk_fma_f32 v[194:195], v[66:67], v[158:159], v[194:195] op_sel_hi:[0,1,1]
	v_pk_fma_f32 v[200:201], v[66:67], v[160:161], v[200:201] op_sel_hi:[0,1,1]
	v_fma_f32 v206, v66, v162, v206
	v_pk_fma_f32 v[196:197], v[66:67], v[158:159], v[196:197] op_sel:[1,0,0]
	v_pk_fma_f32 v[202:203], v[66:67], v[160:161], v[202:203] op_sel:[1,0,0]
	v_fma_f32 v208, v67, v162, v208
	v_pk_fma_f32 v[148:149], v[64:65], v[164:165], v[148:149] op_sel:[1,0,0]
	v_pk_fma_f32 v[198:199], v[64:65], v[166:167], v[198:199] op_sel:[1,0,0]
	v_fma_f32 v204, v65, v168, v204
	v_pk_fma_f32 v[194:195], v[66:67], v[164:165], v[194:195] op_sel:[1,0,0]
	v_pk_fma_f32 v[200:201], v[66:67], v[166:167], v[200:201] op_sel:[1,0,0]
	v_fma_f32 v206, v67, v168, v206
	s_waitcnt lgkmcnt(0)
	v_pk_fma_f32 v[196:197], v[84:85], v[164:165], v[196:197] op_sel_hi:[0,1,1]
	v_pk_fma_f32 v[202:203], v[84:85], v[166:167], v[202:203] op_sel_hi:[0,1,1]
	v_fma_f32 v208, v84, v168, v208
	v_pk_mul_f32 v[210:211], v[60:61], v[148:149] op_sel_hi:[0,1]
	v_pk_mul_f32 v[212:213], v[60:61], v[198:199] op_sel_hi:[0,1]
	v_mul_f32_e64 v214, v60, v204
	v_pk_fma_f32 v[210:211], v[60:61], v[194:195], v[210:211] op_sel:[1,0,0]
	v_pk_fma_f32 v[212:213], v[60:61], v[200:201], v[212:213] op_sel:[1,0,0]
	v_fma_f32 v214, v61, v206, v214
	v_pk_fma_f32 v[210:211], v[62:63], v[196:197], v[210:211] op_sel_hi:[0,1,1]
	v_pk_fma_f32 v[212:213], v[62:63], v[202:203], v[212:213] op_sel_hi:[0,1,1]
	v_fma_f32 v214, v62, v208, v214
	v_pk_fma_f32 v[210:211], v[84:85], v[96:97], v[210:211] op_sel:[1,0,0] neg_lo:[0,0,1] neg_hi:[0,0,1]
	v_pk_fma_f32 v[212:213], v[84:85], v[98:99], v[212:213] op_sel:[1,0,0] neg_lo:[0,0,1] neg_hi:[0,0,1]
	v_fma_f32 v214, v85, v150, -v214
	v_cmp_eq_u32_e64 s[10:11], 1, v87
	v_cmp_eq_u32_e64 s[14:15], 2, v87
	v_cmp_eq_u32_e64 s[20:21], 3, v87
	v_cmp_eq_u32_e64 s[22:23], 4, v87
	v_cmp_eq_u32_e64 s[30:31], 5, v87
	v_add_f32_dpp v96, v148, v148 wave_shr:1 row_mask:0xf bank_mask:0xf bound_ctrl:1
	v_add_f32_dpp v97, v149, v149 wave_shr:1 row_mask:0xf bank_mask:0xf bound_ctrl:1
	v_add_f32_dpp v98, v198, v198 wave_shr:1 row_mask:0xf bank_mask:0xf bound_ctrl:1
	v_add_f32_dpp v99, v199, v199 wave_shr:1 row_mask:0xf bank_mask:0xf bound_ctrl:1
	v_add_f32_dpp v150, v204, v204 wave_shr:1 row_mask:0xf bank_mask:0xf bound_ctrl:1
	v_add_f32_dpp v152, v194, v194 wave_shr:1 row_mask:0xf bank_mask:0xf bound_ctrl:1
	v_add_f32_dpp v153, v195, v195 wave_shr:1 row_mask:0xf bank_mask:0xf bound_ctrl:1
	v_add_f32_dpp v154, v200, v200 wave_shr:1 row_mask:0xf bank_mask:0xf bound_ctrl:1
	v_add_f32_dpp v155, v201, v201 wave_shr:1 row_mask:0xf bank_mask:0xf bound_ctrl:1
	v_add_f32_dpp v156, v206, v206 wave_shr:1 row_mask:0xf bank_mask:0xf bound_ctrl:1
	v_add_f32_dpp v158, v196, v196 wave_shr:1 row_mask:0xf bank_mask:0xf bound_ctrl:1
	v_add_f32_dpp v159, v197, v197 wave_shr:1 row_mask:0xf bank_mask:0xf bound_ctrl:1
	v_add_f32_dpp v160, v202, v202 wave_shr:1 row_mask:0xf bank_mask:0xf bound_ctrl:1
	v_add_f32_dpp v161, v203, v203 wave_shr:1 row_mask:0xf bank_mask:0xf bound_ctrl:1
	v_add_f32_dpp v162, v208, v208 wave_shr:1 row_mask:0xf bank_mask:0xf bound_ctrl:1
	v_add_f32_dpp v164, v210, v210 wave_shr:1 row_mask:0xf bank_mask:0xf bound_ctrl:1
	v_add_f32_dpp v165, v211, v211 wave_shr:1 row_mask:0xf bank_mask:0xf bound_ctrl:1
	v_add_f32_dpp v166, v212, v212 wave_shr:1 row_mask:0xf bank_mask:0xf bound_ctrl:1
	v_add_f32_dpp v167, v213, v213 wave_shr:1 row_mask:0xf bank_mask:0xf bound_ctrl:1
	v_add_f32_dpp v168, v214, v214 wave_shr:1 row_mask:0xf bank_mask:0xf bound_ctrl:1
	v_add_f32_dpp v96, v148, v96 wave_shl:1 row_mask:0xf bank_mask:0xf bound_ctrl:1
	v_add_f32_dpp v97, v149, v97 wave_shl:1 row_mask:0xf bank_mask:0xf bound_ctrl:1
	v_add_f32_dpp v98, v198, v98 wave_shl:1 row_mask:0xf bank_mask:0xf bound_ctrl:1
	v_add_f32_dpp v99, v199, v99 wave_shl:1 row_mask:0xf bank_mask:0xf bound_ctrl:1
	v_add_f32_dpp v150, v204, v150 wave_shl:1 row_mask:0xf bank_mask:0xf bound_ctrl:1
	v_add_f32_dpp v152, v194, v152 wave_shl:1 row_mask:0xf bank_mask:0xf bound_ctrl:1
	v_add_f32_dpp v153, v195, v153 wave_shl:1 row_mask:0xf bank_mask:0xf bound_ctrl:1
	v_add_f32_dpp v154, v200, v154 wave_shl:1 row_mask:0xf bank_mask:0xf bound_ctrl:1
	v_add_f32_dpp v155, v201, v155 wave_shl:1 row_mask:0xf bank_mask:0xf bound_ctrl:1
	v_add_f32_dpp v156, v206, v156 wave_shl:1 row_mask:0xf bank_mask:0xf bound_ctrl:1
	v_add_f32_dpp v158, v196, v158 wave_shl:1 row_mask:0xf bank_mask:0xf bound_ctrl:1
	v_add_f32_dpp v159, v197, v159 wave_shl:1 row_mask:0xf bank_mask:0xf bound_ctrl:1
	v_add_f32_dpp v160, v202, v160 wave_shl:1 row_mask:0xf bank_mask:0xf bound_ctrl:1
	v_add_f32_dpp v161, v203, v161 wave_shl:1 row_mask:0xf bank_mask:0xf bound_ctrl:1
	v_add_f32_dpp v162, v208, v162 wave_shl:1 row_mask:0xf bank_mask:0xf bound_ctrl:1
	v_add_f32_dpp v164, v210, v164 wave_shl:1 row_mask:0xf bank_mask:0xf bound_ctrl:1
	v_add_f32_dpp v165, v211, v165 wave_shl:1 row_mask:0xf bank_mask:0xf bound_ctrl:1
	v_add_f32_dpp v166, v212, v166 wave_shl:1 row_mask:0xf bank_mask:0xf bound_ctrl:1
	v_add_f32_dpp v167, v213, v167 wave_shl:1 row_mask:0xf bank_mask:0xf bound_ctrl:1
	v_add_f32_dpp v168, v214, v168 wave_shl:1 row_mask:0xf bank_mask:0xf bound_ctrl:1
	v_pk_add_f32 v[148:149], v[68:69], v[96:97]
	v_pk_add_f32 v[194:195], v[70:71], v[148:149]
	v_pk_add_f32 v[68:69], v[72:73], v[98:99]
	v_pk_add_f32 v[70:71], v[102:103], v[68:69]
	v_add_f32_e64 v72, v104, v150
	v_add_f32_e64 v102, v174, v72
	v_pk_add_f32 v[104:105], v[106:107], v[152:153]
	v_pk_add_f32 v[174:175], v[176:177], v[104:105]
	v_pk_add_f32 v[106:107], v[108:109], v[154:155]
	v_pk_add_f32 v[176:177], v[178:179], v[106:107]
	v_add_f32_e64 v108, v110, v156
	v_add_f32_e64 v178, v180, v108
	v_pk_add_f32 v[110:111], v[112:113], v[158:159]
	v_pk_add_f32 v[180:181], v[182:183], v[110:111]
	v_pk_add_f32 v[112:113], v[114:115], v[160:161]
	v_pk_add_f32 v[182:183], v[184:185], v[112:113]
	v_add_f32_e64 v114, v116, v162
	v_add_f32_e64 v184, v186, v114
	v_pk_add_f32 v[116:117], v[118:119], v[164:165]
	v_pk_add_f32 v[186:187], v[188:189], v[116:117]
	v_pk_add_f32 v[118:119], v[120:121], v[166:167]
	v_pk_add_f32 v[188:189], v[190:191], v[118:119]
	v_add_f32_e64 v120, v122, v168
	v_add_f32_e64 v190, v192, v120
	v_pk_fma_f32 v[186:187], v[32:33], v[194:195], v[186:187] op_sel_hi:[0,1,1]
	v_pk_fma_f32 v[188:189], v[32:33], v[70:71], v[188:189] op_sel_hi:[0,1,1]
	v_fma_f32 v190, v32, v102, v190
	v_pk_fma_f32 v[186:187], v[32:33], v[174:175], v[186:187] op_sel:[1,0,0]
	v_pk_fma_f32 v[188:189], v[32:33], v[176:177], v[188:189] op_sel:[1,0,0]
	v_fma_f32 v190, v33, v178, v190
	v_pk_fma_f32 v[186:187], v[34:35], v[180:181], v[186:187] op_sel_hi:[0,1,1]
	v_pk_fma_f32 v[188:189], v[34:35], v[182:183], v[188:189] op_sel_hi:[0,1,1]
	v_fma_f32 v190, v34, v184, v190
	v_cndmask_b32_e64 v122, 0, v1, s[10:11]
	v_cndmask_b32_e64 v123, 0, v1, s[14:15]
	v_cndmask_b32_e64 v192, 0, v1, s[20:21]
	v_cndmask_b32_e64 v193, 0, v1, s[22:23]
	v_cndmask_b32_e64 v196, 0, v1, s[30:31]
	v_pk_fma_f32 v[186:187], v[12:13], v[86:87], v[186:187] op_sel_hi:[1,0,1] neg_lo:[0,0,1] neg_hi:[0,0,1]
	v_pk_fma_f32 v[188:189], v[14:15], v[86:87], v[188:189] op_sel_hi:[1,0,1] neg_lo:[0,0,1] neg_hi:[0,0,1]
	v_fma_f32 v190, v16, v86, -v190
	s_add_i32 s4, s34, 4
	s_cmpk_lt_i32 s4, 0x201
	s_cselect_b64 s[12:13], s[0:1], 0
	v_pk_add_f32 v[186:187], v[186:187], v[122:123] neg_lo:[0,1] neg_hi:[0,1]
	v_pk_add_f32 v[188:189], v[188:189], v[192:193] neg_lo:[0,1] neg_hi:[0,1]
	v_add_f32_e64 v190, v190, -v196
	v_pk_mul_f32 v[198:199], v[186:187], v[186:187]
	v_pk_fma_f32 v[198:199], v[188:189], v[188:189], v[198:199]
	v_add_f32_e32 v198, v198, v199
	v_fma_f32 v198, v190, v190, v198
	v_cndmask_b32_e64 v199, 0, v198, s[12:13]
	v_add_f32_e32 v0, v0, v199
	s_add_i32 s4, s34, 9
	s_min_i32 s4, s4, 0x200
	s_mul_i32 s5, s4, 0x804
	s_add_i32 s5, s5, s35
	s_add_i32 s6, s5, 0x0
	s_add_i32 s7, s5, 0x101004
	s_add_i32 s8, s5, 0x202008
	s_add_i32 s11, s5, 0x30300c
	s_add_i32 s15, s5, 0x404010
	s_mul_i32 s9, s4, 0x180c
	s_add_i32 s9, s9, s33
	buffer_load_dword v12, v28, s[16:19], s6 offen nt
	buffer_load_dword v13, v28, s[16:19], s7 offen nt
	buffer_load_dword v14, v28, s[16:19], s8 offen nt
	buffer_load_dword v15, v28, s[16:19], s11 offen nt
	buffer_load_dword v16, v28, s[16:19], s15 offen nt
	buffer_load_dwordx3 v[32:34], v27, s[24:27], s9 offen nt
	s_waitcnt vmcnt(12)
	v_pk_mul_f32 v[60:61], v[46:47], v[56:57] op_sel_hi:[1,0]
	v_pk_mul_f32 v[62:63], v[52:53], v[56:57] op_sel_hi:[1,0]
	v_mul_f32_e64 v64, v54, v56
	v_pk_mul_f32 v[66:67], v[46:47], v[56:57] op_sel:[0,1]
	v_pk_mul_f32 v[70:71], v[52:53], v[56:57] op_sel:[0,1]
	v_mul_f32_e64 v84, v54, v57
	v_pk_mul_f32 v[86:87], v[46:47], v[58:59] op_sel_hi:[1,0]
	v_pk_mul_f32 v[102:103], v[52:53], v[58:59] op_sel_hi:[1,0]
	v_mul_f32_e64 v122, v54, v58
	v_add_f32_dpp v174, v46, v46 wave_shr:1 row_mask:0xf bank_mask:0xf bound_ctrl:1
	v_add_f32_dpp v175, v47, v47 wave_shr:1 row_mask:0xf bank_mask:0xf bound_ctrl:1
	v_add_f32_dpp v176, v52, v52 wave_shr:1 row_mask:0xf bank_mask:0xf bound_ctrl:1
	v_add_f32_dpp v177, v53, v53 wave_shr:1 row_mask:0xf bank_mask:0xf bound_ctrl:1
	v_add_f32_dpp v178, v54, v54 wave_shr:1 row_mask:0xf bank_mask:0xf bound_ctrl:1
	v_add_f32_dpp v180, v60, v60 wave_shr:1 row_mask:0xf bank_mask:0xf bound_ctrl:1
	v_add_f32_dpp v181, v61, v61 wave_shr:1 row_mask:0xf bank_mask:0xf bound_ctrl:1
	v_add_f32_dpp v182, v62, v62 wave_shr:1 row_mask:0xf bank_mask:0xf bound_ctrl:1
	v_add_f32_dpp v183, v63, v63 wave_shr:1 row_mask:0xf bank_mask:0xf bound_ctrl:1
	v_add_f32_dpp v184, v64, v64 wave_shr:1 row_mask:0xf bank_mask:0xf bound_ctrl:1
	v_add_f32_dpp v186, v66, v66 wave_shr:1 row_mask:0xf bank_mask:0xf bound_ctrl:1
	v_add_f32_dpp v187, v67, v67 wave_shr:1 row_mask:0xf bank_mask:0xf bound_ctrl:1
	v_add_f32_dpp v188, v70, v70 wave_shr:1 row_mask:0xf bank_mask:0xf bound_ctrl:1
	v_add_f32_dpp v189, v71, v71 wave_shr:1 row_mask:0xf bank_mask:0xf bound_ctrl:1
	v_add_f32_dpp v190, v84, v84 wave_shr:1 row_mask:0xf bank_mask:0xf bound_ctrl:1
	v_add_f32_dpp v192, v86, v86 wave_shr:1 row_mask:0xf bank_mask:0xf bound_ctrl:1
	v_add_f32_dpp v193, v87, v87 wave_shr:1 row_mask:0xf bank_mask:0xf bound_ctrl:1
	v_add_f32_dpp v194, v102, v102 wave_shr:1 row_mask:0xf bank_mask:0xf bound_ctrl:1
	v_add_f32_dpp v195, v103, v103 wave_shr:1 row_mask:0xf bank_mask:0xf bound_ctrl:1
	v_add_f32_dpp v196, v122, v122 wave_shr:1 row_mask:0xf bank_mask:0xf bound_ctrl:1
	v_add_f32_dpp v174, v46, v174 wave_shl:1 row_mask:0xf bank_mask:0xf bound_ctrl:1
	v_add_f32_dpp v175, v47, v175 wave_shl:1 row_mask:0xf bank_mask:0xf bound_ctrl:1
	v_add_f32_dpp v176, v52, v176 wave_shl:1 row_mask:0xf bank_mask:0xf bound_ctrl:1
	v_add_f32_dpp v177, v53, v177 wave_shl:1 row_mask:0xf bank_mask:0xf bound_ctrl:1
	v_add_f32_dpp v178, v54, v178 wave_shl:1 row_mask:0xf bank_mask:0xf bound_ctrl:1
	v_add_f32_dpp v180, v60, v180 wave_shl:1 row_mask:0xf bank_mask:0xf bound_ctrl:1
	v_add_f32_dpp v181, v61, v181 wave_shl:1 row_mask:0xf bank_mask:0xf bound_ctrl:1
	v_add_f32_dpp v182, v62, v182 wave_shl:1 row_mask:0xf bank_mask:0xf bound_ctrl:1
	v_add_f32_dpp v183, v63, v183 wave_shl:1 row_mask:0xf bank_mask:0xf bound_ctrl:1
	v_add_f32_dpp v184, v64, v184 wave_shl:1 row_mask:0xf bank_mask:0xf bound_ctrl:1
	v_add_f32_dpp v186, v66, v186 wave_shl:1 row_mask:0xf bank_mask:0xf bound_ctrl:1
	v_add_f32_dpp v187, v67, v187 wave_shl:1 row_mask:0xf bank_mask:0xf bound_ctrl:1
	v_add_f32_dpp v188, v70, v188 wave_shl:1 row_mask:0xf bank_mask:0xf bound_ctrl:1
	v_add_f32_dpp v189, v71, v189 wave_shl:1 row_mask:0xf bank_mask:0xf bound_ctrl:1
	v_add_f32_dpp v190, v84, v190 wave_shl:1 row_mask:0xf bank_mask:0xf bound_ctrl:1
	v_add_f32_dpp v192, v86, v192 wave_shl:1 row_mask:0xf bank_mask:0xf bound_ctrl:1
	v_add_f32_dpp v193, v87, v193 wave_shl:1 row_mask:0xf bank_mask:0xf bound_ctrl:1
	v_add_f32_dpp v194, v102, v194 wave_shl:1 row_mask:0xf bank_mask:0xf bound_ctrl:1
	v_add_f32_dpp v195, v103, v195 wave_shl:1 row_mask:0xf bank_mask:0xf bound_ctrl:1
	v_add_f32_dpp v196, v122, v196 wave_shl:1 row_mask:0xf bank_mask:0xf bound_ctrl:1
	s_barrier
	ds_read_b128 v[60:63], v23 offset:3072
	ds_read_b128 v[64:67], v23 offset:4096
	ds_read_b128 v[84:87], v23 offset:5120
	v_pk_add_f32 v[70:71], v[78:79], v[174:175]
	v_pk_add_f32 v[78:79], v[74:75], v[176:177]
	v_add_f32_e64 v74, v76, v178
	v_pk_add_f32 v[76:77], v[80:81], v[180:181]
	v_pk_add_f32 v[80:81], v[82:83], v[182:183]
	v_add_f32_e64 v82, v88, v184
	v_pk_add_f32 v[88:89], v[90:91], v[186:187]
	v_pk_add_f32 v[90:91], v[92:93], v[188:189]
	v_add_f32_e64 v92, v94, v190
	v_pk_add_f32 v[94:95], v[142:143], v[192:193]
	v_pk_add_f32 v[102:103], v[144:145], v[194:195]
	v_add_f32_e64 v122, v146, v196
	s_waitcnt lgkmcnt(2)
	v_pk_fma_f32 v[76:77], v[60:61], v[70:71], v[76:77] op_sel_hi:[0,1,1] neg_lo:[1,0,0] neg_hi:[1,0,0]
	v_pk_fma_f32 v[80:81], v[60:61], v[78:79], v[80:81] op_sel_hi:[0,1,1] neg_lo:[1,0,0] neg_hi:[1,0,0]
	v_fma_f32 v82, -v60, v74, v82
	v_pk_fma_f32 v[88:89], v[60:61], v[70:71], v[88:89] op_sel:[1,0,0] neg_lo:[1,0,0] neg_hi:[1,0,0]
	v_pk_fma_f32 v[90:91], v[60:61], v[78:79], v[90:91] op_sel:[1,0,0] neg_lo:[1,0,0] neg_hi:[1,0,0]
	v_fma_f32 v92, -v61, v74, v92
	v_pk_fma_f32 v[94:95], v[62:63], v[70:71], v[94:95] op_sel_hi:[0,1,1] neg_lo:[1,0,0] neg_hi:[1,0,0]
	v_pk_fma_f32 v[102:103], v[62:63], v[78:79], v[102:103] op_sel_hi:[0,1,1] neg_lo:[1,0,0] neg_hi:[1,0,0]
	v_fma_f32 v122, -v62, v74, v122
	v_pk_mul_f32 v[142:143], v[62:63], v[76:77] op_sel:[1,0]
	v_pk_mul_f32 v[198:199], v[62:63], v[80:81] op_sel:[1,0]
	v_mul_f32_e64 v204, v63, v82
	s_waitcnt lgkmcnt(1)
	v_pk_mul_f32 v[144:145], v[64:65], v[76:77] op_sel_hi:[0,1]
	v_pk_mul_f32 v[200:201], v[64:65], v[80:81] op_sel_hi:[0,1]
	v_mul_f32_e64 v206, v64, v82
	v_pk_mul_f32 v[146:147], v[64:65], v[76:77] op_sel:[1,0]
	v_pk_mul_f32 v[202:203], v[64:65], v[80:81] op_sel:[1,0]
	v_mul_f32_e64 v208, v65, v82
	v_pk_fma_f32 v[142:143], v[64:65], v[88:89], v[142:143] op_sel_hi:[0,1,1]
	v_pk_fma_f32 v[198:199], v[64:65], v[90:91], v[198:199] op_sel_hi:[0,1,1]
	v_fma_f32 v204, v64, v92, v204
	v_pk_fma_f32 v[144:145], v[66:67], v[88:89], v[144:145] op_sel_hi:[0,1,1]
	v_pk_fma_f32 v[200:201], v[66:67], v[90:91], v[200:201] op_sel_hi:[0,1,1]
	v_fma_f32 v206, v66, v92, v206
	v_pk_fma_f32 v[146:147], v[66:67], v[88:89], v[146:147] op_sel:[1,0,0]
	v_pk_fma_f32 v[202:203], v[66:67], v[90:91], v[202:203] op_sel:[1,0,0]
	v_fma_f32 v208, v67, v92, v208
	v_pk_fma_f32 v[142:143], v[64:65], v[94:95], v[142:143] op_sel:[1,0,0]
	v_pk_fma_f32 v[198:199], v[64:65], v[102:103], v[198:199] op_sel:[1,0,0]
	v_fma_f32 v204, v65, v122, v204
	v_pk_fma_f32 v[144:145], v[66:67], v[94:95], v[144:145] op_sel:[1,0,0]
	v_pk_fma_f32 v[200:201], v[66:67], v[102:103], v[200:201] op_sel:[1,0,0]
	v_fma_f32 v206, v67, v122, v206
	s_waitcnt lgkmcnt(0)
	v_pk_fma_f32 v[146:147], v[84:85], v[94:95], v[146:147] op_sel_hi:[0,1,1]
	v_pk_fma_f32 v[202:203], v[84:85], v[102:103], v[202:203] op_sel_hi:[0,1,1]
	v_fma_f32 v208, v84, v122, v208
	v_pk_mul_f32 v[210:211], v[60:61], v[142:143] op_sel_hi:[0,1]
	v_pk_mul_f32 v[212:213], v[60:61], v[198:199] op_sel_hi:[0,1]
	v_mul_f32_e64 v214, v60, v204
	v_pk_fma_f32 v[210:211], v[60:61], v[144:145], v[210:211] op_sel:[1,0,0]
	v_pk_fma_f32 v[212:213], v[60:61], v[200:201], v[212:213] op_sel:[1,0,0]
	v_fma_f32 v214, v61, v206, v214
	v_pk_fma_f32 v[210:211], v[62:63], v[146:147], v[210:211] op_sel_hi:[0,1,1]
	v_pk_fma_f32 v[212:213], v[62:63], v[202:203], v[212:213] op_sel_hi:[0,1,1]
	v_fma_f32 v214, v62, v208, v214
	v_pk_fma_f32 v[210:211], v[84:85], v[70:71], v[210:211] op_sel:[1,0,0] neg_lo:[0,0,1] neg_hi:[0,0,1]
	v_pk_fma_f32 v[212:213], v[84:85], v[78:79], v[212:213] op_sel:[1,0,0] neg_lo:[0,0,1] neg_hi:[0,0,1]
	v_fma_f32 v214, v85, v74, -v214
	v_cmp_eq_u32_e64 s[10:11], 1, v87
	v_cmp_eq_u32_e64 s[14:15], 2, v87
	v_cmp_eq_u32_e64 s[20:21], 3, v87
	v_cmp_eq_u32_e64 s[22:23], 4, v87
	v_cmp_eq_u32_e64 s[30:31], 5, v87
	v_add_f32_dpp v70, v142, v142 wave_shr:1 row_mask:0xf bank_mask:0xf bound_ctrl:1
	v_add_f32_dpp v71, v143, v143 wave_shr:1 row_mask:0xf bank_mask:0xf bound_ctrl:1
	v_add_f32_dpp v74, v198, v198 wave_shr:1 row_mask:0xf bank_mask:0xf bound_ctrl:1
	v_add_f32_dpp v75, v199, v199 wave_shr:1 row_mask:0xf bank_mask:0xf bound_ctrl:1
	v_add_f32_dpp v76, v204, v204 wave_shr:1 row_mask:0xf bank_mask:0xf bound_ctrl:1
	v_add_f32_dpp v78, v144, v144 wave_shr:1 row_mask:0xf bank_mask:0xf bound_ctrl:1
	v_add_f32_dpp v79, v145, v145 wave_shr:1 row_mask:0xf bank_mask:0xf bound_ctrl:1
	v_add_f32_dpp v80, v200, v200 wave_shr:1 row_mask:0xf bank_mask:0xf bound_ctrl:1
	v_add_f32_dpp v81, v201, v201 wave_shr:1 row_mask:0xf bank_mask:0xf bound_ctrl:1
	v_add_f32_dpp v82, v206, v206 wave_shr:1 row_mask:0xf bank_mask:0xf bound_ctrl:1
	v_add_f32_dpp v88, v146, v146 wave_shr:1 row_mask:0xf bank_mask:0xf bound_ctrl:1
	v_add_f32_dpp v89, v147, v147 wave_shr:1 row_mask:0xf bank_mask:0xf bound_ctrl:1
	v_add_f32_dpp v90, v202, v202 wave_shr:1 row_mask:0xf bank_mask:0xf bound_ctrl:1
	v_add_f32_dpp v91, v203, v203 wave_shr:1 row_mask:0xf bank_mask:0xf bound_ctrl:1
	v_add_f32_dpp v92, v208, v208 wave_shr:1 row_mask:0xf bank_mask:0xf bound_ctrl:1
	v_add_f32_dpp v94, v210, v210 wave_shr:1 row_mask:0xf bank_mask:0xf bound_ctrl:1
	v_add_f32_dpp v95, v211, v211 wave_shr:1 row_mask:0xf bank_mask:0xf bound_ctrl:1
	v_add_f32_dpp v102, v212, v212 wave_shr:1 row_mask:0xf bank_mask:0xf bound_ctrl:1
	v_add_f32_dpp v103, v213, v213 wave_shr:1 row_mask:0xf bank_mask:0xf bound_ctrl:1
	v_add_f32_dpp v122, v214, v214 wave_shr:1 row_mask:0xf bank_mask:0xf bound_ctrl:1
	v_add_f32_dpp v70, v142, v70 wave_shl:1 row_mask:0xf bank_mask:0xf bound_ctrl:1
	v_add_f32_dpp v71, v143, v71 wave_shl:1 row_mask:0xf bank_mask:0xf bound_ctrl:1
	v_add_f32_dpp v74, v198, v74 wave_shl:1 row_mask:0xf bank_mask:0xf bound_ctrl:1
	v_add_f32_dpp v75, v199, v75 wave_shl:1 row_mask:0xf bank_mask:0xf bound_ctrl:1
	v_add_f32_dpp v76, v204, v76 wave_shl:1 row_mask:0xf bank_mask:0xf bound_ctrl:1
	v_add_f32_dpp v78, v144, v78 wave_shl:1 row_mask:0xf bank_mask:0xf bound_ctrl:1
	v_add_f32_dpp v79, v145, v79 wave_shl:1 row_mask:0xf bank_mask:0xf bound_ctrl:1
	v_add_f32_dpp v80, v200, v80 wave_shl:1 row_mask:0xf bank_mask:0xf bound_ctrl:1
	v_add_f32_dpp v81, v201, v81 wave_shl:1 row_mask:0xf bank_mask:0xf bound_ctrl:1
	v_add_f32_dpp v82, v206, v82 wave_shl:1 row_mask:0xf bank_mask:0xf bound_ctrl:1
	v_add_f32_dpp v88, v146, v88 wave_shl:1 row_mask:0xf bank_mask:0xf bound_ctrl:1
	v_add_f32_dpp v89, v147, v89 wave_shl:1 row_mask:0xf bank_mask:0xf bound_ctrl:1
	v_add_f32_dpp v90, v202, v90 wave_shl:1 row_mask:0xf bank_mask:0xf bound_ctrl:1
	v_add_f32_dpp v91, v203, v91 wave_shl:1 row_mask:0xf bank_mask:0xf bound_ctrl:1
	v_add_f32_dpp v92, v208, v92 wave_shl:1 row_mask:0xf bank_mask:0xf bound_ctrl:1
	v_add_f32_dpp v94, v210, v94 wave_shl:1 row_mask:0xf bank_mask:0xf bound_ctrl:1
	v_add_f32_dpp v95, v211, v95 wave_shl:1 row_mask:0xf bank_mask:0xf bound_ctrl:1
	v_add_f32_dpp v102, v212, v102 wave_shl:1 row_mask:0xf bank_mask:0xf bound_ctrl:1
	v_add_f32_dpp v103, v213, v103 wave_shl:1 row_mask:0xf bank_mask:0xf bound_ctrl:1
	v_add_f32_dpp v122, v214, v122 wave_shl:1 row_mask:0xf bank_mask:0xf bound_ctrl:1
	v_pk_add_f32 v[142:143], v[148:149], v[70:71]
	v_pk_add_f32 v[144:145], v[68:69], v[74:75]
	v_add_f32_e64 v68, v72, v76
	v_pk_add_f32 v[72:73], v[104:105], v[78:79]
	v_pk_add_f32 v[104:105], v[106:107], v[80:81]
	v_add_f32_e64 v106, v108, v82
	v_pk_add_f32 v[108:109], v[110:111], v[88:89]
	v_pk_add_f32 v[110:111], v[112:113], v[90:91]
	v_add_f32_e64 v112, v114, v92
	v_pk_add_f32 v[114:115], v[116:117], v[94:95]
	v_pk_add_f32 v[116:117], v[118:119], v[102:103]
	v_add_f32_e64 v118, v120, v122
	v_pk_fma_f32 v[114:115], v[36:37], v[142:143], v[114:115] op_sel_hi:[0,1,1]
	v_pk_fma_f32 v[116:117], v[36:37], v[144:145], v[116:117] op_sel_hi:[0,1,1]
	v_fma_f32 v118, v36, v68, v118
	v_pk_fma_f32 v[114:115], v[36:37], v[72:73], v[114:115] op_sel:[1,0,0]
	v_pk_fma_f32 v[116:117], v[36:37], v[104:105], v[116:117] op_sel:[1,0,0]
	v_fma_f32 v118, v37, v106, v118
	v_pk_fma_f32 v[114:115], v[38:39], v[108:109], v[114:115] op_sel_hi:[0,1,1]
	v_pk_fma_f32 v[116:117], v[38:39], v[110:111], v[116:117] op_sel_hi:[0,1,1]
	v_fma_f32 v118, v38, v112, v118
	v_cndmask_b32_e64 v120, 0, v1, s[10:11]
	v_cndmask_b32_e64 v121, 0, v1, s[14:15]
	v_cndmask_b32_e64 v146, 0, v1, s[20:21]
	v_cndmask_b32_e64 v147, 0, v1, s[22:23]
	v_cndmask_b32_e64 v148, 0, v1, s[30:31]
	v_pk_fma_f32 v[114:115], v[20:21], v[86:87], v[114:115] op_sel_hi:[1,0,1] neg_lo:[0,0,1] neg_hi:[0,0,1]
	v_pk_fma_f32 v[116:117], v[24:25], v[86:87], v[116:117] op_sel_hi:[1,0,1] neg_lo:[0,0,1] neg_hi:[0,0,1]
	v_fma_f32 v118, v30, v86, -v118
	s_add_i32 s4, s34, 5
	s_cmpk_lt_i32 s4, 0x201
	s_cselect_b64 s[12:13], s[0:1], 0
	v_pk_add_f32 v[114:115], v[114:115], v[120:121] neg_lo:[0,1] neg_hi:[0,1]
	v_pk_add_f32 v[116:117], v[116:117], v[146:147] neg_lo:[0,1] neg_hi:[0,1]
	v_add_f32_e64 v118, v118, -v148
	v_pk_mul_f32 v[198:199], v[114:115], v[114:115]
	v_pk_fma_f32 v[198:199], v[116:117], v[116:117], v[198:199]
	v_add_f32_e32 v198, v198, v199
	v_fma_f32 v198, v118, v118, v198
	v_cndmask_b32_e64 v199, 0, v198, s[12:13]
	v_add_f32_e32 v0, v0, v199
	s_add_i32 s4, s34, 10
	s_min_i32 s4, s4, 0x200
	s_mul_i32 s5, s4, 0x804
	s_add_i32 s5, s5, s35
	s_add_i32 s6, s5, 0x0
	s_add_i32 s7, s5, 0x101004
	s_add_i32 s8, s5, 0x202008
	s_add_i32 s11, s5, 0x30300c
	s_add_i32 s15, s5, 0x404010
	s_mul_i32 s9, s4, 0x180c
	s_add_i32 s9, s9, s33
	buffer_load_dword v20, v28, s[16:19], s6 offen nt
	buffer_load_dword v21, v28, s[16:19], s7 offen nt
	buffer_load_dword v24, v28, s[16:19], s8 offen nt
	buffer_load_dword v25, v28, s[16:19], s11 offen nt
	buffer_load_dword v30, v28, s[16:19], s15 offen nt
	buffer_load_dwordx3 v[36:38], v27, s[24:27], s9 offen nt
	s_waitcnt vmcnt(12)
	v_pk_mul_f32 v[60:61], v[2:3], v[8:9] op_sel_hi:[1,0]
	v_pk_mul_f32 v[62:63], v[4:5], v[8:9] op_sel_hi:[1,0]
	v_mul_f32_e64 v64, v6, v8
	v_pk_mul_f32 v[66:67], v[2:3], v[8:9] op_sel:[0,1]
	v_pk_mul_f32 v[68:69], v[4:5], v[8:9] op_sel:[0,1]
	v_mul_f32_e64 v72, v6, v9
	v_pk_mul_f32 v[84:85], v[2:3], v[10:11] op_sel_hi:[1,0]
	v_pk_mul_f32 v[86:87], v[4:5], v[10:11] op_sel_hi:[1,0]
	v_mul_f32_e64 v104, v6, v10
	v_add_f32_dpp v106, v2, v2 wave_shr:1 row_mask:0xf bank_mask:0xf bound_ctrl:1
	v_add_f32_dpp v107, v3, v3 wave_shr:1 row_mask:0xf bank_mask:0xf bound_ctrl:1
	v_add_f32_dpp v108, v4, v4 wave_shr:1 row_mask:0xf bank_mask:0xf bound_ctrl:1
	v_add_f32_dpp v109, v5, v5 wave_shr:1 row_mask:0xf bank_mask:0xf bound_ctrl:1
	v_add_f32_dpp v110, v6, v6 wave_shr:1 row_mask:0xf bank_mask:0xf bound_ctrl:1
	v_add_f32_dpp v112, v60, v60 wave_shr:1 row_mask:0xf bank_mask:0xf bound_ctrl:1
	v_add_f32_dpp v113, v61, v61 wave_shr:1 row_mask:0xf bank_mask:0xf bound_ctrl:1
	v_add_f32_dpp v114, v62, v62 wave_shr:1 row_mask:0xf bank_mask:0xf bound_ctrl:1
	v_add_f32_dpp v115, v63, v63 wave_shr:1 row_mask:0xf bank_mask:0xf bound_ctrl:1
	v_add_f32_dpp v116, v64, v64 wave_shr:1 row_mask:0xf bank_mask:0xf bound_ctrl:1
	v_add_f32_dpp v118, v66, v66 wave_shr:1 row_mask:0xf bank_mask:0xf bound_ctrl:1
	v_add_f32_dpp v119, v67, v67 wave_shr:1 row_mask:0xf bank_mask:0xf bound_ctrl:1
	v_add_f32_dpp v120, v68, v68 wave_shr:1 row_mask:0xf bank_mask:0xf bound_ctrl:1
	v_add_f32_dpp v121, v69, v69 wave_shr:1 row_mask:0xf bank_mask:0xf bound_ctrl:1
	v_add_f32_dpp v142, v72, v72 wave_shr:1 row_mask:0xf bank_mask:0xf bound_ctrl:1
	v_add_f32_dpp v144, v84, v84 wave_shr:1 row_mask:0xf bank_mask:0xf bound_ctrl:1
	v_add_f32_dpp v145, v85, v85 wave_shr:1 row_mask:0xf bank_mask:0xf bound_ctrl:1
	v_add_f32_dpp v146, v86, v86 wave_shr:1 row_mask:0xf bank_mask:0xf bound_ctrl:1
	v_add_f32_dpp v147, v87, v87 wave_shr:1 row_mask:0xf bank_mask:0xf bound_ctrl:1
	v_add_f32_dpp v148, v104, v104 wave_shr:1 row_mask:0xf bank_mask:0xf bound_ctrl:1
	v_add_f32_dpp v106, v2, v106 wave_shl:1 row_mask:0xf bank_mask:0xf bound_ctrl:1
	v_add_f32_dpp v107, v3, v107 wave_shl:1 row_mask:0xf bank_mask:0xf bound_ctrl:1
	v_add_f32_dpp v108, v4, v108 wave_shl:1 row_mask:0xf bank_mask:0xf bound_ctrl:1
	v_add_f32_dpp v109, v5, v109 wave_shl:1 row_mask:0xf bank_mask:0xf bound_ctrl:1
	v_add_f32_dpp v110, v6, v110 wave_shl:1 row_mask:0xf bank_mask:0xf bound_ctrl:1
	v_add_f32_dpp v112, v60, v112 wave_shl:1 row_mask:0xf bank_mask:0xf bound_ctrl:1
	v_add_f32_dpp v113, v61, v113 wave_shl:1 row_mask:0xf bank_mask:0xf bound_ctrl:1
	v_add_f32_dpp v114, v62, v114 wave_shl:1 row_mask:0xf bank_mask:0xf bound_ctrl:1
	v_add_f32_dpp v115, v63, v115 wave_shl:1 row_mask:0xf bank_mask:0xf bound_ctrl:1
	v_add_f32_dpp v116, v64, v116 wave_shl:1 row_mask:0xf bank_mask:0xf bound_ctrl:1
	v_add_f32_dpp v118, v66, v118 wave_shl:1 row_mask:0xf bank_mask:0xf bound_ctrl:1
	v_add_f32_dpp v119, v67, v119 wave_shl:1 row_mask:0xf bank_mask:0xf bound_ctrl:1
	v_add_f32_dpp v120, v68, v120 wave_shl:1 row_mask:0xf bank_mask:0xf bound_ctrl:1
	v_add_f32_dpp v121, v69, v121 wave_shl:1 row_mask:0xf bank_mask:0xf bound_ctrl:1
	v_add_f32_dpp v142, v72, v142 wave_shl:1 row_mask:0xf bank_mask:0xf bound_ctrl:1
	v_add_f32_dpp v144, v84, v144 wave_shl:1 row_mask:0xf bank_mask:0xf bound_ctrl:1
	v_add_f32_dpp v145, v85, v145 wave_shl:1 row_mask:0xf bank_mask:0xf bound_ctrl:1
	v_add_f32_dpp v146, v86, v146 wave_shl:1 row_mask:0xf bank_mask:0xf bound_ctrl:1
	v_add_f32_dpp v147, v87, v147 wave_shl:1 row_mask:0xf bank_mask:0xf bound_ctrl:1
	v_add_f32_dpp v148, v104, v148 wave_shl:1 row_mask:0xf bank_mask:0xf bound_ctrl:1
	s_barrier
	ds_read_b128 v[60:63], v23 offset:0
	ds_read_b128 v[64:67], v23 offset:1024
	ds_read_b128 v[84:87], v23 offset:2048
	v_pk_add_f32 v[68:69], v[174:175], v[106:107]
	v_pk_add_f32 v[72:73], v[100:101], v[68:69]
	v_pk_add_f32 v[100:101], v[176:177], v[108:109]
	v_pk_add_f32 v[104:105], v[124:125], v[100:101]
	v_add_f32_e64 v124, v178, v110
	v_add_f32_e64 v174, v126, v124
	v_pk_add_f32 v[126:127], v[180:181], v[112:113]
	v_pk_add_f32 v[176:177], v[128:129], v[126:127]
	v_pk_add_f32 v[128:129], v[182:183], v[114:115]
	v_pk_add_f32 v[178:179], v[130:131], v[128:129]
	v_add_f32_e64 v130, v184, v116
	v_add_f32_e64 v180, v132, v130
	v_pk_add_f32 v[132:133], v[186:187], v[118:119]
	v_pk_add_f32 v[182:183], v[134:135], v[132:133]
	v_pk_add_f32 v[134:135], v[188:189], v[120:121]
	v_pk_add_f32 v[184:185], v[136:137], v[134:135]
	v_add_f32_e64 v136, v190, v142
	v_add_f32_e64 v186, v138, v136
	v_pk_add_f32 v[138:139], v[192:193], v[144:145]
	v_pk_add_f32 v[188:189], v[140:141], v[138:139]
	v_pk_add_f32 v[140:141], v[194:195], v[146:147]
	v_pk_add_f32 v[190:191], v[170:171], v[140:141]
	v_add_f32_e64 v170, v196, v148
	v_add_f32_e64 v192, v172, v170
	s_waitcnt lgkmcnt(2)
	v_pk_fma_f32 v[176:177], v[60:61], v[72:73], v[176:177] op_sel_hi:[0,1,1] neg_lo:[1,0,0] neg_hi:[1,0,0]
	v_pk_fma_f32 v[178:179], v[60:61], v[104:105], v[178:179] op_sel_hi:[0,1,1] neg_lo:[1,0,0] neg_hi:[1,0,0]
	v_fma_f32 v180, -v60, v174, v180
	v_pk_fma_f32 v[182:183], v[60:61], v[72:73], v[182:183] op_sel:[1,0,0] neg_lo:[1,0,0] neg_hi:[1,0,0]
	v_pk_fma_f32 v[184:185], v[60:61], v[104:105], v[184:185] op_sel:[1,0,0] neg_lo:[1,0,0] neg_hi:[1,0,0]
	v_fma_f32 v186, -v61, v174, v186
	v_pk_fma_f32 v[188:189], v[62:63], v[72:73], v[188:189] op_sel_hi:[0,1,1] neg_lo:[1,0,0] neg_hi:[1,0,0]
	v_pk_fma_f32 v[190:191], v[62:63], v[104:105], v[190:191] op_sel_hi:[0,1,1] neg_lo:[1,0,0] neg_hi:[1,0,0]
	v_fma_f32 v192, -v62, v174, v192
	v_pk_mul_f32 v[172:173], v[62:63], v[176:177] op_sel:[1,0]
	v_pk_mul_f32 v[198:199], v[62:63], v[178:179] op_sel:[1,0]
	v_mul_f32_e64 v204, v63, v180
	s_waitcnt lgkmcnt(1)
	v_pk_mul_f32 v[194:195], v[64:65], v[176:177] op_sel_hi:[0,1]
	v_pk_mul_f32 v[200:201], v[64:65], v[178:179] op_sel_hi:[0,1]
	v_mul_f32_e64 v206, v64, v180
	v_pk_mul_f32 v[196:197], v[64:65], v[176:177] op_sel:[1,0]
	v_pk_mul_f32 v[202:203], v[64:65], v[178:179] op_sel:[1,0]
	v_mul_f32_e64 v208, v65, v180
	v_pk_fma_f32 v[172:173], v[64:65], v[182:183], v[172:173] op_sel_hi:[0,1,1]
	v_pk_fma_f32 v[198:199], v[64:65], v[184:185], v[198:199] op_sel_hi:[0,1,1]
	v_fma_f32 v204, v64, v186, v204
	v_pk_fma_f32 v[194:195], v[66:67], v[182:183], v[194:195] op_sel_hi:[0,1,1]
	v_pk_fma_f32 v[200:201], v[66:67], v[184:185], v[200:201] op_sel_hi:[0,1,1]
	v_fma_f32 v206, v66, v186, v206
	v_pk_fma_f32 v[196:197], v[66:67], v[182:183], v[196:197] op_sel:[1,0,0]
	v_pk_fma_f32 v[202:203], v[66:67], v[184:185], v[202:203] op_sel:[1,0,0]
	v_fma_f32 v208, v67, v186, v208
	v_pk_fma_f32 v[172:173], v[64:65], v[188:189], v[172:173] op_sel:[1,0,0]
	v_pk_fma_f32 v[198:199], v[64:65], v[190:191], v[198:199] op_sel:[1,0,0]
	v_fma_f32 v204, v65, v192, v204
	v_pk_fma_f32 v[194:195], v[66:67], v[188:189], v[194:195] op_sel:[1,0,0]
	v_pk_fma_f32 v[200:201], v[66:67], v[190:191], v[200:201] op_sel:[1,0,0]
	v_fma_f32 v206, v67, v192, v206
	s_waitcnt lgkmcnt(0)
	v_pk_fma_f32 v[196:197], v[84:85], v[188:189], v[196:197] op_sel_hi:[0,1,1]
	v_pk_fma_f32 v[202:203], v[84:85], v[190:191], v[202:203] op_sel_hi:[0,1,1]
	v_fma_f32 v208, v84, v192, v208
	v_pk_mul_f32 v[210:211], v[60:61], v[172:173] op_sel_hi:[0,1]
	v_pk_mul_f32 v[212:213], v[60:61], v[198:199] op_sel_hi:[0,1]
	v_mul_f32_e64 v214, v60, v204
	v_pk_fma_f32 v[210:211], v[60:61], v[194:195], v[210:211] op_sel:[1,0,0]
	v_pk_fma_f32 v[212:213], v[60:61], v[200:201], v[212:213] op_sel:[1,0,0]
	v_fma_f32 v214, v61, v206, v214
	v_pk_fma_f32 v[210:211], v[62:63], v[196:197], v[210:211] op_sel_hi:[0,1,1]
	v_pk_fma_f32 v[212:213], v[62:63], v[202:203], v[212:213] op_sel_hi:[0,1,1]
	v_fma_f32 v214, v62, v208, v214
	v_pk_fma_f32 v[210:211], v[84:85], v[72:73], v[210:211] op_sel:[1,0,0] neg_lo:[0,0,1] neg_hi:[0,0,1]
	v_pk_fma_f32 v[212:213], v[84:85], v[104:105], v[212:213] op_sel:[1,0,0] neg_lo:[0,0,1] neg_hi:[0,0,1]
	v_fma_f32 v214, v85, v174, -v214
	v_cmp_eq_u32_e64 s[10:11], 1, v87
	v_cmp_eq_u32_e64 s[14:15], 2, v87
	v_cmp_eq_u32_e64 s[20:21], 3, v87
	v_cmp_eq_u32_e64 s[22:23], 4, v87
	v_cmp_eq_u32_e64 s[30:31], 5, v87
	v_add_f32_dpp v72, v172, v172 wave_shr:1 row_mask:0xf bank_mask:0xf bound_ctrl:1
	v_add_f32_dpp v73, v173, v173 wave_shr:1 row_mask:0xf bank_mask:0xf bound_ctrl:1
	v_add_f32_dpp v104, v198, v198 wave_shr:1 row_mask:0xf bank_mask:0xf bound_ctrl:1
	v_add_f32_dpp v105, v199, v199 wave_shr:1 row_mask:0xf bank_mask:0xf bound_ctrl:1
	v_add_f32_dpp v174, v204, v204 wave_shr:1 row_mask:0xf bank_mask:0xf bound_ctrl:1
	v_add_f32_dpp v176, v194, v194 wave_shr:1 row_mask:0xf bank_mask:0xf bound_ctrl:1
	v_add_f32_dpp v177, v195, v195 wave_shr:1 row_mask:0xf bank_mask:0xf bound_ctrl:1
	v_add_f32_dpp v178, v200, v200 wave_shr:1 row_mask:0xf bank_mask:0xf bound_ctrl:1
	v_add_f32_dpp v179, v201, v201 wave_shr:1 row_mask:0xf bank_mask:0xf bound_ctrl:1
	v_add_f32_dpp v180, v206, v206 wave_shr:1 row_mask:0xf bank_mask:0xf bound_ctrl:1
	v_add_f32_dpp v182, v196, v196 wave_shr:1 row_mask:0xf bank_mask:0xf bound_ctrl:1
	v_add_f32_dpp v183, v197, v197 wave_shr:1 row_mask:0xf bank_mask:0xf bound_ctrl:1
	v_add_f32_dpp v184, v202, v202 wave_shr:1 row_mask:0xf bank_mask:0xf bound_ctrl:1
	v_add_f32_dpp v185, v203, v203 wave_shr:1 row_mask:0xf bank_mask:0xf bound_ctrl:1
	v_add_f32_dpp v186, v208, v208 wave_shr:1 row_mask:0xf bank_mask:0xf bound_ctrl:1
	v_add_f32_dpp v188, v210, v210 wave_shr:1 row_mask:0xf bank_mask:0xf bound_ctrl:1
	v_add_f32_dpp v189, v211, v211 wave_shr:1 row_mask:0xf bank_mask:0xf bound_ctrl:1
	v_add_f32_dpp v190, v212, v212 wave_shr:1 row_mask:0xf bank_mask:0xf bound_ctrl:1
	v_add_f32_dpp v191, v213, v213 wave_shr:1 row_mask:0xf bank_mask:0xf bound_ctrl:1
	v_add_f32_dpp v192, v214, v214 wave_shr:1 row_mask:0xf bank_mask:0xf bound_ctrl:1
	v_add_f32_dpp v72, v172, v72 wave_shl:1 row_mask:0xf bank_mask:0xf bound_ctrl:1
	v_add_f32_dpp v73, v173, v73 wave_shl:1 row_mask:0xf bank_mask:0xf bound_ctrl:1
	v_add_f32_dpp v104, v198, v104 wave_shl:1 row_mask:0xf bank_mask:0xf bound_ctrl:1
	v_add_f32_dpp v105, v199, v105 wave_shl:1 row_mask:0xf bank_mask:0xf bound_ctrl:1
	v_add_f32_dpp v174, v204, v174 wave_shl:1 row_mask:0xf bank_mask:0xf bound_ctrl:1
	v_add_f32_dpp v176, v194, v176 wave_shl:1 row_mask:0xf bank_mask:0xf bound_ctrl:1
	v_add_f32_dpp v177, v195, v177 wave_shl:1 row_mask:0xf bank_mask:0xf bound_ctrl:1
	v_add_f32_dpp v178, v200, v178 wave_shl:1 row_mask:0xf bank_mask:0xf bound_ctrl:1
	v_add_f32_dpp v179, v201, v179 wave_shl:1 row_mask:0xf bank_mask:0xf bound_ctrl:1
	v_add_f32_dpp v180, v206, v180 wave_shl:1 row_mask:0xf bank_mask:0xf bound_ctrl:1
	v_add_f32_dpp v182, v196, v182 wave_shl:1 row_mask:0xf bank_mask:0xf bound_ctrl:1
	v_add_f32_dpp v183, v197, v183 wave_shl:1 row_mask:0xf bank_mask:0xf bound_ctrl:1
	v_add_f32_dpp v184, v202, v184 wave_shl:1 row_mask:0xf bank_mask:0xf bound_ctrl:1
	v_add_f32_dpp v185, v203, v185 wave_shl:1 row_mask:0xf bank_mask:0xf bound_ctrl:1
	v_add_f32_dpp v186, v208, v186 wave_shl:1 row_mask:0xf bank_mask:0xf bound_ctrl:1
	v_add_f32_dpp v188, v210, v188 wave_shl:1 row_mask:0xf bank_mask:0xf bound_ctrl:1
	v_add_f32_dpp v189, v211, v189 wave_shl:1 row_mask:0xf bank_mask:0xf bound_ctrl:1
	v_add_f32_dpp v190, v212, v190 wave_shl:1 row_mask:0xf bank_mask:0xf bound_ctrl:1
	v_add_f32_dpp v191, v213, v191 wave_shl:1 row_mask:0xf bank_mask:0xf bound_ctrl:1
	v_add_f32_dpp v192, v214, v192 wave_shl:1 row_mask:0xf bank_mask:0xf bound_ctrl:1
	v_pk_add_f32 v[172:173], v[70:71], v[72:73]
	v_pk_add_f32 v[194:195], v[96:97], v[172:173]
	v_pk_add_f32 v[70:71], v[74:75], v[104:105]
	v_pk_add_f32 v[96:97], v[98:99], v[70:71]
	v_add_f32_e64 v74, v76, v174
	v_add_f32_e64 v98, v150, v74
	v_pk_add_f32 v[76:77], v[78:79], v[176:177]
	v_pk_add_f32 v[150:151], v[152:153], v[76:77]
	v_pk_add_f32 v[78:79], v[80:81], v[178:179]
	v_pk_add_f32 v[152:153], v[154:155], v[78:79]
	v_add_f32_e64 v80, v82, v180
	v_add_f32_e64 v154, v156, v80
	v_pk_add_f32 v[82:83], v[88:89], v[182:183]
	v_pk_add_f32 v[156:157], v[158:159], v[82:83]
	v_pk_add_f32 v[88:89], v[90:91], v[184:185]
	v_pk_add_f32 v[158:159], v[160:161], v[88:89]
	v_add_f32_e64 v90, v92, v186
	v_add_f32_e64 v160, v162, v90
	v_pk_add_f32 v[92:93], v[94:95], v[188:189]
	v_pk_add_f32 v[162:163], v[164:165], v[92:93]
	v_pk_add_f32 v[94:95], v[102:103], v[190:191]
	v_pk_add_f32 v[164:165], v[166:167], v[94:95]
	v_add_f32_e64 v102, v122, v192
	v_add_f32_e64 v166, v168, v102
	v_pk_fma_f32 v[162:163], v[48:49], v[194:195], v[162:163] op_sel_hi:[0,1,1]
	v_pk_fma_f32 v[164:165], v[48:49], v[96:97], v[164:165] op_sel_hi:[0,1,1]
	v_fma_f32 v166, v48, v98, v166
	v_pk_fma_f32 v[162:163], v[48:49], v[150:151], v[162:163] op_sel:[1,0,0]
	v_pk_fma_f32 v[164:165], v[48:49], v[152:153], v[164:165] op_sel:[1,0,0]
	v_fma_f32 v166, v49, v154, v166
	v_pk_fma_f32 v[162:163], v[50:51], v[156:157], v[162:163] op_sel_hi:[0,1,1]
	v_pk_fma_f32 v[164:165], v[50:51], v[158:159], v[164:165] op_sel_hi:[0,1,1]
	v_fma_f32 v166, v50, v160, v166
	v_cndmask_b32_e64 v122, 0, v1, s[10:11]
	v_cndmask_b32_e64 v123, 0, v1, s[14:15]
	v_cndmask_b32_e64 v168, 0, v1, s[20:21]
	v_cndmask_b32_e64 v169, 0, v1, s[22:23]
	v_cndmask_b32_e64 v196, 0, v1, s[30:31]
	v_pk_fma_f32 v[162:163], v[40:41], v[86:87], v[162:163] op_sel_hi:[1,0,1] neg_lo:[0,0,1] neg_hi:[0,0,1]
	v_pk_fma_f32 v[164:165], v[42:43], v[86:87], v[164:165] op_sel_hi:[1,0,1] neg_lo:[0,0,1] neg_hi:[0,0,1]
	v_fma_f32 v166, v44, v86, -v166
	s_add_i32 s4, s34, 6
	s_cmpk_lt_i32 s4, 0x201
	s_cselect_b64 s[12:13], s[0:1], 0
	v_pk_add_f32 v[162:163], v[162:163], v[122:123] neg_lo:[0,1] neg_hi:[0,1]
	v_pk_add_f32 v[164:165], v[164:165], v[168:169] neg_lo:[0,1] neg_hi:[0,1]
	v_add_f32_e64 v166, v166, -v196
	v_pk_mul_f32 v[198:199], v[162:163], v[162:163]
	v_pk_fma_f32 v[198:199], v[164:165], v[164:165], v[198:199]
	v_add_f32_e32 v198, v198, v199
	v_fma_f32 v198, v166, v166, v198
	v_cndmask_b32_e64 v199, 0, v198, s[12:13]
	v_add_f32_e32 v0, v0, v199
	s_add_i32 s4, s34, 11
	s_min_i32 s4, s4, 0x200
	s_mul_i32 s5, s4, 0x804
	s_add_i32 s5, s5, s35
	s_add_i32 s6, s5, 0x0
	s_add_i32 s7, s5, 0x101004
	s_add_i32 s8, s5, 0x202008
	s_add_i32 s11, s5, 0x30300c
	s_add_i32 s15, s5, 0x404010
	s_mul_i32 s9, s4, 0x180c
	s_add_i32 s9, s9, s33
	buffer_load_dword v40, v28, s[16:19], s6 offen nt
	buffer_load_dword v41, v28, s[16:19], s7 offen nt
	buffer_load_dword v42, v28, s[16:19], s8 offen nt
	buffer_load_dword v43, v28, s[16:19], s11 offen nt
	buffer_load_dword v44, v28, s[16:19], s15 offen nt
	buffer_load_dwordx3 v[48:50], v27, s[24:27], s9 offen nt
	s_waitcnt vmcnt(12)
	v_pk_mul_f32 v[60:61], v[12:13], v[32:33] op_sel_hi:[1,0]
	v_pk_mul_f32 v[62:63], v[14:15], v[32:33] op_sel_hi:[1,0]
	v_mul_f32_e64 v64, v16, v32
	v_pk_mul_f32 v[66:67], v[12:13], v[32:33] op_sel:[0,1]
	v_pk_mul_f32 v[84:85], v[14:15], v[32:33] op_sel:[0,1]
	v_mul_f32_e64 v86, v16, v33
	v_pk_mul_f32 v[96:97], v[12:13], v[34:35] op_sel_hi:[1,0]
	v_pk_mul_f32 v[98:99], v[14:15], v[34:35] op_sel_hi:[1,0]
	v_mul_f32_e64 v122, v16, v34
	v_add_f32_dpp v150, v12, v12 wave_shr:1 row_mask:0xf bank_mask:0xf bound_ctrl:1
	v_add_f32_dpp v151, v13, v13 wave_shr:1 row_mask:0xf bank_mask:0xf bound_ctrl:1
	v_add_f32_dpp v152, v14, v14 wave_shr:1 row_mask:0xf bank_mask:0xf bound_ctrl:1
	v_add_f32_dpp v153, v15, v15 wave_shr:1 row_mask:0xf bank_mask:0xf bound_ctrl:1
	v_add_f32_dpp v154, v16, v16 wave_shr:1 row_mask:0xf bank_mask:0xf bound_ctrl:1
	v_add_f32_dpp v156, v60, v60 wave_shr:1 row_mask:0xf bank_mask:0xf bound_ctrl:1
	v_add_f32_dpp v157, v61, v61 wave_shr:1 row_mask:0xf bank_mask:0xf bound_ctrl:1
	v_add_f32_dpp v158, v62, v62 wave_shr:1 row_mask:0xf bank_mask:0xf bound_ctrl:1
	v_add_f32_dpp v159, v63, v63 wave_shr:1 row_mask:0xf bank_mask:0xf bound_ctrl:1
	v_add_f32_dpp v160, v64, v64 wave_shr:1 row_mask:0xf bank_mask:0xf bound_ctrl:1
	v_add_f32_dpp v162, v66, v66 wave_shr:1 row_mask:0xf bank_mask:0xf bound_ctrl:1
	v_add_f32_dpp v163, v67, v67 wave_shr:1 row_mask:0xf bank_mask:0xf bound_ctrl:1
	v_add_f32_dpp v164, v84, v84 wave_shr:1 row_mask:0xf bank_mask:0xf bound_ctrl:1
	v_add_f32_dpp v165, v85, v85 wave_shr:1 row_mask:0xf bank_mask:0xf bound_ctrl:1
	v_add_f32_dpp v166, v86, v86 wave_shr:1 row_mask:0xf bank_mask:0xf bound_ctrl:1
	v_add_f32_dpp v168, v96, v96 wave_shr:1 row_mask:0xf bank_mask:0xf bound_ctrl:1
	v_add_f32_dpp v169, v97, v97 wave_shr:1 row_mask:0xf bank_mask:0xf bound_ctrl:1
	v_add_f32_dpp v194, v98, v98 wave_shr:1 row_mask:0xf bank_mask:0xf bound_ctrl:1
	v_add_f32_dpp v195, v99, v99 wave_shr:1 row_mask:0xf bank_mask:0xf bound_ctrl:1
	v_add_f32_dpp v196, v122, v122 wave_shr:1 row_mask:0xf bank_mask:0xf bound_ctrl:1
	v_add_f32_dpp v150, v12, v150 wave_shl:1 row_mask:0xf bank_mask:0xf bound_ctrl:1
	v_add_f32_dpp v151, v13, v151 wave_shl:1 row_mask:0xf bank_mask:0xf bound_ctrl:1
	v_add_f32_dpp v152, v14, v152 wave_shl:1 row_mask:0xf bank_mask:0xf bound_ctrl:1
	v_add_f32_dpp v153, v15, v153 wave_shl:1 row_mask:0xf bank_mask:0xf bound_ctrl:1
	v_add_f32_dpp v154, v16, v154 wave_shl:1 row_mask:0xf bank_mask:0xf bound_ctrl:1
	v_add_f32_dpp v156, v60, v156 wave_shl:1 row_mask:0xf bank_mask:0xf bound_ctrl:1
	v_add_f32_dpp v157, v61, v157 wave_shl:1 row_mask:0xf bank_mask:0xf bound_ctrl:1
	v_add_f32_dpp v158, v62, v158 wave_shl:1 row_mask:0xf bank_mask:0xf bound_ctrl:1
	v_add_f32_dpp v159, v63, v159 wave_shl:1 row_mask:0xf bank_mask:0xf bound_ctrl:1
	v_add_f32_dpp v160, v64, v160 wave_shl:1 row_mask:0xf bank_mask:0xf bound_ctrl:1
	v_add_f32_dpp v162, v66, v162 wave_shl:1 row_mask:0xf bank_mask:0xf bound_ctrl:1
	v_add_f32_dpp v163, v67, v163 wave_shl:1 row_mask:0xf bank_mask:0xf bound_ctrl:1
	v_add_f32_dpp v164, v84, v164 wave_shl:1 row_mask:0xf bank_mask:0xf bound_ctrl:1
	v_add_f32_dpp v165, v85, v165 wave_shl:1 row_mask:0xf bank_mask:0xf bound_ctrl:1
	v_add_f32_dpp v166, v86, v166 wave_shl:1 row_mask:0xf bank_mask:0xf bound_ctrl:1
	v_add_f32_dpp v168, v96, v168 wave_shl:1 row_mask:0xf bank_mask:0xf bound_ctrl:1
	v_add_f32_dpp v169, v97, v169 wave_shl:1 row_mask:0xf bank_mask:0xf bound_ctrl:1
	v_add_f32_dpp v194, v98, v194 wave_shl:1 row_mask:0xf bank_mask:0xf bound_ctrl:1
	v_add_f32_dpp v195, v99, v195 wave_shl:1 row_mask:0xf bank_mask:0xf bound_ctrl:1
	v_add_f32_dpp v196, v122, v196 wave_shl:1 row_mask:0xf bank_mask:0xf bound_ctrl:1
	s_barrier
	ds_read_b128 v[60:63], v23 offset:3072
	ds_read_b128 v[64:67], v23 offset:4096
	ds_read_b128 v[84:87], v23 offset:5120
	v_pk_add_f32 v[96:97], v[68:69], v[150:151]
	v_pk_add_f32 v[68:69], v[100:101], v[152:153]
	v_add_f32_e64 v98, v124, v154
	v_pk_add_f32 v[100:101], v[126:127], v[156:157]
	v_pk_add_f32 v[122:123], v[128:129], v[158:159]
	v_add_f32_e64 v124, v130, v160
	v_pk_add_f32 v[126:127], v[132:133], v[162:163]
	v_pk_add_f32 v[128:129], v[134:135], v[164:165]
	v_add_f32_e64 v130, v136, v166
	v_pk_add_f32 v[132:133], v[138:139], v[168:169]
	v_pk_add_f32 v[134:135], v[140:141], v[194:195]
	v_add_f32_e64 v136, v170, v196
	s_waitcnt lgkmcnt(2)
	v_pk_fma_f32 v[100:101], v[60:61], v[96:97], v[100:101] op_sel_hi:[0,1,1] neg_lo:[1,0,0] neg_hi:[1,0,0]
	v_pk_fma_f32 v[122:123], v[60:61], v[68:69], v[122:123] op_sel_hi:[0,1,1] neg_lo:[1,0,0] neg_hi:[1,0,0]
	v_fma_f32 v124, -v60, v98, v124
	v_pk_fma_f32 v[126:127], v[60:61], v[96:97], v[126:127] op_sel:[1,0,0] neg_lo:[1,0,0] neg_hi:[1,0,0]
	v_pk_fma_f32 v[128:129], v[60:61], v[68:69], v[128:129] op_sel:[1,0,0] neg_lo:[1,0,0] neg_hi:[1,0,0]
	v_fma_f32 v130, -v61, v98, v130
	v_pk_fma_f32 v[132:133], v[62:63], v[96:97], v[132:133] op_sel_hi:[0,1,1] neg_lo:[1,0,0] neg_hi:[1,0,0]
	v_pk_fma_f32 v[134:135], v[62:63], v[68:69], v[134:135] op_sel_hi:[0,1,1] neg_lo:[1,0,0] neg_hi:[1,0,0]
	v_fma_f32 v136, -v62, v98, v136
	v_pk_mul_f32 v[138:139], v[62:63], v[100:101] op_sel:[1,0]
	v_pk_mul_f32 v[198:199], v[62:63], v[122:123] op_sel:[1,0]
	v_mul_f32_e64 v204, v63, v124
	s_waitcnt lgkmcnt(1)
	v_pk_mul_f32 v[140:141], v[64:65], v[100:101] op_sel_hi:[0,1]
	v_pk_mul_f32 v[200:201], v[64:65], v[122:123] op_sel_hi:[0,1]
	v_mul_f32_e64 v206, v64, v124
	v_pk_mul_f32 v[170:171], v[64:65], v[100:101] op_sel:[1,0]
	v_pk_mul_f32 v[202:203], v[64:65], v[122:123] op_sel:[1,0]
	v_mul_f32_e64 v208, v65, v124
	v_pk_fma_f32 v[138:139], v[64:65], v[126:127], v[138:139] op_sel_hi:[0,1,1]
	v_pk_fma_f32 v[198:199], v[64:65], v[128:129], v[198:199] op_sel_hi:[0,1,1]
	v_fma_f32 v204, v64, v130, v204
	v_pk_fma_f32 v[140:141], v[66:67], v[126:127], v[140:141] op_sel_hi:[0,1,1]
	v_pk_fma_f32 v[200:201], v[66:67], v[128:129], v[200:201] op_sel_hi:[0,1,1]
	v_fma_f32 v206, v66, v130, v206
	v_pk_fma_f32 v[170:171], v[66:67], v[126:127], v[170:171] op_sel:[1,0,0]
	v_pk_fma_f32 v[202:203], v[66:67], v[128:129], v[202:203] op_sel:[1,0,0]
	v_fma_f32 v208, v67, v130, v208
	v_pk_fma_f32 v[138:139], v[64:65], v[132:133], v[138:139] op_sel:[1,0,0]
	v_pk_fma_f32 v[198:199], v[64:65], v[134:135], v[198:199] op_sel:[1,0,0]
	v_fma_f32 v204, v65, v136, v204
	v_pk_fma_f32 v[140:141], v[66:67], v[132:133], v[140:141] op_sel:[1,0,0]
	v_pk_fma_f32 v[200:201], v[66:67], v[134:135], v[200:201] op_sel:[1,0,0]
	v_fma_f32 v206, v67, v136, v206
	s_waitcnt lgkmcnt(0)
	v_pk_fma_f32 v[170:171], v[84:85], v[132:133], v[170:171] op_sel_hi:[0,1,1]
	v_pk_fma_f32 v[202:203], v[84:85], v[134:135], v[202:203] op_sel_hi:[0,1,1]
	v_fma_f32 v208, v84, v136, v208
	v_pk_mul_f32 v[210:211], v[60:61], v[138:139] op_sel_hi:[0,1]
	v_pk_mul_f32 v[212:213], v[60:61], v[198:199] op_sel_hi:[0,1]
	v_mul_f32_e64 v214, v60, v204
	v_pk_fma_f32 v[210:211], v[60:61], v[140:141], v[210:211] op_sel:[1,0,0]
	v_pk_fma_f32 v[212:213], v[60:61], v[200:201], v[212:213] op_sel:[1,0,0]
	v_fma_f32 v214, v61, v206, v214
	v_pk_fma_f32 v[210:211], v[62:63], v[170:171], v[210:211] op_sel_hi:[0,1,1]
	v_pk_fma_f32 v[212:213], v[62:63], v[202:203], v[212:213] op_sel_hi:[0,1,1]
	v_fma_f32 v214, v62, v208, v214
	v_pk_fma_f32 v[210:211], v[84:85], v[96:97], v[210:211] op_sel:[1,0,0] neg_lo:[0,0,1] neg_hi:[0,0,1]
	v_pk_fma_f32 v[212:213], v[84:85], v[68:69], v[212:213] op_sel:[1,0,0] neg_lo:[0,0,1] neg_hi:[0,0,1]
	v_fma_f32 v214, v85, v98, -v214
	v_cmp_eq_u32_e64 s[10:11], 1, v87
	v_cmp_eq_u32_e64 s[14:15], 2, v87
	v_cmp_eq_u32_e64 s[20:21], 3, v87
	v_cmp_eq_u32_e64 s[22:23], 4, v87
	v_cmp_eq_u32_e64 s[30:31], 5, v87
	v_add_f32_dpp v68, v138, v138 wave_shr:1 row_mask:0xf bank_mask:0xf bound_ctrl:1
	v_add_f32_dpp v69, v139, v139 wave_shr:1 row_mask:0xf bank_mask:0xf bound_ctrl:1
	v_add_f32_dpp v96, v198, v198 wave_shr:1 row_mask:0xf bank_mask:0xf bound_ctrl:1
	v_add_f32_dpp v97, v199, v199 wave_shr:1 row_mask:0xf bank_mask:0xf bound_ctrl:1
	v_add_f32_dpp v98, v204, v204 wave_shr:1 row_mask:0xf bank_mask:0xf bound_ctrl:1
	v_add_f32_dpp v100, v140, v140 wave_shr:1 row_mask:0xf bank_mask:0xf bound_ctrl:1
	v_add_f32_dpp v101, v141, v141 wave_shr:1 row_mask:0xf bank_mask:0xf bound_ctrl:1
	v_add_f32_dpp v122, v200, v200 wave_shr:1 row_mask:0xf bank_mask:0xf bound_ctrl:1
	v_add_f32_dpp v123, v201, v201 wave_shr:1 row_mask:0xf bank_mask:0xf bound_ctrl:1
	v_add_f32_dpp v124, v206, v206 wave_shr:1 row_mask:0xf bank_mask:0xf bound_ctrl:1
	v_add_f32_dpp v126, v170, v170 wave_shr:1 row_mask:0xf bank_mask:0xf bound_ctrl:1
	v_add_f32_dpp v127, v171, v171 wave_shr:1 row_mask:0xf bank_mask:0xf bound_ctrl:1
	v_add_f32_dpp v128, v202, v202 wave_shr:1 row_mask:0xf bank_mask:0xf bound_ctrl:1
	v_add_f32_dpp v129, v203, v203 wave_shr:1 row_mask:0xf bank_mask:0xf bound_ctrl:1
	v_add_f32_dpp v130, v208, v208 wave_shr:1 row_mask:0xf bank_mask:0xf bound_ctrl:1
	v_add_f32_dpp v132, v210, v210 wave_shr:1 row_mask:0xf bank_mask:0xf bound_ctrl:1
	v_add_f32_dpp v133, v211, v211 wave_shr:1 row_mask:0xf bank_mask:0xf bound_ctrl:1
	v_add_f32_dpp v134, v212, v212 wave_shr:1 row_mask:0xf bank_mask:0xf bound_ctrl:1
	v_add_f32_dpp v135, v213, v213 wave_shr:1 row_mask:0xf bank_mask:0xf bound_ctrl:1
	v_add_f32_dpp v136, v214, v214 wave_shr:1 row_mask:0xf bank_mask:0xf bound_ctrl:1
	v_add_f32_dpp v68, v138, v68 wave_shl:1 row_mask:0xf bank_mask:0xf bound_ctrl:1
	v_add_f32_dpp v69, v139, v69 wave_shl:1 row_mask:0xf bank_mask:0xf bound_ctrl:1
	v_add_f32_dpp v96, v198, v96 wave_shl:1 row_mask:0xf bank_mask:0xf bound_ctrl:1
	v_add_f32_dpp v97, v199, v97 wave_shl:1 row_mask:0xf bank_mask:0xf bound_ctrl:1
	v_add_f32_dpp v98, v204, v98 wave_shl:1 row_mask:0xf bank_mask:0xf bound_ctrl:1
	v_add_f32_dpp v100, v140, v100 wave_shl:1 row_mask:0xf bank_mask:0xf bound_ctrl:1
	v_add_f32_dpp v101, v141, v101 wave_shl:1 row_mask:0xf bank_mask:0xf bound_ctrl:1
	v_add_f32_dpp v122, v200, v122 wave_shl:1 row_mask:0xf bank_mask:0xf bound_ctrl:1
	v_add_f32_dpp v123, v201, v123 wave_shl:1 row_mask:0xf bank_mask:0xf bound_ctrl:1
	v_add_f32_dpp v124, v206, v124 wave_shl:1 row_mask:0xf bank_mask:0xf bound_ctrl:1
	v_add_f32_dpp v126, v170, v126 wave_shl:1 row_mask:0xf bank_mask:0xf bound_ctrl:1
	v_add_f32_dpp v127, v171, v127 wave_shl:1 row_mask:0xf bank_mask:0xf bound_ctrl:1
	v_add_f32_dpp v128, v202, v128 wave_shl:1 row_mask:0xf bank_mask:0xf bound_ctrl:1
	v_add_f32_dpp v129, v203, v129 wave_shl:1 row_mask:0xf bank_mask:0xf bound_ctrl:1
	v_add_f32_dpp v130, v208, v130 wave_shl:1 row_mask:0xf bank_mask:0xf bound_ctrl:1
	v_add_f32_dpp v132, v210, v132 wave_shl:1 row_mask:0xf bank_mask:0xf bound_ctrl:1
	v_add_f32_dpp v133, v211, v133 wave_shl:1 row_mask:0xf bank_mask:0xf bound_ctrl:1
	v_add_f32_dpp v134, v212, v134 wave_shl:1 row_mask:0xf bank_mask:0xf bound_ctrl:1
	v_add_f32_dpp v135, v213, v135 wave_shl:1 row_mask:0xf bank_mask:0xf bound_ctrl:1
	v_add_f32_dpp v136, v214, v136 wave_shl:1 row_mask:0xf bank_mask:0xf bound_ctrl:1
	v_pk_add_f32 v[138:139], v[172:173], v[68:69]
	v_pk_add_f32 v[140:141], v[70:71], v[96:97]
	v_add_f32_e64 v70, v74, v98
	v_pk_add_f32 v[74:75], v[76:77], v[100:101]
	v_pk_add_f32 v[76:77], v[78:79], v[122:123]
	v_add_f32_e64 v78, v80, v124
	v_pk_add_f32 v[80:81], v[82:83], v[126:127]
	v_pk_add_f32 v[82:83], v[88:89], v[128:129]
	v_add_f32_e64 v88, v90, v130
	v_pk_add_f32 v[90:91], v[92:93], v[132:133]
	v_pk_add_f32 v[92:93], v[94:95], v[134:135]
	v_add_f32_e64 v94, v102, v136
	v_pk_fma_f32 v[90:91], v[56:57], v[138:139], v[90:91] op_sel_hi:[0,1,1]
	v_pk_fma_f32 v[92:93], v[56:57], v[140:141], v[92:93] op_sel_hi:[0,1,1]
	v_fma_f32 v94, v56, v70, v94
	v_pk_fma_f32 v[90:91], v[56:57], v[74:75], v[90:91] op_sel:[1,0,0]
	v_pk_fma_f32 v[92:93], v[56:57], v[76:77], v[92:93] op_sel:[1,0,0]
	v_fma_f32 v94, v57, v78, v94
	v_pk_fma_f32 v[90:91], v[58:59], v[80:81], v[90:91] op_sel_hi:[0,1,1]
	v_pk_fma_f32 v[92:93], v[58:59], v[82:83], v[92:93] op_sel_hi:[0,1,1]
	v_fma_f32 v94, v58, v88, v94
	v_cndmask_b32_e64 v102, 0, v1, s[10:11]
	v_cndmask_b32_e64 v103, 0, v1, s[14:15]
	v_cndmask_b32_e64 v170, 0, v1, s[20:21]
	v_cndmask_b32_e64 v171, 0, v1, s[22:23]
	v_cndmask_b32_e64 v172, 0, v1, s[30:31]
	v_pk_fma_f32 v[90:91], v[46:47], v[86:87], v[90:91] op_sel_hi:[1,0,1] neg_lo:[0,0,1] neg_hi:[0,0,1]
	v_pk_fma_f32 v[92:93], v[52:53], v[86:87], v[92:93] op_sel_hi:[1,0,1] neg_lo:[0,0,1] neg_hi:[0,0,1]
	v_fma_f32 v94, v54, v86, -v94
	s_add_i32 s4, s34, 7
	s_cmpk_lt_i32 s4, 0x201
	s_cselect_b64 s[12:13], s[0:1], 0
	v_pk_add_f32 v[90:91], v[90:91], v[102:103] neg_lo:[0,1] neg_hi:[0,1]
	v_pk_add_f32 v[92:93], v[92:93], v[170:171] neg_lo:[0,1] neg_hi:[0,1]
	v_add_f32_e64 v94, v94, -v172
	v_pk_mul_f32 v[198:199], v[90:91], v[90:91]
	v_pk_fma_f32 v[198:199], v[92:93], v[92:93], v[198:199]
	v_add_f32_e32 v198, v198, v199
	v_fma_f32 v198, v94, v94, v198
	v_cndmask_b32_e64 v199, 0, v198, s[12:13]
	v_add_f32_e32 v0, v0, v199
	s_waitcnt vmcnt(6)
	v_pk_mul_f32 v[46:47], v[20:21], v[36:37] op_sel_hi:[1,0]
	v_pk_mul_f32 v[52:53], v[24:25], v[36:37] op_sel_hi:[1,0]
	v_mul_f32_e64 v54, v30, v36
	v_pk_mul_f32 v[56:57], v[20:21], v[36:37] op_sel:[0,1]
	v_pk_mul_f32 v[58:59], v[24:25], v[36:37] op_sel:[0,1]
	v_mul_f32_e64 v60, v30, v37
	v_pk_mul_f32 v[62:63], v[20:21], v[38:39] op_sel_hi:[1,0]
	v_pk_mul_f32 v[64:65], v[24:25], v[38:39] op_sel_hi:[1,0]
	v_mul_f32_e64 v66, v30, v38
	v_add_f32_dpp v70, v20, v20 wave_shr:1 row_mask:0xf bank_mask:0xf bound_ctrl:1
	v_add_f32_dpp v71, v21, v21 wave_shr:1 row_mask:0xf bank_mask:0xf bound_ctrl:1
	v_add_f32_dpp v74, v24, v24 wave_shr:1 row_mask:0xf bank_mask:0xf bound_ctrl:1
	v_add_f32_dpp v75, v25, v25 wave_shr:1 row_mask:0xf bank_mask:0xf bound_ctrl:1
	v_add_f32_dpp v76, v30, v30 wave_shr:1 row_mask:0xf bank_mask:0xf bound_ctrl:1
	v_add_f32_dpp v78, v46, v46 wave_shr:1 row_mask:0xf bank_mask:0xf bound_ctrl:1
	v_add_f32_dpp v79, v47, v47 wave_shr:1 row_mask:0xf bank_mask:0xf bound_ctrl:1
	v_add_f32_dpp v80, v52, v52 wave_shr:1 row_mask:0xf bank_mask:0xf bound_ctrl:1
	v_add_f32_dpp v81, v53, v53 wave_shr:1 row_mask:0xf bank_mask:0xf bound_ctrl:1
	v_add_f32_dpp v82, v54, v54 wave_shr:1 row_mask:0xf bank_mask:0xf bound_ctrl:1
	v_add_f32_dpp v84, v56, v56 wave_shr:1 row_mask:0xf bank_mask:0xf bound_ctrl:1
	v_add_f32_dpp v85, v57, v57 wave_shr:1 row_mask:0xf bank_mask:0xf bound_ctrl:1
	v_add_f32_dpp v86, v58, v58 wave_shr:1 row_mask:0xf bank_mask:0xf bound_ctrl:1
	v_add_f32_dpp v87, v59, v59 wave_shr:1 row_mask:0xf bank_mask:0xf bound_ctrl:1
	v_add_f32_dpp v88, v60, v60 wave_shr:1 row_mask:0xf bank_mask:0xf bound_ctrl:1
	v_add_f32_dpp v90, v62, v62 wave_shr:1 row_mask:0xf bank_mask:0xf bound_ctrl:1
	v_add_f32_dpp v91, v63, v63 wave_shr:1 row_mask:0xf bank_mask:0xf bound_ctrl:1
	v_add_f32_dpp v92, v64, v64 wave_shr:1 row_mask:0xf bank_mask:0xf bound_ctrl:1
	v_add_f32_dpp v93, v65, v65 wave_shr:1 row_mask:0xf bank_mask:0xf bound_ctrl:1
	v_add_f32_dpp v94, v66, v66 wave_shr:1 row_mask:0xf bank_mask:0xf bound_ctrl:1
	v_add_f32_dpp v70, v20, v70 wave_shl:1 row_mask:0xf bank_mask:0xf bound_ctrl:1
	v_add_f32_dpp v71, v21, v71 wave_shl:1 row_mask:0xf bank_mask:0xf bound_ctrl:1
	v_add_f32_dpp v74, v24, v74 wave_shl:1 row_mask:0xf bank_mask:0xf bound_ctrl:1
	v_add_f32_dpp v75, v25, v75 wave_shl:1 row_mask:0xf bank_mask:0xf bound_ctrl:1
	v_add_f32_dpp v76, v30, v76 wave_shl:1 row_mask:0xf bank_mask:0xf bound_ctrl:1
	v_add_f32_dpp v78, v46, v78 wave_shl:1 row_mask:0xf bank_mask:0xf bound_ctrl:1
	v_add_f32_dpp v79, v47, v79 wave_shl:1 row_mask:0xf bank_mask:0xf bound_ctrl:1
	v_add_f32_dpp v80, v52, v80 wave_shl:1 row_mask:0xf bank_mask:0xf bound_ctrl:1
	v_add_f32_dpp v81, v53, v81 wave_shl:1 row_mask:0xf bank_mask:0xf bound_ctrl:1
	v_add_f32_dpp v82, v54, v82 wave_shl:1 row_mask:0xf bank_mask:0xf bound_ctrl:1
	v_add_f32_dpp v84, v56, v84 wave_shl:1 row_mask:0xf bank_mask:0xf bound_ctrl:1
	v_add_f32_dpp v85, v57, v85 wave_shl:1 row_mask:0xf bank_mask:0xf bound_ctrl:1
	v_add_f32_dpp v86, v58, v86 wave_shl:1 row_mask:0xf bank_mask:0xf bound_ctrl:1
	v_add_f32_dpp v87, v59, v87 wave_shl:1 row_mask:0xf bank_mask:0xf bound_ctrl:1
	v_add_f32_dpp v88, v60, v88 wave_shl:1 row_mask:0xf bank_mask:0xf bound_ctrl:1
	v_add_f32_dpp v90, v62, v90 wave_shl:1 row_mask:0xf bank_mask:0xf bound_ctrl:1
	v_add_f32_dpp v91, v63, v91 wave_shl:1 row_mask:0xf bank_mask:0xf bound_ctrl:1
	v_add_f32_dpp v92, v64, v92 wave_shl:1 row_mask:0xf bank_mask:0xf bound_ctrl:1
	v_add_f32_dpp v93, v65, v93 wave_shl:1 row_mask:0xf bank_mask:0xf bound_ctrl:1
	v_add_f32_dpp v94, v66, v94 wave_shl:1 row_mask:0xf bank_mask:0xf bound_ctrl:1
	s_barrier
	ds_read_b128 v[52:55], v23 offset:0
	ds_read_b128 v[56:59], v23 offset:1024
	ds_read_b128 v[60:63], v23 offset:2048
	v_pk_add_f32 v[46:47], v[150:151], v[70:71]
	v_pk_add_f32 v[64:65], v[106:107], v[46:47]
	v_pk_add_f32 v[66:67], v[152:153], v[74:75]
	v_pk_add_f32 v[102:103], v[108:109], v[66:67]
	v_add_f32_e64 v106, v154, v76
	v_add_f32_e64 v108, v110, v106
	v_pk_add_f32 v[110:111], v[156:157], v[78:79]
	v_pk_add_f32 v[138:139], v[112:113], v[110:111]
	v_pk_add_f32 v[112:113], v[158:159], v[80:81]
	v_pk_add_f32 v[140:141], v[114:115], v[112:113]
	v_add_f32_e64 v114, v160, v82
	v_add_f32_e64 v150, v116, v114
	v_pk_add_f32 v[116:117], v[162:163], v[84:85]
	v_pk_add_f32 v[152:153], v[118:119], v[116:117]
	v_pk_add_f32 v[118:119], v[164:165], v[86:87]
	v_pk_add_f32 v[154:155], v[120:121], v[118:119]
	v_add_f32_e64 v120, v166, v88
	v_add_f32_e64 v156, v142, v120
	v_pk_add_f32 v[142:143], v[168:169], v[90:91]
	v_pk_add_f32 v[158:159], v[144:145], v[142:143]
	v_pk_add_f32 v[144:145], v[194:195], v[92:93]
	v_pk_add_f32 v[160:161], v[146:147], v[144:145]
	v_add_f32_e64 v146, v196, v94
	v_add_f32_e64 v162, v148, v146
	s_waitcnt lgkmcnt(2)
	v_pk_fma_f32 v[138:139], v[52:53], v[64:65], v[138:139] op_sel_hi:[0,1,1] neg_lo:[1,0,0] neg_hi:[1,0,0]
	v_pk_fma_f32 v[140:141], v[52:53], v[102:103], v[140:141] op_sel_hi:[0,1,1] neg_lo:[1,0,0] neg_hi:[1,0,0]
	v_fma_f32 v150, -v52, v108, v150
	v_pk_fma_f32 v[152:153], v[52:53], v[64:65], v[152:153] op_sel:[1,0,0] neg_lo:[1,0,0] neg_hi:[1,0,0]
	v_pk_fma_f32 v[154:155], v[52:53], v[102:103], v[154:155] op_sel:[1,0,0] neg_lo:[1,0,0] neg_hi:[1,0,0]
	v_fma_f32 v156, -v53, v108, v156
	v_pk_fma_f32 v[158:159], v[54:55], v[64:65], v[158:159] op_sel_hi:[0,1,1] neg_lo:[1,0,0] neg_hi:[1,0,0]
	v_pk_fma_f32 v[160:161], v[54:55], v[102:103], v[160:161] op_sel_hi:[0,1,1] neg_lo:[1,0,0] neg_hi:[1,0,0]
	v_fma_f32 v162, -v54, v108, v162
	v_pk_mul_f32 v[148:149], v[54:55], v[138:139] op_sel:[1,0]
	v_pk_mul_f32 v[168:169], v[54:55], v[140:141] op_sel:[1,0]
	v_mul_f32_e64 v194, v55, v150
	s_waitcnt lgkmcnt(1)
	v_pk_mul_f32 v[164:165], v[56:57], v[138:139] op_sel_hi:[0,1]
	v_pk_mul_f32 v[170:171], v[56:57], v[140:141] op_sel_hi:[0,1]
	v_mul_f32_e64 v196, v56, v150
	v_pk_mul_f32 v[166:167], v[56:57], v[138:139] op_sel:[1,0]
	v_pk_mul_f32 v[172:173], v[56:57], v[140:141] op_sel:[1,0]
	v_mul_f32_e64 v198, v57, v150
	v_pk_fma_f32 v[148:149], v[56:57], v[152:153], v[148:149] op_sel_hi:[0,1,1]
	v_pk_fma_f32 v[168:169], v[56:57], v[154:155], v[168:169] op_sel_hi:[0,1,1]
	v_fma_f32 v194, v56, v156, v194
	v_pk_fma_f32 v[164:165], v[58:59], v[152:153], v[164:165] op_sel_hi:[0,1,1]
	v_pk_fma_f32 v[170:171], v[58:59], v[154:155], v[170:171] op_sel_hi:[0,1,1]
	v_fma_f32 v196, v58, v156, v196
	v_pk_fma_f32 v[166:167], v[58:59], v[152:153], v[166:167] op_sel:[1,0,0]
	v_pk_fma_f32 v[172:173], v[58:59], v[154:155], v[172:173] op_sel:[1,0,0]
	v_fma_f32 v198, v59, v156, v198
	v_pk_fma_f32 v[148:149], v[56:57], v[158:159], v[148:149] op_sel:[1,0,0]
	v_pk_fma_f32 v[168:169], v[56:57], v[160:161], v[168:169] op_sel:[1,0,0]
	v_fma_f32 v194, v57, v162, v194
	v_pk_fma_f32 v[164:165], v[58:59], v[158:159], v[164:165] op_sel:[1,0,0]
	v_pk_fma_f32 v[170:171], v[58:59], v[160:161], v[170:171] op_sel:[1,0,0]
	v_fma_f32 v196, v59, v162, v196
	s_waitcnt lgkmcnt(0)
	v_pk_fma_f32 v[166:167], v[60:61], v[158:159], v[166:167] op_sel_hi:[0,1,1]
	v_pk_fma_f32 v[172:173], v[60:61], v[160:161], v[172:173] op_sel_hi:[0,1,1]
	v_fma_f32 v198, v60, v162, v198
	v_pk_mul_f32 v[200:201], v[52:53], v[148:149] op_sel_hi:[0,1]
	v_pk_mul_f32 v[202:203], v[52:53], v[168:169] op_sel_hi:[0,1]
	v_mul_f32_e64 v204, v52, v194
	v_pk_fma_f32 v[200:201], v[52:53], v[164:165], v[200:201] op_sel:[1,0,0]
	v_pk_fma_f32 v[202:203], v[52:53], v[170:171], v[202:203] op_sel:[1,0,0]
	v_fma_f32 v204, v53, v196, v204
	v_pk_fma_f32 v[200:201], v[54:55], v[166:167], v[200:201] op_sel_hi:[0,1,1]
	v_pk_fma_f32 v[202:203], v[54:55], v[172:173], v[202:203] op_sel_hi:[0,1,1]
	v_fma_f32 v204, v54, v198, v204
	v_pk_fma_f32 v[200:201], v[60:61], v[64:65], v[200:201] op_sel:[1,0,0] neg_lo:[0,0,1] neg_hi:[0,0,1]
	v_pk_fma_f32 v[202:203], v[60:61], v[102:103], v[202:203] op_sel:[1,0,0] neg_lo:[0,0,1] neg_hi:[0,0,1]
	v_fma_f32 v204, v61, v108, -v204
	v_cmp_eq_u32_e64 s[10:11], 1, v63
	v_cmp_eq_u32_e64 s[14:15], 2, v63
	v_cmp_eq_u32_e64 s[20:21], 3, v63
	v_cmp_eq_u32_e64 s[22:23], 4, v63
	v_cmp_eq_u32_e64 s[30:31], 5, v63
	v_add_f32_dpp v64, v148, v148 wave_shr:1 row_mask:0xf bank_mask:0xf bound_ctrl:1
	v_add_f32_dpp v65, v149, v149 wave_shr:1 row_mask:0xf bank_mask:0xf bound_ctrl:1
	v_add_f32_dpp v102, v168, v168 wave_shr:1 row_mask:0xf bank_mask:0xf bound_ctrl:1
	v_add_f32_dpp v103, v169, v169 wave_shr:1 row_mask:0xf bank_mask:0xf bound_ctrl:1
	v_add_f32_dpp v108, v194, v194 wave_shr:1 row_mask:0xf bank_mask:0xf bound_ctrl:1
	v_add_f32_dpp v138, v164, v164 wave_shr:1 row_mask:0xf bank_mask:0xf bound_ctrl:1
	v_add_f32_dpp v139, v165, v165 wave_shr:1 row_mask:0xf bank_mask:0xf bound_ctrl:1
	v_add_f32_dpp v140, v170, v170 wave_shr:1 row_mask:0xf bank_mask:0xf bound_ctrl:1
	v_add_f32_dpp v141, v171, v171 wave_shr:1 row_mask:0xf bank_mask:0xf bound_ctrl:1
	v_add_f32_dpp v150, v196, v196 wave_shr:1 row_mask:0xf bank_mask:0xf bound_ctrl:1
	v_add_f32_dpp v152, v166, v166 wave_shr:1 row_mask:0xf bank_mask:0xf bound_ctrl:1
	v_add_f32_dpp v153, v167, v167 wave_shr:1 row_mask:0xf bank_mask:0xf bound_ctrl:1
	v_add_f32_dpp v154, v172, v172 wave_shr:1 row_mask:0xf bank_mask:0xf bound_ctrl:1
	v_add_f32_dpp v155, v173, v173 wave_shr:1 row_mask:0xf bank_mask:0xf bound_ctrl:1
	v_add_f32_dpp v156, v198, v198 wave_shr:1 row_mask:0xf bank_mask:0xf bound_ctrl:1
	v_add_f32_dpp v158, v200, v200 wave_shr:1 row_mask:0xf bank_mask:0xf bound_ctrl:1
	v_add_f32_dpp v159, v201, v201 wave_shr:1 row_mask:0xf bank_mask:0xf bound_ctrl:1
	v_add_f32_dpp v160, v202, v202 wave_shr:1 row_mask:0xf bank_mask:0xf bound_ctrl:1
	v_add_f32_dpp v161, v203, v203 wave_shr:1 row_mask:0xf bank_mask:0xf bound_ctrl:1
	v_add_f32_dpp v162, v204, v204 wave_shr:1 row_mask:0xf bank_mask:0xf bound_ctrl:1
	v_add_f32_dpp v64, v148, v64 wave_shl:1 row_mask:0xf bank_mask:0xf bound_ctrl:1
	v_add_f32_dpp v65, v149, v65 wave_shl:1 row_mask:0xf bank_mask:0xf bound_ctrl:1
	v_add_f32_dpp v102, v168, v102 wave_shl:1 row_mask:0xf bank_mask:0xf bound_ctrl:1
	v_add_f32_dpp v103, v169, v103 wave_shl:1 row_mask:0xf bank_mask:0xf bound_ctrl:1
	v_add_f32_dpp v108, v194, v108 wave_shl:1 row_mask:0xf bank_mask:0xf bound_ctrl:1
	v_add_f32_dpp v138, v164, v138 wave_shl:1 row_mask:0xf bank_mask:0xf bound_ctrl:1
	v_add_f32_dpp v139, v165, v139 wave_shl:1 row_mask:0xf bank_mask:0xf bound_ctrl:1
	v_add_f32_dpp v140, v170, v140 wave_shl:1 row_mask:0xf bank_mask:0xf bound_ctrl:1
	v_add_f32_dpp v141, v171, v141 wave_shl:1 row_mask:0xf bank_mask:0xf bound_ctrl:1
	v_add_f32_dpp v150, v196, v150 wave_shl:1 row_mask:0xf bank_mask:0xf bound_ctrl:1
	v_add_f32_dpp v152, v166, v152 wave_shl:1 row_mask:0xf bank_mask:0xf bound_ctrl:1
	v_add_f32_dpp v153, v167, v153 wave_shl:1 row_mask:0xf bank_mask:0xf bound_ctrl:1
	v_add_f32_dpp v154, v172, v154 wave_shl:1 row_mask:0xf bank_mask:0xf bound_ctrl:1
	v_add_f32_dpp v155, v173, v155 wave_shl:1 row_mask:0xf bank_mask:0xf bound_ctrl:1
	v_add_f32_dpp v156, v198, v156 wave_shl:1 row_mask:0xf bank_mask:0xf bound_ctrl:1
	v_add_f32_dpp v158, v200, v158 wave_shl:1 row_mask:0xf bank_mask:0xf bound_ctrl:1
	v_add_f32_dpp v159, v201, v159 wave_shl:1 row_mask:0xf bank_mask:0xf bound_ctrl:1
	v_add_f32_dpp v160, v202, v160 wave_shl:1 row_mask:0xf bank_mask:0xf bound_ctrl:1
	v_add_f32_dpp v161, v203, v161 wave_shl:1 row_mask:0xf bank_mask:0xf bound_ctrl:1
	v_add_f32_dpp v162, v204, v162 wave_shl:1 row_mask:0xf bank_mask:0xf bound_ctrl:1
	v_pk_add_f32 v[148:149], v[68:69], v[64:65]
	v_pk_add_f32 v[164:165], v[72:73], v[148:149]
	v_pk_add_f32 v[68:69], v[96:97], v[102:103]
	v_pk_add_f32 v[72:73], v[104:105], v[68:69]
	v_add_f32_e64 v96, v98, v108
	v_add_f32_e64 v104, v174, v96
	v_pk_add_f32 v[98:99], v[100:101], v[138:139]
	v_pk_add_f32 v[166:167], v[176:177], v[98:99]
	v_pk_add_f32 v[100:101], v[122:123], v[140:141]
	v_pk_add_f32 v[168:169], v[178:179], v[100:101]
	v_add_f32_e64 v122, v124, v150
	v_add_f32_e64 v170, v180, v122
	v_pk_add_f32 v[124:125], v[126:127], v[152:153]
	v_pk_add_f32 v[172:173], v[182:183], v[124:125]
	v_pk_add_f32 v[126:127], v[128:129], v[154:155]
	v_pk_add_f32 v[174:175], v[184:185], v[126:127]
	v_add_f32_e64 v128, v130, v156
	v_add_f32_e64 v176, v186, v128
	v_pk_add_f32 v[130:131], v[132:133], v[158:159]
	v_pk_add_f32 v[178:179], v[188:189], v[130:131]
	v_pk_add_f32 v[132:133], v[134:135], v[160:161]
	v_pk_add_f32 v[180:181], v[190:191], v[132:133]
	v_add_f32_e64 v134, v136, v162
	v_add_f32_e64 v182, v192, v134
	v_pk_fma_f32 v[178:179], v[8:9], v[164:165], v[178:179] op_sel_hi:[0,1,1]
	v_pk_fma_f32 v[180:181], v[8:9], v[72:73], v[180:181] op_sel_hi:[0,1,1]
	v_fma_f32 v182, v8, v104, v182
	v_pk_fma_f32 v[178:179], v[8:9], v[166:167], v[178:179] op_sel:[1,0,0]
	v_pk_fma_f32 v[180:181], v[8:9], v[168:169], v[180:181] op_sel:[1,0,0]
	v_fma_f32 v182, v9, v170, v182
	v_pk_fma_f32 v[178:179], v[10:11], v[172:173], v[178:179] op_sel_hi:[0,1,1]
	v_pk_fma_f32 v[180:181], v[10:11], v[174:175], v[180:181] op_sel_hi:[0,1,1]
	v_fma_f32 v182, v10, v176, v182
	v_cndmask_b32_e64 v136, 0, v1, s[10:11]
	v_cndmask_b32_e64 v137, 0, v1, s[14:15]
	v_cndmask_b32_e64 v184, 0, v1, s[20:21]
	v_cndmask_b32_e64 v185, 0, v1, s[22:23]
	v_cndmask_b32_e64 v186, 0, v1, s[30:31]
	v_pk_fma_f32 v[178:179], v[2:3], v[62:63], v[178:179] op_sel_hi:[1,0,1] neg_lo:[0,0,1] neg_hi:[0,0,1]
	v_pk_fma_f32 v[180:181], v[4:5], v[62:63], v[180:181] op_sel_hi:[1,0,1] neg_lo:[0,0,1] neg_hi:[0,0,1]
	v_fma_f32 v182, v6, v62, -v182
	s_add_i32 s4, s34, 8
	s_cmpk_lt_i32 s4, 0x201
	s_cselect_b64 s[12:13], s[0:1], 0
	v_pk_add_f32 v[178:179], v[178:179], v[136:137] neg_lo:[0,1] neg_hi:[0,1]
	v_pk_add_f32 v[180:181], v[180:181], v[184:185] neg_lo:[0,1] neg_hi:[0,1]
	v_add_f32_e64 v182, v182, -v186
	v_pk_mul_f32 v[188:189], v[178:179], v[178:179]
	v_pk_fma_f32 v[188:189], v[180:181], v[180:181], v[188:189]
	v_add_f32_e32 v188, v188, v189
	v_fma_f32 v188, v182, v182, v188
	v_cndmask_b32_e64 v189, 0, v188, s[12:13]
	v_add_f32_e32 v0, v0, v189
	s_waitcnt vmcnt(0)
	v_pk_mul_f32 v[2:3], v[40:41], v[48:49] op_sel_hi:[1,0]
	v_pk_mul_f32 v[4:5], v[42:43], v[48:49] op_sel_hi:[1,0]
	v_mul_f32_e64 v6, v44, v48
	v_pk_mul_f32 v[8:9], v[40:41], v[48:49] op_sel:[0,1]
	v_pk_mul_f32 v[10:11], v[42:43], v[48:49] op_sel:[0,1]
	v_mul_f32_e64 v52, v44, v49
	v_pk_mul_f32 v[54:55], v[40:41], v[50:51] op_sel_hi:[1,0]
	v_pk_mul_f32 v[56:57], v[42:43], v[50:51] op_sel_hi:[1,0]
	v_mul_f32_e64 v58, v44, v50
	v_add_f32_dpp v60, v40, v40 wave_shr:1 row_mask:0xf bank_mask:0xf bound_ctrl:1
	v_add_f32_dpp v61, v41, v41 wave_shr:1 row_mask:0xf bank_mask:0xf bound_ctrl:1
	v_add_f32_dpp v62, v42, v42 wave_shr:1 row_mask:0xf bank_mask:0xf bound_ctrl:1
	v_add_f32_dpp v63, v43, v43 wave_shr:1 row_mask:0xf bank_mask:0xf bound_ctrl:1
	v_add_f32_dpp v72, v44, v44 wave_shr:1 row_mask:0xf bank_mask:0xf bound_ctrl:1
	v_add_f32_dpp v104, v2, v2 wave_shr:1 row_mask:0xf bank_mask:0xf bound_ctrl:1
	v_add_f32_dpp v105, v3, v3 wave_shr:1 row_mask:0xf bank_mask:0xf bound_ctrl:1
	v_add_f32_dpp v136, v4, v4 wave_shr:1 row_mask:0xf bank_mask:0xf bound_ctrl:1
	v_add_f32_dpp v137, v5, v5 wave_shr:1 row_mask:0xf bank_mask:0xf bound_ctrl:1
	v_add_f32_dpp v164, v6, v6 wave_shr:1 row_mask:0xf bank_mask:0xf bound_ctrl:1
	v_add_f32_dpp v166, v8, v8 wave_shr:1 row_mask:0xf bank_mask:0xf bound_ctrl:1
	v_add_f32_dpp v167, v9, v9 wave_shr:1 row_mask:0xf bank_mask:0xf bound_ctrl:1
	v_add_f32_dpp v168, v10, v10 wave_shr:1 row_mask:0xf bank_mask:0xf bound_ctrl:1
	v_add_f32_dpp v169, v11, v11 wave_shr:1 row_mask:0xf bank_mask:0xf bound_ctrl:1
	v_add_f32_dpp v170, v52, v52 wave_shr:1 row_mask:0xf bank_mask:0xf bound_ctrl:1
	v_add_f32_dpp v172, v54, v54 wave_shr:1 row_mask:0xf bank_mask:0xf bound_ctrl:1
	v_add_f32_dpp v173, v55, v55 wave_shr:1 row_mask:0xf bank_mask:0xf bound_ctrl:1
	v_add_f32_dpp v174, v56, v56 wave_shr:1 row_mask:0xf bank_mask:0xf bound_ctrl:1
	v_add_f32_dpp v175, v57, v57 wave_shr:1 row_mask:0xf bank_mask:0xf bound_ctrl:1
	v_add_f32_dpp v176, v58, v58 wave_shr:1 row_mask:0xf bank_mask:0xf bound_ctrl:1
	v_add_f32_dpp v60, v40, v60 wave_shl:1 row_mask:0xf bank_mask:0xf bound_ctrl:1
	v_add_f32_dpp v61, v41, v61 wave_shl:1 row_mask:0xf bank_mask:0xf bound_ctrl:1
	v_add_f32_dpp v62, v42, v62 wave_shl:1 row_mask:0xf bank_mask:0xf bound_ctrl:1
	v_add_f32_dpp v63, v43, v63 wave_shl:1 row_mask:0xf bank_mask:0xf bound_ctrl:1
	v_add_f32_dpp v72, v44, v72 wave_shl:1 row_mask:0xf bank_mask:0xf bound_ctrl:1
	v_add_f32_dpp v104, v2, v104 wave_shl:1 row_mask:0xf bank_mask:0xf bound_ctrl:1
	v_add_f32_dpp v105, v3, v105 wave_shl:1 row_mask:0xf bank_mask:0xf bound_ctrl:1
	v_add_f32_dpp v136, v4, v136 wave_shl:1 row_mask:0xf bank_mask:0xf bound_ctrl:1
	v_add_f32_dpp v137, v5, v137 wave_shl:1 row_mask:0xf bank_mask:0xf bound_ctrl:1
	v_add_f32_dpp v164, v6, v164 wave_shl:1 row_mask:0xf bank_mask:0xf bound_ctrl:1
	v_add_f32_dpp v166, v8, v166 wave_shl:1 row_mask:0xf bank_mask:0xf bound_ctrl:1
	v_add_f32_dpp v167, v9, v167 wave_shl:1 row_mask:0xf bank_mask:0xf bound_ctrl:1
	v_add_f32_dpp v168, v10, v168 wave_shl:1 row_mask:0xf bank_mask:0xf bound_ctrl:1
	v_add_f32_dpp v169, v11, v169 wave_shl:1 row_mask:0xf bank_mask:0xf bound_ctrl:1
	v_add_f32_dpp v170, v52, v170 wave_shl:1 row_mask:0xf bank_mask:0xf bound_ctrl:1
	v_add_f32_dpp v172, v54, v172 wave_shl:1 row_mask:0xf bank_mask:0xf bound_ctrl:1
	v_add_f32_dpp v173, v55, v173 wave_shl:1 row_mask:0xf bank_mask:0xf bound_ctrl:1
	v_add_f32_dpp v174, v56, v174 wave_shl:1 row_mask:0xf bank_mask:0xf bound_ctrl:1
	v_add_f32_dpp v175, v57, v175 wave_shl:1 row_mask:0xf bank_mask:0xf bound_ctrl:1
	v_add_f32_dpp v176, v58, v176 wave_shl:1 row_mask:0xf bank_mask:0xf bound_ctrl:1
	s_barrier
	ds_read_b128 v[4:7], v23 offset:3072
	ds_read_b128 v[8:11], v23 offset:4096
	ds_read_b128 v[52:55], v23 offset:5120
	v_pk_add_f32 v[2:3], v[46:47], v[60:61]
	v_pk_add_f32 v[46:47], v[66:67], v[62:63]
	v_add_f32_e64 v56, v106, v72
	v_pk_add_f32 v[58:59], v[110:111], v[104:105]
	v_pk_add_f32 v[66:67], v[112:113], v[136:137]
	v_add_f32_e64 v106, v114, v164
	v_pk_add_f32 v[110:111], v[116:117], v[166:167]
	v_pk_add_f32 v[112:113], v[118:119], v[168:169]
	v_add_f32_e64 v114, v120, v170
	v_pk_add_f32 v[116:117], v[142:143], v[172:173]
	v_pk_add_f32 v[118:119], v[144:145], v[174:175]
	v_add_f32_e64 v120, v146, v176
	s_waitcnt lgkmcnt(2)
	v_pk_fma_f32 v[58:59], v[4:5], v[2:3], v[58:59] op_sel_hi:[0,1,1] neg_lo:[1,0,0] neg_hi:[1,0,0]
	v_pk_fma_f32 v[66:67], v[4:5], v[46:47], v[66:67] op_sel_hi:[0,1,1] neg_lo:[1,0,0] neg_hi:[1,0,0]
	v_fma_f32 v106, -v4, v56, v106
	v_pk_fma_f32 v[110:111], v[4:5], v[2:3], v[110:111] op_sel:[1,0,0] neg_lo:[1,0,0] neg_hi:[1,0,0]
	v_pk_fma_f32 v[112:113], v[4:5], v[46:47], v[112:113] op_sel:[1,0,0] neg_lo:[1,0,0] neg_hi:[1,0,0]
	v_fma_f32 v114, -v5, v56, v114
	v_pk_fma_f32 v[116:117], v[6:7], v[2:3], v[116:117] op_sel_hi:[0,1,1] neg_lo:[1,0,0] neg_hi:[1,0,0]
	v_pk_fma_f32 v[118:119], v[6:7], v[46:47], v[118:119] op_sel_hi:[0,1,1] neg_lo:[1,0,0] neg_hi:[1,0,0]
	v_fma_f32 v120, -v6, v56, v120
	v_pk_mul_f32 v[142:143], v[6:7], v[58:59] op_sel:[1,0]
	v_pk_mul_f32 v[178:179], v[6:7], v[66:67] op_sel:[1,0]
	v_mul_f32_e64 v184, v7, v106
	s_waitcnt lgkmcnt(1)
	v_pk_mul_f32 v[144:145], v[8:9], v[58:59] op_sel_hi:[0,1]
	v_pk_mul_f32 v[180:181], v[8:9], v[66:67] op_sel_hi:[0,1]
	v_mul_f32_e64 v186, v8, v106
	v_pk_mul_f32 v[146:147], v[8:9], v[58:59] op_sel:[1,0]
	v_pk_mul_f32 v[182:183], v[8:9], v[66:67] op_sel:[1,0]
	v_mul_f32_e64 v188, v9, v106
	v_pk_fma_f32 v[142:143], v[8:9], v[110:111], v[142:143] op_sel_hi:[0,1,1]
	v_pk_fma_f32 v[178:179], v[8:9], v[112:113], v[178:179] op_sel_hi:[0,1,1]
	v_fma_f32 v184, v8, v114, v184
	v_pk_fma_f32 v[144:145], v[10:11], v[110:111], v[144:145] op_sel_hi:[0,1,1]
	v_pk_fma_f32 v[180:181], v[10:11], v[112:113], v[180:181] op_sel_hi:[0,1,1]
	v_fma_f32 v186, v10, v114, v186
	v_pk_fma_f32 v[146:147], v[10:11], v[110:111], v[146:147] op_sel:[1,0,0]
	v_pk_fma_f32 v[182:183], v[10:11], v[112:113], v[182:183] op_sel:[1,0,0]
	v_fma_f32 v188, v11, v114, v188
	v_pk_fma_f32 v[142:143], v[8:9], v[116:117], v[142:143] op_sel:[1,0,0]
	v_pk_fma_f32 v[178:179], v[8:9], v[118:119], v[178:179] op_sel:[1,0,0]
	v_fma_f32 v184, v9, v120, v184
	v_pk_fma_f32 v[144:145], v[10:11], v[116:117], v[144:145] op_sel:[1,0,0]
	v_pk_fma_f32 v[180:181], v[10:11], v[118:119], v[180:181] op_sel:[1,0,0]
	v_fma_f32 v186, v11, v120, v186
	s_waitcnt lgkmcnt(0)
	v_pk_fma_f32 v[146:147], v[52:53], v[116:117], v[146:147] op_sel_hi:[0,1,1]
	v_pk_fma_f32 v[182:183], v[52:53], v[118:119], v[182:183] op_sel_hi:[0,1,1]
	v_fma_f32 v188, v52, v120, v188
	v_pk_mul_f32 v[190:191], v[4:5], v[142:143] op_sel_hi:[0,1]
	v_pk_mul_f32 v[192:193], v[4:5], v[178:179] op_sel_hi:[0,1]
	v_mul_f32_e64 v194, v4, v184
	v_pk_fma_f32 v[190:191], v[4:5], v[144:145], v[190:191] op_sel:[1,0,0]
	v_pk_fma_f32 v[192:193], v[4:5], v[180:181], v[192:193] op_sel:[1,0,0]
	v_fma_f32 v194, v5, v186, v194
	v_pk_fma_f32 v[190:191], v[6:7], v[146:147], v[190:191] op_sel_hi:[0,1,1]
	v_pk_fma_f32 v[192:193], v[6:7], v[182:183], v[192:193] op_sel_hi:[0,1,1]
	v_fma_f32 v194, v6, v188, v194
	v_pk_fma_f32 v[190:191], v[52:53], v[2:3], v[190:191] op_sel:[1,0,0] neg_lo:[0,0,1] neg_hi:[0,0,1]
	v_pk_fma_f32 v[192:193], v[52:53], v[46:47], v[192:193] op_sel:[1,0,0] neg_lo:[0,0,1] neg_hi:[0,0,1]
	v_fma_f32 v194, v53, v56, -v194
	v_cmp_eq_u32_e64 s[10:11], 1, v55
	v_cmp_eq_u32_e64 s[14:15], 2, v55
	v_cmp_eq_u32_e64 s[20:21], 3, v55
	v_cmp_eq_u32_e64 s[22:23], 4, v55
	v_cmp_eq_u32_e64 s[30:31], 5, v55
	v_add_f32_dpp v2, v142, v142 wave_shr:1 row_mask:0xf bank_mask:0xf bound_ctrl:1
	v_add_f32_dpp v3, v143, v143 wave_shr:1 row_mask:0xf bank_mask:0xf bound_ctrl:1
	v_add_f32_dpp v46, v178, v178 wave_shr:1 row_mask:0xf bank_mask:0xf bound_ctrl:1
	v_add_f32_dpp v47, v179, v179 wave_shr:1 row_mask:0xf bank_mask:0xf bound_ctrl:1
	v_add_f32_dpp v56, v184, v184 wave_shr:1 row_mask:0xf bank_mask:0xf bound_ctrl:1
	v_add_f32_dpp v58, v144, v144 wave_shr:1 row_mask:0xf bank_mask:0xf bound_ctrl:1
	v_add_f32_dpp v59, v145, v145 wave_shr:1 row_mask:0xf bank_mask:0xf bound_ctrl:1
	v_add_f32_dpp v66, v180, v180 wave_shr:1 row_mask:0xf bank_mask:0xf bound_ctrl:1
	v_add_f32_dpp v67, v181, v181 wave_shr:1 row_mask:0xf bank_mask:0xf bound_ctrl:1
	v_add_f32_dpp v106, v186, v186 wave_shr:1 row_mask:0xf bank_mask:0xf bound_ctrl:1
	v_add_f32_dpp v110, v146, v146 wave_shr:1 row_mask:0xf bank_mask:0xf bound_ctrl:1
	v_add_f32_dpp v111, v147, v147 wave_shr:1 row_mask:0xf bank_mask:0xf bound_ctrl:1
	v_add_f32_dpp v112, v182, v182 wave_shr:1 row_mask:0xf bank_mask:0xf bound_ctrl:1
	v_add_f32_dpp v113, v183, v183 wave_shr:1 row_mask:0xf bank_mask:0xf bound_ctrl:1
	v_add_f32_dpp v114, v188, v188 wave_shr:1 row_mask:0xf bank_mask:0xf bound_ctrl:1
	v_add_f32_dpp v116, v190, v190 wave_shr:1 row_mask:0xf bank_mask:0xf bound_ctrl:1
	v_add_f32_dpp v117, v191, v191 wave_shr:1 row_mask:0xf bank_mask:0xf bound_ctrl:1
	v_add_f32_dpp v118, v192, v192 wave_shr:1 row_mask:0xf bank_mask:0xf bound_ctrl:1
	v_add_f32_dpp v119, v193, v193 wave_shr:1 row_mask:0xf bank_mask:0xf bound_ctrl:1
	v_add_f32_dpp v120, v194, v194 wave_shr:1 row_mask:0xf bank_mask:0xf bound_ctrl:1
	v_add_f32_dpp v2, v142, v2 wave_shl:1 row_mask:0xf bank_mask:0xf bound_ctrl:1
	v_add_f32_dpp v3, v143, v3 wave_shl:1 row_mask:0xf bank_mask:0xf bound_ctrl:1
	v_add_f32_dpp v46, v178, v46 wave_shl:1 row_mask:0xf bank_mask:0xf bound_ctrl:1
	v_add_f32_dpp v47, v179, v47 wave_shl:1 row_mask:0xf bank_mask:0xf bound_ctrl:1
	v_add_f32_dpp v56, v184, v56 wave_shl:1 row_mask:0xf bank_mask:0xf bound_ctrl:1
	v_add_f32_dpp v58, v144, v58 wave_shl:1 row_mask:0xf bank_mask:0xf bound_ctrl:1
	v_add_f32_dpp v59, v145, v59 wave_shl:1 row_mask:0xf bank_mask:0xf bound_ctrl:1
	v_add_f32_dpp v66, v180, v66 wave_shl:1 row_mask:0xf bank_mask:0xf bound_ctrl:1
	v_add_f32_dpp v67, v181, v67 wave_shl:1 row_mask:0xf bank_mask:0xf bound_ctrl:1
	v_add_f32_dpp v106, v186, v106 wave_shl:1 row_mask:0xf bank_mask:0xf bound_ctrl:1
	v_add_f32_dpp v110, v146, v110 wave_shl:1 row_mask:0xf bank_mask:0xf bound_ctrl:1
	v_add_f32_dpp v111, v147, v111 wave_shl:1 row_mask:0xf bank_mask:0xf bound_ctrl:1
	v_add_f32_dpp v112, v182, v112 wave_shl:1 row_mask:0xf bank_mask:0xf bound_ctrl:1
	v_add_f32_dpp v113, v183, v113 wave_shl:1 row_mask:0xf bank_mask:0xf bound_ctrl:1
	v_add_f32_dpp v114, v188, v114 wave_shl:1 row_mask:0xf bank_mask:0xf bound_ctrl:1
	v_add_f32_dpp v116, v190, v116 wave_shl:1 row_mask:0xf bank_mask:0xf bound_ctrl:1
	v_add_f32_dpp v117, v191, v117 wave_shl:1 row_mask:0xf bank_mask:0xf bound_ctrl:1
	v_add_f32_dpp v118, v192, v118 wave_shl:1 row_mask:0xf bank_mask:0xf bound_ctrl:1
	v_add_f32_dpp v119, v193, v119 wave_shl:1 row_mask:0xf bank_mask:0xf bound_ctrl:1
	v_add_f32_dpp v120, v194, v120 wave_shl:1 row_mask:0xf bank_mask:0xf bound_ctrl:1
	v_pk_add_f32 v[142:143], v[148:149], v[2:3]
	v_pk_add_f32 v[144:145], v[68:69], v[46:47]
	v_add_f32_e64 v68, v96, v56
	v_pk_add_f32 v[96:97], v[98:99], v[58:59]
	v_pk_add_f32 v[98:99], v[100:101], v[66:67]
	v_add_f32_e64 v100, v122, v106
	v_pk_add_f32 v[122:123], v[124:125], v[110:111]
	v_pk_add_f32 v[124:125], v[126:127], v[112:113]
	v_add_f32_e64 v126, v128, v114
	v_pk_add_f32 v[128:129], v[130:131], v[116:117]
	v_pk_add_f32 v[130:131], v[132:133], v[118:119]
	v_add_f32_e64 v132, v134, v120
	v_pk_fma_f32 v[128:129], v[32:33], v[142:143], v[128:129] op_sel_hi:[0,1,1]
	v_pk_fma_f32 v[130:131], v[32:33], v[144:145], v[130:131] op_sel_hi:[0,1,1]
	v_fma_f32 v132, v32, v68, v132
	v_pk_fma_f32 v[128:129], v[32:33], v[96:97], v[128:129] op_sel:[1,0,0]
	v_pk_fma_f32 v[130:131], v[32:33], v[98:99], v[130:131] op_sel:[1,0,0]
	v_fma_f32 v132, v33, v100, v132
	v_pk_fma_f32 v[128:129], v[34:35], v[122:123], v[128:129] op_sel_hi:[0,1,1]
	v_pk_fma_f32 v[130:131], v[34:35], v[124:125], v[130:131] op_sel_hi:[0,1,1]
	v_fma_f32 v132, v34, v126, v132
	v_cndmask_b32_e64 v134, 0, v1, s[10:11]
	v_cndmask_b32_e64 v135, 0, v1, s[14:15]
	v_cndmask_b32_e64 v146, 0, v1, s[20:21]
	v_cndmask_b32_e64 v147, 0, v1, s[22:23]
	v_cndmask_b32_e64 v148, 0, v1, s[30:31]
	v_pk_fma_f32 v[128:129], v[12:13], v[54:55], v[128:129] op_sel_hi:[1,0,1] neg_lo:[0,0,1] neg_hi:[0,0,1]
	v_pk_fma_f32 v[130:131], v[14:15], v[54:55], v[130:131] op_sel_hi:[1,0,1] neg_lo:[0,0,1] neg_hi:[0,0,1]
	v_fma_f32 v132, v16, v54, -v132
	s_add_i32 s4, s34, 9
	s_cmpk_lt_i32 s4, 0x201
	s_cselect_b64 s[12:13], s[0:1], 0
	v_pk_add_f32 v[128:129], v[128:129], v[134:135] neg_lo:[0,1] neg_hi:[0,1]
	v_pk_add_f32 v[130:131], v[130:131], v[146:147] neg_lo:[0,1] neg_hi:[0,1]
	v_add_f32_e64 v132, v132, -v148
	v_pk_mul_f32 v[178:179], v[128:129], v[128:129]
	v_pk_fma_f32 v[178:179], v[130:131], v[130:131], v[178:179]
	v_add_f32_e32 v178, v178, v179
	v_fma_f32 v178, v132, v132, v178
	v_cndmask_b32_e64 v179, 0, v178, s[12:13]
	v_add_f32_e32 v0, v0, v179
.LBB0_29:
	s_nop 1
	v_add_f32_dpp v0, v0, v0 row_shr:1 row_mask:0xf bank_mask:0xf bound_ctrl:1
	v_mov_b32_e32 v2, 0
	v_cmp_eq_u32_e32 vcc, 63, v19
	v_add_f32_dpp v0, v0, v0 row_shr:2 row_mask:0xf bank_mask:0xf bound_ctrl:1
	s_nop 1
	v_add_f32_dpp v0, v0, v0 row_shr:4 row_mask:0xf bank_mask:0xf bound_ctrl:1
	s_nop 1
	v_add_f32_dpp v1, v0, v0 row_shr:8 row_mask:0xf bank_mask:0xf bound_ctrl:1
	v_mov_b32_e32 v0, 0
	s_nop 0
	v_mov_b32_dpp v2, v1 row_bcast:15 row_mask:0xa bank_mask:0xf
	v_add_f32_e32 v1, v1, v2
	v_mov_b32_e32 v2, 0
	s_nop 1
	v_mov_b32_dpp v2, v1 row_bcast:31 row_mask:0xc bank_mask:0xf
	s_and_saveexec_b64 s[0:1], vcc
	s_cbranch_execz .LBB0_31
	s_lshl_b32 s4, s2, 1
	s_add_i32 s4, s3, s4
	s_mov_b32 s5, 0
	s_lshl_b64 s[4:5], s[4:5], 2
	s_add_u32 s4, s28, s4
	s_addc_u32 s5, s29, s5
	v_add_f32_e32 v1, v1, v2
	global_store_dword v0, v1, s[4:5] sc0 sc1

.LBB0_32:
	s_and_b64 vcc, exec, s[0:1]
	s_cbranch_vccz .LBB0_35
	s_mov_b32 s1, 0
	v_cmp_eq_u32_e32 vcc, 0, v19
	s_and_saveexec_b64 s[4:5], vcc
	s_cbranch_execz .LBB0_35
	s_lshl_b32 s0, s2, 1
	s_add_i32 s0, s3, s0
	s_lshl_b64 s[0:1], s[0:1], 2
	s_add_u32 s0, s28, s0
	s_addc_u32 s1, s29, s1
	v_mov_b32_e32 v0, 0
	global_store_dword v0, v0, s[0:1] sc0 sc1

	.amdhsa_kernel _Z16closed_form_mainPKfS0_PKiPf
		.amdhsa_group_segment_fixed_size 6144
		.amdhsa_private_segment_fixed_size 0
		.amdhsa_kernarg_size 32
		.amdhsa_user_sgpr_count 2
		.amdhsa_user_sgpr_dispatch_ptr 0
		.amdhsa_user_sgpr_queue_ptr 0
		.amdhsa_user_sgpr_kernarg_segment_ptr 1
		.amdhsa_user_sgpr_dispatch_id 0
		.amdhsa_user_sgpr_kernarg_preload_length 0
		.amdhsa_user_sgpr_kernarg_preload_offset 0
		.amdhsa_user_sgpr_private_segment_size 0
		.amdhsa_uses_dynamic_stack 0
		.amdhsa_enable_private_segment 0
		.amdhsa_system_sgpr_workgroup_id_x 1
		.amdhsa_system_sgpr_workgroup_id_y 0
		.amdhsa_system_sgpr_workgroup_id_z 0
		.amdhsa_system_sgpr_workgroup_info 0
		.amdhsa_system_vgpr_workitem_id 0
		.amdhsa_next_free_vgpr 216
		.amdhsa_next_free_sgpr 48
		.amdhsa_accum_offset 216
		.amdhsa_reserve_vcc 1
		.amdhsa_float_round_mode_32 0
		.amdhsa_float_round_mode_16_64 0
		.amdhsa_float_denorm_mode_32 3
		.amdhsa_float_denorm_mode_16_64 3
		.amdhsa_dx10_clamp 1
		.amdhsa_ieee_mode 1
		.amdhsa_fp16_overflow 0
		.amdhsa_tg_split 0
		.amdhsa_exception_fp_ieee_invalid_op 0
		.amdhsa_exception_fp_denorm_src 0
		.amdhsa_exception_fp_ieee_div_zero 0
		.amdhsa_exception_fp_ieee_overflow 0
		.amdhsa_exception_fp_ieee_underflow 0
		.amdhsa_exception_fp_ieee_inexact 0
		.amdhsa_exception_int_div_zero 0
	.end_amdhsa_kernel

amdhsa.kernels:
  - .agpr_count:     0
    .args:
      - .address_space:  global
        .offset:         0
        .size:           8
        .value_kind:     global_buffer
      - .address_space:  global
        .offset:         8
        .size:           8
        .value_kind:     global_buffer
      - .address_space:  global
        .offset:         16
        .size:           8
        .value_kind:     global_buffer
      - .address_space:  global
        .offset:         24
        .size:           8
        .value_kind:     global_buffer
    .group_segment_fixed_size: 6144
    .kernarg_segment_align: 8
    .kernarg_segment_size: 32
    .language:       OpenCL C
    .language_version:
      - 2
      - 0
    .max_flat_workgroup_size: 128
    .name:           _Z16closed_form_mainPKfS0_PKiPf
    .private_segment_fixed_size: 0
    .sgpr_count:     54
    .sgpr_spill_count: 0
    .symbol:         _Z16closed_form_mainPKfS0_PKiPf.kd
    .uniform_work_group_size: 1
    .uses_dynamic_stack: false
    .vgpr_count:     216
    .vgpr_spill_count: 0
    .wavefront_size: 64
  - .agpr_count:     0
    .args:
      - .actual_access:  read_only
        .address_space:  global
        .offset:         0
        .size:           8
        .value_kind:     global_buffer
      - .actual_access:  write_only
        .address_space:  global
        .offset:         8
        .size:           8
        .value_kind:     global_buffer
    .group_segment_fixed_size: 0
    .kernarg_segment_align: 8
    .kernarg_segment_size: 16
    .language:       OpenCL C
    .language_version:
      - 2
      - 0
    .max_flat_workgroup_size: 64
    .name:           _Z17closed_form_finalPK15HIP_vector_typeIfLj4EEPf
    .private_segment_fixed_size: 0
    .sgpr_count:     10
    .sgpr_spill_count: 0
    .symbol:         _Z17closed_form_finalPK15HIP_vector_typeIfLj4EEPf.kd
    .uniform_work_group_size: 1
    .uses_dynamic_stack: false
    .vgpr_count:     36
    .vgpr_spill_count: 0
    .wavefront_size: 64
